# wave reductions in LN0/LN1/LN2 (29 sites): ds_bpermute butterflies replaced by DPP row ops + permlane16/32 swaps (same summation tree)
# speedup vs baseline: 1.0208x; 1.0037x over previous
; #define GAS __attribute__((address_space(1)))
; #define FLANE lane_id()
; __device__ __forceinline__ float wave_sum(float v) {
; #pragma unroll
;     for (int o = 1; o < 64; o <<= 1) v += __shfl_xor(v, o);
;     return v;
; __device__ __forceinline__ void p0_prologue(Frame& F) {
;     ...
;         for (int m = m0; m < m1; m += mst) {
;             const GAS f32x4* xr = (const GAS f32x4*)(F.x + (size_t)m * D) + FLANE;
;             f32x4 v[8]; float s = 0.f;
; #pragma unroll
;             for (int j = 0; j < 8; ++j) { v[j] = xr[64 * j]; s += (v[j][0] + v[j][1]) + (v[j][2] + v[j][3]); }
;             const float mean = wave_sum(s) * (1.f / D); float s2 = 0.f;
; #pragma unroll
;             for (int j = 0; j < 8; ++j) { v[j] = v[j] - mean; s2 += (v[j][0] * v[j][0] + v[j][1] * v[j][1]) + (v[j][2] * v[j][2] + v[j][3] * v[j][3]); }
.LBB0_16:
	v_mbcnt_lo_u32_b32 v0, -1, 0
	v_mbcnt_hi_u32_b32 v0, -1, v0
	s_nop 0
	v_ashrrev_i32_e32 v1, 31, v0
	v_lshl_add_u64 v[8:9], v[0:1], 4, s[42:43]
	global_load_dwordx4 v[4:7], v[8:9], off offset:-4096
	global_load_dwordx4 v[0:3], v[8:9], off offset:-3072
	global_load_dwordx4 v[12:15], v[8:9], off offset:-2048
	v_add_co_u32_e32 v10, vcc, 0xfffff000, v8
	global_load_dwordx4 v[16:19], v[8:9], off offset:-1024
	s_nop 0
	v_addc_co_u32_e32 v11, vcc, -1, v9, vcc
	global_load_dwordx4 v[28:31], v[10:11], off offset:-3072
	global_load_dwordx4 v[24:27], v[10:11], off offset:-2048
	global_load_dwordx4 v[20:23], v[10:11], off offset:-1024
	s_nop 0
	global_load_dwordx4 v[8:11], v[8:9], off
	v_cmp_lt_i32_e32 vcc, v47, v46
	s_waitcnt vmcnt(7)
	v_add_f32_e32 v34, v6, v7
	v_cndmask_b32_e32 v32, v45, v47, vcc
	v_lshlrev_b32_e32 v57, 2, v32
	v_add_f32_e32 v32, v4, v5
	s_waitcnt vmcnt(6)
	v_mov_b32_e32 v33, v2
	v_mov_b32_e32 v35, v3
	s_waitcnt vmcnt(5)
	v_mov_b32_e32 v38, v13
	v_mov_b32_e32 v39, v14
	v_mov_b32_e32 v40, v12
	v_mov_b32_e32 v41, v15
	v_pk_add_f32 v[32:33], v[32:33], v[34:35]
	v_pk_add_f32 v[34:35], v[38:39], v[40:41]
	s_waitcnt vmcnt(3)
	v_mov_b32_e32 v38, v28
	s_waitcnt vmcnt(2)
	v_mov_b32_e32 v39, v24
	v_mov_b32_e32 v40, v29
	v_mov_b32_e32 v41, v25
	v_mov_b32_e32 v60, v30
	v_mov_b32_e32 v61, v26
	v_mov_b32_e32 v62, v31
	v_mov_b32_e32 v63, v27
	s_waitcnt vmcnt(1)
	v_mov_b32_e32 v64, v21
	v_mov_b32_e32 v65, v22
	v_mov_b32_e32 v66, v20
	v_mov_b32_e32 v67, v23
	v_pk_add_f32 v[38:39], v[38:39], v[40:41]
	v_pk_add_f32 v[40:41], v[60:61], v[62:63]
	v_pk_add_f32 v[60:61], v[64:65], v[66:67]
	v_pk_add_f32 v[38:39], v[38:39], v[40:41]
	v_pk_add_f32 v[40:41], v[60:61], v[60:61] op_sel:[0,1] op_sel_hi:[1,0]
	v_add_f32_e32 v36, 0, v38
	v_mov_b32_e32 v37, v0
	v_mov_b32_e32 v41, v1
	v_add_f32_e32 v36, v36, v39
	v_pk_add_f32 v[36:37], v[36:37], v[40:41]
	v_pk_add_f32 v[34:35], v[34:35], v[34:35] op_sel:[0,1] op_sel_hi:[1,0]
	v_pk_add_f32 v[32:33], v[36:37], v[32:33]
	v_add_f32_e32 v42, v16, v17
	v_pk_add_f32 v[32:33], v[32:33], v[32:33] op_sel:[0,1] op_sel_hi:[1,0]
	v_add_f32_e32 v58, v18, v19
	s_waitcnt vmcnt(0)
	v_mov_b32_e32 v43, v10
	v_mov_b32_e32 v59, v11
	v_mov_b32_e32 v35, v9
	v_mov_b32_e32 v33, v8
	v_pk_add_f32 v[42:43], v[42:43], v[58:59]
	v_pk_add_f32 v[32:33], v[32:33], v[34:35]
	v_cmp_lt_i32_e32 vcc, v48, v46
	v_pk_add_f32 v[32:33], v[32:33], v[42:43]
	s_nop 0
	v_add_f32_e32 v32, v32, v33
	v_cndmask_b32_e32 v34, v45, v48, vcc
	v_lshlrev_b32_e32 v58, 2, v34
	v_cmp_lt_i32_e32 vcc, v49, v46
	s_waitcnt lgkmcnt(0)
	s_nop 1
	v_add_f32_dpp v32, v32, v32 quad_perm:[1,0,3,2] row_mask:0xf bank_mask:0xf
	v_cndmask_b32_e32 v34, v45, v49, vcc
	v_lshlrev_b32_e32 v59, 2, v34
	v_cmp_lt_i32_e32 vcc, v50, v46
	s_waitcnt lgkmcnt(0)
	s_nop 1
	v_add_f32_dpp v32, v32, v32 quad_perm:[2,3,0,1] row_mask:0xf bank_mask:0xf
	v_cndmask_b32_e32 v34, v45, v50, vcc
	v_lshlrev_b32_e32 v60, 2, v34
	v_cmp_lt_i32_e32 vcc, v51, v46
	s_waitcnt lgkmcnt(0)
	s_nop 1
	v_add_f32_dpp v32, v32, v32 row_half_mirror row_mask:0xf bank_mask:0xf
	v_cndmask_b32_e32 v34, v45, v51, vcc
	v_lshlrev_b32_e32 v61, 2, v34
	v_cmp_lt_i32_e32 vcc, v52, v46
	s_waitcnt lgkmcnt(0)
	s_nop 1
	v_add_f32_dpp v32, v32, v32 row_mirror row_mask:0xf bank_mask:0xf
	v_cndmask_b32_e32 v34, v45, v52, vcc
	v_lshlrev_b32_e32 v62, 2, v34
	s_waitcnt lgkmcnt(0)
	v_mov_b32_e32 v33, v32
	s_nop 1
	v_permlane16_swap_b32_e32 v32, v33
	v_add_f32_e32 v32, v32, v33
	s_waitcnt lgkmcnt(0)
	v_mov_b32_e32 v33, v32
	s_nop 1
	v_permlane32_swap_b32_e32 v32, v33
	v_add_f32_e32 v56, v32, v33
	v_fmamk_f32 v29, v56, 0xba000000, v29
	v_fmamk_f32 v25, v56, 0xba000000, v25
	v_fmamk_f32 v21, v56, 0xba000000, v21
	v_fmamk_f32 v20, v56, 0xba000000, v20
	v_fmamk_f32 v23, v56, 0xba000000, v23
	v_fmac_f32_e32 v22, 0xba000000, v56
	v_fmamk_f32 v35, v56, 0xba000000, v31
	v_fmamk_f32 v27, v56, 0xba000000, v27
	v_fmac_f32_e32 v28, 0xba000000, v56
	v_fmac_f32_e32 v24, 0xba000000, v56
	v_fmamk_f32 v34, v56, 0xba000000, v30
	v_fmamk_f32 v26, v56, 0xba000000, v26
	v_fmamk_f32 v37, v56, 0xba000000, v5
	v_fmamk_f32 v36, v56, 0xba000000, v4
	v_pk_mul_f32 v[4:5], v[22:23], v[22:23]
	v_pk_mul_f32 v[30:31], v[20:21], v[20:21]
	v_mov_b32_e32 v32, v29
	v_mov_b32_e32 v33, v25
	v_mov_b32_e32 v42, v35
	v_mov_b32_e32 v43, v27
	v_fmamk_f32 v39, v56, 0xba000000, v3
	v_fmamk_f32 v38, v56, 0xba000000, v2
	v_mov_b32_e32 v2, v28
	v_mov_b32_e32 v3, v24
	v_mov_b32_e32 v40, v34
	v_mov_b32_e32 v41, v26
	v_pk_mov_b32 v[66:67], v[30:31], v[4:5] op_sel:[1,0]
	v_mov_b32_e32 v31, v5
	v_pk_mul_f32 v[4:5], v[32:33], v[32:33]
	v_pk_mul_f32 v[32:33], v[42:43], v[42:43]
	v_fmac_f32_e32 v6, 0xba000000, v56
	v_pk_fma_f32 v[2:3], v[2:3], v[2:3], v[4:5]
	v_pk_fma_f32 v[4:5], v[40:41], v[40:41], v[32:33]
	v_fmamk_f32 v7, v56, 0xba000000, v7
	v_mul_f32_e32 v44, v36, v36
	v_mul_f32_e32 v64, v6, v6
	v_pk_add_f32 v[30:31], v[66:67], v[30:31]
	v_pk_add_f32 v[2:3], v[2:3], v[4:5]
	v_fmamk_f32 v1, v56, 0xba000000, v1
	v_fmac_f32_e32 v0, 0xba000000, v56
	v_pk_fma_f32 v[42:43], v[36:37], v[36:37], v[44:45] op_sel_hi:[1,1,0]
	v_pk_fma_f32 v[64:65], v[6:7], v[6:7], v[64:65] op_sel_hi:[1,1,0]
	v_pk_add_f32 v[30:31], v[30:31], v[30:31] op_sel_hi:[0,1]
	v_pk_add_f32 v[2:3], v[2:3], v[2:3] op_sel_hi:[0,1]
	v_mul_f32_e32 v42, v0, v0
	v_mul_f32_e32 v64, v1, v1
	v_mul_f32_e32 v30, v38, v38
	v_mul_f32_e32 v2, v39, v39
	v_pk_add_f32 v[4:5], v[42:43], v[64:65]
	v_pk_add_f32 v[2:3], v[30:31], v[2:3]
	v_fmamk_f32 v41, v56, 0xba000000, v13
	v_fmamk_f32 v40, v56, 0xba000000, v12
	v_fmamk_f32 v15, v56, 0xba000000, v15
	v_fmac_f32_e32 v14, 0xba000000, v56
	v_pk_add_f32 v[2:3], v[4:5], v[2:3]
	v_pk_mul_f32 v[4:5], v[14:15], v[14:15]
	v_pk_mul_f32 v[12:13], v[40:41], v[40:41]
	v_fmamk_f32 v16, v56, 0xba000000, v16
	v_pk_mov_b32 v[30:31], v[12:13], v[4:5] op_sel:[1,0]
	v_mov_b32_e32 v13, v5
	v_pk_add_f32 v[4:5], v[30:31], v[12:13]
	v_fmamk_f32 v17, v56, 0xba000000, v17
	v_mul_f32_e32 v12, v16, v16
	v_fmac_f32_e32 v18, 0xba000000, v56
	v_pk_fma_f32 v[12:13], v[16:17], v[16:17], v[12:13] op_sel_hi:[1,1,0]
	v_fmamk_f32 v19, v56, 0xba000000, v19
	v_mul_f32_e32 v12, v18, v18
	v_pk_fma_f32 v[30:31], v[18:19], v[18:19], v[12:13] op_sel_hi:[1,1,0]
	v_fmamk_f32 v9, v56, 0xba000000, v9
	v_fmac_f32_e32 v8, 0xba000000, v56
	v_pk_add_f32 v[2:3], v[2:3], v[2:3] op_sel_hi:[0,1]
	v_pk_add_f32 v[4:5], v[4:5], v[4:5] op_sel_hi:[0,1]
	v_fmamk_f32 v43, v56, 0xba000000, v11
	v_fmamk_f32 v42, v56, 0xba000000, v10
	v_mul_f32_e32 v12, v8, v8
	v_mul_f32_e32 v30, v9, v9
	v_mul_f32_e32 v4, v42, v42
	v_mul_f32_e32 v2, v43, v43
	v_pk_add_f32 v[12:13], v[12:13], v[30:31]
	v_pk_add_f32 v[2:3], v[4:5], v[2:3]
	s_nop 0
	v_pk_add_f32 v[2:3], v[12:13], v[2:3]
	s_nop 0
	v_add_f32_e32 v2, v2, v3
	s_waitcnt lgkmcnt(0)
; #define GAS __attribute__((address_space(1)))
; #define FLANE lane_id()
; __device__ __forceinline__ float wave_sum(float v) {
; #pragma unroll
;     for (int o = 1; o < 64; o <<= 1) v += __shfl_xor(v, o);
;     return v;
; __device__ __forceinline__ void p0_prologue(Frame& F) {
;     ...
;             const float mean = wave_sum(s) * (1.f / D); float s2 = 0.f;
; #pragma unroll
;             for (int j = 0; j < 8; ++j) { v[j] = v[j] - mean; s2 += (v[j][0] * v[j][0] + v[j][1] * v[j][1]) + (v[j][2] * v[j][2] + v[j][3] * v[j][3]); }
;             const float rstd = 1.f / sqrtf(wave_sum(s2) * (1.f / D) + LN_EPS); float am = 0.f;
; #pragma unroll
;             for (int j = 0; j < 8; ++j) { const f32x4 g = *((const GAS f32x4*)F.ln0_g + FLANE + 64 * j), b = *((const GAS f32x4*)F.ln0_b + FLANE + 64 * j);
	s_nop 1
	v_add_f32_dpp v2, v2, v2 quad_perm:[1,0,3,2] row_mask:0xf bank_mask:0xf
	s_waitcnt lgkmcnt(0)
	s_nop 1
	v_add_f32_dpp v2, v2, v2 quad_perm:[2,3,0,1] row_mask:0xf bank_mask:0xf
	s_waitcnt lgkmcnt(0)
	s_nop 1
	v_add_f32_dpp v2, v2, v2 row_half_mirror row_mask:0xf bank_mask:0xf
	s_waitcnt lgkmcnt(0)
	s_nop 1
	v_add_f32_dpp v2, v2, v2 row_mirror row_mask:0xf bank_mask:0xf
	s_waitcnt lgkmcnt(0)
	v_mov_b32_e32 v3, v2
	s_nop 1
	v_permlane16_swap_b32_e32 v2, v3
	v_add_f32_e32 v2, v2, v3
	s_waitcnt lgkmcnt(0)
	v_mov_b32_e32 v3, v2
	s_nop 1
	v_permlane32_swap_b32_e32 v2, v3
	v_add_f32_e32 v44, v2, v3
	v_mbcnt_lo_u32_b32 v2, -1, 0
	v_mbcnt_hi_u32_b32 v2, -1, v2
	v_fmamk_f32 v44, v44, 0x3a000000, v53
	v_ashrrev_i32_e32 v3, 31, v2
	v_lshl_add_u64 v[2:3], v[2:3], 4, s[6:7]
	global_load_dwordx4 v[2:5], v[2:3], off
	v_mbcnt_lo_u32_b32 v10, -1, 0
	v_mbcnt_hi_u32_b32 v10, -1, v10
	v_mul_f32_e32 v63, 0x4f800000, v44
	v_ashrrev_i32_e32 v11, 31, v10
	v_lshl_add_u64 v[10:11], v[10:11], 4, s[8:9]
	global_load_dwordx4 v[10:13], v[10:11], off
	v_mbcnt_lo_u32_b32 v30, -1, 0
	v_mbcnt_hi_u32_b32 v30, -1, v30
	s_nop 0
	v_ashrrev_i32_e32 v31, 31, v30
	v_lshl_add_u64 v[30:31], v[30:31], 4, s[6:7]
	global_load_dwordx4 v[30:33], v[30:31], off offset:1024
	v_mbcnt_lo_u32_b32 v64, -1, 0
	v_mbcnt_hi_u32_b32 v64, -1, v64
	s_nop 0
	v_ashrrev_i32_e32 v65, 31, v64
	v_lshl_add_u64 v[64:65], v[64:65], 4, s[8:9]
	global_load_dwordx4 v[64:67], v[64:65], off offset:1024
	v_mbcnt_lo_u32_b32 v68, -1, 0
	v_mbcnt_hi_u32_b32 v68, -1, v68
	s_nop 0
	v_ashrrev_i32_e32 v69, 31, v68
	v_lshl_add_u64 v[68:69], v[68:69], 4, s[6:7]
	global_load_dwordx4 v[68:71], v[68:69], off offset:2048
	v_mbcnt_lo_u32_b32 v72, -1, 0
	v_mbcnt_hi_u32_b32 v72, -1, v72
	s_nop 0
	v_ashrrev_i32_e32 v73, 31, v72
	v_lshl_add_u64 v[72:73], v[72:73], 4, s[8:9]
	global_load_dwordx4 v[72:75], v[72:73], off offset:2048
	v_mbcnt_lo_u32_b32 v76, -1, 0
	v_mbcnt_hi_u32_b32 v76, -1, v76
	s_nop 0
	v_ashrrev_i32_e32 v77, 31, v76
	v_lshl_add_u64 v[76:77], v[76:77], 4, s[6:7]
	global_load_dwordx4 v[76:79], v[76:77], off offset:3072
	v_mbcnt_lo_u32_b32 v80, -1, 0
	v_mbcnt_hi_u32_b32 v80, -1, v80
	s_nop 0
	v_ashrrev_i32_e32 v81, 31, v80
	v_lshl_add_u64 v[80:81], v[80:81], 4, s[8:9]
	global_load_dwordx4 v[80:83], v[80:81], off offset:3072
	v_mbcnt_lo_u32_b32 v84, -1, 0
	v_mbcnt_hi_u32_b32 v84, -1, v84
	s_nop 0
	v_ashrrev_i32_e32 v85, 31, v84
	v_lshl_add_u64 v[84:85], v[84:85], 4, s[6:7]
	v_add_co_u32_e32 v84, vcc, s31, v84
	s_nop 1
	v_addc_co_u32_e32 v85, vcc, 0, v85, vcc
	global_load_dwordx4 v[84:87], v[84:85], off
	v_mbcnt_lo_u32_b32 v88, -1, 0
	v_mbcnt_hi_u32_b32 v88, -1, v88
	s_nop 0
	v_ashrrev_i32_e32 v89, 31, v88
	v_lshl_add_u64 v[88:89], v[88:89], 4, s[8:9]
	v_add_co_u32_e32 v88, vcc, s31, v88
	s_nop 1
	v_addc_co_u32_e32 v89, vcc, 0, v89, vcc
	global_load_dwordx4 v[88:91], v[88:89], off
	v_mbcnt_lo_u32_b32 v92, -1, 0
	v_mbcnt_hi_u32_b32 v92, -1, v92
	s_nop 0
	v_ashrrev_i32_e32 v93, 31, v92
	v_lshl_add_u64 v[92:93], v[92:93], 4, s[6:7]
	v_add_co_u32_e32 v92, vcc, s31, v92
	s_nop 1
	v_addc_co_u32_e32 v93, vcc, 0, v93, vcc
	global_load_dwordx4 v[92:95], v[92:93], off offset:1024
	v_mbcnt_lo_u32_b32 v96, -1, 0
	v_mbcnt_hi_u32_b32 v96, -1, v96
	s_nop 0
	v_ashrrev_i32_e32 v97, 31, v96
	v_lshl_add_u64 v[96:97], v[96:97], 4, s[8:9]
	v_add_co_u32_e32 v96, vcc, s31, v96
	s_nop 1
	v_addc_co_u32_e32 v97, vcc, 0, v97, vcc
	global_load_dwordx4 v[96:99], v[96:97], off offset:1024
	v_mbcnt_lo_u32_b32 v100, -1, 0
	v_mbcnt_hi_u32_b32 v100, -1, v100
	s_nop 0
	v_ashrrev_i32_e32 v101, 31, v100
	v_lshl_add_u64 v[100:101], v[100:101], 4, s[6:7]
	v_add_co_u32_e32 v100, vcc, s31, v100
	s_nop 1
	v_addc_co_u32_e32 v101, vcc, 0, v101, vcc
	global_load_dwordx4 v[100:103], v[100:101], off offset:2048
	v_mbcnt_lo_u32_b32 v104, -1, 0
	v_mbcnt_hi_u32_b32 v104, -1, v104
	s_nop 0
	v_ashrrev_i32_e32 v105, 31, v104
	v_lshl_add_u64 v[104:105], v[104:105], 4, s[8:9]
	v_add_co_u32_e32 v104, vcc, s31, v104
	s_nop 1
	v_addc_co_u32_e32 v105, vcc, 0, v105, vcc
	global_load_dwordx4 v[104:107], v[104:105], off offset:2048
	v_mbcnt_lo_u32_b32 v108, -1, 0
	v_mbcnt_hi_u32_b32 v108, -1, v108
	s_nop 0
	v_ashrrev_i32_e32 v109, 31, v108
	v_lshl_add_u64 v[108:109], v[108:109], 4, s[6:7]
	v_add_co_u32_e32 v108, vcc, s31, v108
	s_nop 1
	v_addc_co_u32_e32 v109, vcc, 0, v109, vcc
	global_load_dwordx4 v[108:111], v[108:109], off offset:3072
	v_mbcnt_lo_u32_b32 v112, -1, 0
	v_mbcnt_hi_u32_b32 v112, -1, v112
	s_nop 0
	v_ashrrev_i32_e32 v113, 31, v112
	v_lshl_add_u64 v[112:113], v[112:113], 4, s[8:9]
	v_add_co_u32_e32 v112, vcc, s31, v112
	s_nop 1
	v_addc_co_u32_e32 v113, vcc, 0, v113, vcc
	global_load_dwordx4 v[112:115], v[112:113], off offset:3072
	v_cmp_gt_f32_e32 vcc, s19, v44
	s_nop 1
	v_cndmask_b32_e32 v44, v44, v63, vcc
	v_sqrt_f32_e32 v63, v44
	s_nop 0
	v_add_u32_e32 v116, -1, v63
	v_fma_f32 v117, -v116, v63, v44
	v_cmp_ge_f32_e64 s[4:5], 0, v117
	v_add_u32_e32 v117, 1, v63
	s_nop 0
	v_cndmask_b32_e64 v116, v63, v116, s[4:5]
	v_fma_f32 v63, -v117, v63, v44
	v_cmp_lt_f32_e64 s[4:5], 0, v63
	s_nop 1
	v_cndmask_b32_e64 v63, v116, v117, s[4:5]
	v_mul_f32_e32 v116, 0x37800000, v63
	v_cndmask_b32_e32 v63, v63, v116, vcc
	v_cmp_class_f32_e32 vcc, v44, v54
	s_nop 1
	v_cndmask_b32_e32 v44, v63, v44, vcc
	v_div_scale_f32 v63, s[4:5], v44, v44, 1.0
	v_rcp_f32_e32 v116, v63
	s_nop 0
	v_fma_f32 v117, -v63, v116, 1.0
	v_fmac_f32_e32 v116, v117, v116
	v_div_scale_f32 v117, vcc, 1.0, v44, 1.0
	v_mul_f32_e32 v118, v117, v116
	v_fma_f32 v119, -v63, v118, v117
	v_fmac_f32_e32 v118, v119, v116
	v_fma_f32 v63, -v63, v118, v117
	v_div_fmas_f32 v63, v63, v116, v118
	v_div_fixup_f32 v44, v63, v44, 1.0
	v_pk_mul_f32 v[28:29], v[28:29], v[44:45] op_sel_hi:[1,0]
	v_pk_mul_f32 v[34:35], v[34:35], v[44:45] op_sel_hi:[1,0]
	v_pk_mul_f32 v[0:1], v[0:1], v[44:45] op_sel_hi:[1,0]
	s_waitcnt vmcnt(14)
; #define GAS __attribute__((address_space(1)))
; #define FLANE lane_id()
; __device__ __forceinline__ void p0_prologue(Frame& F) {
;     ...
;             for (int j = 0; j < 8; ++j) { const f32x4 g = *((const GAS f32x4*)F.ln0_g + FLANE + 64 * j), b = *((const GAS f32x4*)F.ln0_b + FLANE + 64 * j);
;                 v[j] = v[j] * rstd * g + b; am = fmaxf(am, fmaxf(fmaxf(fabsf(v[j][0]), fabsf(v[j][1])), fmaxf(fabsf(v[j][2]), fabsf(v[j][3])))); }
; #pragma unroll
;             for (int o = 1; o < 64; o <<= 1) am = fmaxf(am, __shfl_xor(am, o));
;             const float sc = am > 0.f ? am * (1.f / 127.f) : 1.f, inv = 1.f / sc;
; #pragma unroll
;             for (int j = 0; j < 8; ++j) { const int q0 = (int)__builtin_rintf(v[j][0] * inv), q1 = (int)__builtin_rintf(v[j][1] * inv), q2 = (int)__builtin_rintf(v[j][2] * inv), q3 = (int)__builtin_rintf(v[j][3] * inv);
;                 h0q[(size_t)m * (D / 4) + FLANE + 64 * j] = (unsigned)(q0 & 0xff) | ((unsigned)(q1 & 0xff) << 8) | ((unsigned)(q2 & 0xff) << 16) | ((unsigned)(q3 & 0xff) << 24); }
	v_pk_fma_f32 v[4:5], v[4:5], v[34:35], v[12:13]
	v_pk_fma_f32 v[2:3], v[2:3], v[28:29], v[10:11]
	v_pk_mul_f32 v[10:11], v[24:25], v[44:45] op_sel_hi:[1,0]
	v_pk_mul_f32 v[12:13], v[26:27], v[44:45] op_sel_hi:[1,0]
	s_waitcnt vmcnt(6)
	v_pk_fma_f32 v[28:29], v[84:85], v[0:1], v[88:89]
	v_pk_mul_f32 v[0:1], v[14:15], v[44:45] op_sel_hi:[1,0]
	v_pk_fma_f32 v[12:13], v[32:33], v[12:13], v[66:67]
	v_pk_fma_f32 v[10:11], v[30:31], v[10:11], v[64:65]
	s_waitcnt vmcnt(4)
	v_pk_fma_f32 v[30:31], v[94:95], v[0:1], v[98:99]
	v_pk_mul_f32 v[0:1], v[18:19], v[44:45] op_sel_hi:[1,0]
	v_pk_mul_f32 v[22:23], v[22:23], v[44:45] op_sel_hi:[1,0]
	v_pk_mul_f32 v[6:7], v[6:7], v[44:45] op_sel_hi:[1,0]
	v_pk_mul_f32 v[20:21], v[20:21], v[44:45] op_sel_hi:[1,0]
	v_pk_fma_f32 v[22:23], v[70:71], v[22:23], v[74:75]
	v_pk_mul_f32 v[24:25], v[36:37], v[44:45] op_sel_hi:[1,0]
	s_waitcnt vmcnt(2)
	v_pk_fma_f32 v[18:19], v[0:1], v[102:103], v[106:107]
	v_max_f32_e64 v0, |v4|, |v5|
	v_max_f32_e64 v1, |v12|, |v13|
	v_pk_fma_f32 v[6:7], v[78:79], v[6:7], v[82:83]
	v_max3_f32 v0, |v2|, |v3|, v0
	v_max3_f32 v1, |v10|, |v11|, v1
	v_pk_fma_f32 v[20:21], v[68:69], v[20:21], v[72:73]
	v_pk_fma_f32 v[24:25], v[76:77], v[24:25], v[80:81]
	v_pk_mul_f32 v[26:27], v[38:39], v[44:45] op_sel_hi:[1,0]
	v_max3_f32 v0, v0, 0, v1
	v_max_f32_e64 v1, |v22|, |v23|
	v_max_f32_e64 v32, |v6|, |v7|
	v_pk_fma_f32 v[26:27], v[86:87], v[26:27], v[90:91]
	v_pk_mul_f32 v[14:15], v[40:41], v[44:45] op_sel_hi:[1,0]
	v_max3_f32 v1, |v20|, |v21|, v1
	v_max3_f32 v32, |v24|, |v25|, v32
	v_pk_fma_f32 v[14:15], v[92:93], v[14:15], v[96:97]
	v_max3_f32 v0, v0, v1, v32
	v_max_f32_e64 v1, |v26|, |v27|
	v_max_f32_e64 v32, |v30|, |v31|
	v_max3_f32 v1, |v28|, |v29|, v1
	v_max3_f32 v32, |v14|, |v15|, v32
	v_max3_f32 v34, v0, v1, v32
	v_pk_mul_f32 v[0:1], v[8:9], v[44:45] op_sel_hi:[1,0]
	v_pk_mul_f32 v[8:9], v[42:43], v[44:45] op_sel_hi:[1,0]
	v_pk_mul_f32 v[16:17], v[16:17], v[44:45] op_sel_hi:[1,0]
	s_waitcnt vmcnt(0)
	v_pk_fma_f32 v[8:9], v[8:9], v[110:111], v[114:115]
	v_pk_fma_f32 v[16:17], v[16:17], v[100:101], v[104:105]
	v_pk_fma_f32 v[32:33], v[0:1], v[108:109], v[112:113]
	v_max_f32_e64 v0, |v18|, |v19|
	v_max_f32_e64 v1, |v8|, |v9|
	v_max3_f32 v0, |v16|, |v17|, v0
	v_max3_f32 v1, |v32|, |v33|, v1
	v_max3_f32 v0, v34, v0, v1
	s_waitcnt lgkmcnt(0)
	s_nop 1
	v_max_f32_dpp v0, v0, v0 quad_perm:[1,0,3,2] row_mask:0xf bank_mask:0xf
	s_waitcnt lgkmcnt(0)
	s_nop 1
	v_max_f32_dpp v0, v0, v0 quad_perm:[2,3,0,1] row_mask:0xf bank_mask:0xf
	s_waitcnt lgkmcnt(0)
	s_nop 1
	v_max_f32_dpp v0, v0, v0 row_half_mirror row_mask:0xf bank_mask:0xf
	s_waitcnt lgkmcnt(0)
	s_nop 1
	v_max_f32_dpp v0, v0, v0 row_mirror row_mask:0xf bank_mask:0xf
	s_waitcnt lgkmcnt(0)
	v_mov_b32_e32 v1, v0
	s_nop 1
	v_permlane16_swap_b32_e32 v0, v1
	v_max_f32_e32 v0, v0, v1
	s_waitcnt lgkmcnt(0)
	v_mov_b32_e32 v1, v0
	s_nop 1
	v_permlane32_swap_b32_e32 v0, v1
	v_max_f32_e32 v0, v0, v1
	v_mul_f32_e32 v1, 0x3c010204, v0
	v_cmp_lt_f32_e32 vcc, 0, v0
	s_nop 1
	v_cndmask_b32_e32 v0, 1.0, v1, vcc
	v_div_scale_f32 v1, s[4:5], v0, v0, 1.0
	v_rcp_f32_e32 v34, v1
	s_add_u32 s4, s28, s38
	s_addc_u32 s5, s29, s39
	v_fma_f32 v35, -v1, v34, 1.0
	v_fmac_f32_e32 v34, v35, v34
	v_div_scale_f32 v35, vcc, 1.0, v0, 1.0
	v_mul_f32_e32 v36, v35, v34
	v_fma_f32 v37, -v1, v36, v35
	v_fmac_f32_e32 v36, v37, v34
	v_fma_f32 v1, -v1, v36, v35
	v_div_fmas_f32 v1, v1, v34, v36
	v_div_fixup_f32 v1, v1, v0, 1.0
	v_mul_f32_e32 v3, v3, v1
	v_mul_f32_e32 v2, v2, v1
	v_rndne_f32_e32 v3, v3
	v_mul_f32_e32 v4, v4, v1
	v_mul_f32_e32 v5, v5, v1
	v_rndne_f32_e32 v2, v2
	v_cvt_i32_f32_e32 v3, v3
	v_rndne_f32_e32 v4, v4
	v_rndne_f32_e32 v5, v5
	v_cvt_i32_f32_e32 v2, v2
	v_cvt_i32_f32_sdwa v4, v4 dst_sel:WORD_1 dst_unused:UNUSED_PAD src0_sel:DWORD
	v_cvt_i32_f32_e32 v5, v5
	v_lshlrev_b32_e32 v3, 8, v3
	v_and_b32_e32 v3, 0xff00, v3
	v_and_b32_e32 v4, 0xff0000, v4
	v_perm_b32 v2, v5, v2, s50
	v_or3_b32 v4, v2, v3, v4
	v_mbcnt_lo_u32_b32 v2, -1, 0
	v_mbcnt_hi_u32_b32 v2, -1, v2
	v_mul_f32_e32 v5, v13, v1
	v_ashrrev_i32_e32 v3, 31, v2
	v_lshl_add_u64 v[2:3], v[2:3], 2, s[4:5]
	v_add_co_u32_e32 v2, vcc, s51, v2
	v_rndne_f32_e32 v5, v5
	s_nop 0
	v_addc_co_u32_e32 v3, vcc, 0, v3, vcc
	global_store_dword v[2:3], v4, off
	v_mul_f32_e32 v3, v11, v1
	v_mul_f32_e32 v2, v10, v1
	v_rndne_f32_e32 v3, v3
	v_mul_f32_e32 v4, v12, v1
	v_rndne_f32_e32 v2, v2
	v_cvt_i32_f32_e32 v3, v3
	v_rndne_f32_e32 v4, v4
	v_cvt_i32_f32_e32 v2, v2
	v_cvt_i32_f32_sdwa v4, v4 dst_sel:WORD_1 dst_unused:UNUSED_PAD src0_sel:DWORD
	v_cvt_i32_f32_e32 v5, v5
	v_lshlrev_b32_e32 v3, 8, v3
	v_and_b32_e32 v3, 0xff00, v3
	v_and_b32_e32 v4, 0xff0000, v4
	v_perm_b32 v2, v5, v2, s50
	v_or3_b32 v4, v2, v3, v4
	v_mbcnt_lo_u32_b32 v2, -1, 0
	v_mbcnt_hi_u32_b32 v2, -1, v2
	v_mul_f32_e32 v5, v23, v1
	v_ashrrev_i32_e32 v3, 31, v2
	v_lshl_add_u64 v[2:3], v[2:3], 2, s[4:5]
	v_add_co_u32_e32 v2, vcc, s51, v2
	v_rndne_f32_e32 v5, v5
	s_nop 0
	v_addc_co_u32_e32 v3, vcc, 0, v3, vcc
	global_store_dword v[2:3], v4, off offset:256
	v_mul_f32_e32 v3, v21, v1
; #define FLANE lane_id()
; __device__ __forceinline__ void p0_prologue(Frame& F) {
;     ...
;             for (int j = 0; j < 8; ++j) { const int q0 = (int)__builtin_rintf(v[j][0] * inv), q1 = (int)__builtin_rintf(v[j][1] * inv), q2 = (int)__builtin_rintf(v[j][2] * inv), q3 = (int)__builtin_rintf(v[j][3] * inv);
;                 h0q[(size_t)m * (D / 4) + FLANE + 64 * j] = (unsigned)(q0 & 0xff) | ((unsigned)(q1 & 0xff) << 8) | ((unsigned)(q2 & 0xff) << 16) | ((unsigned)(q3 & 0xff) << 24); }
;             if (FLANE == 0) { st0[2 * m] = mean; st0[2 * m + 1] = rstd; sx0[m] = sc; }
	v_mul_f32_e32 v2, v20, v1
	v_rndne_f32_e32 v3, v3
	v_mul_f32_e32 v4, v22, v1
	v_rndne_f32_e32 v2, v2
	v_cvt_i32_f32_e32 v3, v3
	v_rndne_f32_e32 v4, v4
	v_cvt_i32_f32_e32 v2, v2
	v_cvt_i32_f32_sdwa v4, v4 dst_sel:WORD_1 dst_unused:UNUSED_PAD src0_sel:DWORD
	v_cvt_i32_f32_e32 v5, v5
	v_lshlrev_b32_e32 v3, 8, v3
	v_and_b32_e32 v3, 0xff00, v3
	v_and_b32_e32 v4, 0xff0000, v4
	v_perm_b32 v2, v5, v2, s50
	v_or3_b32 v4, v2, v3, v4
	v_mbcnt_lo_u32_b32 v2, -1, 0
	v_mbcnt_hi_u32_b32 v2, -1, v2
	v_mul_f32_e32 v5, v7, v1
	v_ashrrev_i32_e32 v3, 31, v2
	v_lshl_add_u64 v[2:3], v[2:3], 2, s[4:5]
	v_add_co_u32_e32 v2, vcc, s51, v2
	v_rndne_f32_e32 v5, v5
	s_nop 0
	v_addc_co_u32_e32 v3, vcc, 0, v3, vcc
	global_store_dword v[2:3], v4, off offset:512
	v_mul_f32_e32 v3, v25, v1
	v_mul_f32_e32 v2, v24, v1
	v_rndne_f32_e32 v3, v3
	v_mul_f32_e32 v4, v6, v1
	v_rndne_f32_e32 v2, v2
	v_cvt_i32_f32_e32 v3, v3
	v_rndne_f32_e32 v4, v4
	v_cvt_i32_f32_e32 v2, v2
	v_cvt_i32_f32_sdwa v4, v4 dst_sel:WORD_1 dst_unused:UNUSED_PAD src0_sel:DWORD
	v_cvt_i32_f32_e32 v5, v5
	v_lshlrev_b32_e32 v3, 8, v3
	v_and_b32_e32 v3, 0xff00, v3
	v_and_b32_e32 v4, 0xff0000, v4
	v_perm_b32 v2, v5, v2, s50
	v_or3_b32 v4, v2, v3, v4
	v_mbcnt_lo_u32_b32 v2, -1, 0
	v_mbcnt_hi_u32_b32 v2, -1, v2
	v_mul_f32_e32 v5, v27, v1
	v_ashrrev_i32_e32 v3, 31, v2
	v_lshl_add_u64 v[2:3], v[2:3], 2, s[4:5]
	v_add_co_u32_e32 v2, vcc, s51, v2
	v_rndne_f32_e32 v5, v5
	s_nop 0
	v_addc_co_u32_e32 v3, vcc, 0, v3, vcc
	global_store_dword v[2:3], v4, off offset:768
	v_mul_f32_e32 v3, v29, v1
	v_mul_f32_e32 v2, v28, v1
	v_rndne_f32_e32 v3, v3
	v_mul_f32_e32 v4, v26, v1
	v_rndne_f32_e32 v2, v2
	v_cvt_i32_f32_e32 v3, v3
	v_rndne_f32_e32 v4, v4
	v_cvt_i32_f32_e32 v2, v2
	v_cvt_i32_f32_sdwa v4, v4 dst_sel:WORD_1 dst_unused:UNUSED_PAD src0_sel:DWORD
	v_cvt_i32_f32_e32 v5, v5
	v_lshlrev_b32_e32 v3, 8, v3
	v_and_b32_e32 v3, 0xff00, v3
	v_and_b32_e32 v4, 0xff0000, v4
	v_perm_b32 v2, v5, v2, s50
	v_or3_b32 v4, v2, v3, v4
	v_mbcnt_lo_u32_b32 v2, -1, 0
	v_mbcnt_hi_u32_b32 v2, -1, v2
	v_mul_f32_e32 v5, v31, v1
	v_ashrrev_i32_e32 v3, 31, v2
	v_lshl_add_u64 v[2:3], v[2:3], 2, s[4:5]
	v_add_co_u32_e32 v2, vcc, s51, v2
	v_rndne_f32_e32 v5, v5
	s_nop 0
	v_addc_co_u32_e32 v3, vcc, 0, v3, vcc
	global_store_dword v[2:3], v4, off offset:1024
	v_mul_f32_e32 v3, v15, v1
	v_mul_f32_e32 v2, v14, v1
	v_rndne_f32_e32 v3, v3
	v_mul_f32_e32 v4, v30, v1
	v_rndne_f32_e32 v2, v2
	v_cvt_i32_f32_e32 v3, v3
	v_rndne_f32_e32 v4, v4
	v_cvt_i32_f32_e32 v2, v2
	v_cvt_i32_f32_sdwa v4, v4 dst_sel:WORD_1 dst_unused:UNUSED_PAD src0_sel:DWORD
	v_cvt_i32_f32_e32 v5, v5
	v_lshlrev_b32_e32 v3, 8, v3
	v_and_b32_e32 v3, 0xff00, v3
	v_and_b32_e32 v4, 0xff0000, v4
	v_perm_b32 v2, v5, v2, s50
	v_or3_b32 v4, v2, v3, v4
	v_mbcnt_lo_u32_b32 v2, -1, 0
	v_mbcnt_hi_u32_b32 v2, -1, v2
	v_mul_f32_e32 v5, v19, v1
	v_ashrrev_i32_e32 v3, 31, v2
	v_lshl_add_u64 v[2:3], v[2:3], 2, s[4:5]
	v_add_co_u32_e32 v2, vcc, s51, v2
	v_rndne_f32_e32 v5, v5
	s_nop 0
	v_addc_co_u32_e32 v3, vcc, 0, v3, vcc
	global_store_dword v[2:3], v4, off offset:1280
	v_mul_f32_e32 v3, v17, v1
	v_mul_f32_e32 v2, v16, v1
	v_rndne_f32_e32 v3, v3
	v_mul_f32_e32 v4, v18, v1
	v_rndne_f32_e32 v2, v2
	v_cvt_i32_f32_e32 v3, v3
	v_rndne_f32_e32 v4, v4
	v_cvt_i32_f32_e32 v2, v2
	v_cvt_i32_f32_sdwa v4, v4 dst_sel:WORD_1 dst_unused:UNUSED_PAD src0_sel:DWORD
	v_cvt_i32_f32_e32 v5, v5
	v_lshlrev_b32_e32 v3, 8, v3
	v_and_b32_e32 v3, 0xff00, v3
	v_and_b32_e32 v4, 0xff0000, v4
	v_perm_b32 v2, v5, v2, s50
	v_or3_b32 v4, v2, v3, v4
	v_mbcnt_lo_u32_b32 v2, -1, 0
	v_mbcnt_hi_u32_b32 v2, -1, v2
	s_nop 0
	v_ashrrev_i32_e32 v3, 31, v2
	v_lshl_add_u64 v[2:3], v[2:3], 2, s[4:5]
	v_add_co_u32_e32 v2, vcc, s51, v2
	s_nop 1
	v_addc_co_u32_e32 v3, vcc, 0, v3, vcc
	global_store_dword v[2:3], v4, off offset:1536
	v_mul_f32_e32 v3, v33, v1
	v_mul_f32_e32 v2, v32, v1
	v_rndne_f32_e32 v3, v3
	v_mul_f32_e32 v4, v8, v1
	v_mul_f32_e32 v1, v9, v1
	v_rndne_f32_e32 v2, v2
	v_cvt_i32_f32_e32 v3, v3
	v_rndne_f32_e32 v4, v4
	v_rndne_f32_e32 v1, v1
	v_cvt_i32_f32_e32 v2, v2
	v_cvt_i32_f32_sdwa v4, v4 dst_sel:WORD_1 dst_unused:UNUSED_PAD src0_sel:DWORD
	v_cvt_i32_f32_e32 v1, v1
	v_lshlrev_b32_e32 v3, 8, v3
	v_and_b32_e32 v3, 0xff00, v3
	v_and_b32_e32 v4, 0xff0000, v4
	v_perm_b32 v1, v1, v2, s50
	v_or3_b32 v1, v1, v3, v4
	v_mbcnt_lo_u32_b32 v2, -1, 0
	v_mbcnt_hi_u32_b32 v2, -1, v2
	s_nop 0
	v_ashrrev_i32_e32 v3, 31, v2
	v_lshl_add_u64 v[2:3], v[2:3], 2, s[4:5]
	v_add_co_u32_e32 v2, vcc, 0x31e00000, v2
	s_nop 1
	v_addc_co_u32_e32 v3, vcc, 0, v3, vcc
	global_store_dword v[2:3], v1, off offset:1792
	v_mbcnt_lo_u32_b32 v1, -1, 0
	v_mbcnt_hi_u32_b32 v1, -1, v1
	s_nop 0
	v_cmp_eq_u32_e32 vcc, 0, v1
	s_and_saveexec_b64 s[4:5], vcc
	s_cbranch_execz .LBB0_15
	s_ashr_i32 s35, s34, 31
	s_lshl_b64 s[52:53], s[34:35], 2
	s_add_u32 s52, s33, s52
	s_addc_u32 s53, s46, s53
	v_mul_f32_e32 v2, 0x3a000000, v56
	s_add_u32 s54, s28, s48
	v_mov_b32_e32 v3, v44
	s_addc_u32 s55, s29, s49
	global_store_dwordx2 v55, v[2:3], s[52:53]
	global_store_dword v55, v0, s[54:55]
	s_branch .LBB0_15

; #define GAS __attribute__((address_space(1)))
; #define FLANE lane_id()
; __device__ __forceinline__ void p6_router(Frame& F) {
;     ...
;             v2u raw[8][8]; const int ln_ = FLANE;
; #pragma unroll
;             for (int rr = 0; rr < 8; ++rr) { const GAS v2u* xr = (const GAS v2u*)(z1 + (size_t)(t0 + F.wave * 8 + rr) * D) + ln_;
; #pragma unroll
;                 for (int j = 0; j < 8; ++j) raw[rr][j] = xr[64 * j]; }
.LBB0_1481:
	s_lshl_b32 s42, s84, 6
	s_add_i32 s6, s42, s65
	s_ashr_i32 s7, s6, 31
	s_lshl_b64 s[4:5], s[6:7], 12
	v_mbcnt_lo_u32_b32 v0, -1, 0
	v_mbcnt_hi_u32_b32 v0, -1, v0
	s_add_u32 s4, s16, s4
	v_ashrrev_i32_e32 v1, 31, v0
	s_addc_u32 s5, s17, s5
	v_lshlrev_b64 v[8:9], 3, v[0:1]
	v_lshl_add_u64 v[10:11], s[4:5], 0, v[8:9]
	global_load_dwordx2 v[6:7], v[10:11], off
	global_load_dwordx2 v[128:129], v[10:11], off offset:512
	global_load_dwordx2 v[126:127], v[10:11], off offset:1024
	global_load_dwordx2 v[124:125], v[10:11], off offset:1536
	global_load_dwordx2 v[4:5], v[10:11], off offset:2048
	global_load_dwordx2 v[0:1], v[10:11], off offset:2560
	global_load_dwordx2 v[2:3], v[10:11], off offset:3072
	global_load_dwordx2 v[136:137], v[10:11], off offset:3584
	v_cmp_lt_i32_e32 vcc, v160, v159
	s_or_b32 s4, s6, 1
	s_ashr_i32 s5, s4, 31
	v_cndmask_b32_e32 v32, v158, v160, vcc
	v_cmp_lt_i32_e32 vcc, v161, v159
	v_lshlrev_b32_e32 v170, 2, v32
	s_lshl_b64 s[4:5], s[4:5], 12
	v_cndmask_b32_e32 v32, v158, v161, vcc
	v_cmp_lt_i32_e32 vcc, v162, v159
	v_lshlrev_b32_e32 v171, 2, v32
	s_add_u32 s4, s16, s4
	v_cndmask_b32_e32 v32, v158, v162, vcc
	v_cmp_lt_i32_e32 vcc, v163, v159
	v_lshlrev_b32_e32 v172, 2, v32
	s_addc_u32 s5, s17, s5
	v_cndmask_b32_e32 v32, v158, v163, vcc
	v_cmp_lt_i32_e32 vcc, v164, v159
	v_lshlrev_b32_e32 v173, 2, v32
	v_lshl_add_u64 v[10:11], s[4:5], 0, v[8:9]
	v_cndmask_b32_e32 v32, v158, v164, vcc
	v_cmp_lt_i32_e32 vcc, v165, v159
	v_lshlrev_b32_e32 v174, 2, v32
	s_or_b32 s4, s6, 2
	v_cndmask_b32_e32 v32, v158, v165, vcc
	v_lshlrev_b32_e32 v175, 2, v32
	s_ashr_i32 s5, s4, 31
	s_lshl_b64 s[4:5], s[4:5], 12
	s_add_u32 s4, s16, s4
	s_addc_u32 s5, s17, s5
	global_load_dwordx2 v[120:121], v[10:11], off
	global_load_dwordx2 v[122:123], v[10:11], off offset:512
	global_load_dwordx2 v[118:119], v[10:11], off offset:1024
	global_load_dwordx2 v[116:117], v[10:11], off offset:1536
	global_load_dwordx2 v[114:115], v[10:11], off offset:2048
	global_load_dwordx2 v[112:113], v[10:11], off offset:2560
	global_load_dwordx2 v[110:111], v[10:11], off offset:3072
	global_load_dwordx2 v[108:109], v[10:11], off offset:3584
	v_lshl_add_u64 v[10:11], s[4:5], 0, v[8:9]
	s_or_b32 s4, s6, 3
	s_ashr_i32 s5, s4, 31
	s_lshl_b64 s[4:5], s[4:5], 12
	s_add_u32 s4, s16, s4
	s_addc_u32 s5, s17, s5
	global_load_dwordx2 v[104:105], v[10:11], off
	global_load_dwordx2 v[106:107], v[10:11], off offset:512
	global_load_dwordx2 v[102:103], v[10:11], off offset:1024
	global_load_dwordx2 v[100:101], v[10:11], off offset:1536
	global_load_dwordx2 v[98:99], v[10:11], off offset:2048
	global_load_dwordx2 v[96:97], v[10:11], off offset:2560
	global_load_dwordx2 v[94:95], v[10:11], off offset:3072
	global_load_dwordx2 v[92:93], v[10:11], off offset:3584
	v_lshl_add_u64 v[10:11], s[4:5], 0, v[8:9]
	s_or_b32 s4, s6, 4
	s_ashr_i32 s5, s4, 31
	s_lshl_b64 s[4:5], s[4:5], 12
	s_add_u32 s4, s16, s4
	s_addc_u32 s5, s17, s5
	global_load_dwordx2 v[88:89], v[10:11], off
	global_load_dwordx2 v[90:91], v[10:11], off offset:512
	global_load_dwordx2 v[86:87], v[10:11], off offset:1024
	global_load_dwordx2 v[84:85], v[10:11], off offset:1536
	global_load_dwordx2 v[82:83], v[10:11], off offset:2048
	global_load_dwordx2 v[80:81], v[10:11], off offset:2560
	global_load_dwordx2 v[78:79], v[10:11], off offset:3072
	global_load_dwordx2 v[76:77], v[10:11], off offset:3584
	v_lshl_add_u64 v[10:11], s[4:5], 0, v[8:9]
	s_or_b32 s4, s6, 5
	s_ashr_i32 s5, s4, 31
	s_lshl_b64 s[4:5], s[4:5], 12
	s_add_u32 s4, s16, s4
	s_addc_u32 s5, s17, s5
	global_load_dwordx2 v[72:73], v[10:11], off
	global_load_dwordx2 v[74:75], v[10:11], off offset:512
	global_load_dwordx2 v[70:71], v[10:11], off offset:1024
	global_load_dwordx2 v[68:69], v[10:11], off offset:1536
	global_load_dwordx2 v[66:67], v[10:11], off offset:2048
	global_load_dwordx2 v[64:65], v[10:11], off offset:2560
	global_load_dwordx2 v[62:63], v[10:11], off offset:3072
	global_load_dwordx2 v[60:61], v[10:11], off offset:3584
	v_lshl_add_u64 v[10:11], s[4:5], 0, v[8:9]
	s_or_b32 s4, s6, 6
	s_ashr_i32 s5, s4, 31
	s_lshl_b64 s[4:5], s[4:5], 12
	s_add_u32 s4, s16, s4
	s_addc_u32 s5, s17, s5
	global_load_dwordx2 v[56:57], v[10:11], off
	global_load_dwordx2 v[58:59], v[10:11], off offset:512
	global_load_dwordx2 v[54:55], v[10:11], off offset:1024
	global_load_dwordx2 v[52:53], v[10:11], off offset:1536
	global_load_dwordx2 v[50:51], v[10:11], off offset:2048
	global_load_dwordx2 v[48:49], v[10:11], off offset:2560
	global_load_dwordx2 v[46:47], v[10:11], off offset:3072
	global_load_dwordx2 v[44:45], v[10:11], off offset:3584
	v_lshl_add_u64 v[10:11], s[4:5], 0, v[8:9]
	s_or_b32 s4, s6, 7
	s_ashr_i32 s5, s4, 31
	s_lshl_b64 s[4:5], s[4:5], 12
	s_add_u32 s4, s16, s4
	s_addc_u32 s5, s17, s5
	v_lshl_add_u64 v[8:9], s[4:5], 0, v[8:9]
	global_load_dwordx2 v[40:41], v[10:11], off
	global_load_dwordx2 v[42:43], v[10:11], off offset:512
	global_load_dwordx2 v[38:39], v[10:11], off offset:1024
	global_load_dwordx2 v[36:37], v[10:11], off offset:1536
	global_load_dwordx2 v[30:31], v[10:11], off offset:2048
	global_load_dwordx2 v[28:29], v[10:11], off offset:2560
	global_load_dwordx2 v[26:27], v[10:11], off offset:3072
	global_load_dwordx2 v[24:25], v[10:11], off offset:3584
	global_load_dwordx2 v[20:21], v[8:9], off
	global_load_dwordx2 v[22:23], v[8:9], off offset:512
	global_load_dwordx2 v[18:19], v[8:9], off offset:1024
	global_load_dwordx2 v[16:17], v[8:9], off offset:1536
	global_load_dwordx2 v[14:15], v[8:9], off offset:2048
	global_load_dwordx2 v[12:13], v[8:9], off offset:2560
	global_load_dwordx2 v[10:11], v[8:9], off offset:3072
	s_nop 0
	global_load_dwordx2 v[8:9], v[8:9], off offset:3584
	s_waitcnt vmcnt(62)
; __device__ __forceinline__ float wave_sum(float v) {
; #pragma unroll
;     for (int o = 1; o < 64; o <<= 1) v += __shfl_xor(v, o);
;     return v;
; __device__ __forceinline__ void p6_router(Frame& F) {
;     ...
;             for (int rr = 0; rr < 8; ++rr) { const int row = F.wave * 8 + rr, m = t0 + row;
;                 f32x4 v[8]; float s = 0.f;
; #pragma unroll
;                 for (int j = 0; j < 8; ++j) { const v2u w = raw[rr][j]; v[j] = (f32x4){bf_lo(w.x), bf_hi(w.x), bf_lo(w.y), bf_hi(w.y)}; s += (v[j][0] + v[j][1]) + (v[j][2] + v[j][3]); }
;                 const float mean = wave_sum(s) * (1.f / D); float s2 = 0.f;
; #pragma unroll
;                 for (int j = 0; j < 8; ++j) { v[j] = v[j] - mean; s2 += (v[j][0] * v[j][0] + v[j][1] * v[j][1]) + (v[j][2] * v[j][2] + v[j][3] * v[j][3]); }
	v_lshlrev_b32_e32 v144, 16, v6
	v_lshlrev_b32_e32 v145, 16, v128
	v_and_b32_e32 v149, 0xffff0000, v128
	v_and_b32_e32 v148, 0xffff0000, v6
	v_lshlrev_b32_e32 v151, 16, v129
	v_lshlrev_b32_e32 v150, 16, v7
	v_and_b32_e32 v157, 0xffff0000, v129
	v_and_b32_e32 v156, 0xffff0000, v7
	v_pk_add_f32 v[6:7], v[144:145], v[148:149]
	v_pk_add_f32 v[128:129], v[150:151], v[156:157]
	s_waitcnt vmcnt(61)
	v_lshlrev_b32_e32 v143, 16, v127
	v_pk_add_f32 v[6:7], v[6:7], v[128:129]
	v_lshlrev_b32_e32 v142, 16, v126
	v_and_b32_e32 v153, 0xffff0000, v127
	v_and_b32_e32 v152, 0xffff0000, v126
	v_add_f32_e32 v6, 0, v6
	v_pk_add_f32 v[126:127], v[142:143], v[152:153]
	v_add_f32_e32 v6, v6, v7
	s_waitcnt vmcnt(60)
	v_lshlrev_b32_e32 v138, 16, v124
	v_and_b32_e32 v139, 0xffff0000, v124
	v_lshlrev_b32_e32 v140, 16, v125
	v_and_b32_e32 v141, 0xffff0000, v125
	s_waitcnt vmcnt(59)
	v_lshlrev_b32_e32 v7, 16, v4
	v_and_b32_e32 v135, 0xffff0000, v4
	v_lshlrev_b32_e32 v133, 16, v5
	v_and_b32_e32 v131, 0xffff0000, v5
	v_pk_add_f32 v[4:5], v[126:127], v[126:127] op_sel:[0,1] op_sel_hi:[1,0]
	v_add_f32_e32 v132, v138, v139
	v_add_f32_e32 v130, v140, v141
	v_mov_b32_e32 v5, v135
	v_pk_add_f32 v[4:5], v[6:7], v[4:5]
	v_pk_add_f32 v[124:125], v[132:133], v[130:131]
	s_waitcnt vmcnt(58)
	v_and_b32_e32 v155, 0xffff0000, v1
	v_pk_add_f32 v[146:147], v[4:5], v[124:125]
	v_lshlrev_b32_e32 v5, 16, v1
	v_lshlrev_b32_e32 v4, 16, v0
	v_and_b32_e32 v154, 0xffff0000, v0
	v_pk_add_f32 v[176:177], v[4:5], v[154:155]
	s_waitcnt vmcnt(57)
	v_lshlrev_b32_e32 v0, 16, v2
	v_and_b32_e32 v1, 0xffff0000, v2
	v_lshlrev_b32_e32 v2, 16, v3
	v_and_b32_e32 v3, 0xffff0000, v3
	s_waitcnt vmcnt(56)
	v_lshlrev_b32_e32 v128, 16, v136
	v_and_b32_e32 v129, 0xffff0000, v136
	v_lshlrev_b32_e32 v127, 16, v137
	v_and_b32_e32 v125, 0xffff0000, v137
	v_pk_add_f32 v[136:137], v[146:147], v[146:147] op_sel:[0,1] op_sel_hi:[1,0]
	v_pk_add_f32 v[146:147], v[176:177], v[176:177] op_sel:[0,1] op_sel_hi:[1,0]
	v_add_f32_e32 v126, v0, v1
	v_add_f32_e32 v124, v2, v3
	v_mov_b32_e32 v137, v128
	v_mov_b32_e32 v147, v129
	v_pk_add_f32 v[136:137], v[136:137], v[146:147]
	v_pk_add_f32 v[146:147], v[126:127], v[124:125]
	s_nop 0
	v_pk_add_f32 v[136:137], v[136:137], v[146:147]
	s_nop 0
	v_add_f32_e32 v6, v136, v137
	s_waitcnt lgkmcnt(0)
	s_nop 1
	v_add_f32_dpp v6, v6, v6 quad_perm:[1,0,3,2] row_mask:0xf bank_mask:0xf
	s_waitcnt lgkmcnt(0)
	s_nop 1
	v_add_f32_dpp v6, v6, v6 quad_perm:[2,3,0,1] row_mask:0xf bank_mask:0xf
	s_waitcnt lgkmcnt(0)
	s_nop 1
	v_add_f32_dpp v6, v6, v6 row_half_mirror row_mask:0xf bank_mask:0xf
	s_waitcnt lgkmcnt(0)
	s_nop 1
	v_add_f32_dpp v6, v6, v6 row_mirror row_mask:0xf bank_mask:0xf
	s_waitcnt lgkmcnt(0)
	v_mov_b32_e32 v32, v6
	s_nop 1
	v_permlane16_swap_b32_e32 v6, v32
	v_add_f32_e32 v6, v6, v32
	s_waitcnt lgkmcnt(0)
	v_mov_b32_e32 v32, v6
	s_nop 1
	v_permlane32_swap_b32_e32 v6, v32
	v_add_f32_e32 v126, v6, v32
	v_fmac_f32_e32 v148, 0xba000000, v126
	v_fmac_f32_e32 v149, 0xba000000, v126
	v_fmac_f32_e32 v156, 0xba000000, v126
	v_fmac_f32_e32 v144, 0xba000000, v126
	v_fmac_f32_e32 v157, 0xba000000, v126
	v_fmac_f32_e32 v145, 0xba000000, v126
	v_mov_b32_e32 v147, v149
	v_mov_b32_e32 v137, v148
	v_pk_mul_f32 v[148:149], v[148:149], v[148:149]
	v_fmac_f32_e32 v150, 0xba000000, v126
	v_fmac_f32_e32 v151, 0xba000000, v126
	v_mov_b32_e32 v146, v145
	v_pk_fma_f32 v[176:177], v[144:145], v[144:145], v[148:149]
	v_mov_b32_e32 v149, v157
	v_mov_b32_e32 v145, v156
	v_pk_mul_f32 v[156:157], v[156:157], v[156:157]
	v_mov_b32_e32 v136, v144
	v_mov_b32_e32 v148, v151
	v_mov_b32_e32 v144, v150
	v_pk_fma_f32 v[150:151], v[150:151], v[150:151], v[156:157]
	v_fmac_f32_e32 v152, 0xba000000, v126
	v_pk_add_f32 v[150:151], v[176:177], v[150:151]
	v_fmac_f32_e32 v153, 0xba000000, v126
	v_fmac_f32_e32 v143, 0xba000000, v126
	v_pk_add_f32 v[156:157], v[150:151], v[150:151] op_sel_hi:[0,1]
	v_fmac_f32_e32 v142, 0xba000000, v126
	v_mov_b32_e32 v150, v143
	v_mov_b32_e32 v151, v153
	v_mov_b32_e32 v143, v152
	v_pk_mul_f32 v[176:177], v[150:151], v[150:151]
	v_pk_mul_f32 v[152:153], v[142:143], v[142:143]
	v_fmac_f32_e32 v138, 0xba000000, v126
	v_pk_mov_b32 v[178:179], v[152:153], v[176:177] op_sel:[1,0]
	v_mov_b32_e32 v153, v177
	v_fmac_f32_e32 v139, 0xba000000, v126
	v_fmac_f32_e32 v140, 0xba000000, v126
	v_mul_f32_e32 v6, v138, v138
	v_pk_add_f32 v[152:153], v[178:179], v[152:153]
	v_fmac_f32_e32 v141, 0xba000000, v126
	v_pk_fma_f32 v[176:177], v[138:139], v[138:139], v[6:7] op_sel_hi:[1,1,0]
	v_mul_f32_e32 v6, v140, v140
	v_pk_add_f32 v[152:153], v[152:153], v[152:153] op_sel_hi:[0,1]
	v_pk_fma_f32 v[178:179], v[140:141], v[140:141], v[6:7] op_sel_hi:[1,1,0]
	v_fmac_f32_e32 v131, 0xba000000, v126
	v_fmac_f32_e32 v133, 0xba000000, v126
	v_fmac_f32_e32 v135, 0xba000000, v126
	v_fmac_f32_e32 v7, 0xba000000, v126
	v_mul_f32_e32 v176, v7, v7
	v_mul_f32_e32 v178, v135, v135
	v_mul_f32_e32 v152, v133, v133
	v_mul_f32_e32 v156, v131, v131
	v_pk_add_f32 v[176:177], v[176:177], v[178:179]
	v_pk_add_f32 v[152:153], v[152:153], v[156:157]
	v_fmac_f32_e32 v154, 0xba000000, v126
	v_pk_add_f32 v[152:153], v[176:177], v[152:153]
	v_fmac_f32_e32 v155, 0xba000000, v126
	v_fmac_f32_e32 v5, 0xba000000, v126
	v_pk_add_f32 v[156:157], v[152:153], v[152:153] op_sel_hi:[0,1]
	v_fmac_f32_e32 v4, 0xba000000, v126
	v_mov_b32_e32 v152, v5
	v_mov_b32_e32 v153, v155
	v_mov_b32_e32 v5, v154
	v_pk_mul_f32 v[176:177], v[152:153], v[152:153]
	v_pk_mul_f32 v[154:155], v[4:5], v[4:5]
	v_fmac_f32_e32 v0, 0xba000000, v126
	v_pk_mov_b32 v[178:179], v[154:155], v[176:177] op_sel:[1,0]
	v_mov_b32_e32 v155, v177
	v_fmac_f32_e32 v1, 0xba000000, v126
	v_fmac_f32_e32 v2, 0xba000000, v126
	v_mul_f32_e32 v6, v0, v0
	v_pk_add_f32 v[154:155], v[178:179], v[154:155]
	v_fmac_f32_e32 v3, 0xba000000, v126
	v_pk_fma_f32 v[176:177], v[0:1], v[0:1], v[6:7] op_sel_hi:[1,1,0]
	v_mul_f32_e32 v6, v2, v2
	v_pk_add_f32 v[154:155], v[154:155], v[154:155] op_sel_hi:[0,1]
	v_pk_fma_f32 v[178:179], v[2:3], v[2:3], v[6:7] op_sel_hi:[1,1,0]
	v_fmac_f32_e32 v125, 0xba000000, v126
	v_fmac_f32_e32 v127, 0xba000000, v126
	v_fmac_f32_e32 v129, 0xba000000, v126
	v_fmac_f32_e32 v128, 0xba000000, v126
	v_mul_f32_e32 v176, v128, v128
	v_mul_f32_e32 v178, v129, v129
	v_mul_f32_e32 v154, v127, v127
	v_mul_f32_e32 v156, v125, v125
	v_pk_add_f32 v[176:177], v[176:177], v[178:179]
	v_pk_add_f32 v[154:155], v[154:155], v[156:157]
	s_nop 0
	v_pk_add_f32 v[154:155], v[176:177], v[154:155]
	s_nop 0
	v_add_f32_e32 v6, v154, v155
	v_mbcnt_lo_u32_b32 v154, -1, 0
	v_mbcnt_hi_u32_b32 v154, -1, v154
	v_ashrrev_i32_e32 v155, 31, v154
	v_lshl_add_u64 v[154:155], v[154:155], 4, s[12:13]
	global_load_dwordx4 v[154:157], v[154:155], off
	v_mbcnt_lo_u32_b32 v176, -1, 0
	v_mbcnt_hi_u32_b32 v176, -1, v176
	s_waitcnt lgkmcnt(0)
; #define GAS __attribute__((address_space(1)))
; #define FLANE lane_id()
; __device__ __forceinline__ void p6_router(Frame& F) {
;     ...
;                 const float rstd = 1.f / sqrtf(wave_sum(s2) * (1.f / D) + LN_EPS);
;                 float am = 0.f;
; #pragma unroll
;                 for (int j = 0; j < 8; ++j) { const f32x4 g = *((const GAS f32x4*)F.ln1_g + FLANE + 64 * j), b = *((const GAS f32x4*)F.ln1_b + FLANE + 64 * j);
;                     v[j] = v[j] * rstd * g + b; am = fmaxf(am, fmaxf(fmaxf(fabsf(v[j][0]), fabsf(v[j][1])), fmaxf(fabsf(v[j][2]), fabsf(v[j][3])))); }
	s_nop 1
	v_add_f32_dpp v6, v6, v6 quad_perm:[1,0,3,2] row_mask:0xf bank_mask:0xf
	v_ashrrev_i32_e32 v177, 31, v176
	v_lshl_add_u64 v[176:177], v[176:177], 4, s[14:15]
	global_load_dwordx4 v[176:179], v[176:177], off
	s_waitcnt lgkmcnt(0)
	s_nop 1
	v_add_f32_dpp v6, v6, v6 quad_perm:[2,3,0,1] row_mask:0xf bank_mask:0xf
	s_waitcnt lgkmcnt(0)
	s_nop 1
	v_add_f32_dpp v6, v6, v6 row_half_mirror row_mask:0xf bank_mask:0xf
	s_waitcnt lgkmcnt(0)
	s_nop 1
	v_add_f32_dpp v6, v6, v6 row_mirror row_mask:0xf bank_mask:0xf
	s_waitcnt lgkmcnt(0)
	v_mov_b32_e32 v32, v6
	s_nop 1
	v_permlane16_swap_b32_e32 v6, v32
	v_add_f32_e32 v6, v6, v32
	s_waitcnt lgkmcnt(0)
	v_mov_b32_e32 v32, v6
	s_nop 1
	v_permlane32_swap_b32_e32 v6, v32
	v_add_f32_e32 v6, v6, v32
	v_fmamk_f32 v6, v6, 0x3a000000, v166
	v_cmp_gt_f32_e32 vcc, s22, v6
	v_mul_f32_e32 v32, 0x4f800000, v6
	s_nop 0
	v_cndmask_b32_e32 v6, v6, v32, vcc
	v_sqrt_f32_e32 v32, v6
	s_nop 0
	v_add_u32_e32 v124, -1, v32
	v_fma_f32 v130, -v124, v32, v6
	v_cmp_ge_f32_e64 s[4:5], 0, v130
	v_add_u32_e32 v130, 1, v32
	s_nop 0
	v_cndmask_b32_e64 v124, v32, v124, s[4:5]
	v_fma_f32 v32, -v130, v32, v6
	v_cmp_lt_f32_e64 s[4:5], 0, v32
	s_nop 1
	v_cndmask_b32_e64 v32, v124, v130, s[4:5]
	v_mul_f32_e32 v124, 0x37800000, v32
	v_cndmask_b32_e32 v32, v32, v124, vcc
	v_cmp_class_f32_e32 vcc, v6, v167
	s_nop 1
	v_cndmask_b32_e32 v6, v32, v6, vcc
	v_div_scale_f32 v32, s[4:5], v6, v6, 1.0
	v_rcp_f32_e32 v124, v32
	s_nop 0
	v_fma_f32 v130, -v32, v124, 1.0
	v_fmac_f32_e32 v124, v130, v124
	v_div_scale_f32 v130, vcc, 1.0, v6, 1.0
	v_mul_f32_e32 v132, v130, v124
	v_fma_f32 v134, -v32, v132, v130
	v_fmac_f32_e32 v132, v134, v124
	v_fma_f32 v32, -v32, v132, v130
	v_div_fmas_f32 v32, v32, v124, v132
	v_div_fixup_f32 v32, v32, v6, 1.0
	v_pk_mul_f32 v[180:181], v[136:137], v[32:33] op_sel_hi:[1,0]
	v_pk_mul_f32 v[136:137], v[144:145], v[32:33] op_sel_hi:[1,0]
	v_mov_b32_e32 v134, v7
	v_pk_mul_f32 v[4:5], v[4:5], v[32:33] op_sel_hi:[1,0]
	v_pk_mul_f32 v[2:3], v[2:3], v[32:33] op_sel_hi:[1,0]
	v_pk_mul_f32 v[0:1], v[0:1], v[32:33] op_sel_hi:[1,0]
	v_pk_mul_f32 v[128:129], v[128:129], v[32:33] op_sel_hi:[1,0]
	s_waitcnt vmcnt(0)
	v_pk_fma_f32 v[144:145], v[154:155], v[180:181], v[176:177]
	v_mbcnt_lo_u32_b32 v154, -1, 0
	v_mbcnt_hi_u32_b32 v154, -1, v154
	v_pk_fma_f32 v[136:137], v[156:157], v[136:137], v[178:179]
	v_ashrrev_i32_e32 v155, 31, v154
	v_lshl_add_u64 v[154:155], v[154:155], 4, s[12:13]
	global_load_dwordx4 v[154:157], v[154:155], off offset:1024
	v_mbcnt_lo_u32_b32 v176, -1, 0
	v_mbcnt_hi_u32_b32 v176, -1, v176
	v_pk_mul_f32 v[180:181], v[146:147], v[32:33] op_sel_hi:[1,0]
	v_ashrrev_i32_e32 v177, 31, v176
	v_lshl_add_u64 v[176:177], v[176:177], 4, s[14:15]
	global_load_dwordx4 v[176:179], v[176:177], off offset:1024
	v_pk_mul_f32 v[146:147], v[148:149], v[32:33] op_sel_hi:[1,0]
	v_max_f32_e64 v6, |v136|, |v137|
	v_max3_f32 v6, |v144|, |v145|, v6
	s_waitcnt vmcnt(0)
	v_pk_fma_f32 v[148:149], v[154:155], v[180:181], v[176:177]
	v_mbcnt_lo_u32_b32 v154, -1, 0
	v_mbcnt_hi_u32_b32 v154, -1, v154
	v_pk_fma_f32 v[146:147], v[156:157], v[146:147], v[178:179]
	v_ashrrev_i32_e32 v155, 31, v154
	v_lshl_add_u64 v[154:155], v[154:155], 4, s[12:13]
	global_load_dwordx4 v[154:157], v[154:155], off offset:2048
	v_mbcnt_lo_u32_b32 v176, -1, 0
	v_mbcnt_hi_u32_b32 v176, -1, v176
	v_pk_mul_f32 v[180:181], v[142:143], v[32:33] op_sel_hi:[1,0]
	v_ashrrev_i32_e32 v177, 31, v176
	v_lshl_add_u64 v[176:177], v[176:177], 4, s[14:15]
	global_load_dwordx4 v[176:179], v[176:177], off offset:2048
	v_pk_mul_f32 v[142:143], v[150:151], v[32:33] op_sel_hi:[1,0]
	v_max_f32_e64 v124, |v146|, |v147|
	v_max3_f32 v124, |v148|, |v149|, v124
	v_max3_f32 v6, v6, 0, v124
	s_waitcnt vmcnt(0)
	v_pk_fma_f32 v[150:151], v[154:155], v[180:181], v[176:177]
	v_mbcnt_lo_u32_b32 v154, -1, 0
	v_mbcnt_hi_u32_b32 v154, -1, v154
	v_pk_fma_f32 v[142:143], v[156:157], v[142:143], v[178:179]
	v_ashrrev_i32_e32 v155, 31, v154
	v_lshl_add_u64 v[154:155], v[154:155], 4, s[12:13]
	global_load_dwordx4 v[154:157], v[154:155], off offset:3072
	v_mbcnt_lo_u32_b32 v176, -1, 0
	v_mbcnt_hi_u32_b32 v176, -1, v176
	v_pk_mul_f32 v[180:181], v[138:139], v[32:33] op_sel_hi:[1,0]
	v_ashrrev_i32_e32 v177, 31, v176
	v_lshl_add_u64 v[176:177], v[176:177], 4, s[14:15]
	global_load_dwordx4 v[176:179], v[176:177], off offset:3072
	v_pk_mul_f32 v[138:139], v[140:141], v[32:33] op_sel_hi:[1,0]
	v_max_f32_e64 v124, |v142|, |v143|
	v_max3_f32 v124, |v150|, |v151|, v124
	s_waitcnt vmcnt(0)
	v_pk_fma_f32 v[140:141], v[154:155], v[180:181], v[176:177]
	v_mbcnt_lo_u32_b32 v154, -1, 0
	v_mbcnt_hi_u32_b32 v154, -1, v154
	v_pk_fma_f32 v[138:139], v[156:157], v[138:139], v[178:179]
	v_ashrrev_i32_e32 v155, 31, v154
	v_lshl_add_u64 v[154:155], v[154:155], 4, s[12:13]
	v_add_co_u32_e32 v154, vcc, s23, v154
	v_max_f32_e64 v130, |v138|, |v139|
	s_nop 0
	v_addc_co_u32_e32 v155, vcc, 0, v155, vcc
	global_load_dwordx4 v[154:157], v[154:155], off
	v_mbcnt_lo_u32_b32 v176, -1, 0
	v_mbcnt_hi_u32_b32 v176, -1, v176
	v_max3_f32 v130, |v140|, |v141|, v130
	v_ashrrev_i32_e32 v177, 31, v176
	v_lshl_add_u64 v[176:177], v[176:177], 4, s[14:15]
	v_add_co_u32_e32 v176, vcc, s23, v176
	v_max3_f32 v124, v6, v124, v130
	s_nop 0
	v_addc_co_u32_e32 v177, vcc, 0, v177, vcc
	global_load_dwordx4 v[176:179], v[176:177], off
	v_mov_b32_e32 v130, v133
	v_pk_mul_f32 v[130:131], v[130:131], v[32:33] op_sel_hi:[1,0]
	v_pk_mul_f32 v[6:7], v[134:135], v[32:33] op_sel_hi:[1,0]
	s_waitcnt vmcnt(0)
; #define FLANE lane_id()
; __device__ __forceinline__ void p6_router(Frame& F) {
;     ...
;                     v[j] = v[j] * rstd * g + b; am = fmaxf(am, fmaxf(fmaxf(fabsf(v[j][0]), fabsf(v[j][1])), fmaxf(fabsf(v[j][2]), fabsf(v[j][3])))); }
; #pragma unroll
;                 for (int o = 1; o < 64; o <<= 1) am = fmaxf(am, __shfl_xor(am, o));
;                 const float sc = am > 0.f ? am * (1.f / 127.f) : 1.f, inv = 1.f / sc;
; #pragma unroll
;                 for (int j = 0; j < 8; ++j) { const int q0 = (int)__builtin_rintf(v[j][0] * inv), q1 = (int)__builtin_rintf(v[j][1] * inv), q2 = (int)__builtin_rintf(v[j][2] * inv), q3 = (int)__builtin_rintf(v[j][3] * inv);
;                     h1q[(size_t)m * (D / 4) + FLANE + 64 * j] = (unsigned)(q0 & 0xff) | ((unsigned)(q1 & 0xff) << 8) | ((unsigned)(q2 & 0xff) << 16) | ((unsigned)(q3 & 0xff) << 24); }
	v_pk_fma_f32 v[130:131], v[156:157], v[130:131], v[178:179]
	v_pk_fma_f32 v[132:133], v[154:155], v[6:7], v[176:177]
	v_max_f32_e64 v6, |v130|, |v131|
	v_max3_f32 v180, |v132|, |v133|, v6
	v_mbcnt_lo_u32_b32 v6, -1, 0
	v_mbcnt_hi_u32_b32 v6, -1, v6
	s_nop 0
	v_ashrrev_i32_e32 v7, 31, v6
	v_lshl_add_u64 v[6:7], v[6:7], 4, s[12:13]
	v_add_co_u32_e32 v6, vcc, s23, v6
	s_nop 1
	v_addc_co_u32_e32 v7, vcc, 0, v7, vcc
	global_load_dwordx4 v[154:157], v[6:7], off offset:1024
	v_mbcnt_lo_u32_b32 v6, -1, 0
	v_mbcnt_hi_u32_b32 v6, -1, v6
	s_nop 0
	v_ashrrev_i32_e32 v7, 31, v6
	v_lshl_add_u64 v[6:7], v[6:7], 4, s[14:15]
	v_add_co_u32_e32 v6, vcc, s23, v6
	s_nop 1
	v_addc_co_u32_e32 v7, vcc, 0, v7, vcc
	global_load_dwordx4 v[176:179], v[6:7], off offset:1024
	v_pk_mul_f32 v[6:7], v[152:153], v[32:33] op_sel_hi:[1,0]
	s_waitcnt vmcnt(0)
	v_pk_fma_f32 v[152:153], v[154:155], v[4:5], v[176:177]
	v_pk_fma_f32 v[134:135], v[156:157], v[6:7], v[178:179]
	s_nop 0
	v_max_f32_e64 v4, |v134|, |v135|
	v_max3_f32 v4, |v152|, |v153|, v4
	v_max3_f32 v180, v124, v180, v4
	v_mbcnt_lo_u32_b32 v4, -1, 0
	v_mbcnt_hi_u32_b32 v4, -1, v4
	v_mov_b32_e32 v124, v127
	v_ashrrev_i32_e32 v5, 31, v4
	v_lshl_add_u64 v[4:5], v[4:5], 4, s[12:13]
	v_add_co_u32_e32 v4, vcc, s23, v4
	v_pk_mul_f32 v[124:125], v[124:125], v[32:33] op_sel_hi:[1,0]
	s_nop 0
	v_addc_co_u32_e32 v5, vcc, 0, v5, vcc
	global_load_dwordx4 v[4:7], v[4:5], off offset:2048
	v_mbcnt_lo_u32_b32 v154, -1, 0
	v_mbcnt_hi_u32_b32 v154, -1, v154
	s_nop 0
	v_ashrrev_i32_e32 v155, 31, v154
	v_lshl_add_u64 v[154:155], v[154:155], 4, s[14:15]
	v_add_co_u32_e32 v154, vcc, s23, v154
	s_nop 1
	v_addc_co_u32_e32 v155, vcc, 0, v155, vcc
	global_load_dwordx4 v[176:179], v[154:155], off offset:2048
	s_waitcnt vmcnt(0)
	v_pk_fma_f32 v[154:155], v[2:3], v[6:7], v[178:179]
	v_pk_fma_f32 v[156:157], v[0:1], v[4:5], v[176:177]
	v_max_f32_e64 v0, |v154|, |v155|
	v_max3_f32 v176, |v156|, |v157|, v0
	v_mbcnt_lo_u32_b32 v0, -1, 0
	v_mbcnt_hi_u32_b32 v0, -1, v0
	s_nop 0
	v_ashrrev_i32_e32 v1, 31, v0
	v_lshl_add_u64 v[0:1], v[0:1], 4, s[12:13]
	v_add_co_u32_e32 v0, vcc, s23, v0
	s_nop 1
	v_addc_co_u32_e32 v1, vcc, 0, v1, vcc
	global_load_dwordx4 v[0:3], v[0:1], off offset:3072
	v_mbcnt_lo_u32_b32 v4, -1, 0
	v_mbcnt_hi_u32_b32 v4, -1, v4
	s_nop 0
	v_ashrrev_i32_e32 v5, 31, v4
	v_lshl_add_u64 v[4:5], v[4:5], 4, s[14:15]
	v_add_co_u32_e32 v4, vcc, s23, v4
	s_nop 1
	v_addc_co_u32_e32 v5, vcc, 0, v5, vcc
	global_load_dwordx4 v[4:7], v[4:5], off offset:3072
	s_waitcnt vmcnt(0)
	v_pk_fma_f32 v[2:3], v[124:125], v[2:3], v[6:7]
	v_pk_fma_f32 v[4:5], v[128:129], v[0:1], v[4:5]
	v_max_f32_e64 v0, |v2|, |v3|
	v_max3_f32 v0, |v4|, |v5|, v0
	v_max3_f32 v0, v180, v176, v0
	s_waitcnt lgkmcnt(0)
	s_nop 1
	v_max_f32_dpp v0, v0, v0 quad_perm:[1,0,3,2] row_mask:0xf bank_mask:0xf
	s_waitcnt lgkmcnt(0)
	s_nop 1
	v_max_f32_dpp v0, v0, v0 quad_perm:[2,3,0,1] row_mask:0xf bank_mask:0xf
	s_waitcnt lgkmcnt(0)
	s_nop 1
	v_max_f32_dpp v0, v0, v0 row_half_mirror row_mask:0xf bank_mask:0xf
	s_waitcnt lgkmcnt(0)
	s_nop 1
	v_max_f32_dpp v0, v0, v0 row_mirror row_mask:0xf bank_mask:0xf
	s_waitcnt lgkmcnt(0)
	v_mov_b32_e32 v1, v0
	s_nop 1
	v_permlane16_swap_b32_e32 v0, v1
	v_max_f32_e32 v0, v0, v1
	s_waitcnt lgkmcnt(0)
	v_mov_b32_e32 v1, v0
	s_nop 1
	v_permlane32_swap_b32_e32 v0, v1
	v_max_f32_e32 v0, v0, v1
	v_cmp_lt_f32_e32 vcc, 0, v0
	v_mul_f32_e32 v0, 0x3c010204, v0
	s_nop 0
	v_cndmask_b32_e32 v0, 1.0, v0, vcc
	v_div_scale_f32 v1, s[4:5], v0, v0, 1.0
	v_rcp_f32_e32 v6, v1
	s_lshl_b64 s[4:5], s[6:7], 11
	s_add_u32 s4, s3, s4
	s_addc_u32 s5, s24, s5
	v_fma_f32 v7, -v1, v6, 1.0
	v_fmac_f32_e32 v6, v7, v6
	v_div_scale_f32 v7, vcc, 1.0, v0, 1.0
	v_mul_f32_e32 v124, v7, v6
	v_fma_f32 v125, -v1, v124, v7
	v_fmac_f32_e32 v124, v125, v6
	v_fma_f32 v1, -v1, v124, v7
	v_div_fmas_f32 v1, v1, v6, v124
	v_div_fixup_f32 v1, v1, v0, 1.0
	v_mul_f32_e32 v7, v145, v1
	v_mul_f32_e32 v6, v144, v1
	v_rndne_f32_e32 v7, v7
	v_mul_f32_e32 v124, v136, v1
	v_mul_f32_e32 v125, v137, v1
	v_rndne_f32_e32 v6, v6
	v_cvt_i32_f32_e32 v7, v7
	v_rndne_f32_e32 v124, v124
	v_rndne_f32_e32 v125, v125
	v_cvt_i32_f32_e32 v6, v6
	v_cvt_i32_f32_sdwa v124, v124 dst_sel:WORD_1 dst_unused:UNUSED_PAD src0_sel:DWORD
	v_cvt_i32_f32_e32 v125, v125
	v_lshlrev_b32_e32 v7, 8, v7
	v_and_b32_e32 v7, 0xff00, v7
	v_and_b32_e32 v124, 0xff0000, v124
	v_perm_b32 v6, v125, v6, s1
	v_or3_b32 v124, v6, v7, v124
	v_mbcnt_lo_u32_b32 v6, -1, 0
	v_mbcnt_hi_u32_b32 v6, -1, v6
	v_mul_f32_e32 v125, v147, v1
	v_ashrrev_i32_e32 v7, 31, v6
	v_lshl_add_u64 v[6:7], v[6:7], 2, s[4:5]
	global_store_dword v[6:7], v124, off
	v_mul_f32_e32 v7, v149, v1
	v_mul_f32_e32 v6, v148, v1
	v_rndne_f32_e32 v7, v7
	v_mul_f32_e32 v124, v146, v1
	v_rndne_f32_e32 v6, v6
	v_cvt_i32_f32_e32 v7, v7
	v_rndne_f32_e32 v124, v124
	v_rndne_f32_e32 v125, v125
	v_cvt_i32_f32_e32 v6, v6
	v_cvt_i32_f32_sdwa v124, v124 dst_sel:WORD_1 dst_unused:UNUSED_PAD src0_sel:DWORD
	v_cvt_i32_f32_e32 v125, v125
	v_lshlrev_b32_e32 v7, 8, v7
	v_and_b32_e32 v7, 0xff00, v7
	v_and_b32_e32 v124, 0xff0000, v124
	v_perm_b32 v6, v125, v6, s1
	v_or3_b32 v124, v6, v7, v124
	v_mbcnt_lo_u32_b32 v6, -1, 0
	v_mbcnt_hi_u32_b32 v6, -1, v6
	v_mul_f32_e32 v125, v143, v1
	v_ashrrev_i32_e32 v7, 31, v6
	v_lshl_add_u64 v[6:7], v[6:7], 2, s[4:5]
	global_store_dword v[6:7], v124, off offset:256
	v_mul_f32_e32 v7, v151, v1
	v_mul_f32_e32 v6, v150, v1
	v_rndne_f32_e32 v7, v7
	v_mul_f32_e32 v124, v142, v1
	v_rndne_f32_e32 v6, v6
	v_cvt_i32_f32_e32 v7, v7
	v_rndne_f32_e32 v124, v124
	v_rndne_f32_e32 v125, v125
	v_cvt_i32_f32_e32 v6, v6
	v_cvt_i32_f32_sdwa v124, v124 dst_sel:WORD_1 dst_unused:UNUSED_PAD src0_sel:DWORD
; #define FLANE lane_id()
; __device__ __forceinline__ void p6_router(Frame& F) {
;     ...
;                 for (int j = 0; j < 8; ++j) { const int q0 = (int)__builtin_rintf(v[j][0] * inv), q1 = (int)__builtin_rintf(v[j][1] * inv), q2 = (int)__builtin_rintf(v[j][2] * inv), q3 = (int)__builtin_rintf(v[j][3] * inv);
;                     h1q[(size_t)m * (D / 4) + FLANE + 64 * j] = (unsigned)(q0 & 0xff) | ((unsigned)(q1 & 0xff) << 8) | ((unsigned)(q2 & 0xff) << 16) | ((unsigned)(q3 & 0xff) << 24); }
;                 if (FLANE == 0) { st1[2 * m] = mean; st1[2 * m + 1] = rstd; stl[2 * row] = mean; stl[2 * row + 1] = rstd; sxg[m] = sc; sxl[row] = sc; }
	v_cvt_i32_f32_e32 v125, v125
	v_lshlrev_b32_e32 v7, 8, v7
	v_and_b32_e32 v7, 0xff00, v7
	v_and_b32_e32 v124, 0xff0000, v124
	v_perm_b32 v6, v125, v6, s1
	v_or3_b32 v124, v6, v7, v124
	v_mbcnt_lo_u32_b32 v6, -1, 0
	v_mbcnt_hi_u32_b32 v6, -1, v6
	v_mul_f32_e32 v125, v139, v1
	v_ashrrev_i32_e32 v7, 31, v6
	v_lshl_add_u64 v[6:7], v[6:7], 2, s[4:5]
	global_store_dword v[6:7], v124, off offset:512
	v_mul_f32_e32 v7, v141, v1
	v_mul_f32_e32 v6, v140, v1
	v_rndne_f32_e32 v7, v7
	v_mul_f32_e32 v124, v138, v1
	v_rndne_f32_e32 v6, v6
	v_cvt_i32_f32_e32 v7, v7
	v_rndne_f32_e32 v124, v124
	v_rndne_f32_e32 v125, v125
	v_cvt_i32_f32_e32 v6, v6
	v_cvt_i32_f32_sdwa v124, v124 dst_sel:WORD_1 dst_unused:UNUSED_PAD src0_sel:DWORD
	v_cvt_i32_f32_e32 v125, v125
	v_lshlrev_b32_e32 v7, 8, v7
	v_and_b32_e32 v7, 0xff00, v7
	v_and_b32_e32 v124, 0xff0000, v124
	v_perm_b32 v6, v125, v6, s1
	v_or3_b32 v124, v6, v7, v124
	v_mbcnt_lo_u32_b32 v6, -1, 0
	v_mbcnt_hi_u32_b32 v6, -1, v6
	v_mul_f32_e32 v125, v131, v1
	v_ashrrev_i32_e32 v7, 31, v6
	v_lshl_add_u64 v[6:7], v[6:7], 2, s[4:5]
	global_store_dword v[6:7], v124, off offset:768
	v_mul_f32_e32 v7, v133, v1
	v_mul_f32_e32 v6, v132, v1
	v_rndne_f32_e32 v7, v7
	v_mul_f32_e32 v124, v130, v1
	v_rndne_f32_e32 v6, v6
	v_cvt_i32_f32_e32 v7, v7
	v_rndne_f32_e32 v124, v124
	v_rndne_f32_e32 v125, v125
	v_cvt_i32_f32_e32 v6, v6
	v_cvt_i32_f32_sdwa v124, v124 dst_sel:WORD_1 dst_unused:UNUSED_PAD src0_sel:DWORD
	v_cvt_i32_f32_e32 v125, v125
	v_lshlrev_b32_e32 v7, 8, v7
	v_and_b32_e32 v7, 0xff00, v7
	v_and_b32_e32 v124, 0xff0000, v124
	v_perm_b32 v6, v125, v6, s1
	v_or3_b32 v124, v6, v7, v124
	v_mbcnt_lo_u32_b32 v6, -1, 0
	v_mbcnt_hi_u32_b32 v6, -1, v6
	v_mul_f32_e32 v125, v135, v1
	v_ashrrev_i32_e32 v7, 31, v6
	v_lshl_add_u64 v[6:7], v[6:7], 2, s[4:5]
	global_store_dword v[6:7], v124, off offset:1024
	v_mul_f32_e32 v7, v153, v1
	v_mul_f32_e32 v6, v152, v1
	v_rndne_f32_e32 v7, v7
	v_mul_f32_e32 v124, v134, v1
	v_rndne_f32_e32 v6, v6
	v_cvt_i32_f32_e32 v7, v7
	v_rndne_f32_e32 v124, v124
	v_rndne_f32_e32 v125, v125
	v_cvt_i32_f32_e32 v6, v6
	v_cvt_i32_f32_sdwa v124, v124 dst_sel:WORD_1 dst_unused:UNUSED_PAD src0_sel:DWORD
	v_cvt_i32_f32_e32 v125, v125
	v_lshlrev_b32_e32 v7, 8, v7
	v_and_b32_e32 v7, 0xff00, v7
	v_and_b32_e32 v124, 0xff0000, v124
	v_perm_b32 v6, v125, v6, s1
	v_or3_b32 v124, v6, v7, v124
	v_mbcnt_lo_u32_b32 v6, -1, 0
	v_mbcnt_hi_u32_b32 v6, -1, v6
	v_mul_f32_e32 v125, v155, v1
	v_ashrrev_i32_e32 v7, 31, v6
	v_lshl_add_u64 v[6:7], v[6:7], 2, s[4:5]
	global_store_dword v[6:7], v124, off offset:1280
	v_mul_f32_e32 v7, v157, v1
	v_mul_f32_e32 v6, v156, v1
	v_rndne_f32_e32 v7, v7
	v_mul_f32_e32 v124, v154, v1
	v_rndne_f32_e32 v6, v6
	v_cvt_i32_f32_e32 v7, v7
	v_rndne_f32_e32 v124, v124
	v_rndne_f32_e32 v125, v125
	v_mul_f32_e32 v5, v5, v1
	v_cvt_i32_f32_e32 v6, v6
	v_cvt_i32_f32_sdwa v124, v124 dst_sel:WORD_1 dst_unused:UNUSED_PAD src0_sel:DWORD
	v_cvt_i32_f32_e32 v125, v125
	v_mul_f32_e32 v4, v4, v1
	v_rndne_f32_e32 v5, v5
	v_mul_f32_e32 v2, v2, v1
	v_mul_f32_e32 v1, v3, v1
	v_rndne_f32_e32 v4, v4
	v_cvt_i32_f32_e32 v5, v5
	v_rndne_f32_e32 v2, v2
	v_rndne_f32_e32 v1, v1
	v_cvt_i32_f32_e32 v4, v4
	v_cvt_i32_f32_sdwa v2, v2 dst_sel:WORD_1 dst_unused:UNUSED_PAD src0_sel:DWORD
	v_cvt_i32_f32_e32 v1, v1
	v_lshlrev_b32_e32 v7, 8, v7
	v_and_b32_e32 v7, 0xff00, v7
	v_and_b32_e32 v124, 0xff0000, v124
	v_perm_b32 v6, v125, v6, s1
	v_or3_b32 v124, v6, v7, v124
	v_mbcnt_lo_u32_b32 v6, -1, 0
	v_mbcnt_hi_u32_b32 v6, -1, v6
	v_lshlrev_b32_e32 v3, 8, v5
	v_ashrrev_i32_e32 v7, 31, v6
	v_lshl_add_u64 v[6:7], v[6:7], 2, s[4:5]
	v_and_b32_e32 v3, 0xff00, v3
	v_and_b32_e32 v2, 0xff0000, v2
	v_perm_b32 v1, v1, v4, s1
	global_store_dword v[6:7], v124, off offset:1536
	v_or3_b32 v1, v1, v3, v2
	v_mbcnt_lo_u32_b32 v2, -1, 0
	v_mbcnt_hi_u32_b32 v2, -1, v2
	s_nop 0
	v_ashrrev_i32_e32 v3, 31, v2
	v_lshl_add_u64 v[2:3], v[2:3], 2, s[4:5]
	global_store_dword v[2:3], v1, off offset:1792
	v_mbcnt_lo_u32_b32 v1, -1, 0
	v_mbcnt_hi_u32_b32 v1, -1, v1
	s_nop 0
	v_cmp_eq_u32_e32 vcc, 0, v1
	s_and_saveexec_b64 s[4:5], vcc
	s_cbranch_execz .LBB0_1483
	s_lshl_b32 s8, s6, 1
	s_ashr_i32 s9, s8, 31
	s_lshl_b64 s[8:9], s[8:9], 2
	s_add_u32 s8, s27, s8
	s_addc_u32 s9, s64, s9
	s_add_i32 s0, s88, 0
	s_add_i32 s0, s0, 0x18c00
	s_lshl_b64 s[6:7], s[6:7], 2
	v_mul_f32_e32 v2, 0x3a000000, v126
	v_mov_b32_e32 v3, v32
	v_mov_b32_e32 v1, s0
	s_add_u32 s6, s25, s6
	v_readlane_b32 s0, v255, 20
	ds_write_b64 v1, v[2:3]
	s_addc_u32 s7, s26, s7
	v_mov_b32_e32 v1, s0
	global_store_dwordx2 v33, v[2:3], s[8:9]
	global_store_dword v33, v0, s[6:7]
	ds_write_b32 v1, v0
; __device__ __forceinline__ float wave_sum(float v) {
; #pragma unroll
;     for (int o = 1; o < 64; o <<= 1) v += __shfl_xor(v, o);
;     return v;
; __device__ __forceinline__ void p6_router(Frame& F) {
;     ...
;             for (int rr = 0; rr < 8; ++rr) { const int row = F.wave * 8 + rr, m = t0 + row;
;                 f32x4 v[8]; float s = 0.f;
; #pragma unroll
;                 for (int j = 0; j < 8; ++j) { const v2u w = raw[rr][j]; v[j] = (f32x4){bf_lo(w.x), bf_hi(w.x), bf_lo(w.y), bf_hi(w.y)}; s += (v[j][0] + v[j][1]) + (v[j][2] + v[j][3]); }
;                 const float mean = wave_sum(s) * (1.f / D); float s2 = 0.f;
; #pragma unroll
;                 for (int j = 0; j < 8; ++j) { v[j] = v[j] - mean; s2 += (v[j][0] * v[j][0] + v[j][1] * v[j][1]) + (v[j][2] * v[j][2] + v[j][3] * v[j][3]); }
.LBB0_1483:
	s_or_b64 exec, exec, s[4:5]
	v_lshlrev_b32_e32 v125, 16, v122
	v_lshlrev_b32_e32 v124, 16, v120
	v_and_b32_e32 v137, 0xffff0000, v122
	v_and_b32_e32 v136, 0xffff0000, v120
	v_lshlrev_b32_e32 v139, 16, v123
	v_lshlrev_b32_e32 v138, 16, v121
	v_and_b32_e32 v141, 0xffff0000, v123
	v_and_b32_e32 v140, 0xffff0000, v121
	v_pk_add_f32 v[0:1], v[124:125], v[136:137]
	v_pk_add_f32 v[2:3], v[138:139], v[140:141]
	v_lshlrev_b32_e32 v123, 16, v119
	v_pk_add_f32 v[0:1], v[0:1], v[2:3]
	v_lshlrev_b32_e32 v122, 16, v118
	v_add_f32_e32 v0, 0, v0
	v_and_b32_e32 v143, 0xffff0000, v119
	v_and_b32_e32 v142, 0xffff0000, v118
	v_add_f32_e32 v6, v0, v1
	v_pk_add_f32 v[0:1], v[122:123], v[142:143]
	v_lshlrev_b32_e32 v126, 16, v116
	v_and_b32_e32 v127, 0xffff0000, v116
	v_lshlrev_b32_e32 v128, 16, v117
	v_and_b32_e32 v129, 0xffff0000, v117
	v_and_b32_e32 v135, 0xffff0000, v114
	v_pk_add_f32 v[0:1], v[0:1], v[0:1] op_sel:[0,1] op_sel_hi:[1,0]
	v_add_f32_e32 v132, v126, v127
	v_add_f32_e32 v130, v128, v129
	v_lshlrev_b32_e32 v7, 16, v114
	v_lshlrev_b32_e32 v133, 16, v115
	v_and_b32_e32 v131, 0xffff0000, v115
	v_mov_b32_e32 v1, v135
	v_pk_add_f32 v[0:1], v[6:7], v[0:1]
	v_pk_add_f32 v[2:3], v[132:133], v[130:131]
	v_lshlrev_b32_e32 v5, 16, v113
	v_lshlrev_b32_e32 v4, 16, v112
	v_and_b32_e32 v145, 0xffff0000, v113
	v_and_b32_e32 v144, 0xffff0000, v112
	v_pk_add_f32 v[116:117], v[0:1], v[2:3]
	v_pk_add_f32 v[118:119], v[4:5], v[144:145]
	v_lshlrev_b32_e32 v0, 16, v110
	v_and_b32_e32 v1, 0xffff0000, v110
	v_lshlrev_b32_e32 v2, 16, v111
	v_and_b32_e32 v3, 0xffff0000, v111
	v_lshlrev_b32_e32 v114, 16, v108
	v_and_b32_e32 v115, 0xffff0000, v108
	v_lshlrev_b32_e32 v113, 16, v109
	v_and_b32_e32 v111, 0xffff0000, v109
	v_pk_add_f32 v[108:109], v[116:117], v[116:117] op_sel:[0,1] op_sel_hi:[1,0]
	v_pk_add_f32 v[116:117], v[118:119], v[118:119] op_sel:[0,1] op_sel_hi:[1,0]
	v_add_f32_e32 v112, v0, v1
	v_add_f32_e32 v110, v2, v3
	v_mov_b32_e32 v109, v114
	v_mov_b32_e32 v117, v115
	v_pk_add_f32 v[108:109], v[108:109], v[116:117]
	v_pk_add_f32 v[116:117], v[112:113], v[110:111]
	v_readlane_b32 s0, v255, 16
	v_pk_add_f32 v[108:109], v[108:109], v[116:117]
	s_nop 0
	v_add_f32_e32 v6, v108, v109
	s_waitcnt lgkmcnt(0)
	s_nop 1
	v_add_f32_dpp v6, v6, v6 quad_perm:[1,0,3,2] row_mask:0xf bank_mask:0xf
	s_waitcnt lgkmcnt(0)
	s_nop 1
	v_add_f32_dpp v6, v6, v6 quad_perm:[2,3,0,1] row_mask:0xf bank_mask:0xf
	s_waitcnt lgkmcnt(0)
	s_nop 1
	v_add_f32_dpp v6, v6, v6 row_half_mirror row_mask:0xf bank_mask:0xf
	s_waitcnt lgkmcnt(0)
	s_nop 1
	v_add_f32_dpp v6, v6, v6 row_mirror row_mask:0xf bank_mask:0xf
	s_waitcnt lgkmcnt(0)
	v_mov_b32_e32 v32, v6
	s_nop 1
	v_permlane16_swap_b32_e32 v6, v32
	v_add_f32_e32 v6, v6, v32
	s_waitcnt lgkmcnt(0)
	v_mov_b32_e32 v32, v6
	s_nop 1
	v_permlane32_swap_b32_e32 v6, v32
	v_add_f32_e32 v112, v6, v32
	v_fmac_f32_e32 v140, 0xba000000, v112
	v_fmac_f32_e32 v136, 0xba000000, v112
	v_fmac_f32_e32 v141, 0xba000000, v112
	v_fmac_f32_e32 v137, 0xba000000, v112
	v_fmac_f32_e32 v138, 0xba000000, v112
	v_fmac_f32_e32 v124, 0xba000000, v112
	v_fmac_f32_e32 v139, 0xba000000, v112
	v_fmac_f32_e32 v125, 0xba000000, v112
	v_mov_b32_e32 v119, v137
	v_mov_b32_e32 v109, v136
	v_pk_mul_f32 v[116:117], v[136:137], v[136:137]
	v_pk_mul_f32 v[136:137], v[140:141], v[140:141]
	v_mov_b32_e32 v118, v125
	v_mov_b32_e32 v108, v124
	v_pk_fma_f32 v[124:125], v[124:125], v[124:125], v[116:117]
	v_pk_fma_f32 v[136:137], v[138:139], v[138:139], v[136:137]
	v_fmac_f32_e32 v142, 0xba000000, v112
	v_pk_add_f32 v[124:125], v[124:125], v[136:137]
	v_fmac_f32_e32 v143, 0xba000000, v112
	v_fmac_f32_e32 v123, 0xba000000, v112
	v_pk_add_f32 v[136:137], v[124:125], v[124:125] op_sel_hi:[0,1]
	v_fmac_f32_e32 v122, 0xba000000, v112
	v_mov_b32_e32 v124, v123
	v_mov_b32_e32 v125, v143
	v_mov_b32_e32 v123, v142
	v_mov_b32_e32 v120, v139
	v_mov_b32_e32 v121, v141
	v_mov_b32_e32 v116, v138
	v_mov_b32_e32 v117, v140
	v_pk_mul_f32 v[138:139], v[124:125], v[124:125]
	v_pk_mul_f32 v[140:141], v[122:123], v[122:123]
	v_fmac_f32_e32 v126, 0xba000000, v112
	v_pk_mov_b32 v[142:143], v[140:141], v[138:139] op_sel:[1,0]
	v_mov_b32_e32 v141, v139
	v_fmac_f32_e32 v127, 0xba000000, v112
	v_fmac_f32_e32 v128, 0xba000000, v112
	v_mul_f32_e32 v6, v126, v126
	v_pk_add_f32 v[138:139], v[142:143], v[140:141]
	v_fmac_f32_e32 v129, 0xba000000, v112
	v_pk_fma_f32 v[140:141], v[126:127], v[126:127], v[6:7] op_sel_hi:[1,1,0]
	v_mul_f32_e32 v6, v128, v128
	v_pk_add_f32 v[138:139], v[138:139], v[138:139] op_sel_hi:[0,1]
	v_pk_fma_f32 v[142:143], v[128:129], v[128:129], v[6:7] op_sel_hi:[1,1,0]
	v_fmac_f32_e32 v131, 0xba000000, v112
	v_fmac_f32_e32 v133, 0xba000000, v112
	v_fmac_f32_e32 v135, 0xba000000, v112
	v_fmac_f32_e32 v7, 0xba000000, v112
	v_mul_f32_e32 v140, v7, v7
	v_mul_f32_e32 v142, v135, v135
	v_mul_f32_e32 v138, v133, v133
	v_mul_f32_e32 v136, v131, v131
	v_pk_add_f32 v[140:141], v[140:141], v[142:143]
	v_pk_add_f32 v[136:137], v[138:139], v[136:137]
	v_fmac_f32_e32 v144, 0xba000000, v112
	v_pk_add_f32 v[136:137], v[140:141], v[136:137]
	v_fmac_f32_e32 v145, 0xba000000, v112
	v_fmac_f32_e32 v5, 0xba000000, v112
	v_pk_add_f32 v[138:139], v[136:137], v[136:137] op_sel_hi:[0,1]
	v_fmac_f32_e32 v4, 0xba000000, v112
	v_mov_b32_e32 v136, v5
	v_mov_b32_e32 v137, v145
	v_mov_b32_e32 v5, v144
	v_pk_mul_f32 v[140:141], v[136:137], v[136:137]
	v_pk_mul_f32 v[142:143], v[4:5], v[4:5]
	v_fmac_f32_e32 v0, 0xba000000, v112
	v_pk_mov_b32 v[144:145], v[142:143], v[140:141] op_sel:[1,0]
	v_mov_b32_e32 v143, v141
	v_fmac_f32_e32 v1, 0xba000000, v112
	v_fmac_f32_e32 v2, 0xba000000, v112
	v_mul_f32_e32 v6, v0, v0
	v_pk_add_f32 v[140:141], v[144:145], v[142:143]
	v_fmac_f32_e32 v3, 0xba000000, v112
	v_pk_fma_f32 v[142:143], v[0:1], v[0:1], v[6:7] op_sel_hi:[1,1,0]
	v_mul_f32_e32 v6, v2, v2
	v_pk_add_f32 v[140:141], v[140:141], v[140:141] op_sel_hi:[0,1]
	v_pk_fma_f32 v[144:145], v[2:3], v[2:3], v[6:7] op_sel_hi:[1,1,0]
	v_fmac_f32_e32 v111, 0xba000000, v112
	v_fmac_f32_e32 v113, 0xba000000, v112
	v_fmac_f32_e32 v115, 0xba000000, v112
	v_fmac_f32_e32 v114, 0xba000000, v112
	v_mul_f32_e32 v142, v114, v114
	v_mul_f32_e32 v144, v115, v115
	v_mul_f32_e32 v140, v113, v113
	v_mul_f32_e32 v138, v111, v111
	v_pk_add_f32 v[142:143], v[142:143], v[144:145]
	v_pk_add_f32 v[138:139], v[140:141], v[138:139]
	s_nop 0
	v_pk_add_f32 v[138:139], v[142:143], v[138:139]
	s_nop 0
	v_add_f32_e32 v6, v138, v139
	v_mbcnt_lo_u32_b32 v138, -1, 0
	v_mbcnt_hi_u32_b32 v138, -1, v138
	v_ashrrev_i32_e32 v139, 31, v138
	v_lshl_add_u64 v[138:139], v[138:139], 4, s[12:13]
	global_load_dwordx4 v[138:141], v[138:139], off
	v_mbcnt_lo_u32_b32 v142, -1, 0
	v_mbcnt_hi_u32_b32 v142, -1, v142
	s_waitcnt lgkmcnt(0)
; #define GAS __attribute__((address_space(1)))
; #define FLANE lane_id()
; __device__ __forceinline__ void p6_router(Frame& F) {
;     ...
;                 const float rstd = 1.f / sqrtf(wave_sum(s2) * (1.f / D) + LN_EPS);
;                 float am = 0.f;
; #pragma unroll
;                 for (int j = 0; j < 8; ++j) { const f32x4 g = *((const GAS f32x4*)F.ln1_g + FLANE + 64 * j), b = *((const GAS f32x4*)F.ln1_b + FLANE + 64 * j);
;                     v[j] = v[j] * rstd * g + b; am = fmaxf(am, fmaxf(fmaxf(fabsf(v[j][0]), fabsf(v[j][1])), fmaxf(fabsf(v[j][2]), fabsf(v[j][3])))); }
	s_nop 1
	v_add_f32_dpp v6, v6, v6 quad_perm:[1,0,3,2] row_mask:0xf bank_mask:0xf
	v_ashrrev_i32_e32 v143, 31, v142
	v_lshl_add_u64 v[142:143], v[142:143], 4, s[14:15]
	global_load_dwordx4 v[142:145], v[142:143], off
	s_waitcnt lgkmcnt(0)
	s_nop 1
	v_add_f32_dpp v6, v6, v6 quad_perm:[2,3,0,1] row_mask:0xf bank_mask:0xf
	s_waitcnt lgkmcnt(0)
	s_nop 1
	v_add_f32_dpp v6, v6, v6 row_half_mirror row_mask:0xf bank_mask:0xf
	s_waitcnt lgkmcnt(0)
	s_nop 1
	v_add_f32_dpp v6, v6, v6 row_mirror row_mask:0xf bank_mask:0xf
	s_waitcnt lgkmcnt(0)
	v_mov_b32_e32 v32, v6
	s_nop 1
	v_permlane16_swap_b32_e32 v6, v32
	v_add_f32_e32 v6, v6, v32
	s_waitcnt lgkmcnt(0)
	v_mov_b32_e32 v32, v6
	s_nop 1
	v_permlane32_swap_b32_e32 v6, v32
	v_add_f32_e32 v6, v6, v32
	v_fmamk_f32 v6, v6, 0x3a000000, v166
	v_cmp_gt_f32_e32 vcc, s22, v6
	v_mul_f32_e32 v32, 0x4f800000, v6
	s_nop 0
	v_cndmask_b32_e32 v6, v6, v32, vcc
	v_sqrt_f32_e32 v32, v6
	s_nop 0
	v_add_u32_e32 v110, -1, v32
	v_fma_f32 v130, -v110, v32, v6
	v_cmp_ge_f32_e64 s[4:5], 0, v130
	v_add_u32_e32 v130, 1, v32
	s_nop 0
	v_cndmask_b32_e64 v110, v32, v110, s[4:5]
	v_fma_f32 v32, -v130, v32, v6
	v_cmp_lt_f32_e64 s[4:5], 0, v32
	s_nop 1
	v_cndmask_b32_e64 v32, v110, v130, s[4:5]
	v_mul_f32_e32 v110, 0x37800000, v32
	v_cndmask_b32_e32 v32, v32, v110, vcc
	v_cmp_class_f32_e32 vcc, v6, v167
	s_nop 1
	v_cndmask_b32_e32 v6, v32, v6, vcc
	v_div_scale_f32 v32, s[4:5], v6, v6, 1.0
	v_rcp_f32_e32 v110, v32
	s_add_i32 s4, s42, s0
	s_ashr_i32 s5, s4, 31
	v_fma_f32 v130, -v32, v110, 1.0
	v_fmac_f32_e32 v110, v130, v110
	v_div_scale_f32 v130, vcc, 1.0, v6, 1.0
	v_mul_f32_e32 v132, v130, v110
	v_fma_f32 v134, -v32, v132, v130
	v_fmac_f32_e32 v132, v134, v110
	v_fma_f32 v32, -v32, v132, v130
	v_div_fmas_f32 v32, v32, v110, v132
	v_div_fixup_f32 v32, v32, v6, 1.0
	v_pk_mul_f32 v[146:147], v[108:109], v[32:33] op_sel_hi:[1,0]
	v_pk_mul_f32 v[108:109], v[116:117], v[32:33] op_sel_hi:[1,0]
	v_mov_b32_e32 v134, v7
	v_pk_mul_f32 v[4:5], v[4:5], v[32:33] op_sel_hi:[1,0]
	v_pk_mul_f32 v[2:3], v[2:3], v[32:33] op_sel_hi:[1,0]
	v_pk_mul_f32 v[0:1], v[0:1], v[32:33] op_sel_hi:[1,0]
	v_pk_mul_f32 v[114:115], v[114:115], v[32:33] op_sel_hi:[1,0]
	s_waitcnt vmcnt(0)
	v_pk_fma_f32 v[116:117], v[138:139], v[146:147], v[142:143]
	v_mbcnt_lo_u32_b32 v138, -1, 0
	v_mbcnt_hi_u32_b32 v138, -1, v138
	v_pk_fma_f32 v[108:109], v[140:141], v[108:109], v[144:145]
	v_ashrrev_i32_e32 v139, 31, v138
	v_lshl_add_u64 v[138:139], v[138:139], 4, s[12:13]
	global_load_dwordx4 v[138:141], v[138:139], off offset:1024
	v_mbcnt_lo_u32_b32 v142, -1, 0
	v_mbcnt_hi_u32_b32 v142, -1, v142
	v_pk_mul_f32 v[146:147], v[118:119], v[32:33] op_sel_hi:[1,0]
	v_ashrrev_i32_e32 v143, 31, v142
	v_lshl_add_u64 v[142:143], v[142:143], 4, s[14:15]
	global_load_dwordx4 v[142:145], v[142:143], off offset:1024
	v_pk_mul_f32 v[118:119], v[120:121], v[32:33] op_sel_hi:[1,0]
	v_max_f32_e64 v6, |v108|, |v109|
	v_max3_f32 v6, |v116|, |v117|, v6
	s_waitcnt vmcnt(0)
	v_pk_fma_f32 v[120:121], v[138:139], v[146:147], v[142:143]
	v_mbcnt_lo_u32_b32 v138, -1, 0
	v_mbcnt_hi_u32_b32 v138, -1, v138
	v_pk_fma_f32 v[118:119], v[140:141], v[118:119], v[144:145]
	v_ashrrev_i32_e32 v139, 31, v138
	v_lshl_add_u64 v[138:139], v[138:139], 4, s[12:13]
	global_load_dwordx4 v[138:141], v[138:139], off offset:2048
	v_mbcnt_lo_u32_b32 v142, -1, 0
	v_mbcnt_hi_u32_b32 v142, -1, v142
	v_pk_mul_f32 v[146:147], v[122:123], v[32:33] op_sel_hi:[1,0]
	v_ashrrev_i32_e32 v143, 31, v142
	v_lshl_add_u64 v[142:143], v[142:143], 4, s[14:15]
	global_load_dwordx4 v[142:145], v[142:143], off offset:2048
	v_pk_mul_f32 v[122:123], v[124:125], v[32:33] op_sel_hi:[1,0]
	v_max_f32_e64 v110, |v118|, |v119|
	v_max3_f32 v110, |v120|, |v121|, v110
	v_max3_f32 v6, v6, 0, v110
	s_waitcnt vmcnt(0)
	v_pk_fma_f32 v[124:125], v[138:139], v[146:147], v[142:143]
	v_mbcnt_lo_u32_b32 v138, -1, 0
	v_mbcnt_hi_u32_b32 v138, -1, v138
	v_pk_fma_f32 v[122:123], v[140:141], v[122:123], v[144:145]
	v_ashrrev_i32_e32 v139, 31, v138
	v_lshl_add_u64 v[138:139], v[138:139], 4, s[12:13]
	global_load_dwordx4 v[138:141], v[138:139], off offset:3072
	v_mbcnt_lo_u32_b32 v142, -1, 0
	v_mbcnt_hi_u32_b32 v142, -1, v142
	v_pk_mul_f32 v[146:147], v[126:127], v[32:33] op_sel_hi:[1,0]
	v_ashrrev_i32_e32 v143, 31, v142
	v_lshl_add_u64 v[142:143], v[142:143], 4, s[14:15]
	global_load_dwordx4 v[142:145], v[142:143], off offset:3072
	v_pk_mul_f32 v[126:127], v[128:129], v[32:33] op_sel_hi:[1,0]
	v_max_f32_e64 v110, |v122|, |v123|
	v_max3_f32 v110, |v124|, |v125|, v110
	s_waitcnt vmcnt(0)
	v_pk_fma_f32 v[128:129], v[138:139], v[146:147], v[142:143]
	v_mbcnt_lo_u32_b32 v138, -1, 0
	v_mbcnt_hi_u32_b32 v138, -1, v138
	v_pk_fma_f32 v[126:127], v[140:141], v[126:127], v[144:145]
	v_ashrrev_i32_e32 v139, 31, v138
	v_lshl_add_u64 v[138:139], v[138:139], 4, s[12:13]
	v_add_co_u32_e32 v138, vcc, s23, v138
	v_max_f32_e64 v130, |v126|, |v127|
	s_nop 0
	v_addc_co_u32_e32 v139, vcc, 0, v139, vcc
	global_load_dwordx4 v[138:141], v[138:139], off
	v_mbcnt_lo_u32_b32 v142, -1, 0
	v_mbcnt_hi_u32_b32 v142, -1, v142
	v_max3_f32 v130, |v128|, |v129|, v130
	v_ashrrev_i32_e32 v143, 31, v142
	v_lshl_add_u64 v[142:143], v[142:143], 4, s[14:15]
	v_add_co_u32_e32 v142, vcc, s23, v142
	v_max3_f32 v110, v6, v110, v130
	s_nop 0
	v_addc_co_u32_e32 v143, vcc, 0, v143, vcc
	global_load_dwordx4 v[142:145], v[142:143], off
	v_mov_b32_e32 v130, v133
	v_pk_mul_f32 v[130:131], v[130:131], v[32:33] op_sel_hi:[1,0]
	v_pk_mul_f32 v[6:7], v[134:135], v[32:33] op_sel_hi:[1,0]
	s_waitcnt vmcnt(0)
; #define FLANE lane_id()
; __device__ __forceinline__ void p6_router(Frame& F) {
;     ...
;                     v[j] = v[j] * rstd * g + b; am = fmaxf(am, fmaxf(fmaxf(fabsf(v[j][0]), fabsf(v[j][1])), fmaxf(fabsf(v[j][2]), fabsf(v[j][3])))); }
; #pragma unroll
;                 for (int o = 1; o < 64; o <<= 1) am = fmaxf(am, __shfl_xor(am, o));
;                 const float sc = am > 0.f ? am * (1.f / 127.f) : 1.f, inv = 1.f / sc;
; #pragma unroll
;                 for (int j = 0; j < 8; ++j) { const int q0 = (int)__builtin_rintf(v[j][0] * inv), q1 = (int)__builtin_rintf(v[j][1] * inv), q2 = (int)__builtin_rintf(v[j][2] * inv), q3 = (int)__builtin_rintf(v[j][3] * inv);
;                     h1q[(size_t)m * (D / 4) + FLANE + 64 * j] = (unsigned)(q0 & 0xff) | ((unsigned)(q1 & 0xff) << 8) | ((unsigned)(q2 & 0xff) << 16) | ((unsigned)(q3 & 0xff) << 24); }
	v_pk_fma_f32 v[130:131], v[140:141], v[130:131], v[144:145]
	v_pk_fma_f32 v[132:133], v[138:139], v[6:7], v[142:143]
	v_max_f32_e64 v6, |v130|, |v131|
	v_max3_f32 v146, |v132|, |v133|, v6
	v_mbcnt_lo_u32_b32 v6, -1, 0
	v_mbcnt_hi_u32_b32 v6, -1, v6
	s_nop 0
	v_ashrrev_i32_e32 v7, 31, v6
	v_lshl_add_u64 v[6:7], v[6:7], 4, s[12:13]
	v_add_co_u32_e32 v6, vcc, s23, v6
	s_nop 1
	v_addc_co_u32_e32 v7, vcc, 0, v7, vcc
	global_load_dwordx4 v[138:141], v[6:7], off offset:1024
	v_mbcnt_lo_u32_b32 v6, -1, 0
	v_mbcnt_hi_u32_b32 v6, -1, v6
	s_nop 0
	v_ashrrev_i32_e32 v7, 31, v6
	v_lshl_add_u64 v[6:7], v[6:7], 4, s[14:15]
	v_add_co_u32_e32 v6, vcc, s23, v6
	s_nop 1
	v_addc_co_u32_e32 v7, vcc, 0, v7, vcc
	global_load_dwordx4 v[142:145], v[6:7], off offset:1024
	v_pk_mul_f32 v[6:7], v[136:137], v[32:33] op_sel_hi:[1,0]
	s_waitcnt vmcnt(0)
	v_pk_fma_f32 v[136:137], v[138:139], v[4:5], v[142:143]
	v_pk_fma_f32 v[134:135], v[140:141], v[6:7], v[144:145]
	s_nop 0
	v_max_f32_e64 v4, |v134|, |v135|
	v_max3_f32 v4, |v136|, |v137|, v4
	v_max3_f32 v144, v110, v146, v4
	v_mbcnt_lo_u32_b32 v4, -1, 0
	v_mbcnt_hi_u32_b32 v4, -1, v4
	v_mov_b32_e32 v110, v113
	v_ashrrev_i32_e32 v5, 31, v4
	v_lshl_add_u64 v[4:5], v[4:5], 4, s[12:13]
	v_add_co_u32_e32 v4, vcc, s23, v4
	v_pk_mul_f32 v[110:111], v[110:111], v[32:33] op_sel_hi:[1,0]
	s_nop 0
	v_addc_co_u32_e32 v5, vcc, 0, v5, vcc
	global_load_dwordx4 v[4:7], v[4:5], off offset:2048
	v_mbcnt_lo_u32_b32 v138, -1, 0
	v_mbcnt_hi_u32_b32 v138, -1, v138
	s_nop 0
	v_ashrrev_i32_e32 v139, 31, v138
	v_lshl_add_u64 v[138:139], v[138:139], 4, s[14:15]
	v_add_co_u32_e32 v138, vcc, s23, v138
	s_nop 1
	v_addc_co_u32_e32 v139, vcc, 0, v139, vcc
	global_load_dwordx4 v[140:143], v[138:139], off offset:2048
	s_waitcnt vmcnt(0)
	v_pk_fma_f32 v[138:139], v[2:3], v[6:7], v[142:143]
	v_pk_fma_f32 v[140:141], v[0:1], v[4:5], v[140:141]
	v_max_f32_e64 v0, |v138|, |v139|
	v_max3_f32 v142, |v140|, |v141|, v0
	v_mbcnt_lo_u32_b32 v0, -1, 0
	v_mbcnt_hi_u32_b32 v0, -1, v0
	s_nop 0
	v_ashrrev_i32_e32 v1, 31, v0
	v_lshl_add_u64 v[0:1], v[0:1], 4, s[12:13]
	v_add_co_u32_e32 v0, vcc, s23, v0
	s_nop 1
	v_addc_co_u32_e32 v1, vcc, 0, v1, vcc
	global_load_dwordx4 v[0:3], v[0:1], off offset:3072
	v_mbcnt_lo_u32_b32 v4, -1, 0
	v_mbcnt_hi_u32_b32 v4, -1, v4
	s_nop 0
	v_ashrrev_i32_e32 v5, 31, v4
	v_lshl_add_u64 v[4:5], v[4:5], 4, s[14:15]
	v_add_co_u32_e32 v4, vcc, s23, v4
	s_nop 1
	v_addc_co_u32_e32 v5, vcc, 0, v5, vcc
	global_load_dwordx4 v[4:7], v[4:5], off offset:3072
	s_waitcnt vmcnt(0)
	v_pk_fma_f32 v[2:3], v[110:111], v[2:3], v[6:7]
	v_pk_fma_f32 v[4:5], v[114:115], v[0:1], v[4:5]
	v_max_f32_e64 v0, |v2|, |v3|
	v_max3_f32 v0, |v4|, |v5|, v0
	v_max3_f32 v0, v144, v142, v0
	s_waitcnt lgkmcnt(0)
	s_nop 1
	v_max_f32_dpp v0, v0, v0 quad_perm:[1,0,3,2] row_mask:0xf bank_mask:0xf
	s_waitcnt lgkmcnt(0)
	s_nop 1
	v_max_f32_dpp v0, v0, v0 quad_perm:[2,3,0,1] row_mask:0xf bank_mask:0xf
	s_waitcnt lgkmcnt(0)
	s_nop 1
	v_max_f32_dpp v0, v0, v0 row_half_mirror row_mask:0xf bank_mask:0xf
	s_waitcnt lgkmcnt(0)
	s_nop 1
	v_max_f32_dpp v0, v0, v0 row_mirror row_mask:0xf bank_mask:0xf
	s_waitcnt lgkmcnt(0)
	v_mov_b32_e32 v1, v0
	s_nop 1
	v_permlane16_swap_b32_e32 v0, v1
	v_max_f32_e32 v0, v0, v1
	s_waitcnt lgkmcnt(0)
	v_mov_b32_e32 v1, v0
	s_nop 1
	v_permlane32_swap_b32_e32 v0, v1
	v_max_f32_e32 v0, v0, v1
	v_cmp_lt_f32_e32 vcc, 0, v0
	v_mul_f32_e32 v0, 0x3c010204, v0
	s_nop 0
	v_cndmask_b32_e32 v0, 1.0, v0, vcc
	v_div_scale_f32 v1, s[6:7], v0, v0, 1.0
	v_rcp_f32_e32 v6, v1
	s_lshl_b64 s[6:7], s[4:5], 11
	s_add_u32 s6, s3, s6
	s_addc_u32 s7, s24, s7
	v_fma_f32 v7, -v1, v6, 1.0
	v_fmac_f32_e32 v6, v7, v6
	v_div_scale_f32 v7, vcc, 1.0, v0, 1.0
	v_mul_f32_e32 v110, v7, v6
	v_fma_f32 v111, -v1, v110, v7
	v_fmac_f32_e32 v110, v111, v6
	v_fma_f32 v1, -v1, v110, v7
	v_div_fmas_f32 v1, v1, v6, v110
	v_div_fixup_f32 v1, v1, v0, 1.0
	v_mul_f32_e32 v7, v117, v1
	v_mul_f32_e32 v6, v116, v1
	v_rndne_f32_e32 v7, v7
	v_mul_f32_e32 v108, v108, v1
	v_mul_f32_e32 v109, v109, v1
	v_rndne_f32_e32 v6, v6
	v_cvt_i32_f32_e32 v7, v7
	v_rndne_f32_e32 v108, v108
	v_rndne_f32_e32 v109, v109
	v_cvt_i32_f32_e32 v6, v6
	v_cvt_i32_f32_sdwa v108, v108 dst_sel:WORD_1 dst_unused:UNUSED_PAD src0_sel:DWORD
	v_cvt_i32_f32_e32 v109, v109
	v_lshlrev_b32_e32 v7, 8, v7
	v_and_b32_e32 v7, 0xff00, v7
	v_and_b32_e32 v108, 0xff0000, v108
	v_perm_b32 v6, v109, v6, s1
	v_or3_b32 v108, v6, v7, v108
	v_mbcnt_lo_u32_b32 v6, -1, 0
	v_mbcnt_hi_u32_b32 v6, -1, v6
	v_mul_f32_e32 v109, v119, v1
	v_ashrrev_i32_e32 v7, 31, v6
	v_lshl_add_u64 v[6:7], v[6:7], 2, s[6:7]
	global_store_dword v[6:7], v108, off
	v_mul_f32_e32 v7, v121, v1
	v_mul_f32_e32 v6, v120, v1
	v_rndne_f32_e32 v7, v7
	v_mul_f32_e32 v108, v118, v1
	v_rndne_f32_e32 v6, v6
	v_cvt_i32_f32_e32 v7, v7
	v_rndne_f32_e32 v108, v108
	v_rndne_f32_e32 v109, v109
	v_cvt_i32_f32_e32 v6, v6
	v_cvt_i32_f32_sdwa v108, v108 dst_sel:WORD_1 dst_unused:UNUSED_PAD src0_sel:DWORD
	v_cvt_i32_f32_e32 v109, v109
	v_lshlrev_b32_e32 v7, 8, v7
	v_and_b32_e32 v7, 0xff00, v7
	v_and_b32_e32 v108, 0xff0000, v108
	v_perm_b32 v6, v109, v6, s1
	v_or3_b32 v108, v6, v7, v108
	v_mbcnt_lo_u32_b32 v6, -1, 0
	v_mbcnt_hi_u32_b32 v6, -1, v6
	v_mul_f32_e32 v109, v123, v1
	v_ashrrev_i32_e32 v7, 31, v6
	v_lshl_add_u64 v[6:7], v[6:7], 2, s[6:7]
	global_store_dword v[6:7], v108, off offset:256
	v_mul_f32_e32 v7, v125, v1
	v_mul_f32_e32 v6, v124, v1
	v_rndne_f32_e32 v7, v7
	v_mul_f32_e32 v108, v122, v1
	v_rndne_f32_e32 v6, v6
	v_cvt_i32_f32_e32 v7, v7
	v_rndne_f32_e32 v108, v108
	v_rndne_f32_e32 v109, v109
	v_cvt_i32_f32_e32 v6, v6
	v_cvt_i32_f32_sdwa v108, v108 dst_sel:WORD_1 dst_unused:UNUSED_PAD src0_sel:DWORD
; #define FLANE lane_id()
; __device__ __forceinline__ void p6_router(Frame& F) {
;     ...
;                 for (int j = 0; j < 8; ++j) { const int q0 = (int)__builtin_rintf(v[j][0] * inv), q1 = (int)__builtin_rintf(v[j][1] * inv), q2 = (int)__builtin_rintf(v[j][2] * inv), q3 = (int)__builtin_rintf(v[j][3] * inv);
;                     h1q[(size_t)m * (D / 4) + FLANE + 64 * j] = (unsigned)(q0 & 0xff) | ((unsigned)(q1 & 0xff) << 8) | ((unsigned)(q2 & 0xff) << 16) | ((unsigned)(q3 & 0xff) << 24); }
;                 if (FLANE == 0) { st1[2 * m] = mean; st1[2 * m + 1] = rstd; stl[2 * row] = mean; stl[2 * row + 1] = rstd; sxg[m] = sc; sxl[row] = sc; }
	v_cvt_i32_f32_e32 v109, v109
	v_lshlrev_b32_e32 v7, 8, v7
	v_and_b32_e32 v7, 0xff00, v7
	v_and_b32_e32 v108, 0xff0000, v108
	v_perm_b32 v6, v109, v6, s1
	v_or3_b32 v108, v6, v7, v108
	v_mbcnt_lo_u32_b32 v6, -1, 0
	v_mbcnt_hi_u32_b32 v6, -1, v6
	v_mul_f32_e32 v109, v127, v1
	v_ashrrev_i32_e32 v7, 31, v6
	v_lshl_add_u64 v[6:7], v[6:7], 2, s[6:7]
	global_store_dword v[6:7], v108, off offset:512
	v_mul_f32_e32 v7, v129, v1
	v_mul_f32_e32 v6, v128, v1
	v_rndne_f32_e32 v7, v7
	v_mul_f32_e32 v108, v126, v1
	v_rndne_f32_e32 v6, v6
	v_cvt_i32_f32_e32 v7, v7
	v_rndne_f32_e32 v108, v108
	v_rndne_f32_e32 v109, v109
	v_cvt_i32_f32_e32 v6, v6
	v_cvt_i32_f32_sdwa v108, v108 dst_sel:WORD_1 dst_unused:UNUSED_PAD src0_sel:DWORD
	v_cvt_i32_f32_e32 v109, v109
	v_lshlrev_b32_e32 v7, 8, v7
	v_and_b32_e32 v7, 0xff00, v7
	v_and_b32_e32 v108, 0xff0000, v108
	v_perm_b32 v6, v109, v6, s1
	v_or3_b32 v108, v6, v7, v108
	v_mbcnt_lo_u32_b32 v6, -1, 0
	v_mbcnt_hi_u32_b32 v6, -1, v6
	v_mul_f32_e32 v109, v131, v1
	v_ashrrev_i32_e32 v7, 31, v6
	v_lshl_add_u64 v[6:7], v[6:7], 2, s[6:7]
	global_store_dword v[6:7], v108, off offset:768
	v_mul_f32_e32 v7, v133, v1
	v_mul_f32_e32 v6, v132, v1
	v_rndne_f32_e32 v7, v7
	v_mul_f32_e32 v108, v130, v1
	v_rndne_f32_e32 v6, v6
	v_cvt_i32_f32_e32 v7, v7
	v_rndne_f32_e32 v108, v108
	v_rndne_f32_e32 v109, v109
	v_cvt_i32_f32_e32 v6, v6
	v_cvt_i32_f32_sdwa v108, v108 dst_sel:WORD_1 dst_unused:UNUSED_PAD src0_sel:DWORD
	v_cvt_i32_f32_e32 v109, v109
	v_lshlrev_b32_e32 v7, 8, v7
	v_and_b32_e32 v7, 0xff00, v7
	v_and_b32_e32 v108, 0xff0000, v108
	v_perm_b32 v6, v109, v6, s1
	v_or3_b32 v108, v6, v7, v108
	v_mbcnt_lo_u32_b32 v6, -1, 0
	v_mbcnt_hi_u32_b32 v6, -1, v6
	v_mul_f32_e32 v109, v135, v1
	v_ashrrev_i32_e32 v7, 31, v6
	v_lshl_add_u64 v[6:7], v[6:7], 2, s[6:7]
	global_store_dword v[6:7], v108, off offset:1024
	v_mul_f32_e32 v7, v137, v1
	v_mul_f32_e32 v6, v136, v1
	v_rndne_f32_e32 v7, v7
	v_mul_f32_e32 v108, v134, v1
	v_rndne_f32_e32 v6, v6
	v_cvt_i32_f32_e32 v7, v7
	v_rndne_f32_e32 v108, v108
	v_rndne_f32_e32 v109, v109
	v_cvt_i32_f32_e32 v6, v6
	v_cvt_i32_f32_sdwa v108, v108 dst_sel:WORD_1 dst_unused:UNUSED_PAD src0_sel:DWORD
	v_cvt_i32_f32_e32 v109, v109
	v_lshlrev_b32_e32 v7, 8, v7
	v_and_b32_e32 v7, 0xff00, v7
	v_and_b32_e32 v108, 0xff0000, v108
	v_perm_b32 v6, v109, v6, s1
	v_or3_b32 v108, v6, v7, v108
	v_mbcnt_lo_u32_b32 v6, -1, 0
	v_mbcnt_hi_u32_b32 v6, -1, v6
	v_mul_f32_e32 v109, v139, v1
	v_ashrrev_i32_e32 v7, 31, v6
	v_lshl_add_u64 v[6:7], v[6:7], 2, s[6:7]
	global_store_dword v[6:7], v108, off offset:1280
	v_mul_f32_e32 v7, v141, v1
	v_mul_f32_e32 v6, v140, v1
	v_rndne_f32_e32 v7, v7
	v_mul_f32_e32 v108, v138, v1
	v_rndne_f32_e32 v6, v6
	v_cvt_i32_f32_e32 v7, v7
	v_rndne_f32_e32 v108, v108
	v_rndne_f32_e32 v109, v109
	v_mul_f32_e32 v5, v5, v1
	v_cvt_i32_f32_e32 v6, v6
	v_cvt_i32_f32_sdwa v108, v108 dst_sel:WORD_1 dst_unused:UNUSED_PAD src0_sel:DWORD
	v_cvt_i32_f32_e32 v109, v109
	v_mul_f32_e32 v4, v4, v1
	v_rndne_f32_e32 v5, v5
	v_mul_f32_e32 v2, v2, v1
	v_mul_f32_e32 v1, v3, v1
	v_rndne_f32_e32 v4, v4
	v_cvt_i32_f32_e32 v5, v5
	v_rndne_f32_e32 v2, v2
	v_rndne_f32_e32 v1, v1
	v_cvt_i32_f32_e32 v4, v4
	v_cvt_i32_f32_sdwa v2, v2 dst_sel:WORD_1 dst_unused:UNUSED_PAD src0_sel:DWORD
	v_cvt_i32_f32_e32 v1, v1
	v_lshlrev_b32_e32 v7, 8, v7
	v_and_b32_e32 v7, 0xff00, v7
	v_and_b32_e32 v108, 0xff0000, v108
	v_perm_b32 v6, v109, v6, s1
	v_or3_b32 v108, v6, v7, v108
	v_mbcnt_lo_u32_b32 v6, -1, 0
	v_mbcnt_hi_u32_b32 v6, -1, v6
	v_lshlrev_b32_e32 v3, 8, v5
	v_ashrrev_i32_e32 v7, 31, v6
	v_lshl_add_u64 v[6:7], v[6:7], 2, s[6:7]
	v_and_b32_e32 v3, 0xff00, v3
	v_and_b32_e32 v2, 0xff0000, v2
	v_perm_b32 v1, v1, v4, s1
	global_store_dword v[6:7], v108, off offset:1536
	v_or3_b32 v1, v1, v3, v2
	v_mbcnt_lo_u32_b32 v2, -1, 0
	v_mbcnt_hi_u32_b32 v2, -1, v2
	s_nop 0
	v_ashrrev_i32_e32 v3, 31, v2
	v_lshl_add_u64 v[2:3], v[2:3], 2, s[6:7]
	global_store_dword v[2:3], v1, off offset:1792
	v_mbcnt_lo_u32_b32 v1, -1, 0
	v_mbcnt_hi_u32_b32 v1, -1, v1
	s_nop 0
	v_cmp_eq_u32_e32 vcc, 0, v1
	s_and_saveexec_b64 s[6:7], vcc
	s_cbranch_execz .LBB0_1485
	s_lshl_b32 s8, s4, 1
	s_ashr_i32 s9, s8, 31
	s_lshl_b64 s[8:9], s[8:9], 2
	s_add_u32 s8, s27, s8
	s_addc_u32 s9, s64, s9
	v_readlane_b32 s0, v255, 42
	s_lshl_b64 s[4:5], s[4:5], 2
	v_mul_f32_e32 v2, 0x3a000000, v112
	v_mov_b32_e32 v3, v32
	v_mov_b32_e32 v1, s0
	s_add_u32 s4, s25, s4
	v_readlane_b32 s0, v255, 24
	ds_write_b64 v1, v[2:3]
	s_addc_u32 s5, s26, s5
	v_mov_b32_e32 v1, s0
	global_store_dwordx2 v33, v[2:3], s[8:9]
	global_store_dword v33, v0, s[4:5]
	ds_write_b32 v1, v0
; __device__ __forceinline__ float wave_sum(float v) {
; #pragma unroll
;     for (int o = 1; o < 64; o <<= 1) v += __shfl_xor(v, o);
;     return v;
; __device__ __forceinline__ void p6_router(Frame& F) {
;     ...
;             for (int rr = 0; rr < 8; ++rr) { const int row = F.wave * 8 + rr, m = t0 + row;
;                 f32x4 v[8]; float s = 0.f;
; #pragma unroll
;                 for (int j = 0; j < 8; ++j) { const v2u w = raw[rr][j]; v[j] = (f32x4){bf_lo(w.x), bf_hi(w.x), bf_lo(w.y), bf_hi(w.y)}; s += (v[j][0] + v[j][1]) + (v[j][2] + v[j][3]); }
;                 const float mean = wave_sum(s) * (1.f / D); float s2 = 0.f;
; #pragma unroll
;                 for (int j = 0; j < 8; ++j) { v[j] = v[j] - mean; s2 += (v[j][0] * v[j][0] + v[j][1] * v[j][1]) + (v[j][2] * v[j][2] + v[j][3] * v[j][3]); }
.LBB0_1485:
	s_or_b64 exec, exec, s[6:7]
	v_lshlrev_b32_e32 v109, 16, v106
	v_lshlrev_b32_e32 v108, 16, v104
	v_and_b32_e32 v121, 0xffff0000, v106
	v_and_b32_e32 v120, 0xffff0000, v104
	v_lshlrev_b32_e32 v123, 16, v107
	v_lshlrev_b32_e32 v122, 16, v105
	v_and_b32_e32 v125, 0xffff0000, v107
	v_and_b32_e32 v124, 0xffff0000, v105
	v_pk_add_f32 v[0:1], v[108:109], v[120:121]
	v_pk_add_f32 v[2:3], v[122:123], v[124:125]
	v_lshlrev_b32_e32 v107, 16, v103
	v_pk_add_f32 v[0:1], v[0:1], v[2:3]
	v_lshlrev_b32_e32 v106, 16, v102
	v_add_f32_e32 v0, 0, v0
	v_and_b32_e32 v127, 0xffff0000, v103
	v_and_b32_e32 v126, 0xffff0000, v102
	v_add_f32_e32 v6, v0, v1
	v_pk_add_f32 v[0:1], v[106:107], v[126:127]
	v_lshlrev_b32_e32 v110, 16, v100
	v_and_b32_e32 v111, 0xffff0000, v100
	v_lshlrev_b32_e32 v112, 16, v101
	v_and_b32_e32 v113, 0xffff0000, v101
	v_and_b32_e32 v119, 0xffff0000, v98
	v_pk_add_f32 v[0:1], v[0:1], v[0:1] op_sel:[0,1] op_sel_hi:[1,0]
	v_add_f32_e32 v116, v110, v111
	v_add_f32_e32 v114, v112, v113
	v_lshlrev_b32_e32 v7, 16, v98
	v_lshlrev_b32_e32 v117, 16, v99
	v_and_b32_e32 v115, 0xffff0000, v99
	v_mov_b32_e32 v1, v119
	v_pk_add_f32 v[0:1], v[6:7], v[0:1]
	v_pk_add_f32 v[2:3], v[116:117], v[114:115]
	v_lshlrev_b32_e32 v5, 16, v97
	v_lshlrev_b32_e32 v4, 16, v96
	v_and_b32_e32 v129, 0xffff0000, v97
	v_and_b32_e32 v128, 0xffff0000, v96
	v_pk_add_f32 v[100:101], v[0:1], v[2:3]
	v_pk_add_f32 v[102:103], v[4:5], v[128:129]
	v_lshlrev_b32_e32 v0, 16, v94
	v_and_b32_e32 v1, 0xffff0000, v94
	v_lshlrev_b32_e32 v2, 16, v95
	v_and_b32_e32 v3, 0xffff0000, v95
	v_lshlrev_b32_e32 v98, 16, v92
	v_and_b32_e32 v99, 0xffff0000, v92
	v_lshlrev_b32_e32 v97, 16, v93
	v_and_b32_e32 v95, 0xffff0000, v93
	v_pk_add_f32 v[92:93], v[100:101], v[100:101] op_sel:[0,1] op_sel_hi:[1,0]
	v_pk_add_f32 v[100:101], v[102:103], v[102:103] op_sel:[0,1] op_sel_hi:[1,0]
	v_add_f32_e32 v96, v0, v1
	v_add_f32_e32 v94, v2, v3
	v_mov_b32_e32 v93, v98
	v_mov_b32_e32 v101, v99
	v_pk_add_f32 v[92:93], v[92:93], v[100:101]
	v_pk_add_f32 v[100:101], v[96:97], v[94:95]
	v_readlane_b32 s0, v255, 18
	v_pk_add_f32 v[92:93], v[92:93], v[100:101]
	s_nop 0
	v_add_f32_e32 v6, v92, v93
	s_waitcnt lgkmcnt(0)
	s_nop 1
	v_add_f32_dpp v6, v6, v6 quad_perm:[1,0,3,2] row_mask:0xf bank_mask:0xf
	s_waitcnt lgkmcnt(0)
	s_nop 1
	v_add_f32_dpp v6, v6, v6 quad_perm:[2,3,0,1] row_mask:0xf bank_mask:0xf
	s_waitcnt lgkmcnt(0)
	s_nop 1
	v_add_f32_dpp v6, v6, v6 row_half_mirror row_mask:0xf bank_mask:0xf
	s_waitcnt lgkmcnt(0)
	s_nop 1
	v_add_f32_dpp v6, v6, v6 row_mirror row_mask:0xf bank_mask:0xf
	s_waitcnt lgkmcnt(0)
	v_mov_b32_e32 v32, v6
	s_nop 1
	v_permlane16_swap_b32_e32 v6, v32
	v_add_f32_e32 v6, v6, v32
	s_waitcnt lgkmcnt(0)
	v_mov_b32_e32 v32, v6
	s_nop 1
	v_permlane32_swap_b32_e32 v6, v32
	v_add_f32_e32 v96, v6, v32
	v_fmac_f32_e32 v124, 0xba000000, v96
	v_fmac_f32_e32 v120, 0xba000000, v96
	v_fmac_f32_e32 v125, 0xba000000, v96
	v_fmac_f32_e32 v121, 0xba000000, v96
	v_fmac_f32_e32 v122, 0xba000000, v96
	v_fmac_f32_e32 v108, 0xba000000, v96
	v_fmac_f32_e32 v123, 0xba000000, v96
	v_fmac_f32_e32 v109, 0xba000000, v96
	v_mov_b32_e32 v103, v121
	v_mov_b32_e32 v93, v120
	v_pk_mul_f32 v[100:101], v[120:121], v[120:121]
	v_pk_mul_f32 v[120:121], v[124:125], v[124:125]
	v_mov_b32_e32 v102, v109
	v_mov_b32_e32 v92, v108
	v_pk_fma_f32 v[108:109], v[108:109], v[108:109], v[100:101]
	v_pk_fma_f32 v[120:121], v[122:123], v[122:123], v[120:121]
	v_fmac_f32_e32 v126, 0xba000000, v96
	v_pk_add_f32 v[108:109], v[108:109], v[120:121]
	v_fmac_f32_e32 v127, 0xba000000, v96
	v_fmac_f32_e32 v107, 0xba000000, v96
	v_pk_add_f32 v[120:121], v[108:109], v[108:109] op_sel_hi:[0,1]
	v_fmac_f32_e32 v106, 0xba000000, v96
	v_mov_b32_e32 v108, v107
	v_mov_b32_e32 v109, v127
	v_mov_b32_e32 v107, v126
	v_mov_b32_e32 v104, v123
	v_mov_b32_e32 v105, v125
	v_mov_b32_e32 v100, v122
	v_mov_b32_e32 v101, v124
	v_pk_mul_f32 v[122:123], v[108:109], v[108:109]
	v_pk_mul_f32 v[124:125], v[106:107], v[106:107]
	v_fmac_f32_e32 v110, 0xba000000, v96
	v_pk_mov_b32 v[126:127], v[124:125], v[122:123] op_sel:[1,0]
	v_mov_b32_e32 v125, v123
	v_fmac_f32_e32 v111, 0xba000000, v96
	v_fmac_f32_e32 v112, 0xba000000, v96
	v_mul_f32_e32 v6, v110, v110
	v_pk_add_f32 v[122:123], v[126:127], v[124:125]
	v_fmac_f32_e32 v113, 0xba000000, v96
	v_pk_fma_f32 v[124:125], v[110:111], v[110:111], v[6:7] op_sel_hi:[1,1,0]
	v_mul_f32_e32 v6, v112, v112
	v_pk_add_f32 v[122:123], v[122:123], v[122:123] op_sel_hi:[0,1]
	v_pk_fma_f32 v[126:127], v[112:113], v[112:113], v[6:7] op_sel_hi:[1,1,0]
	v_fmac_f32_e32 v115, 0xba000000, v96
	v_fmac_f32_e32 v117, 0xba000000, v96
	v_fmac_f32_e32 v119, 0xba000000, v96
	v_fmac_f32_e32 v7, 0xba000000, v96
	v_mul_f32_e32 v124, v7, v7
	v_mul_f32_e32 v126, v119, v119
	v_mul_f32_e32 v122, v117, v117
	v_mul_f32_e32 v120, v115, v115
	v_pk_add_f32 v[124:125], v[124:125], v[126:127]
	v_pk_add_f32 v[120:121], v[122:123], v[120:121]
	v_fmac_f32_e32 v128, 0xba000000, v96
	v_pk_add_f32 v[120:121], v[124:125], v[120:121]
	v_fmac_f32_e32 v129, 0xba000000, v96
	v_fmac_f32_e32 v5, 0xba000000, v96
	v_pk_add_f32 v[122:123], v[120:121], v[120:121] op_sel_hi:[0,1]
	v_fmac_f32_e32 v4, 0xba000000, v96
	v_mov_b32_e32 v120, v5
	v_mov_b32_e32 v121, v129
	v_mov_b32_e32 v5, v128
	v_pk_mul_f32 v[124:125], v[120:121], v[120:121]
	v_pk_mul_f32 v[126:127], v[4:5], v[4:5]
	v_fmac_f32_e32 v0, 0xba000000, v96
	v_pk_mov_b32 v[128:129], v[126:127], v[124:125] op_sel:[1,0]
	v_mov_b32_e32 v127, v125
	v_fmac_f32_e32 v1, 0xba000000, v96
	v_fmac_f32_e32 v2, 0xba000000, v96
	v_mul_f32_e32 v6, v0, v0
	v_pk_add_f32 v[124:125], v[128:129], v[126:127]
	v_fmac_f32_e32 v3, 0xba000000, v96
	v_pk_fma_f32 v[126:127], v[0:1], v[0:1], v[6:7] op_sel_hi:[1,1,0]
	v_mul_f32_e32 v6, v2, v2
	v_pk_add_f32 v[124:125], v[124:125], v[124:125] op_sel_hi:[0,1]
	v_pk_fma_f32 v[128:129], v[2:3], v[2:3], v[6:7] op_sel_hi:[1,1,0]
	v_fmac_f32_e32 v95, 0xba000000, v96
	v_fmac_f32_e32 v97, 0xba000000, v96
	v_fmac_f32_e32 v99, 0xba000000, v96
	v_fmac_f32_e32 v98, 0xba000000, v96
	v_mul_f32_e32 v126, v98, v98
	v_mul_f32_e32 v128, v99, v99
	v_mul_f32_e32 v124, v97, v97
	v_mul_f32_e32 v122, v95, v95
	v_pk_add_f32 v[126:127], v[126:127], v[128:129]
	v_pk_add_f32 v[122:123], v[124:125], v[122:123]
	s_nop 0
	v_pk_add_f32 v[122:123], v[126:127], v[122:123]
	s_nop 0
	v_add_f32_e32 v6, v122, v123
	v_mbcnt_lo_u32_b32 v122, -1, 0
	v_mbcnt_hi_u32_b32 v122, -1, v122
	v_ashrrev_i32_e32 v123, 31, v122
	v_lshl_add_u64 v[122:123], v[122:123], 4, s[12:13]
	global_load_dwordx4 v[122:125], v[122:123], off
	v_mbcnt_lo_u32_b32 v126, -1, 0
	v_mbcnt_hi_u32_b32 v126, -1, v126
	s_waitcnt lgkmcnt(0)
; #define GAS __attribute__((address_space(1)))
; #define FLANE lane_id()
; __device__ __forceinline__ void p6_router(Frame& F) {
;     ...
;                 const float rstd = 1.f / sqrtf(wave_sum(s2) * (1.f / D) + LN_EPS);
;                 float am = 0.f;
; #pragma unroll
;                 for (int j = 0; j < 8; ++j) { const f32x4 g = *((const GAS f32x4*)F.ln1_g + FLANE + 64 * j), b = *((const GAS f32x4*)F.ln1_b + FLANE + 64 * j);
;                     v[j] = v[j] * rstd * g + b; am = fmaxf(am, fmaxf(fmaxf(fabsf(v[j][0]), fabsf(v[j][1])), fmaxf(fabsf(v[j][2]), fabsf(v[j][3])))); }
	s_nop 1
	v_add_f32_dpp v6, v6, v6 quad_perm:[1,0,3,2] row_mask:0xf bank_mask:0xf
	v_ashrrev_i32_e32 v127, 31, v126
	v_lshl_add_u64 v[126:127], v[126:127], 4, s[14:15]
	global_load_dwordx4 v[126:129], v[126:127], off
	s_waitcnt lgkmcnt(0)
	s_nop 1
	v_add_f32_dpp v6, v6, v6 quad_perm:[2,3,0,1] row_mask:0xf bank_mask:0xf
	s_waitcnt lgkmcnt(0)
	s_nop 1
	v_add_f32_dpp v6, v6, v6 row_half_mirror row_mask:0xf bank_mask:0xf
	s_waitcnt lgkmcnt(0)
	s_nop 1
	v_add_f32_dpp v6, v6, v6 row_mirror row_mask:0xf bank_mask:0xf
	s_waitcnt lgkmcnt(0)
	v_mov_b32_e32 v32, v6
	s_nop 1
	v_permlane16_swap_b32_e32 v6, v32
	v_add_f32_e32 v6, v6, v32
	s_waitcnt lgkmcnt(0)
	v_mov_b32_e32 v32, v6
	s_nop 1
	v_permlane32_swap_b32_e32 v6, v32
	v_add_f32_e32 v6, v6, v32
	v_fmamk_f32 v6, v6, 0x3a000000, v166
	v_cmp_gt_f32_e32 vcc, s22, v6
	v_mul_f32_e32 v32, 0x4f800000, v6
	s_nop 0
	v_cndmask_b32_e32 v6, v6, v32, vcc
	v_sqrt_f32_e32 v32, v6
	s_nop 0
	v_add_u32_e32 v94, -1, v32
	v_fma_f32 v114, -v94, v32, v6
	v_cmp_ge_f32_e64 s[4:5], 0, v114
	v_add_u32_e32 v114, 1, v32
	s_nop 0
	v_cndmask_b32_e64 v94, v32, v94, s[4:5]
	v_fma_f32 v32, -v114, v32, v6
	v_cmp_lt_f32_e64 s[4:5], 0, v32
	s_nop 1
	v_cndmask_b32_e64 v32, v94, v114, s[4:5]
	v_mul_f32_e32 v94, 0x37800000, v32
	v_cndmask_b32_e32 v32, v32, v94, vcc
	v_cmp_class_f32_e32 vcc, v6, v167
	s_nop 1
	v_cndmask_b32_e32 v6, v32, v6, vcc
	v_div_scale_f32 v32, s[4:5], v6, v6, 1.0
	v_rcp_f32_e32 v94, v32
	s_add_i32 s4, s42, s0
	s_ashr_i32 s5, s4, 31
	v_fma_f32 v114, -v32, v94, 1.0
	v_fmac_f32_e32 v94, v114, v94
	v_div_scale_f32 v114, vcc, 1.0, v6, 1.0
	v_mul_f32_e32 v116, v114, v94
	v_fma_f32 v118, -v32, v116, v114
	v_fmac_f32_e32 v116, v118, v94
	v_fma_f32 v32, -v32, v116, v114
	v_div_fmas_f32 v32, v32, v94, v116
	v_div_fixup_f32 v32, v32, v6, 1.0
	v_pk_mul_f32 v[130:131], v[92:93], v[32:33] op_sel_hi:[1,0]
	v_pk_mul_f32 v[92:93], v[100:101], v[32:33] op_sel_hi:[1,0]
	v_mov_b32_e32 v118, v7
	v_pk_mul_f32 v[4:5], v[4:5], v[32:33] op_sel_hi:[1,0]
	v_pk_mul_f32 v[2:3], v[2:3], v[32:33] op_sel_hi:[1,0]
	v_pk_mul_f32 v[0:1], v[0:1], v[32:33] op_sel_hi:[1,0]
	v_pk_mul_f32 v[98:99], v[98:99], v[32:33] op_sel_hi:[1,0]
	s_waitcnt vmcnt(0)
	v_pk_fma_f32 v[100:101], v[122:123], v[130:131], v[126:127]
	v_mbcnt_lo_u32_b32 v122, -1, 0
	v_mbcnt_hi_u32_b32 v122, -1, v122
	v_pk_fma_f32 v[92:93], v[124:125], v[92:93], v[128:129]
	v_ashrrev_i32_e32 v123, 31, v122
	v_lshl_add_u64 v[122:123], v[122:123], 4, s[12:13]
	global_load_dwordx4 v[122:125], v[122:123], off offset:1024
	v_mbcnt_lo_u32_b32 v126, -1, 0
	v_mbcnt_hi_u32_b32 v126, -1, v126
	v_pk_mul_f32 v[130:131], v[102:103], v[32:33] op_sel_hi:[1,0]
	v_ashrrev_i32_e32 v127, 31, v126
	v_lshl_add_u64 v[126:127], v[126:127], 4, s[14:15]
	global_load_dwordx4 v[126:129], v[126:127], off offset:1024
	v_pk_mul_f32 v[102:103], v[104:105], v[32:33] op_sel_hi:[1,0]
	v_max_f32_e64 v6, |v92|, |v93|
	v_max3_f32 v6, |v100|, |v101|, v6
	s_waitcnt vmcnt(0)
	v_pk_fma_f32 v[104:105], v[122:123], v[130:131], v[126:127]
	v_mbcnt_lo_u32_b32 v122, -1, 0
	v_mbcnt_hi_u32_b32 v122, -1, v122
	v_pk_fma_f32 v[102:103], v[124:125], v[102:103], v[128:129]
	v_ashrrev_i32_e32 v123, 31, v122
	v_lshl_add_u64 v[122:123], v[122:123], 4, s[12:13]
	global_load_dwordx4 v[122:125], v[122:123], off offset:2048
	v_mbcnt_lo_u32_b32 v126, -1, 0
	v_mbcnt_hi_u32_b32 v126, -1, v126
	v_pk_mul_f32 v[130:131], v[106:107], v[32:33] op_sel_hi:[1,0]
	v_ashrrev_i32_e32 v127, 31, v126
	v_lshl_add_u64 v[126:127], v[126:127], 4, s[14:15]
	global_load_dwordx4 v[126:129], v[126:127], off offset:2048
	v_pk_mul_f32 v[106:107], v[108:109], v[32:33] op_sel_hi:[1,0]
	v_max_f32_e64 v94, |v102|, |v103|
	v_max3_f32 v94, |v104|, |v105|, v94
	v_max3_f32 v6, v6, 0, v94
	s_waitcnt vmcnt(0)
	v_pk_fma_f32 v[108:109], v[122:123], v[130:131], v[126:127]
	v_mbcnt_lo_u32_b32 v122, -1, 0
	v_mbcnt_hi_u32_b32 v122, -1, v122
	v_pk_fma_f32 v[106:107], v[124:125], v[106:107], v[128:129]
	v_ashrrev_i32_e32 v123, 31, v122
	v_lshl_add_u64 v[122:123], v[122:123], 4, s[12:13]
	global_load_dwordx4 v[122:125], v[122:123], off offset:3072
	v_mbcnt_lo_u32_b32 v126, -1, 0
	v_mbcnt_hi_u32_b32 v126, -1, v126
	v_pk_mul_f32 v[130:131], v[110:111], v[32:33] op_sel_hi:[1,0]
	v_ashrrev_i32_e32 v127, 31, v126
	v_lshl_add_u64 v[126:127], v[126:127], 4, s[14:15]
	global_load_dwordx4 v[126:129], v[126:127], off offset:3072
	v_pk_mul_f32 v[110:111], v[112:113], v[32:33] op_sel_hi:[1,0]
	v_max_f32_e64 v94, |v106|, |v107|
	v_max3_f32 v94, |v108|, |v109|, v94
	s_waitcnt vmcnt(0)
	v_pk_fma_f32 v[112:113], v[122:123], v[130:131], v[126:127]
	v_mbcnt_lo_u32_b32 v122, -1, 0
	v_mbcnt_hi_u32_b32 v122, -1, v122
	v_pk_fma_f32 v[110:111], v[124:125], v[110:111], v[128:129]
	v_ashrrev_i32_e32 v123, 31, v122
	v_lshl_add_u64 v[122:123], v[122:123], 4, s[12:13]
	v_add_co_u32_e32 v122, vcc, s23, v122
	v_max_f32_e64 v114, |v110|, |v111|
	s_nop 0
	v_addc_co_u32_e32 v123, vcc, 0, v123, vcc
	global_load_dwordx4 v[122:125], v[122:123], off
	v_mbcnt_lo_u32_b32 v126, -1, 0
	v_mbcnt_hi_u32_b32 v126, -1, v126
	v_max3_f32 v114, |v112|, |v113|, v114
	v_ashrrev_i32_e32 v127, 31, v126
	v_lshl_add_u64 v[126:127], v[126:127], 4, s[14:15]
	v_add_co_u32_e32 v126, vcc, s23, v126
	v_max3_f32 v94, v6, v94, v114
	s_nop 0
	v_addc_co_u32_e32 v127, vcc, 0, v127, vcc
	global_load_dwordx4 v[126:129], v[126:127], off
	v_mov_b32_e32 v114, v117
	v_pk_mul_f32 v[114:115], v[114:115], v[32:33] op_sel_hi:[1,0]
	v_pk_mul_f32 v[6:7], v[118:119], v[32:33] op_sel_hi:[1,0]
	s_waitcnt vmcnt(0)
; #define GAS __attribute__((address_space(1)))
; #define FLANE lane_id()
; __device__ __forceinline__ void p6_router(Frame& F) {
;     ...
;                 for (int j = 0; j < 8; ++j) { const f32x4 g = *((const GAS f32x4*)F.ln1_g + FLANE + 64 * j), b = *((const GAS f32x4*)F.ln1_b + FLANE + 64 * j);
;                     v[j] = v[j] * rstd * g + b; am = fmaxf(am, fmaxf(fmaxf(fabsf(v[j][0]), fabsf(v[j][1])), fmaxf(fabsf(v[j][2]), fabsf(v[j][3])))); }
; #pragma unroll
;                 for (int o = 1; o < 64; o <<= 1) am = fmaxf(am, __shfl_xor(am, o));
;                 const float sc = am > 0.f ? am * (1.f / 127.f) : 1.f, inv = 1.f / sc;
; #pragma unroll
;                 for (int j = 0; j < 8; ++j) { const int q0 = (int)__builtin_rintf(v[j][0] * inv), q1 = (int)__builtin_rintf(v[j][1] * inv), q2 = (int)__builtin_rintf(v[j][2] * inv), q3 = (int)__builtin_rintf(v[j][3] * inv);
;                     h1q[(size_t)m * (D / 4) + FLANE + 64 * j] = (unsigned)(q0 & 0xff) | ((unsigned)(q1 & 0xff) << 8) | ((unsigned)(q2 & 0xff) << 16) | ((unsigned)(q3 & 0xff) << 24); }
	v_pk_fma_f32 v[114:115], v[124:125], v[114:115], v[128:129]
	v_pk_fma_f32 v[116:117], v[122:123], v[6:7], v[126:127]
	v_max_f32_e64 v6, |v114|, |v115|
	v_max3_f32 v130, |v116|, |v117|, v6
	v_mbcnt_lo_u32_b32 v6, -1, 0
	v_mbcnt_hi_u32_b32 v6, -1, v6
	s_nop 0
	v_ashrrev_i32_e32 v7, 31, v6
	v_lshl_add_u64 v[6:7], v[6:7], 4, s[12:13]
	v_add_co_u32_e32 v6, vcc, s23, v6
	s_nop 1
	v_addc_co_u32_e32 v7, vcc, 0, v7, vcc
	global_load_dwordx4 v[122:125], v[6:7], off offset:1024
	v_mbcnt_lo_u32_b32 v6, -1, 0
	v_mbcnt_hi_u32_b32 v6, -1, v6
	s_nop 0
	v_ashrrev_i32_e32 v7, 31, v6
	v_lshl_add_u64 v[6:7], v[6:7], 4, s[14:15]
	v_add_co_u32_e32 v6, vcc, s23, v6
	s_nop 1
	v_addc_co_u32_e32 v7, vcc, 0, v7, vcc
	global_load_dwordx4 v[126:129], v[6:7], off offset:1024
	v_pk_mul_f32 v[6:7], v[120:121], v[32:33] op_sel_hi:[1,0]
	s_waitcnt vmcnt(0)
	v_pk_fma_f32 v[120:121], v[122:123], v[4:5], v[126:127]
	v_pk_fma_f32 v[118:119], v[124:125], v[6:7], v[128:129]
	s_nop 0
	v_max_f32_e64 v4, |v118|, |v119|
	v_max3_f32 v4, |v120|, |v121|, v4
	v_max3_f32 v128, v94, v130, v4
	v_mbcnt_lo_u32_b32 v4, -1, 0
	v_mbcnt_hi_u32_b32 v4, -1, v4
	v_mov_b32_e32 v94, v97
	v_ashrrev_i32_e32 v5, 31, v4
	v_lshl_add_u64 v[4:5], v[4:5], 4, s[12:13]
	v_add_co_u32_e32 v4, vcc, s23, v4
	v_pk_mul_f32 v[94:95], v[94:95], v[32:33] op_sel_hi:[1,0]
	s_nop 0
	v_addc_co_u32_e32 v5, vcc, 0, v5, vcc
	global_load_dwordx4 v[4:7], v[4:5], off offset:2048
	v_mbcnt_lo_u32_b32 v122, -1, 0
	v_mbcnt_hi_u32_b32 v122, -1, v122
	s_nop 0
	v_ashrrev_i32_e32 v123, 31, v122
	v_lshl_add_u64 v[122:123], v[122:123], 4, s[14:15]
	v_add_co_u32_e32 v122, vcc, s23, v122
	s_nop 1
	v_addc_co_u32_e32 v123, vcc, 0, v123, vcc
	global_load_dwordx4 v[124:127], v[122:123], off offset:2048
	s_waitcnt vmcnt(0)
	v_pk_fma_f32 v[122:123], v[2:3], v[6:7], v[126:127]
	v_pk_fma_f32 v[124:125], v[0:1], v[4:5], v[124:125]
	v_max_f32_e64 v0, |v122|, |v123|
	v_max3_f32 v126, |v124|, |v125|, v0
	v_mbcnt_lo_u32_b32 v0, -1, 0
	v_mbcnt_hi_u32_b32 v0, -1, v0
	s_nop 0
	v_ashrrev_i32_e32 v1, 31, v0
	v_lshl_add_u64 v[0:1], v[0:1], 4, s[12:13]
	v_add_co_u32_e32 v0, vcc, s23, v0
	s_nop 1
	v_addc_co_u32_e32 v1, vcc, 0, v1, vcc
	global_load_dwordx4 v[0:3], v[0:1], off offset:3072
	v_mbcnt_lo_u32_b32 v4, -1, 0
	v_mbcnt_hi_u32_b32 v4, -1, v4
	s_nop 0
	v_ashrrev_i32_e32 v5, 31, v4
	v_lshl_add_u64 v[4:5], v[4:5], 4, s[14:15]
	v_add_co_u32_e32 v4, vcc, s23, v4
	s_nop 1
	v_addc_co_u32_e32 v5, vcc, 0, v5, vcc
	global_load_dwordx4 v[4:7], v[4:5], off offset:3072
	s_waitcnt vmcnt(0)
	v_pk_fma_f32 v[2:3], v[94:95], v[2:3], v[6:7]
	v_pk_fma_f32 v[4:5], v[98:99], v[0:1], v[4:5]
	v_max_f32_e64 v0, |v2|, |v3|
	v_max3_f32 v0, |v4|, |v5|, v0
	v_max3_f32 v0, v128, v126, v0
	s_waitcnt lgkmcnt(0)
	s_nop 1
	v_max_f32_dpp v0, v0, v0 quad_perm:[1,0,3,2] row_mask:0xf bank_mask:0xf
	s_waitcnt lgkmcnt(0)
	s_nop 1
	v_max_f32_dpp v0, v0, v0 quad_perm:[2,3,0,1] row_mask:0xf bank_mask:0xf
	s_waitcnt lgkmcnt(0)
	s_nop 1
	v_max_f32_dpp v0, v0, v0 row_half_mirror row_mask:0xf bank_mask:0xf
	s_waitcnt lgkmcnt(0)
	s_nop 1
	v_max_f32_dpp v0, v0, v0 row_mirror row_mask:0xf bank_mask:0xf
	s_waitcnt lgkmcnt(0)
	v_mov_b32_e32 v1, v0
	s_nop 1
	v_permlane16_swap_b32_e32 v0, v1
	v_max_f32_e32 v0, v0, v1
	s_waitcnt lgkmcnt(0)
	v_mov_b32_e32 v1, v0
	s_nop 1
	v_permlane32_swap_b32_e32 v0, v1
	v_max_f32_e32 v0, v0, v1
	v_cmp_lt_f32_e32 vcc, 0, v0
	v_mul_f32_e32 v0, 0x3c010204, v0
	s_nop 0
	v_cndmask_b32_e32 v0, 1.0, v0, vcc
	v_div_scale_f32 v1, s[6:7], v0, v0, 1.0
	v_rcp_f32_e32 v6, v1
	s_lshl_b64 s[6:7], s[4:5], 11
	s_add_u32 s6, s3, s6
	s_addc_u32 s7, s24, s7
	v_fma_f32 v7, -v1, v6, 1.0
	v_fmac_f32_e32 v6, v7, v6
	v_div_scale_f32 v7, vcc, 1.0, v0, 1.0
	v_mul_f32_e32 v94, v7, v6
	v_fma_f32 v95, -v1, v94, v7
	v_fmac_f32_e32 v94, v95, v6
	v_fma_f32 v1, -v1, v94, v7
	v_div_fmas_f32 v1, v1, v6, v94
	v_div_fixup_f32 v1, v1, v0, 1.0
	v_mul_f32_e32 v7, v101, v1
	v_mul_f32_e32 v6, v100, v1
	v_rndne_f32_e32 v7, v7
	v_mul_f32_e32 v92, v92, v1
	v_mul_f32_e32 v93, v93, v1
	v_rndne_f32_e32 v6, v6
	v_cvt_i32_f32_e32 v7, v7
	v_rndne_f32_e32 v92, v92
	v_rndne_f32_e32 v93, v93
	v_cvt_i32_f32_e32 v6, v6
	v_cvt_i32_f32_sdwa v92, v92 dst_sel:WORD_1 dst_unused:UNUSED_PAD src0_sel:DWORD
	v_cvt_i32_f32_e32 v93, v93
	v_lshlrev_b32_e32 v7, 8, v7
	v_and_b32_e32 v7, 0xff00, v7
	v_and_b32_e32 v92, 0xff0000, v92
	v_perm_b32 v6, v93, v6, s1
	v_or3_b32 v92, v6, v7, v92
	v_mbcnt_lo_u32_b32 v6, -1, 0
	v_mbcnt_hi_u32_b32 v6, -1, v6
	v_mul_f32_e32 v93, v103, v1
	v_ashrrev_i32_e32 v7, 31, v6
	v_lshl_add_u64 v[6:7], v[6:7], 2, s[6:7]
	global_store_dword v[6:7], v92, off
	v_mul_f32_e32 v7, v105, v1
	v_mul_f32_e32 v6, v104, v1
	v_rndne_f32_e32 v7, v7
	v_mul_f32_e32 v92, v102, v1
	v_rndne_f32_e32 v6, v6
	v_cvt_i32_f32_e32 v7, v7
	v_rndne_f32_e32 v92, v92
	v_rndne_f32_e32 v93, v93
	v_cvt_i32_f32_e32 v6, v6
	v_cvt_i32_f32_sdwa v92, v92 dst_sel:WORD_1 dst_unused:UNUSED_PAD src0_sel:DWORD
	v_cvt_i32_f32_e32 v93, v93
	v_lshlrev_b32_e32 v7, 8, v7
	v_and_b32_e32 v7, 0xff00, v7
	v_and_b32_e32 v92, 0xff0000, v92
	v_perm_b32 v6, v93, v6, s1
	v_or3_b32 v92, v6, v7, v92
	v_mbcnt_lo_u32_b32 v6, -1, 0
	v_mbcnt_hi_u32_b32 v6, -1, v6
	v_mul_f32_e32 v93, v107, v1
	v_ashrrev_i32_e32 v7, 31, v6
	v_lshl_add_u64 v[6:7], v[6:7], 2, s[6:7]
	global_store_dword v[6:7], v92, off offset:256
	v_mul_f32_e32 v7, v109, v1
	v_mul_f32_e32 v6, v108, v1
	v_rndne_f32_e32 v7, v7
	v_mul_f32_e32 v92, v106, v1
	v_rndne_f32_e32 v6, v6
	v_cvt_i32_f32_e32 v7, v7
	v_rndne_f32_e32 v92, v92
	v_rndne_f32_e32 v93, v93
	v_cvt_i32_f32_e32 v6, v6
	v_cvt_i32_f32_sdwa v92, v92 dst_sel:WORD_1 dst_unused:UNUSED_PAD src0_sel:DWORD
	v_cvt_i32_f32_e32 v93, v93
	v_lshlrev_b32_e32 v7, 8, v7
; #define FLANE lane_id()
; __device__ __forceinline__ void p6_router(Frame& F) {
;     ...
;                 for (int j = 0; j < 8; ++j) { const int q0 = (int)__builtin_rintf(v[j][0] * inv), q1 = (int)__builtin_rintf(v[j][1] * inv), q2 = (int)__builtin_rintf(v[j][2] * inv), q3 = (int)__builtin_rintf(v[j][3] * inv);
;                     h1q[(size_t)m * (D / 4) + FLANE + 64 * j] = (unsigned)(q0 & 0xff) | ((unsigned)(q1 & 0xff) << 8) | ((unsigned)(q2 & 0xff) << 16) | ((unsigned)(q3 & 0xff) << 24); }
;                 if (FLANE == 0) { st1[2 * m] = mean; st1[2 * m + 1] = rstd; stl[2 * row] = mean; stl[2 * row + 1] = rstd; sxg[m] = sc; sxl[row] = sc; }
	v_and_b32_e32 v7, 0xff00, v7
	v_and_b32_e32 v92, 0xff0000, v92
	v_perm_b32 v6, v93, v6, s1
	v_or3_b32 v92, v6, v7, v92
	v_mbcnt_lo_u32_b32 v6, -1, 0
	v_mbcnt_hi_u32_b32 v6, -1, v6
	v_mul_f32_e32 v93, v111, v1
	v_ashrrev_i32_e32 v7, 31, v6
	v_lshl_add_u64 v[6:7], v[6:7], 2, s[6:7]
	global_store_dword v[6:7], v92, off offset:512
	v_mul_f32_e32 v7, v113, v1
	v_mul_f32_e32 v6, v112, v1
	v_rndne_f32_e32 v7, v7
	v_mul_f32_e32 v92, v110, v1
	v_rndne_f32_e32 v6, v6
	v_cvt_i32_f32_e32 v7, v7
	v_rndne_f32_e32 v92, v92
	v_rndne_f32_e32 v93, v93
	v_cvt_i32_f32_e32 v6, v6
	v_cvt_i32_f32_sdwa v92, v92 dst_sel:WORD_1 dst_unused:UNUSED_PAD src0_sel:DWORD
	v_cvt_i32_f32_e32 v93, v93
	v_lshlrev_b32_e32 v7, 8, v7
	v_and_b32_e32 v7, 0xff00, v7
	v_and_b32_e32 v92, 0xff0000, v92
	v_perm_b32 v6, v93, v6, s1
	v_or3_b32 v92, v6, v7, v92
	v_mbcnt_lo_u32_b32 v6, -1, 0
	v_mbcnt_hi_u32_b32 v6, -1, v6
	v_mul_f32_e32 v93, v115, v1
	v_ashrrev_i32_e32 v7, 31, v6
	v_lshl_add_u64 v[6:7], v[6:7], 2, s[6:7]
	global_store_dword v[6:7], v92, off offset:768
	v_mul_f32_e32 v7, v117, v1
	v_mul_f32_e32 v6, v116, v1
	v_rndne_f32_e32 v7, v7
	v_mul_f32_e32 v92, v114, v1
	v_rndne_f32_e32 v6, v6
	v_cvt_i32_f32_e32 v7, v7
	v_rndne_f32_e32 v92, v92
	v_rndne_f32_e32 v93, v93
	v_cvt_i32_f32_e32 v6, v6
	v_cvt_i32_f32_sdwa v92, v92 dst_sel:WORD_1 dst_unused:UNUSED_PAD src0_sel:DWORD
	v_cvt_i32_f32_e32 v93, v93
	v_lshlrev_b32_e32 v7, 8, v7
	v_and_b32_e32 v7, 0xff00, v7
	v_and_b32_e32 v92, 0xff0000, v92
	v_perm_b32 v6, v93, v6, s1
	v_or3_b32 v92, v6, v7, v92
	v_mbcnt_lo_u32_b32 v6, -1, 0
	v_mbcnt_hi_u32_b32 v6, -1, v6
	v_mul_f32_e32 v93, v119, v1
	v_ashrrev_i32_e32 v7, 31, v6
	v_lshl_add_u64 v[6:7], v[6:7], 2, s[6:7]
	global_store_dword v[6:7], v92, off offset:1024
	v_mul_f32_e32 v7, v121, v1
	v_mul_f32_e32 v6, v120, v1
	v_rndne_f32_e32 v7, v7
	v_mul_f32_e32 v92, v118, v1
	v_rndne_f32_e32 v6, v6
	v_cvt_i32_f32_e32 v7, v7
	v_rndne_f32_e32 v92, v92
	v_rndne_f32_e32 v93, v93
	v_cvt_i32_f32_e32 v6, v6
	v_cvt_i32_f32_sdwa v92, v92 dst_sel:WORD_1 dst_unused:UNUSED_PAD src0_sel:DWORD
	v_cvt_i32_f32_e32 v93, v93
	v_lshlrev_b32_e32 v7, 8, v7
	v_and_b32_e32 v7, 0xff00, v7
	v_and_b32_e32 v92, 0xff0000, v92
	v_perm_b32 v6, v93, v6, s1
	v_or3_b32 v92, v6, v7, v92
	v_mbcnt_lo_u32_b32 v6, -1, 0
	v_mbcnt_hi_u32_b32 v6, -1, v6
	v_mul_f32_e32 v93, v123, v1
	v_ashrrev_i32_e32 v7, 31, v6
	v_lshl_add_u64 v[6:7], v[6:7], 2, s[6:7]
	global_store_dword v[6:7], v92, off offset:1280
	v_mul_f32_e32 v7, v125, v1
	v_mul_f32_e32 v6, v124, v1
	v_rndne_f32_e32 v7, v7
	v_mul_f32_e32 v92, v122, v1
	v_rndne_f32_e32 v6, v6
	v_cvt_i32_f32_e32 v7, v7
	v_rndne_f32_e32 v92, v92
	v_rndne_f32_e32 v93, v93
	v_mul_f32_e32 v5, v5, v1
	v_cvt_i32_f32_e32 v6, v6
	v_cvt_i32_f32_sdwa v92, v92 dst_sel:WORD_1 dst_unused:UNUSED_PAD src0_sel:DWORD
	v_cvt_i32_f32_e32 v93, v93
	v_mul_f32_e32 v4, v4, v1
	v_rndne_f32_e32 v5, v5
	v_mul_f32_e32 v2, v2, v1
	v_mul_f32_e32 v1, v3, v1
	v_rndne_f32_e32 v4, v4
	v_cvt_i32_f32_e32 v5, v5
	v_rndne_f32_e32 v2, v2
	v_rndne_f32_e32 v1, v1
	v_cvt_i32_f32_e32 v4, v4
	v_cvt_i32_f32_sdwa v2, v2 dst_sel:WORD_1 dst_unused:UNUSED_PAD src0_sel:DWORD
	v_cvt_i32_f32_e32 v1, v1
	v_lshlrev_b32_e32 v7, 8, v7
	v_and_b32_e32 v7, 0xff00, v7
	v_and_b32_e32 v92, 0xff0000, v92
	v_perm_b32 v6, v93, v6, s1
	v_or3_b32 v92, v6, v7, v92
	v_mbcnt_lo_u32_b32 v6, -1, 0
	v_mbcnt_hi_u32_b32 v6, -1, v6
	v_lshlrev_b32_e32 v3, 8, v5
	v_ashrrev_i32_e32 v7, 31, v6
	v_lshl_add_u64 v[6:7], v[6:7], 2, s[6:7]
	v_and_b32_e32 v3, 0xff00, v3
	v_and_b32_e32 v2, 0xff0000, v2
	v_perm_b32 v1, v1, v4, s1
	global_store_dword v[6:7], v92, off offset:1536
	v_or3_b32 v1, v1, v3, v2
	v_mbcnt_lo_u32_b32 v2, -1, 0
	v_mbcnt_hi_u32_b32 v2, -1, v2
	s_nop 0
	v_ashrrev_i32_e32 v3, 31, v2
	v_lshl_add_u64 v[2:3], v[2:3], 2, s[6:7]
	global_store_dword v[2:3], v1, off offset:1792
	v_mbcnt_lo_u32_b32 v1, -1, 0
	v_mbcnt_hi_u32_b32 v1, -1, v1
	s_nop 0
	v_cmp_eq_u32_e32 vcc, 0, v1
	s_and_saveexec_b64 s[6:7], vcc
	s_cbranch_execz .LBB0_1487
	s_lshl_b32 s8, s4, 1
	s_ashr_i32 s9, s8, 31
	s_lshl_b64 s[8:9], s[8:9], 2
	s_add_u32 s8, s27, s8
	s_addc_u32 s9, s64, s9
	v_readlane_b32 s0, v255, 43
	s_lshl_b64 s[4:5], s[4:5], 2
	v_mul_f32_e32 v2, 0x3a000000, v96
	v_mov_b32_e32 v3, v32
	v_mov_b32_e32 v1, s0
	s_add_u32 s4, s25, s4
	v_readlane_b32 s0, v255, 29
	ds_write_b64 v1, v[2:3]
	s_addc_u32 s5, s26, s5
	v_mov_b32_e32 v1, s0
	global_store_dwordx2 v33, v[2:3], s[8:9]
	global_store_dword v33, v0, s[4:5]
	ds_write_b32 v1, v0
; __device__ __forceinline__ void p6_router(Frame& F) {
;     ...
;                 for (int j = 0; j < 8; ++j) { const v2u w = raw[rr][j]; v[j] = (f32x4){bf_lo(w.x), bf_hi(w.x), bf_lo(w.y), bf_hi(w.y)}; s += (v[j][0] + v[j][1]) + (v[j][2] + v[j][3]); }
;                 const float mean = wave_sum(s) * (1.f / D); float s2 = 0.f;
; #pragma unroll
;                 for (int j = 0; j < 8; ++j) { v[j] = v[j] - mean; s2 += (v[j][0] * v[j][0] + v[j][1] * v[j][1]) + (v[j][2] * v[j][2] + v[j][3] * v[j][3]); }
;                 const float rstd = 1.f / sqrtf(wave_sum(s2) * (1.f / D) + LN_EPS);
.LBB0_1487:
	s_or_b64 exec, exec, s[6:7]
	v_lshlrev_b32_e32 v93, 16, v90
	v_lshlrev_b32_e32 v92, 16, v88
	v_and_b32_e32 v105, 0xffff0000, v90
	v_and_b32_e32 v104, 0xffff0000, v88
	v_lshlrev_b32_e32 v107, 16, v91
	v_lshlrev_b32_e32 v106, 16, v89
	v_and_b32_e32 v109, 0xffff0000, v91
	v_and_b32_e32 v108, 0xffff0000, v89
	v_pk_add_f32 v[0:1], v[92:93], v[104:105]
	v_pk_add_f32 v[2:3], v[106:107], v[108:109]
	v_lshlrev_b32_e32 v91, 16, v87
	v_pk_add_f32 v[0:1], v[0:1], v[2:3]
	v_lshlrev_b32_e32 v90, 16, v86
	v_add_f32_e32 v0, 0, v0
	v_and_b32_e32 v111, 0xffff0000, v87
	v_and_b32_e32 v110, 0xffff0000, v86
	v_add_f32_e32 v6, v0, v1
	v_pk_add_f32 v[0:1], v[90:91], v[110:111]
	v_lshlrev_b32_e32 v94, 16, v84
	v_and_b32_e32 v95, 0xffff0000, v84
	v_lshlrev_b32_e32 v96, 16, v85
	v_and_b32_e32 v97, 0xffff0000, v85
	v_and_b32_e32 v103, 0xffff0000, v82
	v_pk_add_f32 v[0:1], v[0:1], v[0:1] op_sel:[0,1] op_sel_hi:[1,0]
	v_add_f32_e32 v100, v94, v95
	v_add_f32_e32 v98, v96, v97
	v_lshlrev_b32_e32 v7, 16, v82
	v_lshlrev_b32_e32 v101, 16, v83
	v_and_b32_e32 v99, 0xffff0000, v83
	v_mov_b32_e32 v1, v103
	v_pk_add_f32 v[0:1], v[6:7], v[0:1]
	v_pk_add_f32 v[2:3], v[100:101], v[98:99]
	v_lshlrev_b32_e32 v5, 16, v81
	v_lshlrev_b32_e32 v4, 16, v80
	v_and_b32_e32 v113, 0xffff0000, v81
	v_and_b32_e32 v112, 0xffff0000, v80
	v_pk_add_f32 v[84:85], v[0:1], v[2:3]
	v_pk_add_f32 v[86:87], v[4:5], v[112:113]
	v_lshlrev_b32_e32 v0, 16, v78
	v_and_b32_e32 v1, 0xffff0000, v78
	v_lshlrev_b32_e32 v2, 16, v79
	v_and_b32_e32 v3, 0xffff0000, v79
	v_lshlrev_b32_e32 v82, 16, v76
	v_and_b32_e32 v83, 0xffff0000, v76
	v_lshlrev_b32_e32 v81, 16, v77
	v_and_b32_e32 v79, 0xffff0000, v77
	v_pk_add_f32 v[76:77], v[84:85], v[84:85] op_sel:[0,1] op_sel_hi:[1,0]
	v_pk_add_f32 v[84:85], v[86:87], v[86:87] op_sel:[0,1] op_sel_hi:[1,0]
	v_add_f32_e32 v80, v0, v1
	v_add_f32_e32 v78, v2, v3
	v_mov_b32_e32 v77, v82
	v_mov_b32_e32 v85, v83
	v_pk_add_f32 v[76:77], v[76:77], v[84:85]
	v_pk_add_f32 v[84:85], v[80:81], v[78:79]
	s_nop 0
	v_pk_add_f32 v[76:77], v[76:77], v[84:85]
	s_nop 0
	v_add_f32_e32 v6, v76, v77
	s_waitcnt lgkmcnt(0)
	s_nop 1
	v_add_f32_dpp v6, v6, v6 quad_perm:[1,0,3,2] row_mask:0xf bank_mask:0xf
	s_waitcnt lgkmcnt(0)
	s_nop 1
	v_add_f32_dpp v6, v6, v6 quad_perm:[2,3,0,1] row_mask:0xf bank_mask:0xf
	s_waitcnt lgkmcnt(0)
	s_nop 1
	v_add_f32_dpp v6, v6, v6 row_half_mirror row_mask:0xf bank_mask:0xf
	s_waitcnt lgkmcnt(0)
	s_nop 1
	v_add_f32_dpp v6, v6, v6 row_mirror row_mask:0xf bank_mask:0xf
	s_waitcnt lgkmcnt(0)
	v_mov_b32_e32 v32, v6
	s_nop 1
	v_permlane16_swap_b32_e32 v6, v32
	v_add_f32_e32 v6, v6, v32
	s_waitcnt lgkmcnt(0)
	v_mov_b32_e32 v32, v6
	s_nop 1
	v_permlane32_swap_b32_e32 v6, v32
	v_add_f32_e32 v80, v6, v32
	v_fmac_f32_e32 v108, 0xba000000, v80
	v_fmac_f32_e32 v104, 0xba000000, v80
	v_fmac_f32_e32 v109, 0xba000000, v80
	v_fmac_f32_e32 v105, 0xba000000, v80
	v_fmac_f32_e32 v106, 0xba000000, v80
	v_fmac_f32_e32 v92, 0xba000000, v80
	v_fmac_f32_e32 v107, 0xba000000, v80
	v_fmac_f32_e32 v93, 0xba000000, v80
	v_mov_b32_e32 v87, v105
	v_mov_b32_e32 v77, v104
	v_pk_mul_f32 v[84:85], v[104:105], v[104:105]
	v_pk_mul_f32 v[104:105], v[108:109], v[108:109]
	v_mov_b32_e32 v86, v93
	v_mov_b32_e32 v76, v92
	v_pk_fma_f32 v[92:93], v[92:93], v[92:93], v[84:85]
	v_pk_fma_f32 v[104:105], v[106:107], v[106:107], v[104:105]
	v_fmac_f32_e32 v110, 0xba000000, v80
	v_pk_add_f32 v[92:93], v[92:93], v[104:105]
	v_fmac_f32_e32 v111, 0xba000000, v80
	v_fmac_f32_e32 v91, 0xba000000, v80
	v_pk_add_f32 v[104:105], v[92:93], v[92:93] op_sel_hi:[0,1]
	v_fmac_f32_e32 v90, 0xba000000, v80
	v_mov_b32_e32 v92, v91
	v_mov_b32_e32 v93, v111
	v_mov_b32_e32 v91, v110
	v_mov_b32_e32 v88, v107
	v_mov_b32_e32 v89, v109
	v_mov_b32_e32 v84, v106
	v_mov_b32_e32 v85, v108
	v_pk_mul_f32 v[106:107], v[92:93], v[92:93]
	v_pk_mul_f32 v[108:109], v[90:91], v[90:91]
	v_fmac_f32_e32 v94, 0xba000000, v80
	v_pk_mov_b32 v[110:111], v[108:109], v[106:107] op_sel:[1,0]
	v_mov_b32_e32 v109, v107
	v_fmac_f32_e32 v95, 0xba000000, v80
	v_fmac_f32_e32 v96, 0xba000000, v80
	v_mul_f32_e32 v6, v94, v94
	v_pk_add_f32 v[106:107], v[110:111], v[108:109]
	v_fmac_f32_e32 v97, 0xba000000, v80
	v_pk_fma_f32 v[108:109], v[94:95], v[94:95], v[6:7] op_sel_hi:[1,1,0]
	v_mul_f32_e32 v6, v96, v96
	v_pk_add_f32 v[106:107], v[106:107], v[106:107] op_sel_hi:[0,1]
	v_pk_fma_f32 v[110:111], v[96:97], v[96:97], v[6:7] op_sel_hi:[1,1,0]
	v_fmac_f32_e32 v99, 0xba000000, v80
	v_fmac_f32_e32 v101, 0xba000000, v80
	v_fmac_f32_e32 v103, 0xba000000, v80
	v_fmac_f32_e32 v7, 0xba000000, v80
	v_mul_f32_e32 v108, v7, v7
	v_mul_f32_e32 v110, v103, v103
	v_mul_f32_e32 v106, v101, v101
	v_mul_f32_e32 v104, v99, v99
	v_pk_add_f32 v[108:109], v[108:109], v[110:111]
	v_pk_add_f32 v[104:105], v[106:107], v[104:105]
	v_fmac_f32_e32 v112, 0xba000000, v80
	v_pk_add_f32 v[104:105], v[108:109], v[104:105]
	v_fmac_f32_e32 v113, 0xba000000, v80
	v_fmac_f32_e32 v5, 0xba000000, v80
	v_pk_add_f32 v[106:107], v[104:105], v[104:105] op_sel_hi:[0,1]
	v_fmac_f32_e32 v4, 0xba000000, v80
	v_mov_b32_e32 v104, v5
	v_mov_b32_e32 v105, v113
	v_mov_b32_e32 v5, v112
	v_pk_mul_f32 v[108:109], v[104:105], v[104:105]
	v_pk_mul_f32 v[110:111], v[4:5], v[4:5]
	v_fmac_f32_e32 v0, 0xba000000, v80
	v_pk_mov_b32 v[112:113], v[110:111], v[108:109] op_sel:[1,0]
	v_mov_b32_e32 v111, v109
	v_fmac_f32_e32 v1, 0xba000000, v80
	v_fmac_f32_e32 v2, 0xba000000, v80
	v_mul_f32_e32 v6, v0, v0
	v_pk_add_f32 v[108:109], v[112:113], v[110:111]
	v_fmac_f32_e32 v3, 0xba000000, v80
	v_pk_fma_f32 v[110:111], v[0:1], v[0:1], v[6:7] op_sel_hi:[1,1,0]
	v_mul_f32_e32 v6, v2, v2
	v_pk_add_f32 v[108:109], v[108:109], v[108:109] op_sel_hi:[0,1]
	v_pk_fma_f32 v[112:113], v[2:3], v[2:3], v[6:7] op_sel_hi:[1,1,0]
	v_fmac_f32_e32 v79, 0xba000000, v80
	v_fmac_f32_e32 v81, 0xba000000, v80
	v_fmac_f32_e32 v83, 0xba000000, v80
	v_fmac_f32_e32 v82, 0xba000000, v80
	v_mul_f32_e32 v110, v82, v82
	v_mul_f32_e32 v112, v83, v83
	v_mul_f32_e32 v108, v81, v81
	v_mul_f32_e32 v106, v79, v79
	v_pk_add_f32 v[110:111], v[110:111], v[112:113]
	v_pk_add_f32 v[106:107], v[108:109], v[106:107]
	s_nop 0
	v_pk_add_f32 v[106:107], v[110:111], v[106:107]
	s_nop 0
	v_add_f32_e32 v6, v106, v107
	v_mbcnt_lo_u32_b32 v106, -1, 0
	v_mbcnt_hi_u32_b32 v106, -1, v106
	v_ashrrev_i32_e32 v107, 31, v106
	v_lshl_add_u64 v[106:107], v[106:107], 4, s[12:13]
	global_load_dwordx4 v[106:109], v[106:107], off
	v_mbcnt_lo_u32_b32 v110, -1, 0
	v_mbcnt_hi_u32_b32 v110, -1, v110
	s_waitcnt lgkmcnt(0)
; #define GAS __attribute__((address_space(1)))
; #define FLANE lane_id()
; __device__ __forceinline__ void p6_router(Frame& F) {
;     ...
;                 const float rstd = 1.f / sqrtf(wave_sum(s2) * (1.f / D) + LN_EPS);
;                 float am = 0.f;
; #pragma unroll
;                 for (int j = 0; j < 8; ++j) { const f32x4 g = *((const GAS f32x4*)F.ln1_g + FLANE + 64 * j), b = *((const GAS f32x4*)F.ln1_b + FLANE + 64 * j);
;                     v[j] = v[j] * rstd * g + b; am = fmaxf(am, fmaxf(fmaxf(fabsf(v[j][0]), fabsf(v[j][1])), fmaxf(fabsf(v[j][2]), fabsf(v[j][3])))); }
	s_nop 1
	v_add_f32_dpp v6, v6, v6 quad_perm:[1,0,3,2] row_mask:0xf bank_mask:0xf
	v_ashrrev_i32_e32 v111, 31, v110
	v_lshl_add_u64 v[110:111], v[110:111], 4, s[14:15]
	global_load_dwordx4 v[110:113], v[110:111], off
	s_waitcnt lgkmcnt(0)
	s_nop 1
	v_add_f32_dpp v6, v6, v6 quad_perm:[2,3,0,1] row_mask:0xf bank_mask:0xf
	s_waitcnt lgkmcnt(0)
	s_nop 1
	v_add_f32_dpp v6, v6, v6 row_half_mirror row_mask:0xf bank_mask:0xf
	s_waitcnt lgkmcnt(0)
	s_nop 1
	v_add_f32_dpp v6, v6, v6 row_mirror row_mask:0xf bank_mask:0xf
	s_waitcnt lgkmcnt(0)
	v_mov_b32_e32 v32, v6
	s_nop 1
	v_permlane16_swap_b32_e32 v6, v32
	v_add_f32_e32 v6, v6, v32
	s_waitcnt lgkmcnt(0)
	v_mov_b32_e32 v32, v6
	s_nop 1
	v_permlane32_swap_b32_e32 v6, v32
	v_add_f32_e32 v6, v6, v32
	v_fmamk_f32 v6, v6, 0x3a000000, v166
	v_cmp_gt_f32_e32 vcc, s22, v6
	v_mul_f32_e32 v32, 0x4f800000, v6
	s_nop 0
	v_cndmask_b32_e32 v6, v6, v32, vcc
	v_sqrt_f32_e32 v32, v6
	s_nop 0
	v_add_u32_e32 v78, -1, v32
	v_fma_f32 v98, -v78, v32, v6
	v_cmp_ge_f32_e64 s[4:5], 0, v98
	v_add_u32_e32 v98, 1, v32
	s_nop 0
	v_cndmask_b32_e64 v78, v32, v78, s[4:5]
	v_fma_f32 v32, -v98, v32, v6
	v_cmp_lt_f32_e64 s[4:5], 0, v32
	s_nop 1
	v_cndmask_b32_e64 v32, v78, v98, s[4:5]
	v_mul_f32_e32 v78, 0x37800000, v32
	v_cndmask_b32_e32 v32, v32, v78, vcc
	v_cmp_class_f32_e32 vcc, v6, v167
	s_nop 1
	v_cndmask_b32_e32 v6, v32, v6, vcc
	v_div_scale_f32 v32, s[4:5], v6, v6, 1.0
	v_rcp_f32_e32 v78, v32
	s_add_i32 s4, s42, s71
	s_ashr_i32 s5, s4, 31
	v_fma_f32 v98, -v32, v78, 1.0
	v_fmac_f32_e32 v78, v98, v78
	v_div_scale_f32 v98, vcc, 1.0, v6, 1.0
	v_mul_f32_e32 v100, v98, v78
	v_fma_f32 v102, -v32, v100, v98
	v_fmac_f32_e32 v100, v102, v78
	v_fma_f32 v32, -v32, v100, v98
	v_div_fmas_f32 v32, v32, v78, v100
	v_div_fixup_f32 v32, v32, v6, 1.0
	v_pk_mul_f32 v[114:115], v[76:77], v[32:33] op_sel_hi:[1,0]
	v_pk_mul_f32 v[76:77], v[84:85], v[32:33] op_sel_hi:[1,0]
	v_mov_b32_e32 v102, v7
	v_pk_mul_f32 v[4:5], v[4:5], v[32:33] op_sel_hi:[1,0]
	v_pk_mul_f32 v[2:3], v[2:3], v[32:33] op_sel_hi:[1,0]
	v_pk_mul_f32 v[0:1], v[0:1], v[32:33] op_sel_hi:[1,0]
	v_pk_mul_f32 v[82:83], v[82:83], v[32:33] op_sel_hi:[1,0]
	s_waitcnt vmcnt(0)
	v_pk_fma_f32 v[84:85], v[106:107], v[114:115], v[110:111]
	v_mbcnt_lo_u32_b32 v106, -1, 0
	v_mbcnt_hi_u32_b32 v106, -1, v106
	v_pk_fma_f32 v[76:77], v[108:109], v[76:77], v[112:113]
	v_ashrrev_i32_e32 v107, 31, v106
	v_lshl_add_u64 v[106:107], v[106:107], 4, s[12:13]
	global_load_dwordx4 v[106:109], v[106:107], off offset:1024
	v_mbcnt_lo_u32_b32 v110, -1, 0
	v_mbcnt_hi_u32_b32 v110, -1, v110
	v_pk_mul_f32 v[114:115], v[86:87], v[32:33] op_sel_hi:[1,0]
	v_ashrrev_i32_e32 v111, 31, v110
	v_lshl_add_u64 v[110:111], v[110:111], 4, s[14:15]
	global_load_dwordx4 v[110:113], v[110:111], off offset:1024
	v_pk_mul_f32 v[86:87], v[88:89], v[32:33] op_sel_hi:[1,0]
	v_max_f32_e64 v6, |v76|, |v77|
	v_max3_f32 v6, |v84|, |v85|, v6
	s_waitcnt vmcnt(0)
	v_pk_fma_f32 v[88:89], v[106:107], v[114:115], v[110:111]
	v_mbcnt_lo_u32_b32 v106, -1, 0
	v_mbcnt_hi_u32_b32 v106, -1, v106
	v_pk_fma_f32 v[86:87], v[108:109], v[86:87], v[112:113]
	v_ashrrev_i32_e32 v107, 31, v106
	v_lshl_add_u64 v[106:107], v[106:107], 4, s[12:13]
	global_load_dwordx4 v[106:109], v[106:107], off offset:2048
	v_mbcnt_lo_u32_b32 v110, -1, 0
	v_mbcnt_hi_u32_b32 v110, -1, v110
	v_pk_mul_f32 v[114:115], v[90:91], v[32:33] op_sel_hi:[1,0]
	v_ashrrev_i32_e32 v111, 31, v110
	v_lshl_add_u64 v[110:111], v[110:111], 4, s[14:15]
	global_load_dwordx4 v[110:113], v[110:111], off offset:2048
	v_pk_mul_f32 v[90:91], v[92:93], v[32:33] op_sel_hi:[1,0]
	v_max_f32_e64 v78, |v86|, |v87|
	v_max3_f32 v78, |v88|, |v89|, v78
	v_max3_f32 v6, v6, 0, v78
	s_waitcnt vmcnt(0)
	v_pk_fma_f32 v[92:93], v[106:107], v[114:115], v[110:111]
	v_mbcnt_lo_u32_b32 v106, -1, 0
	v_mbcnt_hi_u32_b32 v106, -1, v106
	v_pk_fma_f32 v[90:91], v[108:109], v[90:91], v[112:113]
	v_ashrrev_i32_e32 v107, 31, v106
	v_lshl_add_u64 v[106:107], v[106:107], 4, s[12:13]
	global_load_dwordx4 v[106:109], v[106:107], off offset:3072
	v_mbcnt_lo_u32_b32 v110, -1, 0
	v_mbcnt_hi_u32_b32 v110, -1, v110
	v_pk_mul_f32 v[114:115], v[94:95], v[32:33] op_sel_hi:[1,0]
	v_ashrrev_i32_e32 v111, 31, v110
	v_lshl_add_u64 v[110:111], v[110:111], 4, s[14:15]
	global_load_dwordx4 v[110:113], v[110:111], off offset:3072
	v_pk_mul_f32 v[94:95], v[96:97], v[32:33] op_sel_hi:[1,0]
	v_max_f32_e64 v78, |v90|, |v91|
	v_max3_f32 v78, |v92|, |v93|, v78
	s_waitcnt vmcnt(0)
	v_pk_fma_f32 v[96:97], v[106:107], v[114:115], v[110:111]
	v_mbcnt_lo_u32_b32 v106, -1, 0
	v_mbcnt_hi_u32_b32 v106, -1, v106
	v_pk_fma_f32 v[94:95], v[108:109], v[94:95], v[112:113]
	v_ashrrev_i32_e32 v107, 31, v106
	v_lshl_add_u64 v[106:107], v[106:107], 4, s[12:13]
	v_add_co_u32_e32 v106, vcc, s23, v106
	v_max_f32_e64 v98, |v94|, |v95|
	s_nop 0
	v_addc_co_u32_e32 v107, vcc, 0, v107, vcc
	global_load_dwordx4 v[106:109], v[106:107], off
	v_mbcnt_lo_u32_b32 v110, -1, 0
	v_mbcnt_hi_u32_b32 v110, -1, v110
	v_max3_f32 v98, |v96|, |v97|, v98
	v_ashrrev_i32_e32 v111, 31, v110
	v_lshl_add_u64 v[110:111], v[110:111], 4, s[14:15]
	v_add_co_u32_e32 v110, vcc, s23, v110
	v_max3_f32 v78, v6, v78, v98
	s_nop 0
	v_addc_co_u32_e32 v111, vcc, 0, v111, vcc
	global_load_dwordx4 v[110:113], v[110:111], off
	v_mov_b32_e32 v98, v101
	v_pk_mul_f32 v[98:99], v[98:99], v[32:33] op_sel_hi:[1,0]
	v_pk_mul_f32 v[6:7], v[102:103], v[32:33] op_sel_hi:[1,0]
	s_waitcnt vmcnt(0)
; #define GAS __attribute__((address_space(1)))
; #define FLANE lane_id()
; __device__ __forceinline__ void p6_router(Frame& F) {
;     ...
;                 for (int j = 0; j < 8; ++j) { const f32x4 g = *((const GAS f32x4*)F.ln1_g + FLANE + 64 * j), b = *((const GAS f32x4*)F.ln1_b + FLANE + 64 * j);
;                     v[j] = v[j] * rstd * g + b; am = fmaxf(am, fmaxf(fmaxf(fabsf(v[j][0]), fabsf(v[j][1])), fmaxf(fabsf(v[j][2]), fabsf(v[j][3])))); }
; #pragma unroll
;                 for (int o = 1; o < 64; o <<= 1) am = fmaxf(am, __shfl_xor(am, o));
;                 const float sc = am > 0.f ? am * (1.f / 127.f) : 1.f, inv = 1.f / sc;
; #pragma unroll
;                 for (int j = 0; j < 8; ++j) { const int q0 = (int)__builtin_rintf(v[j][0] * inv), q1 = (int)__builtin_rintf(v[j][1] * inv), q2 = (int)__builtin_rintf(v[j][2] * inv), q3 = (int)__builtin_rintf(v[j][3] * inv);
;                     h1q[(size_t)m * (D / 4) + FLANE + 64 * j] = (unsigned)(q0 & 0xff) | ((unsigned)(q1 & 0xff) << 8) | ((unsigned)(q2 & 0xff) << 16) | ((unsigned)(q3 & 0xff) << 24); }
	v_pk_fma_f32 v[98:99], v[108:109], v[98:99], v[112:113]
	v_pk_fma_f32 v[100:101], v[106:107], v[6:7], v[110:111]
	v_max_f32_e64 v6, |v98|, |v99|
	v_max3_f32 v114, |v100|, |v101|, v6
	v_mbcnt_lo_u32_b32 v6, -1, 0
	v_mbcnt_hi_u32_b32 v6, -1, v6
	s_nop 0
	v_ashrrev_i32_e32 v7, 31, v6
	v_lshl_add_u64 v[6:7], v[6:7], 4, s[12:13]
	v_add_co_u32_e32 v6, vcc, s23, v6
	s_nop 1
	v_addc_co_u32_e32 v7, vcc, 0, v7, vcc
	global_load_dwordx4 v[106:109], v[6:7], off offset:1024
	v_mbcnt_lo_u32_b32 v6, -1, 0
	v_mbcnt_hi_u32_b32 v6, -1, v6
	s_nop 0
	v_ashrrev_i32_e32 v7, 31, v6
	v_lshl_add_u64 v[6:7], v[6:7], 4, s[14:15]
	v_add_co_u32_e32 v6, vcc, s23, v6
	s_nop 1
	v_addc_co_u32_e32 v7, vcc, 0, v7, vcc
	global_load_dwordx4 v[110:113], v[6:7], off offset:1024
	v_pk_mul_f32 v[6:7], v[104:105], v[32:33] op_sel_hi:[1,0]
	s_waitcnt vmcnt(0)
	v_pk_fma_f32 v[104:105], v[106:107], v[4:5], v[110:111]
	v_pk_fma_f32 v[102:103], v[108:109], v[6:7], v[112:113]
	s_nop 0
	v_max_f32_e64 v4, |v102|, |v103|
	v_max3_f32 v4, |v104|, |v105|, v4
	v_max3_f32 v112, v78, v114, v4
	v_mbcnt_lo_u32_b32 v4, -1, 0
	v_mbcnt_hi_u32_b32 v4, -1, v4
	v_mov_b32_e32 v78, v81
	v_ashrrev_i32_e32 v5, 31, v4
	v_lshl_add_u64 v[4:5], v[4:5], 4, s[12:13]
	v_add_co_u32_e32 v4, vcc, s23, v4
	v_pk_mul_f32 v[78:79], v[78:79], v[32:33] op_sel_hi:[1,0]
	s_nop 0
	v_addc_co_u32_e32 v5, vcc, 0, v5, vcc
	global_load_dwordx4 v[4:7], v[4:5], off offset:2048
	v_mbcnt_lo_u32_b32 v106, -1, 0
	v_mbcnt_hi_u32_b32 v106, -1, v106
	s_nop 0
	v_ashrrev_i32_e32 v107, 31, v106
	v_lshl_add_u64 v[106:107], v[106:107], 4, s[14:15]
	v_add_co_u32_e32 v106, vcc, s23, v106
	s_nop 1
	v_addc_co_u32_e32 v107, vcc, 0, v107, vcc
	global_load_dwordx4 v[108:111], v[106:107], off offset:2048
	s_waitcnt vmcnt(0)
	v_pk_fma_f32 v[106:107], v[2:3], v[6:7], v[110:111]
	v_pk_fma_f32 v[108:109], v[0:1], v[4:5], v[108:109]
	v_max_f32_e64 v0, |v106|, |v107|
	v_max3_f32 v110, |v108|, |v109|, v0
	v_mbcnt_lo_u32_b32 v0, -1, 0
	v_mbcnt_hi_u32_b32 v0, -1, v0
	s_nop 0
	v_ashrrev_i32_e32 v1, 31, v0
	v_lshl_add_u64 v[0:1], v[0:1], 4, s[12:13]
	v_add_co_u32_e32 v0, vcc, s23, v0
	s_nop 1
	v_addc_co_u32_e32 v1, vcc, 0, v1, vcc
	global_load_dwordx4 v[0:3], v[0:1], off offset:3072
	v_mbcnt_lo_u32_b32 v4, -1, 0
	v_mbcnt_hi_u32_b32 v4, -1, v4
	s_nop 0
	v_ashrrev_i32_e32 v5, 31, v4
	v_lshl_add_u64 v[4:5], v[4:5], 4, s[14:15]
	v_add_co_u32_e32 v4, vcc, s23, v4
	s_nop 1
	v_addc_co_u32_e32 v5, vcc, 0, v5, vcc
	global_load_dwordx4 v[4:7], v[4:5], off offset:3072
	s_waitcnt vmcnt(0)
	v_pk_fma_f32 v[2:3], v[78:79], v[2:3], v[6:7]
	v_pk_fma_f32 v[4:5], v[82:83], v[0:1], v[4:5]
	v_max_f32_e64 v0, |v2|, |v3|
	v_max3_f32 v0, |v4|, |v5|, v0
	v_max3_f32 v0, v112, v110, v0
	s_waitcnt lgkmcnt(0)
	s_nop 1
	v_max_f32_dpp v0, v0, v0 quad_perm:[1,0,3,2] row_mask:0xf bank_mask:0xf
	s_waitcnt lgkmcnt(0)
	s_nop 1
	v_max_f32_dpp v0, v0, v0 quad_perm:[2,3,0,1] row_mask:0xf bank_mask:0xf
	s_waitcnt lgkmcnt(0)
	s_nop 1
	v_max_f32_dpp v0, v0, v0 row_half_mirror row_mask:0xf bank_mask:0xf
	s_waitcnt lgkmcnt(0)
	s_nop 1
	v_max_f32_dpp v0, v0, v0 row_mirror row_mask:0xf bank_mask:0xf
	s_waitcnt lgkmcnt(0)
	v_mov_b32_e32 v1, v0
	s_nop 1
	v_permlane16_swap_b32_e32 v0, v1
	v_max_f32_e32 v0, v0, v1
	s_waitcnt lgkmcnt(0)
	v_mov_b32_e32 v1, v0
	s_nop 1
	v_permlane32_swap_b32_e32 v0, v1
	v_max_f32_e32 v0, v0, v1
	v_cmp_lt_f32_e32 vcc, 0, v0
	v_mul_f32_e32 v0, 0x3c010204, v0
	s_nop 0
	v_cndmask_b32_e32 v0, 1.0, v0, vcc
	v_div_scale_f32 v1, s[6:7], v0, v0, 1.0
	v_rcp_f32_e32 v6, v1
	s_lshl_b64 s[6:7], s[4:5], 11
	s_add_u32 s6, s3, s6
	s_addc_u32 s7, s24, s7
	v_fma_f32 v7, -v1, v6, 1.0
	v_fmac_f32_e32 v6, v7, v6
	v_div_scale_f32 v7, vcc, 1.0, v0, 1.0
	v_mul_f32_e32 v78, v7, v6
	v_fma_f32 v79, -v1, v78, v7
	v_fmac_f32_e32 v78, v79, v6
	v_fma_f32 v1, -v1, v78, v7
	v_div_fmas_f32 v1, v1, v6, v78
	v_div_fixup_f32 v1, v1, v0, 1.0
	v_mul_f32_e32 v7, v85, v1
	v_mul_f32_e32 v6, v84, v1
	v_rndne_f32_e32 v7, v7
	v_mul_f32_e32 v76, v76, v1
	v_mul_f32_e32 v77, v77, v1
	v_rndne_f32_e32 v6, v6
	v_cvt_i32_f32_e32 v7, v7
	v_rndne_f32_e32 v76, v76
	v_rndne_f32_e32 v77, v77
	v_cvt_i32_f32_e32 v6, v6
	v_cvt_i32_f32_sdwa v76, v76 dst_sel:WORD_1 dst_unused:UNUSED_PAD src0_sel:DWORD
	v_cvt_i32_f32_e32 v77, v77
	v_lshlrev_b32_e32 v7, 8, v7
	v_and_b32_e32 v7, 0xff00, v7
	v_and_b32_e32 v76, 0xff0000, v76
	v_perm_b32 v6, v77, v6, s1
	v_or3_b32 v76, v6, v7, v76
	v_mbcnt_lo_u32_b32 v6, -1, 0
	v_mbcnt_hi_u32_b32 v6, -1, v6
	v_mul_f32_e32 v77, v87, v1
	v_ashrrev_i32_e32 v7, 31, v6
	v_lshl_add_u64 v[6:7], v[6:7], 2, s[6:7]
	global_store_dword v[6:7], v76, off
	v_mul_f32_e32 v7, v89, v1
	v_mul_f32_e32 v6, v88, v1
	v_rndne_f32_e32 v7, v7
	v_mul_f32_e32 v76, v86, v1
	v_rndne_f32_e32 v6, v6
	v_cvt_i32_f32_e32 v7, v7
	v_rndne_f32_e32 v76, v76
	v_rndne_f32_e32 v77, v77
	v_cvt_i32_f32_e32 v6, v6
	v_cvt_i32_f32_sdwa v76, v76 dst_sel:WORD_1 dst_unused:UNUSED_PAD src0_sel:DWORD
	v_cvt_i32_f32_e32 v77, v77
	v_lshlrev_b32_e32 v7, 8, v7
	v_and_b32_e32 v7, 0xff00, v7
	v_and_b32_e32 v76, 0xff0000, v76
	v_perm_b32 v6, v77, v6, s1
	v_or3_b32 v76, v6, v7, v76
	v_mbcnt_lo_u32_b32 v6, -1, 0
	v_mbcnt_hi_u32_b32 v6, -1, v6
	v_mul_f32_e32 v77, v91, v1
	v_ashrrev_i32_e32 v7, 31, v6
	v_lshl_add_u64 v[6:7], v[6:7], 2, s[6:7]
	global_store_dword v[6:7], v76, off offset:256
	v_mul_f32_e32 v7, v93, v1
	v_mul_f32_e32 v6, v92, v1
	v_rndne_f32_e32 v7, v7
	v_mul_f32_e32 v76, v90, v1
	v_rndne_f32_e32 v6, v6
	v_cvt_i32_f32_e32 v7, v7
	v_rndne_f32_e32 v76, v76
	v_rndne_f32_e32 v77, v77
	v_cvt_i32_f32_e32 v6, v6
	v_cvt_i32_f32_sdwa v76, v76 dst_sel:WORD_1 dst_unused:UNUSED_PAD src0_sel:DWORD
	v_cvt_i32_f32_e32 v77, v77
	v_lshlrev_b32_e32 v7, 8, v7
; #define FLANE lane_id()
; __device__ __forceinline__ void p6_router(Frame& F) {
;     ...
;                 for (int j = 0; j < 8; ++j) { const int q0 = (int)__builtin_rintf(v[j][0] * inv), q1 = (int)__builtin_rintf(v[j][1] * inv), q2 = (int)__builtin_rintf(v[j][2] * inv), q3 = (int)__builtin_rintf(v[j][3] * inv);
;                     h1q[(size_t)m * (D / 4) + FLANE + 64 * j] = (unsigned)(q0 & 0xff) | ((unsigned)(q1 & 0xff) << 8) | ((unsigned)(q2 & 0xff) << 16) | ((unsigned)(q3 & 0xff) << 24); }
;                 if (FLANE == 0) { st1[2 * m] = mean; st1[2 * m + 1] = rstd; stl[2 * row] = mean; stl[2 * row + 1] = rstd; sxg[m] = sc; sxl[row] = sc; }
	v_and_b32_e32 v7, 0xff00, v7
	v_and_b32_e32 v76, 0xff0000, v76
	v_perm_b32 v6, v77, v6, s1
	v_or3_b32 v76, v6, v7, v76
	v_mbcnt_lo_u32_b32 v6, -1, 0
	v_mbcnt_hi_u32_b32 v6, -1, v6
	v_mul_f32_e32 v77, v95, v1
	v_ashrrev_i32_e32 v7, 31, v6
	v_lshl_add_u64 v[6:7], v[6:7], 2, s[6:7]
	global_store_dword v[6:7], v76, off offset:512
	v_mul_f32_e32 v7, v97, v1
	v_mul_f32_e32 v6, v96, v1
	v_rndne_f32_e32 v7, v7
	v_mul_f32_e32 v76, v94, v1
	v_rndne_f32_e32 v6, v6
	v_cvt_i32_f32_e32 v7, v7
	v_rndne_f32_e32 v76, v76
	v_rndne_f32_e32 v77, v77
	v_cvt_i32_f32_e32 v6, v6
	v_cvt_i32_f32_sdwa v76, v76 dst_sel:WORD_1 dst_unused:UNUSED_PAD src0_sel:DWORD
	v_cvt_i32_f32_e32 v77, v77
	v_lshlrev_b32_e32 v7, 8, v7
	v_and_b32_e32 v7, 0xff00, v7
	v_and_b32_e32 v76, 0xff0000, v76
	v_perm_b32 v6, v77, v6, s1
	v_or3_b32 v76, v6, v7, v76
	v_mbcnt_lo_u32_b32 v6, -1, 0
	v_mbcnt_hi_u32_b32 v6, -1, v6
	v_mul_f32_e32 v77, v99, v1
	v_ashrrev_i32_e32 v7, 31, v6
	v_lshl_add_u64 v[6:7], v[6:7], 2, s[6:7]
	global_store_dword v[6:7], v76, off offset:768
	v_mul_f32_e32 v7, v101, v1
	v_mul_f32_e32 v6, v100, v1
	v_rndne_f32_e32 v7, v7
	v_mul_f32_e32 v76, v98, v1
	v_rndne_f32_e32 v6, v6
	v_cvt_i32_f32_e32 v7, v7
	v_rndne_f32_e32 v76, v76
	v_rndne_f32_e32 v77, v77
	v_cvt_i32_f32_e32 v6, v6
	v_cvt_i32_f32_sdwa v76, v76 dst_sel:WORD_1 dst_unused:UNUSED_PAD src0_sel:DWORD
	v_cvt_i32_f32_e32 v77, v77
	v_lshlrev_b32_e32 v7, 8, v7
	v_and_b32_e32 v7, 0xff00, v7
	v_and_b32_e32 v76, 0xff0000, v76
	v_perm_b32 v6, v77, v6, s1
	v_or3_b32 v76, v6, v7, v76
	v_mbcnt_lo_u32_b32 v6, -1, 0
	v_mbcnt_hi_u32_b32 v6, -1, v6
	v_mul_f32_e32 v77, v103, v1
	v_ashrrev_i32_e32 v7, 31, v6
	v_lshl_add_u64 v[6:7], v[6:7], 2, s[6:7]
	global_store_dword v[6:7], v76, off offset:1024
	v_mul_f32_e32 v7, v105, v1
	v_mul_f32_e32 v6, v104, v1
	v_rndne_f32_e32 v7, v7
	v_mul_f32_e32 v76, v102, v1
	v_rndne_f32_e32 v6, v6
	v_cvt_i32_f32_e32 v7, v7
	v_rndne_f32_e32 v76, v76
	v_rndne_f32_e32 v77, v77
	v_cvt_i32_f32_e32 v6, v6
	v_cvt_i32_f32_sdwa v76, v76 dst_sel:WORD_1 dst_unused:UNUSED_PAD src0_sel:DWORD
	v_cvt_i32_f32_e32 v77, v77
	v_lshlrev_b32_e32 v7, 8, v7
	v_and_b32_e32 v7, 0xff00, v7
	v_and_b32_e32 v76, 0xff0000, v76
	v_perm_b32 v6, v77, v6, s1
	v_or3_b32 v76, v6, v7, v76
	v_mbcnt_lo_u32_b32 v6, -1, 0
	v_mbcnt_hi_u32_b32 v6, -1, v6
	v_mul_f32_e32 v77, v107, v1
	v_ashrrev_i32_e32 v7, 31, v6
	v_lshl_add_u64 v[6:7], v[6:7], 2, s[6:7]
	global_store_dword v[6:7], v76, off offset:1280
	v_mul_f32_e32 v7, v109, v1
	v_mul_f32_e32 v6, v108, v1
	v_rndne_f32_e32 v7, v7
	v_mul_f32_e32 v76, v106, v1
	v_rndne_f32_e32 v6, v6
	v_cvt_i32_f32_e32 v7, v7
	v_rndne_f32_e32 v76, v76
	v_rndne_f32_e32 v77, v77
	v_mul_f32_e32 v5, v5, v1
	v_cvt_i32_f32_e32 v6, v6
	v_cvt_i32_f32_sdwa v76, v76 dst_sel:WORD_1 dst_unused:UNUSED_PAD src0_sel:DWORD
	v_cvt_i32_f32_e32 v77, v77
	v_mul_f32_e32 v4, v4, v1
	v_rndne_f32_e32 v5, v5
	v_mul_f32_e32 v2, v2, v1
	v_mul_f32_e32 v1, v3, v1
	v_rndne_f32_e32 v4, v4
	v_cvt_i32_f32_e32 v5, v5
	v_rndne_f32_e32 v2, v2
	v_rndne_f32_e32 v1, v1
	v_cvt_i32_f32_e32 v4, v4
	v_cvt_i32_f32_sdwa v2, v2 dst_sel:WORD_1 dst_unused:UNUSED_PAD src0_sel:DWORD
	v_cvt_i32_f32_e32 v1, v1
	v_lshlrev_b32_e32 v7, 8, v7
	v_and_b32_e32 v7, 0xff00, v7
	v_and_b32_e32 v76, 0xff0000, v76
	v_perm_b32 v6, v77, v6, s1
	v_or3_b32 v76, v6, v7, v76
	v_mbcnt_lo_u32_b32 v6, -1, 0
	v_mbcnt_hi_u32_b32 v6, -1, v6
	v_lshlrev_b32_e32 v3, 8, v5
	v_ashrrev_i32_e32 v7, 31, v6
	v_lshl_add_u64 v[6:7], v[6:7], 2, s[6:7]
	v_and_b32_e32 v3, 0xff00, v3
	v_and_b32_e32 v2, 0xff0000, v2
	v_perm_b32 v1, v1, v4, s1
	global_store_dword v[6:7], v76, off offset:1536
	v_or3_b32 v1, v1, v3, v2
	v_mbcnt_lo_u32_b32 v2, -1, 0
	v_mbcnt_hi_u32_b32 v2, -1, v2
	s_nop 0
	v_ashrrev_i32_e32 v3, 31, v2
	v_lshl_add_u64 v[2:3], v[2:3], 2, s[6:7]
	global_store_dword v[2:3], v1, off offset:1792
	v_mbcnt_lo_u32_b32 v1, -1, 0
	v_mbcnt_hi_u32_b32 v1, -1, v1
	s_nop 0
	v_cmp_eq_u32_e32 vcc, 0, v1
	s_and_saveexec_b64 s[6:7], vcc
	s_cbranch_execz .LBB0_1489
	s_lshl_b32 s8, s4, 1
	s_ashr_i32 s9, s8, 31
	s_lshl_b64 s[8:9], s[8:9], 2
	s_add_u32 s8, s27, s8
	s_addc_u32 s9, s64, s9
	v_readlane_b32 s0, v255, 44
	s_lshl_b64 s[4:5], s[4:5], 2
	v_mul_f32_e32 v2, 0x3a000000, v80
	v_mov_b32_e32 v3, v32
	v_mov_b32_e32 v1, s0
	s_add_u32 s4, s25, s4
	v_readlane_b32 s0, v255, 31
	ds_write_b64 v1, v[2:3]
	s_addc_u32 s5, s26, s5
	v_mov_b32_e32 v1, s0
	global_store_dwordx2 v33, v[2:3], s[8:9]
	global_store_dword v33, v0, s[4:5]
	ds_write_b32 v1, v0
; __device__ __forceinline__ void p6_router(Frame& F) {
;     ...
;                 for (int j = 0; j < 8; ++j) { const v2u w = raw[rr][j]; v[j] = (f32x4){bf_lo(w.x), bf_hi(w.x), bf_lo(w.y), bf_hi(w.y)}; s += (v[j][0] + v[j][1]) + (v[j][2] + v[j][3]); }
;                 const float mean = wave_sum(s) * (1.f / D); float s2 = 0.f;
; #pragma unroll
;                 for (int j = 0; j < 8; ++j) { v[j] = v[j] - mean; s2 += (v[j][0] * v[j][0] + v[j][1] * v[j][1]) + (v[j][2] * v[j][2] + v[j][3] * v[j][3]); }
;                 const float rstd = 1.f / sqrtf(wave_sum(s2) * (1.f / D) + LN_EPS);
.LBB0_1489:
	s_or_b64 exec, exec, s[6:7]
	v_lshlrev_b32_e32 v77, 16, v74
	v_lshlrev_b32_e32 v76, 16, v72
	v_and_b32_e32 v89, 0xffff0000, v74
	v_and_b32_e32 v88, 0xffff0000, v72
	v_lshlrev_b32_e32 v91, 16, v75
	v_lshlrev_b32_e32 v90, 16, v73
	v_and_b32_e32 v93, 0xffff0000, v75
	v_and_b32_e32 v92, 0xffff0000, v73
	v_pk_add_f32 v[0:1], v[76:77], v[88:89]
	v_pk_add_f32 v[2:3], v[90:91], v[92:93]
	v_lshlrev_b32_e32 v75, 16, v71
	v_pk_add_f32 v[0:1], v[0:1], v[2:3]
	v_lshlrev_b32_e32 v74, 16, v70
	v_add_f32_e32 v0, 0, v0
	v_and_b32_e32 v95, 0xffff0000, v71
	v_and_b32_e32 v94, 0xffff0000, v70
	v_add_f32_e32 v6, v0, v1
	v_pk_add_f32 v[0:1], v[74:75], v[94:95]
	v_lshlrev_b32_e32 v78, 16, v68
	v_and_b32_e32 v79, 0xffff0000, v68
	v_lshlrev_b32_e32 v80, 16, v69
	v_and_b32_e32 v81, 0xffff0000, v69
	v_and_b32_e32 v87, 0xffff0000, v66
	v_pk_add_f32 v[0:1], v[0:1], v[0:1] op_sel:[0,1] op_sel_hi:[1,0]
	v_add_f32_e32 v84, v78, v79
	v_add_f32_e32 v82, v80, v81
	v_lshlrev_b32_e32 v7, 16, v66
	v_lshlrev_b32_e32 v85, 16, v67
	v_and_b32_e32 v83, 0xffff0000, v67
	v_mov_b32_e32 v1, v87
	v_pk_add_f32 v[0:1], v[6:7], v[0:1]
	v_pk_add_f32 v[2:3], v[84:85], v[82:83]
	v_lshlrev_b32_e32 v5, 16, v65
	v_lshlrev_b32_e32 v4, 16, v64
	v_and_b32_e32 v97, 0xffff0000, v65
	v_and_b32_e32 v96, 0xffff0000, v64
	v_pk_add_f32 v[68:69], v[0:1], v[2:3]
	v_pk_add_f32 v[70:71], v[4:5], v[96:97]
	v_lshlrev_b32_e32 v0, 16, v62
	v_and_b32_e32 v1, 0xffff0000, v62
	v_lshlrev_b32_e32 v2, 16, v63
	v_and_b32_e32 v3, 0xffff0000, v63
	v_lshlrev_b32_e32 v66, 16, v60
	v_and_b32_e32 v67, 0xffff0000, v60
	v_lshlrev_b32_e32 v65, 16, v61
	v_and_b32_e32 v63, 0xffff0000, v61
	v_pk_add_f32 v[60:61], v[68:69], v[68:69] op_sel:[0,1] op_sel_hi:[1,0]
	v_pk_add_f32 v[68:69], v[70:71], v[70:71] op_sel:[0,1] op_sel_hi:[1,0]
	v_add_f32_e32 v64, v0, v1
	v_add_f32_e32 v62, v2, v3
	v_mov_b32_e32 v61, v66
	v_mov_b32_e32 v69, v67
	v_pk_add_f32 v[60:61], v[60:61], v[68:69]
	v_pk_add_f32 v[68:69], v[64:65], v[62:63]
	s_nop 0
	v_pk_add_f32 v[60:61], v[60:61], v[68:69]
	s_nop 0
	v_add_f32_e32 v6, v60, v61
	s_waitcnt lgkmcnt(0)
	s_nop 1
	v_add_f32_dpp v6, v6, v6 quad_perm:[1,0,3,2] row_mask:0xf bank_mask:0xf
	s_waitcnt lgkmcnt(0)
	s_nop 1
	v_add_f32_dpp v6, v6, v6 quad_perm:[2,3,0,1] row_mask:0xf bank_mask:0xf
	s_waitcnt lgkmcnt(0)
	s_nop 1
	v_add_f32_dpp v6, v6, v6 row_half_mirror row_mask:0xf bank_mask:0xf
	s_waitcnt lgkmcnt(0)
	s_nop 1
	v_add_f32_dpp v6, v6, v6 row_mirror row_mask:0xf bank_mask:0xf
	s_waitcnt lgkmcnt(0)
	v_mov_b32_e32 v32, v6
	s_nop 1
	v_permlane16_swap_b32_e32 v6, v32
	v_add_f32_e32 v6, v6, v32
	s_waitcnt lgkmcnt(0)
	v_mov_b32_e32 v32, v6
	s_nop 1
	v_permlane32_swap_b32_e32 v6, v32
	v_add_f32_e32 v64, v6, v32
	v_fmac_f32_e32 v92, 0xba000000, v64
	v_fmac_f32_e32 v88, 0xba000000, v64
	v_fmac_f32_e32 v93, 0xba000000, v64
	v_fmac_f32_e32 v89, 0xba000000, v64
	v_fmac_f32_e32 v90, 0xba000000, v64
	v_fmac_f32_e32 v76, 0xba000000, v64
	v_fmac_f32_e32 v91, 0xba000000, v64
	v_fmac_f32_e32 v77, 0xba000000, v64
	v_mov_b32_e32 v71, v89
	v_mov_b32_e32 v61, v88
	v_pk_mul_f32 v[68:69], v[88:89], v[88:89]
	v_pk_mul_f32 v[88:89], v[92:93], v[92:93]
	v_mov_b32_e32 v70, v77
	v_mov_b32_e32 v60, v76
	v_pk_fma_f32 v[76:77], v[76:77], v[76:77], v[68:69]
	v_pk_fma_f32 v[88:89], v[90:91], v[90:91], v[88:89]
	v_fmac_f32_e32 v94, 0xba000000, v64
	v_pk_add_f32 v[76:77], v[76:77], v[88:89]
	v_fmac_f32_e32 v95, 0xba000000, v64
	v_fmac_f32_e32 v75, 0xba000000, v64
	v_pk_add_f32 v[88:89], v[76:77], v[76:77] op_sel_hi:[0,1]
	v_fmac_f32_e32 v74, 0xba000000, v64
	v_mov_b32_e32 v76, v75
	v_mov_b32_e32 v77, v95
	v_mov_b32_e32 v75, v94
	v_mov_b32_e32 v72, v91
	v_mov_b32_e32 v73, v93
	v_mov_b32_e32 v68, v90
	v_mov_b32_e32 v69, v92
	v_pk_mul_f32 v[90:91], v[76:77], v[76:77]
	v_pk_mul_f32 v[92:93], v[74:75], v[74:75]
	v_fmac_f32_e32 v78, 0xba000000, v64
	v_pk_mov_b32 v[94:95], v[92:93], v[90:91] op_sel:[1,0]
	v_mov_b32_e32 v93, v91
	v_fmac_f32_e32 v79, 0xba000000, v64
	v_fmac_f32_e32 v80, 0xba000000, v64
	v_mul_f32_e32 v6, v78, v78
	v_pk_add_f32 v[90:91], v[94:95], v[92:93]
	v_fmac_f32_e32 v81, 0xba000000, v64
	v_pk_fma_f32 v[92:93], v[78:79], v[78:79], v[6:7] op_sel_hi:[1,1,0]
	v_mul_f32_e32 v6, v80, v80
	v_pk_add_f32 v[90:91], v[90:91], v[90:91] op_sel_hi:[0,1]
	v_pk_fma_f32 v[94:95], v[80:81], v[80:81], v[6:7] op_sel_hi:[1,1,0]
	v_fmac_f32_e32 v83, 0xba000000, v64
	v_fmac_f32_e32 v85, 0xba000000, v64
	v_fmac_f32_e32 v87, 0xba000000, v64
	v_fmac_f32_e32 v7, 0xba000000, v64
	v_mul_f32_e32 v92, v7, v7
	v_mul_f32_e32 v94, v87, v87
	v_mul_f32_e32 v90, v85, v85
	v_mul_f32_e32 v88, v83, v83
	v_pk_add_f32 v[92:93], v[92:93], v[94:95]
	v_pk_add_f32 v[88:89], v[90:91], v[88:89]
	v_fmac_f32_e32 v96, 0xba000000, v64
	v_pk_add_f32 v[88:89], v[92:93], v[88:89]
	v_fmac_f32_e32 v97, 0xba000000, v64
	v_fmac_f32_e32 v5, 0xba000000, v64
	v_pk_add_f32 v[90:91], v[88:89], v[88:89] op_sel_hi:[0,1]
	v_fmac_f32_e32 v4, 0xba000000, v64
	v_mov_b32_e32 v88, v5
	v_mov_b32_e32 v89, v97
	v_mov_b32_e32 v5, v96
	v_pk_mul_f32 v[92:93], v[88:89], v[88:89]
	v_pk_mul_f32 v[94:95], v[4:5], v[4:5]
	v_fmac_f32_e32 v0, 0xba000000, v64
	v_pk_mov_b32 v[96:97], v[94:95], v[92:93] op_sel:[1,0]
	v_mov_b32_e32 v95, v93
	v_fmac_f32_e32 v1, 0xba000000, v64
	v_fmac_f32_e32 v2, 0xba000000, v64
	v_mul_f32_e32 v6, v0, v0
	v_pk_add_f32 v[92:93], v[96:97], v[94:95]
	v_fmac_f32_e32 v3, 0xba000000, v64
	v_pk_fma_f32 v[94:95], v[0:1], v[0:1], v[6:7] op_sel_hi:[1,1,0]
	v_mul_f32_e32 v6, v2, v2
	v_pk_add_f32 v[92:93], v[92:93], v[92:93] op_sel_hi:[0,1]
	v_pk_fma_f32 v[96:97], v[2:3], v[2:3], v[6:7] op_sel_hi:[1,1,0]
	v_fmac_f32_e32 v63, 0xba000000, v64
	v_fmac_f32_e32 v65, 0xba000000, v64
	v_fmac_f32_e32 v67, 0xba000000, v64
	v_fmac_f32_e32 v66, 0xba000000, v64
	v_mul_f32_e32 v94, v66, v66
	v_mul_f32_e32 v96, v67, v67
	v_mul_f32_e32 v92, v65, v65
	v_mul_f32_e32 v90, v63, v63
	v_pk_add_f32 v[94:95], v[94:95], v[96:97]
	v_pk_add_f32 v[90:91], v[92:93], v[90:91]
	s_nop 0
	v_pk_add_f32 v[90:91], v[94:95], v[90:91]
	s_nop 0
	v_add_f32_e32 v6, v90, v91
	v_mbcnt_lo_u32_b32 v90, -1, 0
	v_mbcnt_hi_u32_b32 v90, -1, v90
	v_ashrrev_i32_e32 v91, 31, v90
	v_lshl_add_u64 v[90:91], v[90:91], 4, s[12:13]
	global_load_dwordx4 v[90:93], v[90:91], off
	v_mbcnt_lo_u32_b32 v94, -1, 0
	v_mbcnt_hi_u32_b32 v94, -1, v94
	s_waitcnt lgkmcnt(0)
; #define GAS __attribute__((address_space(1)))
; #define FLANE lane_id()
; __device__ __forceinline__ void p6_router(Frame& F) {
;     ...
;                 const float rstd = 1.f / sqrtf(wave_sum(s2) * (1.f / D) + LN_EPS);
;                 float am = 0.f;
; #pragma unroll
;                 for (int j = 0; j < 8; ++j) { const f32x4 g = *((const GAS f32x4*)F.ln1_g + FLANE + 64 * j), b = *((const GAS f32x4*)F.ln1_b + FLANE + 64 * j);
;                     v[j] = v[j] * rstd * g + b; am = fmaxf(am, fmaxf(fmaxf(fabsf(v[j][0]), fabsf(v[j][1])), fmaxf(fabsf(v[j][2]), fabsf(v[j][3])))); }
	s_nop 1
	v_add_f32_dpp v6, v6, v6 quad_perm:[1,0,3,2] row_mask:0xf bank_mask:0xf
	v_ashrrev_i32_e32 v95, 31, v94
	v_lshl_add_u64 v[94:95], v[94:95], 4, s[14:15]
	global_load_dwordx4 v[94:97], v[94:95], off
	s_waitcnt lgkmcnt(0)
	s_nop 1
	v_add_f32_dpp v6, v6, v6 quad_perm:[2,3,0,1] row_mask:0xf bank_mask:0xf
	s_waitcnt lgkmcnt(0)
	s_nop 1
	v_add_f32_dpp v6, v6, v6 row_half_mirror row_mask:0xf bank_mask:0xf
	s_waitcnt lgkmcnt(0)
	s_nop 1
	v_add_f32_dpp v6, v6, v6 row_mirror row_mask:0xf bank_mask:0xf
	s_waitcnt lgkmcnt(0)
	v_mov_b32_e32 v32, v6
	s_nop 1
	v_permlane16_swap_b32_e32 v6, v32
	v_add_f32_e32 v6, v6, v32
	s_waitcnt lgkmcnt(0)
	v_mov_b32_e32 v32, v6
	s_nop 1
	v_permlane32_swap_b32_e32 v6, v32
	v_add_f32_e32 v6, v6, v32
	v_fmamk_f32 v6, v6, 0x3a000000, v166
	v_cmp_gt_f32_e32 vcc, s22, v6
	v_mul_f32_e32 v32, 0x4f800000, v6
	s_nop 0
	v_cndmask_b32_e32 v6, v6, v32, vcc
	v_sqrt_f32_e32 v32, v6
	s_nop 0
	v_add_u32_e32 v62, -1, v32
	v_fma_f32 v82, -v62, v32, v6
	v_cmp_ge_f32_e64 s[4:5], 0, v82
	v_add_u32_e32 v82, 1, v32
	s_nop 0
	v_cndmask_b32_e64 v62, v32, v62, s[4:5]
	v_fma_f32 v32, -v82, v32, v6
	v_cmp_lt_f32_e64 s[4:5], 0, v32
	s_nop 1
	v_cndmask_b32_e64 v32, v62, v82, s[4:5]
	v_mul_f32_e32 v62, 0x37800000, v32
	v_cndmask_b32_e32 v32, v32, v62, vcc
	v_cmp_class_f32_e32 vcc, v6, v167
	s_nop 1
	v_cndmask_b32_e32 v6, v32, v6, vcc
	v_div_scale_f32 v32, s[4:5], v6, v6, 1.0
	v_rcp_f32_e32 v62, v32
	s_add_i32 s4, s42, s73
	s_ashr_i32 s5, s4, 31
	v_fma_f32 v82, -v32, v62, 1.0
	v_fmac_f32_e32 v62, v82, v62
	v_div_scale_f32 v82, vcc, 1.0, v6, 1.0
	v_mul_f32_e32 v84, v82, v62
	v_fma_f32 v86, -v32, v84, v82
	v_fmac_f32_e32 v84, v86, v62
	v_fma_f32 v32, -v32, v84, v82
	v_div_fmas_f32 v32, v32, v62, v84
	v_div_fixup_f32 v32, v32, v6, 1.0
	v_pk_mul_f32 v[98:99], v[60:61], v[32:33] op_sel_hi:[1,0]
	v_pk_mul_f32 v[60:61], v[68:69], v[32:33] op_sel_hi:[1,0]
	v_mov_b32_e32 v86, v7
	v_pk_mul_f32 v[4:5], v[4:5], v[32:33] op_sel_hi:[1,0]
	v_pk_mul_f32 v[2:3], v[2:3], v[32:33] op_sel_hi:[1,0]
	v_pk_mul_f32 v[0:1], v[0:1], v[32:33] op_sel_hi:[1,0]
	v_pk_mul_f32 v[66:67], v[66:67], v[32:33] op_sel_hi:[1,0]
	s_waitcnt vmcnt(0)
	v_pk_fma_f32 v[68:69], v[90:91], v[98:99], v[94:95]
	v_mbcnt_lo_u32_b32 v90, -1, 0
	v_mbcnt_hi_u32_b32 v90, -1, v90
	v_pk_fma_f32 v[60:61], v[92:93], v[60:61], v[96:97]
	v_ashrrev_i32_e32 v91, 31, v90
	v_lshl_add_u64 v[90:91], v[90:91], 4, s[12:13]
	global_load_dwordx4 v[90:93], v[90:91], off offset:1024
	v_mbcnt_lo_u32_b32 v94, -1, 0
	v_mbcnt_hi_u32_b32 v94, -1, v94
	v_pk_mul_f32 v[98:99], v[70:71], v[32:33] op_sel_hi:[1,0]
	v_ashrrev_i32_e32 v95, 31, v94
	v_lshl_add_u64 v[94:95], v[94:95], 4, s[14:15]
	global_load_dwordx4 v[94:97], v[94:95], off offset:1024
	v_pk_mul_f32 v[70:71], v[72:73], v[32:33] op_sel_hi:[1,0]
	v_max_f32_e64 v6, |v60|, |v61|
	v_max3_f32 v6, |v68|, |v69|, v6
	s_waitcnt vmcnt(0)
	v_pk_fma_f32 v[72:73], v[90:91], v[98:99], v[94:95]
	v_mbcnt_lo_u32_b32 v90, -1, 0
	v_mbcnt_hi_u32_b32 v90, -1, v90
	v_pk_fma_f32 v[70:71], v[92:93], v[70:71], v[96:97]
	v_ashrrev_i32_e32 v91, 31, v90
	v_lshl_add_u64 v[90:91], v[90:91], 4, s[12:13]
	global_load_dwordx4 v[90:93], v[90:91], off offset:2048
	v_mbcnt_lo_u32_b32 v94, -1, 0
	v_mbcnt_hi_u32_b32 v94, -1, v94
	v_pk_mul_f32 v[98:99], v[74:75], v[32:33] op_sel_hi:[1,0]
	v_ashrrev_i32_e32 v95, 31, v94
	v_lshl_add_u64 v[94:95], v[94:95], 4, s[14:15]
	global_load_dwordx4 v[94:97], v[94:95], off offset:2048
	v_pk_mul_f32 v[74:75], v[76:77], v[32:33] op_sel_hi:[1,0]
	v_max_f32_e64 v62, |v70|, |v71|
	v_max3_f32 v62, |v72|, |v73|, v62
	v_max3_f32 v6, v6, 0, v62
	s_waitcnt vmcnt(0)
	v_pk_fma_f32 v[76:77], v[90:91], v[98:99], v[94:95]
	v_mbcnt_lo_u32_b32 v90, -1, 0
	v_mbcnt_hi_u32_b32 v90, -1, v90
	v_pk_fma_f32 v[74:75], v[92:93], v[74:75], v[96:97]
	v_ashrrev_i32_e32 v91, 31, v90
	v_lshl_add_u64 v[90:91], v[90:91], 4, s[12:13]
	global_load_dwordx4 v[90:93], v[90:91], off offset:3072
	v_mbcnt_lo_u32_b32 v94, -1, 0
	v_mbcnt_hi_u32_b32 v94, -1, v94
	v_pk_mul_f32 v[98:99], v[78:79], v[32:33] op_sel_hi:[1,0]
	v_ashrrev_i32_e32 v95, 31, v94
	v_lshl_add_u64 v[94:95], v[94:95], 4, s[14:15]
	global_load_dwordx4 v[94:97], v[94:95], off offset:3072
	v_pk_mul_f32 v[78:79], v[80:81], v[32:33] op_sel_hi:[1,0]
	v_max_f32_e64 v62, |v74|, |v75|
	v_max3_f32 v62, |v76|, |v77|, v62
	s_waitcnt vmcnt(0)
	v_pk_fma_f32 v[80:81], v[90:91], v[98:99], v[94:95]
	v_mbcnt_lo_u32_b32 v90, -1, 0
	v_mbcnt_hi_u32_b32 v90, -1, v90
	v_pk_fma_f32 v[78:79], v[92:93], v[78:79], v[96:97]
	v_ashrrev_i32_e32 v91, 31, v90
	v_lshl_add_u64 v[90:91], v[90:91], 4, s[12:13]
	v_add_co_u32_e32 v90, vcc, s23, v90
	v_max_f32_e64 v82, |v78|, |v79|
	s_nop 0
	v_addc_co_u32_e32 v91, vcc, 0, v91, vcc
	global_load_dwordx4 v[90:93], v[90:91], off
	v_mbcnt_lo_u32_b32 v94, -1, 0
	v_mbcnt_hi_u32_b32 v94, -1, v94
	v_max3_f32 v82, |v80|, |v81|, v82
	v_ashrrev_i32_e32 v95, 31, v94
	v_lshl_add_u64 v[94:95], v[94:95], 4, s[14:15]
	v_add_co_u32_e32 v94, vcc, s23, v94
	v_max3_f32 v62, v6, v62, v82
	s_nop 0
	v_addc_co_u32_e32 v95, vcc, 0, v95, vcc
	global_load_dwordx4 v[94:97], v[94:95], off
	v_mov_b32_e32 v82, v85
	v_pk_mul_f32 v[82:83], v[82:83], v[32:33] op_sel_hi:[1,0]
	v_pk_mul_f32 v[6:7], v[86:87], v[32:33] op_sel_hi:[1,0]
	s_waitcnt vmcnt(0)
	v_pk_fma_f32 v[82:83], v[92:93], v[82:83], v[96:97]
	v_pk_fma_f32 v[84:85], v[90:91], v[6:7], v[94:95]
	v_max_f32_e64 v6, |v82|, |v83|
	v_max3_f32 v98, |v84|, |v85|, v6
	v_mbcnt_lo_u32_b32 v6, -1, 0
	v_mbcnt_hi_u32_b32 v6, -1, v6
	s_nop 0
	v_ashrrev_i32_e32 v7, 31, v6
	v_lshl_add_u64 v[6:7], v[6:7], 4, s[12:13]
	v_add_co_u32_e32 v6, vcc, s23, v6
	s_nop 1
	v_addc_co_u32_e32 v7, vcc, 0, v7, vcc
	global_load_dwordx4 v[90:93], v[6:7], off offset:1024
	v_mbcnt_lo_u32_b32 v6, -1, 0
	v_mbcnt_hi_u32_b32 v6, -1, v6
	s_nop 0
	v_ashrrev_i32_e32 v7, 31, v6
	v_lshl_add_u64 v[6:7], v[6:7], 4, s[14:15]
	v_add_co_u32_e32 v6, vcc, s23, v6
	s_nop 1
	v_addc_co_u32_e32 v7, vcc, 0, v7, vcc
	global_load_dwordx4 v[94:97], v[6:7], off offset:1024
	v_pk_mul_f32 v[6:7], v[88:89], v[32:33] op_sel_hi:[1,0]
	s_waitcnt vmcnt(0)
; #define GAS __attribute__((address_space(1)))
; #define FLANE lane_id()
; __device__ __forceinline__ void p6_router(Frame& F) {
;     ...
;                 for (int j = 0; j < 8; ++j) { const f32x4 g = *((const GAS f32x4*)F.ln1_g + FLANE + 64 * j), b = *((const GAS f32x4*)F.ln1_b + FLANE + 64 * j);
;                     v[j] = v[j] * rstd * g + b; am = fmaxf(am, fmaxf(fmaxf(fabsf(v[j][0]), fabsf(v[j][1])), fmaxf(fabsf(v[j][2]), fabsf(v[j][3])))); }
; #pragma unroll
;                 for (int o = 1; o < 64; o <<= 1) am = fmaxf(am, __shfl_xor(am, o));
;                 const float sc = am > 0.f ? am * (1.f / 127.f) : 1.f, inv = 1.f / sc;
; #pragma unroll
;                 for (int j = 0; j < 8; ++j) { const int q0 = (int)__builtin_rintf(v[j][0] * inv), q1 = (int)__builtin_rintf(v[j][1] * inv), q2 = (int)__builtin_rintf(v[j][2] * inv), q3 = (int)__builtin_rintf(v[j][3] * inv);
;                     h1q[(size_t)m * (D / 4) + FLANE + 64 * j] = (unsigned)(q0 & 0xff) | ((unsigned)(q1 & 0xff) << 8) | ((unsigned)(q2 & 0xff) << 16) | ((unsigned)(q3 & 0xff) << 24); }
	v_pk_fma_f32 v[88:89], v[90:91], v[4:5], v[94:95]
	v_pk_fma_f32 v[86:87], v[92:93], v[6:7], v[96:97]
	s_nop 0
	v_max_f32_e64 v4, |v86|, |v87|
	v_max3_f32 v4, |v88|, |v89|, v4
	v_max3_f32 v96, v62, v98, v4
	v_mbcnt_lo_u32_b32 v4, -1, 0
	v_mbcnt_hi_u32_b32 v4, -1, v4
	v_mov_b32_e32 v62, v65
	v_ashrrev_i32_e32 v5, 31, v4
	v_lshl_add_u64 v[4:5], v[4:5], 4, s[12:13]
	v_add_co_u32_e32 v4, vcc, s23, v4
	v_pk_mul_f32 v[62:63], v[62:63], v[32:33] op_sel_hi:[1,0]
	s_nop 0
	v_addc_co_u32_e32 v5, vcc, 0, v5, vcc
	global_load_dwordx4 v[4:7], v[4:5], off offset:2048
	v_mbcnt_lo_u32_b32 v90, -1, 0
	v_mbcnt_hi_u32_b32 v90, -1, v90
	s_nop 0
	v_ashrrev_i32_e32 v91, 31, v90
	v_lshl_add_u64 v[90:91], v[90:91], 4, s[14:15]
	v_add_co_u32_e32 v90, vcc, s23, v90
	s_nop 1
	v_addc_co_u32_e32 v91, vcc, 0, v91, vcc
	global_load_dwordx4 v[92:95], v[90:91], off offset:2048
	s_waitcnt vmcnt(0)
	v_pk_fma_f32 v[90:91], v[2:3], v[6:7], v[94:95]
	v_pk_fma_f32 v[92:93], v[0:1], v[4:5], v[92:93]
	v_max_f32_e64 v0, |v90|, |v91|
	v_max3_f32 v94, |v92|, |v93|, v0
	v_mbcnt_lo_u32_b32 v0, -1, 0
	v_mbcnt_hi_u32_b32 v0, -1, v0
	s_nop 0
	v_ashrrev_i32_e32 v1, 31, v0
	v_lshl_add_u64 v[0:1], v[0:1], 4, s[12:13]
	v_add_co_u32_e32 v0, vcc, s23, v0
	s_nop 1
	v_addc_co_u32_e32 v1, vcc, 0, v1, vcc
	global_load_dwordx4 v[0:3], v[0:1], off offset:3072
	v_mbcnt_lo_u32_b32 v4, -1, 0
	v_mbcnt_hi_u32_b32 v4, -1, v4
	s_nop 0
	v_ashrrev_i32_e32 v5, 31, v4
	v_lshl_add_u64 v[4:5], v[4:5], 4, s[14:15]
	v_add_co_u32_e32 v4, vcc, s23, v4
	s_nop 1
	v_addc_co_u32_e32 v5, vcc, 0, v5, vcc
	global_load_dwordx4 v[4:7], v[4:5], off offset:3072
	s_waitcnt vmcnt(0)
	v_pk_fma_f32 v[2:3], v[62:63], v[2:3], v[6:7]
	v_pk_fma_f32 v[4:5], v[66:67], v[0:1], v[4:5]
	v_max_f32_e64 v0, |v2|, |v3|
	v_max3_f32 v0, |v4|, |v5|, v0
	v_max3_f32 v0, v96, v94, v0
	s_waitcnt lgkmcnt(0)
	s_nop 1
	v_max_f32_dpp v0, v0, v0 quad_perm:[1,0,3,2] row_mask:0xf bank_mask:0xf
	s_waitcnt lgkmcnt(0)
	s_nop 1
	v_max_f32_dpp v0, v0, v0 quad_perm:[2,3,0,1] row_mask:0xf bank_mask:0xf
	s_waitcnt lgkmcnt(0)
	s_nop 1
	v_max_f32_dpp v0, v0, v0 row_half_mirror row_mask:0xf bank_mask:0xf
	s_waitcnt lgkmcnt(0)
	s_nop 1
	v_max_f32_dpp v0, v0, v0 row_mirror row_mask:0xf bank_mask:0xf
	s_waitcnt lgkmcnt(0)
	v_mov_b32_e32 v1, v0
	s_nop 1
	v_permlane16_swap_b32_e32 v0, v1
	v_max_f32_e32 v0, v0, v1
	s_waitcnt lgkmcnt(0)
	v_mov_b32_e32 v1, v0
	s_nop 1
	v_permlane32_swap_b32_e32 v0, v1
	v_max_f32_e32 v0, v0, v1
	v_cmp_lt_f32_e32 vcc, 0, v0
	v_mul_f32_e32 v0, 0x3c010204, v0
	s_nop 0
	v_cndmask_b32_e32 v0, 1.0, v0, vcc
	v_div_scale_f32 v1, s[6:7], v0, v0, 1.0
	v_rcp_f32_e32 v6, v1
	s_lshl_b64 s[6:7], s[4:5], 11
	s_add_u32 s6, s3, s6
	s_addc_u32 s7, s24, s7
	v_fma_f32 v7, -v1, v6, 1.0
	v_fmac_f32_e32 v6, v7, v6
	v_div_scale_f32 v7, vcc, 1.0, v0, 1.0
	v_mul_f32_e32 v62, v7, v6
	v_fma_f32 v63, -v1, v62, v7
	v_fmac_f32_e32 v62, v63, v6
	v_fma_f32 v1, -v1, v62, v7
	v_div_fmas_f32 v1, v1, v6, v62
	v_div_fixup_f32 v1, v1, v0, 1.0
	v_mul_f32_e32 v7, v69, v1
	v_mul_f32_e32 v6, v68, v1
	v_rndne_f32_e32 v7, v7
	v_mul_f32_e32 v60, v60, v1
	v_mul_f32_e32 v61, v61, v1
	v_rndne_f32_e32 v6, v6
	v_cvt_i32_f32_e32 v7, v7
	v_rndne_f32_e32 v60, v60
	v_rndne_f32_e32 v61, v61
	v_cvt_i32_f32_e32 v6, v6
	v_cvt_i32_f32_sdwa v60, v60 dst_sel:WORD_1 dst_unused:UNUSED_PAD src0_sel:DWORD
	v_cvt_i32_f32_e32 v61, v61
	v_lshlrev_b32_e32 v7, 8, v7
	v_and_b32_e32 v7, 0xff00, v7
	v_and_b32_e32 v60, 0xff0000, v60
	v_perm_b32 v6, v61, v6, s1
	v_or3_b32 v60, v6, v7, v60
	v_mbcnt_lo_u32_b32 v6, -1, 0
	v_mbcnt_hi_u32_b32 v6, -1, v6
	v_mul_f32_e32 v61, v71, v1
	v_ashrrev_i32_e32 v7, 31, v6
	v_lshl_add_u64 v[6:7], v[6:7], 2, s[6:7]
	global_store_dword v[6:7], v60, off
	v_mul_f32_e32 v7, v73, v1
	v_mul_f32_e32 v6, v72, v1
	v_rndne_f32_e32 v7, v7
	v_mul_f32_e32 v60, v70, v1
	v_rndne_f32_e32 v6, v6
	v_cvt_i32_f32_e32 v7, v7
	v_rndne_f32_e32 v60, v60
	v_rndne_f32_e32 v61, v61
	v_cvt_i32_f32_e32 v6, v6
	v_cvt_i32_f32_sdwa v60, v60 dst_sel:WORD_1 dst_unused:UNUSED_PAD src0_sel:DWORD
	v_cvt_i32_f32_e32 v61, v61
	v_lshlrev_b32_e32 v7, 8, v7
	v_and_b32_e32 v7, 0xff00, v7
	v_and_b32_e32 v60, 0xff0000, v60
	v_perm_b32 v6, v61, v6, s1
	v_or3_b32 v60, v6, v7, v60
	v_mbcnt_lo_u32_b32 v6, -1, 0
	v_mbcnt_hi_u32_b32 v6, -1, v6
	v_mul_f32_e32 v61, v75, v1
	v_ashrrev_i32_e32 v7, 31, v6
	v_lshl_add_u64 v[6:7], v[6:7], 2, s[6:7]
	global_store_dword v[6:7], v60, off offset:256
	v_mul_f32_e32 v7, v77, v1
	v_mul_f32_e32 v6, v76, v1
	v_rndne_f32_e32 v7, v7
	v_mul_f32_e32 v60, v74, v1
	v_rndne_f32_e32 v6, v6
	v_cvt_i32_f32_e32 v7, v7
	v_rndne_f32_e32 v60, v60
	v_rndne_f32_e32 v61, v61
	v_cvt_i32_f32_e32 v6, v6
	v_cvt_i32_f32_sdwa v60, v60 dst_sel:WORD_1 dst_unused:UNUSED_PAD src0_sel:DWORD
	v_cvt_i32_f32_e32 v61, v61
	v_lshlrev_b32_e32 v7, 8, v7
	v_and_b32_e32 v7, 0xff00, v7
	v_and_b32_e32 v60, 0xff0000, v60
	v_perm_b32 v6, v61, v6, s1
	v_or3_b32 v60, v6, v7, v60
	v_mbcnt_lo_u32_b32 v6, -1, 0
	v_mbcnt_hi_u32_b32 v6, -1, v6
	v_mul_f32_e32 v61, v79, v1
	v_ashrrev_i32_e32 v7, 31, v6
	v_lshl_add_u64 v[6:7], v[6:7], 2, s[6:7]
	global_store_dword v[6:7], v60, off offset:512
	v_mul_f32_e32 v7, v81, v1
	v_mul_f32_e32 v6, v80, v1
	v_rndne_f32_e32 v7, v7
	v_mul_f32_e32 v60, v78, v1
	v_rndne_f32_e32 v6, v6
	v_cvt_i32_f32_e32 v7, v7
	v_rndne_f32_e32 v60, v60
	v_rndne_f32_e32 v61, v61
	v_cvt_i32_f32_e32 v6, v6
	v_cvt_i32_f32_sdwa v60, v60 dst_sel:WORD_1 dst_unused:UNUSED_PAD src0_sel:DWORD
	v_cvt_i32_f32_e32 v61, v61
	v_lshlrev_b32_e32 v7, 8, v7
	v_and_b32_e32 v7, 0xff00, v7
	v_and_b32_e32 v60, 0xff0000, v60
	v_perm_b32 v6, v61, v6, s1
	v_or3_b32 v60, v6, v7, v60
	v_mbcnt_lo_u32_b32 v6, -1, 0
	v_mbcnt_hi_u32_b32 v6, -1, v6
; #define FLANE lane_id()
; __device__ __forceinline__ void p6_router(Frame& F) {
;     ...
;                 for (int j = 0; j < 8; ++j) { const v2u w = raw[rr][j]; v[j] = (f32x4){bf_lo(w.x), bf_hi(w.x), bf_lo(w.y), bf_hi(w.y)}; s += (v[j][0] + v[j][1]) + (v[j][2] + v[j][3]); }
;                 const float mean = wave_sum(s) * (1.f / D); float s2 = 0.f;
;     ...
;                 for (int j = 0; j < 8; ++j) { const int q0 = (int)__builtin_rintf(v[j][0] * inv), q1 = (int)__builtin_rintf(v[j][1] * inv), q2 = (int)__builtin_rintf(v[j][2] * inv), q3 = (int)__builtin_rintf(v[j][3] * inv);
;                     h1q[(size_t)m * (D / 4) + FLANE + 64 * j] = (unsigned)(q0 & 0xff) | ((unsigned)(q1 & 0xff) << 8) | ((unsigned)(q2 & 0xff) << 16) | ((unsigned)(q3 & 0xff) << 24); }
;                 if (FLANE == 0) { st1[2 * m] = mean; st1[2 * m + 1] = rstd; stl[2 * row] = mean; stl[2 * row + 1] = rstd; sxg[m] = sc; sxl[row] = sc; }
	v_mul_f32_e32 v61, v83, v1
	v_ashrrev_i32_e32 v7, 31, v6
	v_lshl_add_u64 v[6:7], v[6:7], 2, s[6:7]
	global_store_dword v[6:7], v60, off offset:768
	v_mul_f32_e32 v7, v85, v1
	v_mul_f32_e32 v6, v84, v1
	v_rndne_f32_e32 v7, v7
	v_mul_f32_e32 v60, v82, v1
	v_rndne_f32_e32 v6, v6
	v_cvt_i32_f32_e32 v7, v7
	v_rndne_f32_e32 v60, v60
	v_rndne_f32_e32 v61, v61
	v_cvt_i32_f32_e32 v6, v6
	v_cvt_i32_f32_sdwa v60, v60 dst_sel:WORD_1 dst_unused:UNUSED_PAD src0_sel:DWORD
	v_cvt_i32_f32_e32 v61, v61
	v_lshlrev_b32_e32 v7, 8, v7
	v_and_b32_e32 v7, 0xff00, v7
	v_and_b32_e32 v60, 0xff0000, v60
	v_perm_b32 v6, v61, v6, s1
	v_or3_b32 v60, v6, v7, v60
	v_mbcnt_lo_u32_b32 v6, -1, 0
	v_mbcnt_hi_u32_b32 v6, -1, v6
	v_mul_f32_e32 v61, v87, v1
	v_ashrrev_i32_e32 v7, 31, v6
	v_lshl_add_u64 v[6:7], v[6:7], 2, s[6:7]
	global_store_dword v[6:7], v60, off offset:1024
	v_mul_f32_e32 v7, v89, v1
	v_mul_f32_e32 v6, v88, v1
	v_rndne_f32_e32 v7, v7
	v_mul_f32_e32 v60, v86, v1
	v_rndne_f32_e32 v6, v6
	v_cvt_i32_f32_e32 v7, v7
	v_rndne_f32_e32 v60, v60
	v_rndne_f32_e32 v61, v61
	v_cvt_i32_f32_e32 v6, v6
	v_cvt_i32_f32_sdwa v60, v60 dst_sel:WORD_1 dst_unused:UNUSED_PAD src0_sel:DWORD
	v_cvt_i32_f32_e32 v61, v61
	v_lshlrev_b32_e32 v7, 8, v7
	v_and_b32_e32 v7, 0xff00, v7
	v_and_b32_e32 v60, 0xff0000, v60
	v_perm_b32 v6, v61, v6, s1
	v_or3_b32 v60, v6, v7, v60
	v_mbcnt_lo_u32_b32 v6, -1, 0
	v_mbcnt_hi_u32_b32 v6, -1, v6
	v_mul_f32_e32 v61, v91, v1
	v_ashrrev_i32_e32 v7, 31, v6
	v_lshl_add_u64 v[6:7], v[6:7], 2, s[6:7]
	global_store_dword v[6:7], v60, off offset:1280
	v_mul_f32_e32 v7, v93, v1
	v_mul_f32_e32 v6, v92, v1
	v_rndne_f32_e32 v7, v7
	v_mul_f32_e32 v60, v90, v1
	v_rndne_f32_e32 v6, v6
	v_cvt_i32_f32_e32 v7, v7
	v_rndne_f32_e32 v60, v60
	v_rndne_f32_e32 v61, v61
	v_mul_f32_e32 v5, v5, v1
	v_cvt_i32_f32_e32 v6, v6
	v_cvt_i32_f32_sdwa v60, v60 dst_sel:WORD_1 dst_unused:UNUSED_PAD src0_sel:DWORD
	v_cvt_i32_f32_e32 v61, v61
	v_mul_f32_e32 v4, v4, v1
	v_rndne_f32_e32 v5, v5
	v_mul_f32_e32 v2, v2, v1
	v_mul_f32_e32 v1, v3, v1
	v_rndne_f32_e32 v4, v4
	v_cvt_i32_f32_e32 v5, v5
	v_rndne_f32_e32 v2, v2
	v_rndne_f32_e32 v1, v1
	v_cvt_i32_f32_e32 v4, v4
	v_cvt_i32_f32_sdwa v2, v2 dst_sel:WORD_1 dst_unused:UNUSED_PAD src0_sel:DWORD
	v_cvt_i32_f32_e32 v1, v1
	v_lshlrev_b32_e32 v7, 8, v7
	v_and_b32_e32 v7, 0xff00, v7
	v_and_b32_e32 v60, 0xff0000, v60
	v_perm_b32 v6, v61, v6, s1
	v_or3_b32 v60, v6, v7, v60
	v_mbcnt_lo_u32_b32 v6, -1, 0
	v_mbcnt_hi_u32_b32 v6, -1, v6
	v_lshlrev_b32_e32 v3, 8, v5
	v_ashrrev_i32_e32 v7, 31, v6
	v_lshl_add_u64 v[6:7], v[6:7], 2, s[6:7]
	v_and_b32_e32 v3, 0xff00, v3
	v_and_b32_e32 v2, 0xff0000, v2
	v_perm_b32 v1, v1, v4, s1
	global_store_dword v[6:7], v60, off offset:1536
	v_or3_b32 v1, v1, v3, v2
	v_mbcnt_lo_u32_b32 v2, -1, 0
	v_mbcnt_hi_u32_b32 v2, -1, v2
	s_nop 0
	v_ashrrev_i32_e32 v3, 31, v2
	v_lshl_add_u64 v[2:3], v[2:3], 2, s[6:7]
	global_store_dword v[2:3], v1, off offset:1792
	v_mbcnt_lo_u32_b32 v1, -1, 0
	v_mbcnt_hi_u32_b32 v1, -1, v1
	s_nop 0
	v_cmp_eq_u32_e32 vcc, 0, v1
	s_and_saveexec_b64 s[6:7], vcc
	s_cbranch_execz .LBB0_1491
	s_lshl_b32 s8, s4, 1
	s_ashr_i32 s9, s8, 31
	s_lshl_b64 s[8:9], s[8:9], 2
	s_add_u32 s8, s27, s8
	s_addc_u32 s9, s64, s9
	v_readlane_b32 s0, v255, 45
	s_lshl_b64 s[4:5], s[4:5], 2
	v_mul_f32_e32 v2, 0x3a000000, v64
	v_mov_b32_e32 v3, v32
	v_mov_b32_e32 v1, s0
	s_add_u32 s4, s25, s4
	v_readlane_b32 s0, v255, 32
	ds_write_b64 v1, v[2:3]
	s_addc_u32 s5, s26, s5
	v_mov_b32_e32 v1, s0
	global_store_dwordx2 v33, v[2:3], s[8:9]
	global_store_dword v33, v0, s[4:5]
	ds_write_b32 v1, v0
.LBB0_1491:
	s_or_b64 exec, exec, s[6:7]
	v_lshlrev_b32_e32 v61, 16, v58
	v_lshlrev_b32_e32 v60, 16, v56
	v_and_b32_e32 v73, 0xffff0000, v58
	v_and_b32_e32 v72, 0xffff0000, v56
	v_lshlrev_b32_e32 v75, 16, v59
	v_lshlrev_b32_e32 v74, 16, v57
	v_and_b32_e32 v77, 0xffff0000, v59
	v_and_b32_e32 v76, 0xffff0000, v57
	v_pk_add_f32 v[0:1], v[60:61], v[72:73]
	v_pk_add_f32 v[2:3], v[74:75], v[76:77]
	v_lshlrev_b32_e32 v59, 16, v55
	v_pk_add_f32 v[0:1], v[0:1], v[2:3]
	v_lshlrev_b32_e32 v58, 16, v54
	v_add_f32_e32 v0, 0, v0
	v_and_b32_e32 v79, 0xffff0000, v55
	v_and_b32_e32 v78, 0xffff0000, v54
	v_add_f32_e32 v6, v0, v1
	v_pk_add_f32 v[0:1], v[58:59], v[78:79]
	v_lshlrev_b32_e32 v62, 16, v52
	v_and_b32_e32 v63, 0xffff0000, v52
	v_lshlrev_b32_e32 v64, 16, v53
	v_and_b32_e32 v65, 0xffff0000, v53
	v_and_b32_e32 v71, 0xffff0000, v50
	v_pk_add_f32 v[0:1], v[0:1], v[0:1] op_sel:[0,1] op_sel_hi:[1,0]
	v_add_f32_e32 v68, v62, v63
	v_add_f32_e32 v66, v64, v65
	v_lshlrev_b32_e32 v7, 16, v50
	v_lshlrev_b32_e32 v69, 16, v51
	v_and_b32_e32 v67, 0xffff0000, v51
	v_mov_b32_e32 v1, v71
	v_pk_add_f32 v[0:1], v[6:7], v[0:1]
	v_pk_add_f32 v[2:3], v[68:69], v[66:67]
	v_lshlrev_b32_e32 v5, 16, v49
	v_lshlrev_b32_e32 v4, 16, v48
	v_and_b32_e32 v81, 0xffff0000, v49
	v_and_b32_e32 v80, 0xffff0000, v48
	v_pk_add_f32 v[52:53], v[0:1], v[2:3]
	v_pk_add_f32 v[54:55], v[4:5], v[80:81]
	v_lshlrev_b32_e32 v0, 16, v46
	v_and_b32_e32 v1, 0xffff0000, v46
	v_lshlrev_b32_e32 v2, 16, v47
	v_and_b32_e32 v3, 0xffff0000, v47
	v_lshlrev_b32_e32 v50, 16, v44
	v_and_b32_e32 v51, 0xffff0000, v44
	v_lshlrev_b32_e32 v49, 16, v45
	v_and_b32_e32 v47, 0xffff0000, v45
	v_pk_add_f32 v[44:45], v[52:53], v[52:53] op_sel:[0,1] op_sel_hi:[1,0]
	v_pk_add_f32 v[52:53], v[54:55], v[54:55] op_sel:[0,1] op_sel_hi:[1,0]
	v_add_f32_e32 v48, v0, v1
	v_add_f32_e32 v46, v2, v3
	v_mov_b32_e32 v45, v50
	v_mov_b32_e32 v53, v51
	v_pk_add_f32 v[44:45], v[44:45], v[52:53]
	v_pk_add_f32 v[52:53], v[48:49], v[46:47]
	s_nop 0
	v_pk_add_f32 v[44:45], v[44:45], v[52:53]
	s_nop 0
	v_add_f32_e32 v6, v44, v45
	s_waitcnt lgkmcnt(0)
; __device__ __forceinline__ void p6_router(Frame& F) {
;     ...
;                 const float mean = wave_sum(s) * (1.f / D); float s2 = 0.f;
; #pragma unroll
;                 for (int j = 0; j < 8; ++j) { v[j] = v[j] - mean; s2 += (v[j][0] * v[j][0] + v[j][1] * v[j][1]) + (v[j][2] * v[j][2] + v[j][3] * v[j][3]); }
;                 const float rstd = 1.f / sqrtf(wave_sum(s2) * (1.f / D) + LN_EPS);
	s_nop 1
	v_add_f32_dpp v6, v6, v6 quad_perm:[1,0,3,2] row_mask:0xf bank_mask:0xf
	s_waitcnt lgkmcnt(0)
	s_nop 1
	v_add_f32_dpp v6, v6, v6 quad_perm:[2,3,0,1] row_mask:0xf bank_mask:0xf
	s_waitcnt lgkmcnt(0)
	s_nop 1
	v_add_f32_dpp v6, v6, v6 row_half_mirror row_mask:0xf bank_mask:0xf
	s_waitcnt lgkmcnt(0)
	s_nop 1
	v_add_f32_dpp v6, v6, v6 row_mirror row_mask:0xf bank_mask:0xf
	s_waitcnt lgkmcnt(0)
	v_mov_b32_e32 v32, v6
	s_nop 1
	v_permlane16_swap_b32_e32 v6, v32
	v_add_f32_e32 v6, v6, v32
	s_waitcnt lgkmcnt(0)
	v_mov_b32_e32 v32, v6
	s_nop 1
	v_permlane32_swap_b32_e32 v6, v32
	v_add_f32_e32 v48, v6, v32
	v_fmac_f32_e32 v76, 0xba000000, v48
	v_fmac_f32_e32 v72, 0xba000000, v48
	v_fmac_f32_e32 v77, 0xba000000, v48
	v_fmac_f32_e32 v73, 0xba000000, v48
	v_fmac_f32_e32 v74, 0xba000000, v48
	v_fmac_f32_e32 v60, 0xba000000, v48
	v_fmac_f32_e32 v75, 0xba000000, v48
	v_fmac_f32_e32 v61, 0xba000000, v48
	v_mov_b32_e32 v55, v73
	v_mov_b32_e32 v45, v72
	v_pk_mul_f32 v[52:53], v[72:73], v[72:73]
	v_pk_mul_f32 v[72:73], v[76:77], v[76:77]
	v_mov_b32_e32 v54, v61
	v_mov_b32_e32 v44, v60
	v_pk_fma_f32 v[60:61], v[60:61], v[60:61], v[52:53]
	v_pk_fma_f32 v[72:73], v[74:75], v[74:75], v[72:73]
	v_fmac_f32_e32 v78, 0xba000000, v48
	v_pk_add_f32 v[60:61], v[60:61], v[72:73]
	v_fmac_f32_e32 v79, 0xba000000, v48
	v_fmac_f32_e32 v59, 0xba000000, v48
	v_pk_add_f32 v[72:73], v[60:61], v[60:61] op_sel_hi:[0,1]
	v_fmac_f32_e32 v58, 0xba000000, v48
	v_mov_b32_e32 v60, v59
	v_mov_b32_e32 v61, v79
	v_mov_b32_e32 v59, v78
	v_mov_b32_e32 v56, v75
	v_mov_b32_e32 v57, v77
	v_mov_b32_e32 v52, v74
	v_mov_b32_e32 v53, v76
	v_pk_mul_f32 v[74:75], v[60:61], v[60:61]
	v_pk_mul_f32 v[76:77], v[58:59], v[58:59]
	v_fmac_f32_e32 v62, 0xba000000, v48
	v_pk_mov_b32 v[78:79], v[76:77], v[74:75] op_sel:[1,0]
	v_mov_b32_e32 v77, v75
	v_fmac_f32_e32 v63, 0xba000000, v48
	v_fmac_f32_e32 v64, 0xba000000, v48
	v_mul_f32_e32 v6, v62, v62
	v_pk_add_f32 v[74:75], v[78:79], v[76:77]
	v_fmac_f32_e32 v65, 0xba000000, v48
	v_pk_fma_f32 v[76:77], v[62:63], v[62:63], v[6:7] op_sel_hi:[1,1,0]
	v_mul_f32_e32 v6, v64, v64
	v_pk_add_f32 v[74:75], v[74:75], v[74:75] op_sel_hi:[0,1]
	v_pk_fma_f32 v[78:79], v[64:65], v[64:65], v[6:7] op_sel_hi:[1,1,0]
	v_fmac_f32_e32 v67, 0xba000000, v48
	v_fmac_f32_e32 v69, 0xba000000, v48
	v_fmac_f32_e32 v71, 0xba000000, v48
	v_fmac_f32_e32 v7, 0xba000000, v48
	v_mul_f32_e32 v76, v7, v7
	v_mul_f32_e32 v78, v71, v71
	v_mul_f32_e32 v74, v69, v69
	v_mul_f32_e32 v72, v67, v67
	v_pk_add_f32 v[76:77], v[76:77], v[78:79]
	v_pk_add_f32 v[72:73], v[74:75], v[72:73]
	v_fmac_f32_e32 v80, 0xba000000, v48
	v_pk_add_f32 v[72:73], v[76:77], v[72:73]
	v_fmac_f32_e32 v81, 0xba000000, v48
	v_fmac_f32_e32 v5, 0xba000000, v48
	v_pk_add_f32 v[74:75], v[72:73], v[72:73] op_sel_hi:[0,1]
	v_fmac_f32_e32 v4, 0xba000000, v48
	v_mov_b32_e32 v72, v5
	v_mov_b32_e32 v73, v81
	v_mov_b32_e32 v5, v80
	v_pk_mul_f32 v[76:77], v[72:73], v[72:73]
	v_pk_mul_f32 v[78:79], v[4:5], v[4:5]
	v_fmac_f32_e32 v0, 0xba000000, v48
	v_pk_mov_b32 v[80:81], v[78:79], v[76:77] op_sel:[1,0]
	v_mov_b32_e32 v79, v77
	v_fmac_f32_e32 v1, 0xba000000, v48
	v_fmac_f32_e32 v2, 0xba000000, v48
	v_mul_f32_e32 v6, v0, v0
	v_pk_add_f32 v[76:77], v[80:81], v[78:79]
	v_fmac_f32_e32 v3, 0xba000000, v48
	v_pk_fma_f32 v[78:79], v[0:1], v[0:1], v[6:7] op_sel_hi:[1,1,0]
	v_mul_f32_e32 v6, v2, v2
	v_pk_add_f32 v[76:77], v[76:77], v[76:77] op_sel_hi:[0,1]
	v_pk_fma_f32 v[80:81], v[2:3], v[2:3], v[6:7] op_sel_hi:[1,1,0]
	v_fmac_f32_e32 v47, 0xba000000, v48
	v_fmac_f32_e32 v49, 0xba000000, v48
	v_fmac_f32_e32 v51, 0xba000000, v48
	v_fmac_f32_e32 v50, 0xba000000, v48
	v_mul_f32_e32 v78, v50, v50
	v_mul_f32_e32 v80, v51, v51
	v_mul_f32_e32 v76, v49, v49
	v_mul_f32_e32 v74, v47, v47
	v_pk_add_f32 v[78:79], v[78:79], v[80:81]
	v_pk_add_f32 v[74:75], v[76:77], v[74:75]
	s_nop 0
	v_pk_add_f32 v[74:75], v[78:79], v[74:75]
	s_nop 0
	v_add_f32_e32 v6, v74, v75
	v_mbcnt_lo_u32_b32 v74, -1, 0
	v_mbcnt_hi_u32_b32 v74, -1, v74
	v_ashrrev_i32_e32 v75, 31, v74
	v_lshl_add_u64 v[74:75], v[74:75], 4, s[12:13]
	global_load_dwordx4 v[74:77], v[74:75], off
	v_mbcnt_lo_u32_b32 v78, -1, 0
	v_mbcnt_hi_u32_b32 v78, -1, v78
	s_waitcnt lgkmcnt(0)
	s_nop 1
	v_add_f32_dpp v6, v6, v6 quad_perm:[1,0,3,2] row_mask:0xf bank_mask:0xf
	v_ashrrev_i32_e32 v79, 31, v78
	v_lshl_add_u64 v[78:79], v[78:79], 4, s[14:15]
	global_load_dwordx4 v[78:81], v[78:79], off
	s_waitcnt lgkmcnt(0)
	s_nop 1
	v_add_f32_dpp v6, v6, v6 quad_perm:[2,3,0,1] row_mask:0xf bank_mask:0xf
	s_waitcnt lgkmcnt(0)
	s_nop 1
	v_add_f32_dpp v6, v6, v6 row_half_mirror row_mask:0xf bank_mask:0xf
	s_waitcnt lgkmcnt(0)
	s_nop 1
	v_add_f32_dpp v6, v6, v6 row_mirror row_mask:0xf bank_mask:0xf
	s_waitcnt lgkmcnt(0)
	v_mov_b32_e32 v32, v6
	s_nop 1
	v_permlane16_swap_b32_e32 v6, v32
	v_add_f32_e32 v6, v6, v32
	s_waitcnt lgkmcnt(0)
	v_mov_b32_e32 v32, v6
	s_nop 1
	v_permlane32_swap_b32_e32 v6, v32
	v_add_f32_e32 v6, v6, v32
	v_fmamk_f32 v6, v6, 0x3a000000, v166
	v_cmp_gt_f32_e32 vcc, s22, v6
	v_mul_f32_e32 v32, 0x4f800000, v6
	s_nop 0
	v_cndmask_b32_e32 v6, v6, v32, vcc
	v_sqrt_f32_e32 v32, v6
	s_nop 0
	v_add_u32_e32 v46, -1, v32
	v_fma_f32 v66, -v46, v32, v6
	v_cmp_ge_f32_e64 s[4:5], 0, v66
	v_add_u32_e32 v66, 1, v32
	s_nop 0
	v_cndmask_b32_e64 v46, v32, v46, s[4:5]
	v_fma_f32 v32, -v66, v32, v6
	v_cmp_lt_f32_e64 s[4:5], 0, v32
	s_nop 1
	v_cndmask_b32_e64 v32, v46, v66, s[4:5]
	v_mul_f32_e32 v46, 0x37800000, v32
	v_cndmask_b32_e32 v32, v32, v46, vcc
	v_cmp_class_f32_e32 vcc, v6, v167
	s_nop 1
	v_cndmask_b32_e32 v6, v32, v6, vcc
	v_div_scale_f32 v32, s[4:5], v6, v6, 1.0
	v_rcp_f32_e32 v46, v32
	s_add_i32 s4, s42, s75
	s_ashr_i32 s5, s4, 31
	v_fma_f32 v66, -v32, v46, 1.0
	v_fmac_f32_e32 v46, v66, v46
	v_div_scale_f32 v66, vcc, 1.0, v6, 1.0
	v_mul_f32_e32 v68, v66, v46
	v_fma_f32 v70, -v32, v68, v66
	v_fmac_f32_e32 v68, v70, v46
	v_fma_f32 v32, -v32, v68, v66
	v_div_fmas_f32 v32, v32, v46, v68
	v_div_fixup_f32 v32, v32, v6, 1.0
	v_pk_mul_f32 v[82:83], v[44:45], v[32:33] op_sel_hi:[1,0]
	v_pk_mul_f32 v[44:45], v[52:53], v[32:33] op_sel_hi:[1,0]
	v_mov_b32_e32 v70, v7
	v_pk_mul_f32 v[4:5], v[4:5], v[32:33] op_sel_hi:[1,0]
	v_pk_mul_f32 v[2:3], v[2:3], v[32:33] op_sel_hi:[1,0]
	v_pk_mul_f32 v[0:1], v[0:1], v[32:33] op_sel_hi:[1,0]
	v_pk_mul_f32 v[50:51], v[50:51], v[32:33] op_sel_hi:[1,0]
	s_waitcnt vmcnt(0)
; #define GAS __attribute__((address_space(1)))
; #define FLANE lane_id()
; __device__ __forceinline__ void p6_router(Frame& F) {
;     ...
;                 for (int j = 0; j < 8; ++j) { const f32x4 g = *((const GAS f32x4*)F.ln1_g + FLANE + 64 * j), b = *((const GAS f32x4*)F.ln1_b + FLANE + 64 * j);
;                     v[j] = v[j] * rstd * g + b; am = fmaxf(am, fmaxf(fmaxf(fabsf(v[j][0]), fabsf(v[j][1])), fmaxf(fabsf(v[j][2]), fabsf(v[j][3])))); }
; #pragma unroll
;                 for (int o = 1; o < 64; o <<= 1) am = fmaxf(am, __shfl_xor(am, o));
	v_pk_fma_f32 v[52:53], v[74:75], v[82:83], v[78:79]
	v_mbcnt_lo_u32_b32 v74, -1, 0
	v_mbcnt_hi_u32_b32 v74, -1, v74
	v_pk_fma_f32 v[44:45], v[76:77], v[44:45], v[80:81]
	v_ashrrev_i32_e32 v75, 31, v74
	v_lshl_add_u64 v[74:75], v[74:75], 4, s[12:13]
	global_load_dwordx4 v[74:77], v[74:75], off offset:1024
	v_mbcnt_lo_u32_b32 v78, -1, 0
	v_mbcnt_hi_u32_b32 v78, -1, v78
	v_pk_mul_f32 v[82:83], v[54:55], v[32:33] op_sel_hi:[1,0]
	v_ashrrev_i32_e32 v79, 31, v78
	v_lshl_add_u64 v[78:79], v[78:79], 4, s[14:15]
	global_load_dwordx4 v[78:81], v[78:79], off offset:1024
	v_pk_mul_f32 v[54:55], v[56:57], v[32:33] op_sel_hi:[1,0]
	v_max_f32_e64 v6, |v44|, |v45|
	v_max3_f32 v6, |v52|, |v53|, v6
	s_waitcnt vmcnt(0)
	v_pk_fma_f32 v[56:57], v[74:75], v[82:83], v[78:79]
	v_mbcnt_lo_u32_b32 v74, -1, 0
	v_mbcnt_hi_u32_b32 v74, -1, v74
	v_pk_fma_f32 v[54:55], v[76:77], v[54:55], v[80:81]
	v_ashrrev_i32_e32 v75, 31, v74
	v_lshl_add_u64 v[74:75], v[74:75], 4, s[12:13]
	global_load_dwordx4 v[74:77], v[74:75], off offset:2048
	v_mbcnt_lo_u32_b32 v78, -1, 0
	v_mbcnt_hi_u32_b32 v78, -1, v78
	v_pk_mul_f32 v[82:83], v[58:59], v[32:33] op_sel_hi:[1,0]
	v_ashrrev_i32_e32 v79, 31, v78
	v_lshl_add_u64 v[78:79], v[78:79], 4, s[14:15]
	global_load_dwordx4 v[78:81], v[78:79], off offset:2048
	v_pk_mul_f32 v[58:59], v[60:61], v[32:33] op_sel_hi:[1,0]
	v_max_f32_e64 v46, |v54|, |v55|
	v_max3_f32 v46, |v56|, |v57|, v46
	v_max3_f32 v6, v6, 0, v46
	s_waitcnt vmcnt(0)
	v_pk_fma_f32 v[60:61], v[74:75], v[82:83], v[78:79]
	v_mbcnt_lo_u32_b32 v74, -1, 0
	v_mbcnt_hi_u32_b32 v74, -1, v74
	v_pk_fma_f32 v[58:59], v[76:77], v[58:59], v[80:81]
	v_ashrrev_i32_e32 v75, 31, v74
	v_lshl_add_u64 v[74:75], v[74:75], 4, s[12:13]
	global_load_dwordx4 v[74:77], v[74:75], off offset:3072
	v_mbcnt_lo_u32_b32 v78, -1, 0
	v_mbcnt_hi_u32_b32 v78, -1, v78
	v_pk_mul_f32 v[82:83], v[62:63], v[32:33] op_sel_hi:[1,0]
	v_ashrrev_i32_e32 v79, 31, v78
	v_lshl_add_u64 v[78:79], v[78:79], 4, s[14:15]
	global_load_dwordx4 v[78:81], v[78:79], off offset:3072
	v_pk_mul_f32 v[62:63], v[64:65], v[32:33] op_sel_hi:[1,0]
	v_max_f32_e64 v46, |v58|, |v59|
	v_max3_f32 v46, |v60|, |v61|, v46
	s_waitcnt vmcnt(0)
	v_pk_fma_f32 v[64:65], v[74:75], v[82:83], v[78:79]
	v_mbcnt_lo_u32_b32 v74, -1, 0
	v_mbcnt_hi_u32_b32 v74, -1, v74
	v_pk_fma_f32 v[62:63], v[76:77], v[62:63], v[80:81]
	v_ashrrev_i32_e32 v75, 31, v74
	v_lshl_add_u64 v[74:75], v[74:75], 4, s[12:13]
	v_add_co_u32_e32 v74, vcc, s23, v74
	v_max_f32_e64 v66, |v62|, |v63|
	s_nop 0
	v_addc_co_u32_e32 v75, vcc, 0, v75, vcc
	global_load_dwordx4 v[74:77], v[74:75], off
	v_mbcnt_lo_u32_b32 v78, -1, 0
	v_mbcnt_hi_u32_b32 v78, -1, v78
	v_max3_f32 v66, |v64|, |v65|, v66
	v_ashrrev_i32_e32 v79, 31, v78
	v_lshl_add_u64 v[78:79], v[78:79], 4, s[14:15]
	v_add_co_u32_e32 v78, vcc, s23, v78
	v_max3_f32 v46, v6, v46, v66
	s_nop 0
	v_addc_co_u32_e32 v79, vcc, 0, v79, vcc
	global_load_dwordx4 v[78:81], v[78:79], off
	v_mov_b32_e32 v66, v69
	v_pk_mul_f32 v[66:67], v[66:67], v[32:33] op_sel_hi:[1,0]
	v_pk_mul_f32 v[6:7], v[70:71], v[32:33] op_sel_hi:[1,0]
	s_waitcnt vmcnt(0)
	v_pk_fma_f32 v[66:67], v[76:77], v[66:67], v[80:81]
	v_pk_fma_f32 v[68:69], v[74:75], v[6:7], v[78:79]
	v_max_f32_e64 v6, |v66|, |v67|
	v_max3_f32 v82, |v68|, |v69|, v6
	v_mbcnt_lo_u32_b32 v6, -1, 0
	v_mbcnt_hi_u32_b32 v6, -1, v6
	s_nop 0
	v_ashrrev_i32_e32 v7, 31, v6
	v_lshl_add_u64 v[6:7], v[6:7], 4, s[12:13]
	v_add_co_u32_e32 v6, vcc, s23, v6
	s_nop 1
	v_addc_co_u32_e32 v7, vcc, 0, v7, vcc
	global_load_dwordx4 v[74:77], v[6:7], off offset:1024
	v_mbcnt_lo_u32_b32 v6, -1, 0
	v_mbcnt_hi_u32_b32 v6, -1, v6
	s_nop 0
	v_ashrrev_i32_e32 v7, 31, v6
	v_lshl_add_u64 v[6:7], v[6:7], 4, s[14:15]
	v_add_co_u32_e32 v6, vcc, s23, v6
	s_nop 1
	v_addc_co_u32_e32 v7, vcc, 0, v7, vcc
	global_load_dwordx4 v[78:81], v[6:7], off offset:1024
	v_pk_mul_f32 v[6:7], v[72:73], v[32:33] op_sel_hi:[1,0]
	s_waitcnt vmcnt(0)
	v_pk_fma_f32 v[72:73], v[74:75], v[4:5], v[78:79]
	v_pk_fma_f32 v[70:71], v[76:77], v[6:7], v[80:81]
	s_nop 0
	v_max_f32_e64 v4, |v70|, |v71|
	v_max3_f32 v4, |v72|, |v73|, v4
	v_max3_f32 v80, v46, v82, v4
	v_mbcnt_lo_u32_b32 v4, -1, 0
	v_mbcnt_hi_u32_b32 v4, -1, v4
	v_mov_b32_e32 v46, v49
	v_ashrrev_i32_e32 v5, 31, v4
	v_lshl_add_u64 v[4:5], v[4:5], 4, s[12:13]
	v_add_co_u32_e32 v4, vcc, s23, v4
	v_pk_mul_f32 v[46:47], v[46:47], v[32:33] op_sel_hi:[1,0]
	s_nop 0
	v_addc_co_u32_e32 v5, vcc, 0, v5, vcc
	global_load_dwordx4 v[4:7], v[4:5], off offset:2048
	v_mbcnt_lo_u32_b32 v74, -1, 0
	v_mbcnt_hi_u32_b32 v74, -1, v74
	s_nop 0
	v_ashrrev_i32_e32 v75, 31, v74
	v_lshl_add_u64 v[74:75], v[74:75], 4, s[14:15]
	v_add_co_u32_e32 v74, vcc, s23, v74
	s_nop 1
	v_addc_co_u32_e32 v75, vcc, 0, v75, vcc
	global_load_dwordx4 v[76:79], v[74:75], off offset:2048
	s_waitcnt vmcnt(0)
	v_pk_fma_f32 v[74:75], v[2:3], v[6:7], v[78:79]
	v_pk_fma_f32 v[76:77], v[0:1], v[4:5], v[76:77]
	v_max_f32_e64 v0, |v74|, |v75|
	v_max3_f32 v78, |v76|, |v77|, v0
	v_mbcnt_lo_u32_b32 v0, -1, 0
	v_mbcnt_hi_u32_b32 v0, -1, v0
	s_nop 0
	v_ashrrev_i32_e32 v1, 31, v0
	v_lshl_add_u64 v[0:1], v[0:1], 4, s[12:13]
	v_add_co_u32_e32 v0, vcc, s23, v0
	s_nop 1
	v_addc_co_u32_e32 v1, vcc, 0, v1, vcc
	global_load_dwordx4 v[0:3], v[0:1], off offset:3072
	v_mbcnt_lo_u32_b32 v4, -1, 0
	v_mbcnt_hi_u32_b32 v4, -1, v4
	s_nop 0
	v_ashrrev_i32_e32 v5, 31, v4
	v_lshl_add_u64 v[4:5], v[4:5], 4, s[14:15]
	v_add_co_u32_e32 v4, vcc, s23, v4
	s_nop 1
	v_addc_co_u32_e32 v5, vcc, 0, v5, vcc
	global_load_dwordx4 v[4:7], v[4:5], off offset:3072
	s_waitcnt vmcnt(0)
	v_pk_fma_f32 v[2:3], v[46:47], v[2:3], v[6:7]
	v_pk_fma_f32 v[4:5], v[50:51], v[0:1], v[4:5]
	v_max_f32_e64 v0, |v2|, |v3|
	v_max3_f32 v0, |v4|, |v5|, v0
	v_max3_f32 v0, v80, v78, v0
	s_waitcnt lgkmcnt(0)
; #define FLANE lane_id()
; __device__ __forceinline__ void p6_router(Frame& F) {
;     ...
;                 for (int o = 1; o < 64; o <<= 1) am = fmaxf(am, __shfl_xor(am, o));
;                 const float sc = am > 0.f ? am * (1.f / 127.f) : 1.f, inv = 1.f / sc;
; #pragma unroll
;                 for (int j = 0; j < 8; ++j) { const int q0 = (int)__builtin_rintf(v[j][0] * inv), q1 = (int)__builtin_rintf(v[j][1] * inv), q2 = (int)__builtin_rintf(v[j][2] * inv), q3 = (int)__builtin_rintf(v[j][3] * inv);
;                     h1q[(size_t)m * (D / 4) + FLANE + 64 * j] = (unsigned)(q0 & 0xff) | ((unsigned)(q1 & 0xff) << 8) | ((unsigned)(q2 & 0xff) << 16) | ((unsigned)(q3 & 0xff) << 24); }
	s_nop 1
	v_max_f32_dpp v0, v0, v0 quad_perm:[1,0,3,2] row_mask:0xf bank_mask:0xf
	s_waitcnt lgkmcnt(0)
	s_nop 1
	v_max_f32_dpp v0, v0, v0 quad_perm:[2,3,0,1] row_mask:0xf bank_mask:0xf
	s_waitcnt lgkmcnt(0)
	s_nop 1
	v_max_f32_dpp v0, v0, v0 row_half_mirror row_mask:0xf bank_mask:0xf
	s_waitcnt lgkmcnt(0)
	s_nop 1
	v_max_f32_dpp v0, v0, v0 row_mirror row_mask:0xf bank_mask:0xf
	s_waitcnt lgkmcnt(0)
	v_mov_b32_e32 v1, v0
	s_nop 1
	v_permlane16_swap_b32_e32 v0, v1
	v_max_f32_e32 v0, v0, v1
	s_waitcnt lgkmcnt(0)
	v_mov_b32_e32 v1, v0
	s_nop 1
	v_permlane32_swap_b32_e32 v0, v1
	v_max_f32_e32 v0, v0, v1
	v_cmp_lt_f32_e32 vcc, 0, v0
	v_mul_f32_e32 v0, 0x3c010204, v0
	s_nop 0
	v_cndmask_b32_e32 v0, 1.0, v0, vcc
	v_div_scale_f32 v1, s[6:7], v0, v0, 1.0
	v_rcp_f32_e32 v6, v1
	s_lshl_b64 s[6:7], s[4:5], 11
	s_add_u32 s6, s3, s6
	s_addc_u32 s7, s24, s7
	v_fma_f32 v7, -v1, v6, 1.0
	v_fmac_f32_e32 v6, v7, v6
	v_div_scale_f32 v7, vcc, 1.0, v0, 1.0
	v_mul_f32_e32 v46, v7, v6
	v_fma_f32 v47, -v1, v46, v7
	v_fmac_f32_e32 v46, v47, v6
	v_fma_f32 v1, -v1, v46, v7
	v_div_fmas_f32 v1, v1, v6, v46
	v_div_fixup_f32 v1, v1, v0, 1.0
	v_mul_f32_e32 v7, v53, v1
	v_mul_f32_e32 v6, v52, v1
	v_rndne_f32_e32 v7, v7
	v_mul_f32_e32 v44, v44, v1
	v_mul_f32_e32 v45, v45, v1
	v_rndne_f32_e32 v6, v6
	v_cvt_i32_f32_e32 v7, v7
	v_rndne_f32_e32 v44, v44
	v_rndne_f32_e32 v45, v45
	v_cvt_i32_f32_e32 v6, v6
	v_cvt_i32_f32_sdwa v44, v44 dst_sel:WORD_1 dst_unused:UNUSED_PAD src0_sel:DWORD
	v_cvt_i32_f32_e32 v45, v45
	v_lshlrev_b32_e32 v7, 8, v7
	v_and_b32_e32 v7, 0xff00, v7
	v_and_b32_e32 v44, 0xff0000, v44
	v_perm_b32 v6, v45, v6, s1
	v_or3_b32 v44, v6, v7, v44
	v_mbcnt_lo_u32_b32 v6, -1, 0
	v_mbcnt_hi_u32_b32 v6, -1, v6
	v_mul_f32_e32 v45, v55, v1
	v_ashrrev_i32_e32 v7, 31, v6
	v_lshl_add_u64 v[6:7], v[6:7], 2, s[6:7]
	global_store_dword v[6:7], v44, off
	v_mul_f32_e32 v7, v57, v1
	v_mul_f32_e32 v6, v56, v1
	v_rndne_f32_e32 v7, v7
	v_mul_f32_e32 v44, v54, v1
	v_rndne_f32_e32 v6, v6
	v_cvt_i32_f32_e32 v7, v7
	v_rndne_f32_e32 v44, v44
	v_rndne_f32_e32 v45, v45
	v_cvt_i32_f32_e32 v6, v6
	v_cvt_i32_f32_sdwa v44, v44 dst_sel:WORD_1 dst_unused:UNUSED_PAD src0_sel:DWORD
	v_cvt_i32_f32_e32 v45, v45
	v_lshlrev_b32_e32 v7, 8, v7
	v_and_b32_e32 v7, 0xff00, v7
	v_and_b32_e32 v44, 0xff0000, v44
	v_perm_b32 v6, v45, v6, s1
	v_or3_b32 v44, v6, v7, v44
	v_mbcnt_lo_u32_b32 v6, -1, 0
	v_mbcnt_hi_u32_b32 v6, -1, v6
	v_mul_f32_e32 v45, v59, v1
	v_ashrrev_i32_e32 v7, 31, v6
	v_lshl_add_u64 v[6:7], v[6:7], 2, s[6:7]
	global_store_dword v[6:7], v44, off offset:256
	v_mul_f32_e32 v7, v61, v1
	v_mul_f32_e32 v6, v60, v1
	v_rndne_f32_e32 v7, v7
	v_mul_f32_e32 v44, v58, v1
	v_rndne_f32_e32 v6, v6
	v_cvt_i32_f32_e32 v7, v7
	v_rndne_f32_e32 v44, v44
	v_rndne_f32_e32 v45, v45
	v_cvt_i32_f32_e32 v6, v6
	v_cvt_i32_f32_sdwa v44, v44 dst_sel:WORD_1 dst_unused:UNUSED_PAD src0_sel:DWORD
	v_cvt_i32_f32_e32 v45, v45
	v_lshlrev_b32_e32 v7, 8, v7
	v_and_b32_e32 v7, 0xff00, v7
	v_and_b32_e32 v44, 0xff0000, v44
	v_perm_b32 v6, v45, v6, s1
	v_or3_b32 v44, v6, v7, v44
	v_mbcnt_lo_u32_b32 v6, -1, 0
	v_mbcnt_hi_u32_b32 v6, -1, v6
	v_mul_f32_e32 v45, v63, v1
	v_ashrrev_i32_e32 v7, 31, v6
	v_lshl_add_u64 v[6:7], v[6:7], 2, s[6:7]
	global_store_dword v[6:7], v44, off offset:512
	v_mul_f32_e32 v7, v65, v1
	v_mul_f32_e32 v6, v64, v1
	v_rndne_f32_e32 v7, v7
	v_mul_f32_e32 v44, v62, v1
	v_rndne_f32_e32 v6, v6
	v_cvt_i32_f32_e32 v7, v7
	v_rndne_f32_e32 v44, v44
	v_rndne_f32_e32 v45, v45
	v_cvt_i32_f32_e32 v6, v6
	v_cvt_i32_f32_sdwa v44, v44 dst_sel:WORD_1 dst_unused:UNUSED_PAD src0_sel:DWORD
	v_cvt_i32_f32_e32 v45, v45
	v_lshlrev_b32_e32 v7, 8, v7
	v_and_b32_e32 v7, 0xff00, v7
	v_and_b32_e32 v44, 0xff0000, v44
	v_perm_b32 v6, v45, v6, s1
	v_or3_b32 v44, v6, v7, v44
	v_mbcnt_lo_u32_b32 v6, -1, 0
	v_mbcnt_hi_u32_b32 v6, -1, v6
	v_mul_f32_e32 v45, v67, v1
	v_ashrrev_i32_e32 v7, 31, v6
	v_lshl_add_u64 v[6:7], v[6:7], 2, s[6:7]
	global_store_dword v[6:7], v44, off offset:768
	v_mul_f32_e32 v7, v69, v1
	v_mul_f32_e32 v6, v68, v1
	v_rndne_f32_e32 v7, v7
	v_mul_f32_e32 v44, v66, v1
	v_rndne_f32_e32 v6, v6
	v_cvt_i32_f32_e32 v7, v7
	v_rndne_f32_e32 v44, v44
	v_rndne_f32_e32 v45, v45
	v_cvt_i32_f32_e32 v6, v6
	v_cvt_i32_f32_sdwa v44, v44 dst_sel:WORD_1 dst_unused:UNUSED_PAD src0_sel:DWORD
	v_cvt_i32_f32_e32 v45, v45
	v_lshlrev_b32_e32 v7, 8, v7
	v_and_b32_e32 v7, 0xff00, v7
	v_and_b32_e32 v44, 0xff0000, v44
	v_perm_b32 v6, v45, v6, s1
	v_or3_b32 v44, v6, v7, v44
	v_mbcnt_lo_u32_b32 v6, -1, 0
	v_mbcnt_hi_u32_b32 v6, -1, v6
	v_mul_f32_e32 v45, v71, v1
	v_ashrrev_i32_e32 v7, 31, v6
	v_lshl_add_u64 v[6:7], v[6:7], 2, s[6:7]
	global_store_dword v[6:7], v44, off offset:1024
	v_mul_f32_e32 v7, v73, v1
	v_mul_f32_e32 v6, v72, v1
	v_rndne_f32_e32 v7, v7
	v_mul_f32_e32 v44, v70, v1
	v_rndne_f32_e32 v6, v6
	v_cvt_i32_f32_e32 v7, v7
	v_rndne_f32_e32 v44, v44
	v_rndne_f32_e32 v45, v45
	v_cvt_i32_f32_e32 v6, v6
	v_cvt_i32_f32_sdwa v44, v44 dst_sel:WORD_1 dst_unused:UNUSED_PAD src0_sel:DWORD
	v_cvt_i32_f32_e32 v45, v45
	v_lshlrev_b32_e32 v7, 8, v7
	v_and_b32_e32 v7, 0xff00, v7
	v_and_b32_e32 v44, 0xff0000, v44
	v_perm_b32 v6, v45, v6, s1
	v_or3_b32 v44, v6, v7, v44
	v_mbcnt_lo_u32_b32 v6, -1, 0
	v_mbcnt_hi_u32_b32 v6, -1, v6
	v_mul_f32_e32 v45, v75, v1
	v_ashrrev_i32_e32 v7, 31, v6
	v_lshl_add_u64 v[6:7], v[6:7], 2, s[6:7]
	global_store_dword v[6:7], v44, off offset:1280
	v_mul_f32_e32 v7, v77, v1
	v_mul_f32_e32 v6, v76, v1
	v_rndne_f32_e32 v7, v7
	v_mul_f32_e32 v44, v74, v1
	v_rndne_f32_e32 v6, v6
	v_cvt_i32_f32_e32 v7, v7
	v_rndne_f32_e32 v44, v44
	v_rndne_f32_e32 v45, v45
	v_mul_f32_e32 v5, v5, v1
	v_cvt_i32_f32_e32 v6, v6
	v_cvt_i32_f32_sdwa v44, v44 dst_sel:WORD_1 dst_unused:UNUSED_PAD src0_sel:DWORD
	v_cvt_i32_f32_e32 v45, v45
	v_mul_f32_e32 v4, v4, v1
	v_rndne_f32_e32 v5, v5
	v_mul_f32_e32 v2, v2, v1
	v_mul_f32_e32 v1, v3, v1
	v_rndne_f32_e32 v4, v4
	v_cvt_i32_f32_e32 v5, v5
	v_rndne_f32_e32 v2, v2
	v_rndne_f32_e32 v1, v1
	v_cvt_i32_f32_e32 v4, v4
	v_cvt_i32_f32_sdwa v2, v2 dst_sel:WORD_1 dst_unused:UNUSED_PAD src0_sel:DWORD
	v_cvt_i32_f32_e32 v1, v1
	v_lshlrev_b32_e32 v7, 8, v7
	v_and_b32_e32 v7, 0xff00, v7
	v_and_b32_e32 v44, 0xff0000, v44
	v_perm_b32 v6, v45, v6, s1
	v_or3_b32 v44, v6, v7, v44
	v_mbcnt_lo_u32_b32 v6, -1, 0
	v_mbcnt_hi_u32_b32 v6, -1, v6
	v_lshlrev_b32_e32 v3, 8, v5
	v_ashrrev_i32_e32 v7, 31, v6
	v_lshl_add_u64 v[6:7], v[6:7], 2, s[6:7]
	v_and_b32_e32 v3, 0xff00, v3
	v_and_b32_e32 v2, 0xff0000, v2
	v_perm_b32 v1, v1, v4, s1
	global_store_dword v[6:7], v44, off offset:1536
	v_or3_b32 v1, v1, v3, v2
	v_mbcnt_lo_u32_b32 v2, -1, 0
	v_mbcnt_hi_u32_b32 v2, -1, v2
	s_nop 0
	v_ashrrev_i32_e32 v3, 31, v2
	v_lshl_add_u64 v[2:3], v[2:3], 2, s[6:7]
	global_store_dword v[2:3], v1, off offset:1792
	v_mbcnt_lo_u32_b32 v1, -1, 0
	v_mbcnt_hi_u32_b32 v1, -1, v1
	s_nop 0
	v_cmp_eq_u32_e32 vcc, 0, v1
	s_and_saveexec_b64 s[6:7], vcc
	s_cbranch_execz .LBB0_1493
; #define FLANE lane_id()
; __device__ __forceinline__ void p6_router(Frame& F) {
;     ...
;                 for (int j = 0; j < 8; ++j) { const v2u w = raw[rr][j]; v[j] = (f32x4){bf_lo(w.x), bf_hi(w.x), bf_lo(w.y), bf_hi(w.y)}; s += (v[j][0] + v[j][1]) + (v[j][2] + v[j][3]); }
;                 const float mean = wave_sum(s) * (1.f / D); float s2 = 0.f;
; #pragma unroll
;                 for (int j = 0; j < 8; ++j) { v[j] = v[j] - mean; s2 += (v[j][0] * v[j][0] + v[j][1] * v[j][1]) + (v[j][2] * v[j][2] + v[j][3] * v[j][3]); }
;                 const float rstd = 1.f / sqrtf(wave_sum(s2) * (1.f / D) + LN_EPS);
;     ...
;                 if (FLANE == 0) { st1[2 * m] = mean; st1[2 * m + 1] = rstd; stl[2 * row] = mean; stl[2 * row + 1] = rstd; sxg[m] = sc; sxl[row] = sc; }
	s_lshl_b32 s8, s4, 1
	s_ashr_i32 s9, s8, 31
	s_lshl_b64 s[8:9], s[8:9], 2
	s_add_u32 s8, s27, s8
	s_addc_u32 s9, s64, s9
	v_readlane_b32 s0, v255, 46
	s_lshl_b64 s[4:5], s[4:5], 2
	v_mul_f32_e32 v2, 0x3a000000, v48
	v_mov_b32_e32 v3, v32
	v_mov_b32_e32 v1, s0
	s_add_u32 s4, s25, s4
	v_readlane_b32 s0, v255, 34
	ds_write_b64 v1, v[2:3]
	s_addc_u32 s5, s26, s5
	v_mov_b32_e32 v1, s0
	global_store_dwordx2 v33, v[2:3], s[8:9]
	global_store_dword v33, v0, s[4:5]
	ds_write_b32 v1, v0
.LBB0_1493:
	s_or_b64 exec, exec, s[6:7]
	v_lshlrev_b32_e32 v47, 16, v42
	v_lshlrev_b32_e32 v46, 16, v40
	v_and_b32_e32 v59, 0xffff0000, v42
	v_and_b32_e32 v58, 0xffff0000, v40
	v_lshlrev_b32_e32 v61, 16, v43
	v_lshlrev_b32_e32 v60, 16, v41
	v_and_b32_e32 v63, 0xffff0000, v43
	v_and_b32_e32 v62, 0xffff0000, v41
	v_pk_add_f32 v[0:1], v[46:47], v[58:59]
	v_pk_add_f32 v[2:3], v[60:61], v[62:63]
	v_lshlrev_b32_e32 v45, 16, v39
	v_pk_add_f32 v[0:1], v[0:1], v[2:3]
	v_lshlrev_b32_e32 v44, 16, v38
	v_add_f32_e32 v0, 0, v0
	v_and_b32_e32 v65, 0xffff0000, v39
	v_and_b32_e32 v64, 0xffff0000, v38
	v_add_f32_e32 v6, v0, v1
	v_pk_add_f32 v[0:1], v[44:45], v[64:65]
	v_lshlrev_b32_e32 v48, 16, v36
	v_and_b32_e32 v49, 0xffff0000, v36
	v_lshlrev_b32_e32 v50, 16, v37
	v_and_b32_e32 v51, 0xffff0000, v37
	v_and_b32_e32 v57, 0xffff0000, v30
	v_pk_add_f32 v[0:1], v[0:1], v[0:1] op_sel:[0,1] op_sel_hi:[1,0]
	v_add_f32_e32 v54, v48, v49
	v_add_f32_e32 v52, v50, v51
	v_lshlrev_b32_e32 v7, 16, v30
	v_lshlrev_b32_e32 v55, 16, v31
	v_and_b32_e32 v53, 0xffff0000, v31
	v_mov_b32_e32 v1, v57
	v_pk_add_f32 v[0:1], v[6:7], v[0:1]
	v_pk_add_f32 v[2:3], v[54:55], v[52:53]
	v_lshlrev_b32_e32 v5, 16, v29
	v_lshlrev_b32_e32 v4, 16, v28
	v_and_b32_e32 v67, 0xffff0000, v29
	v_and_b32_e32 v66, 0xffff0000, v28
	v_pk_add_f32 v[36:37], v[0:1], v[2:3]
	v_pk_add_f32 v[38:39], v[4:5], v[66:67]
	v_lshlrev_b32_e32 v0, 16, v26
	v_and_b32_e32 v1, 0xffff0000, v26
	v_lshlrev_b32_e32 v2, 16, v27
	v_and_b32_e32 v3, 0xffff0000, v27
	v_lshlrev_b32_e32 v30, 16, v24
	v_and_b32_e32 v31, 0xffff0000, v24
	v_lshlrev_b32_e32 v29, 16, v25
	v_and_b32_e32 v27, 0xffff0000, v25
	v_pk_add_f32 v[24:25], v[36:37], v[36:37] op_sel:[0,1] op_sel_hi:[1,0]
	v_pk_add_f32 v[36:37], v[38:39], v[38:39] op_sel:[0,1] op_sel_hi:[1,0]
	v_add_f32_e32 v28, v0, v1
	v_add_f32_e32 v26, v2, v3
	v_mov_b32_e32 v25, v30
	v_mov_b32_e32 v37, v31
	v_pk_add_f32 v[24:25], v[24:25], v[36:37]
	v_pk_add_f32 v[36:37], v[28:29], v[26:27]
	s_nop 0
	v_pk_add_f32 v[24:25], v[24:25], v[36:37]
	s_nop 0
	v_add_f32_e32 v6, v24, v25
	s_waitcnt lgkmcnt(0)
	s_nop 1
	v_add_f32_dpp v6, v6, v6 quad_perm:[1,0,3,2] row_mask:0xf bank_mask:0xf
	s_waitcnt lgkmcnt(0)
	s_nop 1
	v_add_f32_dpp v6, v6, v6 quad_perm:[2,3,0,1] row_mask:0xf bank_mask:0xf
	s_waitcnt lgkmcnt(0)
	s_nop 1
	v_add_f32_dpp v6, v6, v6 row_half_mirror row_mask:0xf bank_mask:0xf
	s_waitcnt lgkmcnt(0)
	s_nop 1
	v_add_f32_dpp v6, v6, v6 row_mirror row_mask:0xf bank_mask:0xf
	s_waitcnt lgkmcnt(0)
	v_mov_b32_e32 v24, v6
	s_nop 1
	v_permlane16_swap_b32_e32 v6, v24
	v_add_f32_e32 v6, v6, v24
	s_waitcnt lgkmcnt(0)
	v_mov_b32_e32 v24, v6
	s_nop 1
	v_permlane32_swap_b32_e32 v6, v24
	v_add_f32_e32 v25, v6, v24
	v_fmac_f32_e32 v62, 0xba000000, v25
	v_fmac_f32_e32 v58, 0xba000000, v25
	v_fmac_f32_e32 v63, 0xba000000, v25
	v_fmac_f32_e32 v59, 0xba000000, v25
	v_fmac_f32_e32 v60, 0xba000000, v25
	v_fmac_f32_e32 v46, 0xba000000, v25
	v_fmac_f32_e32 v61, 0xba000000, v25
	v_fmac_f32_e32 v47, 0xba000000, v25
	v_mov_b32_e32 v41, v59
	v_mov_b32_e32 v37, v58
	v_pk_mul_f32 v[38:39], v[58:59], v[58:59]
	v_pk_mul_f32 v[58:59], v[62:63], v[62:63]
	v_mov_b32_e32 v40, v47
	v_mov_b32_e32 v36, v46
	v_pk_fma_f32 v[46:47], v[46:47], v[46:47], v[38:39]
	v_pk_fma_f32 v[58:59], v[60:61], v[60:61], v[58:59]
	v_fmac_f32_e32 v64, 0xba000000, v25
	v_pk_add_f32 v[46:47], v[46:47], v[58:59]
	v_fmac_f32_e32 v65, 0xba000000, v25
	v_fmac_f32_e32 v45, 0xba000000, v25
	v_pk_add_f32 v[58:59], v[46:47], v[46:47] op_sel_hi:[0,1]
	v_fmac_f32_e32 v44, 0xba000000, v25
	v_mov_b32_e32 v46, v45
	v_mov_b32_e32 v47, v65
	v_mov_b32_e32 v45, v64
	v_mov_b32_e32 v42, v61
	v_mov_b32_e32 v43, v63
	v_mov_b32_e32 v38, v60
	v_mov_b32_e32 v39, v62
	v_pk_mul_f32 v[60:61], v[46:47], v[46:47]
	v_pk_mul_f32 v[62:63], v[44:45], v[44:45]
	v_fmac_f32_e32 v48, 0xba000000, v25
	v_pk_mov_b32 v[64:65], v[62:63], v[60:61] op_sel:[1,0]
	v_mov_b32_e32 v63, v61
	v_fmac_f32_e32 v49, 0xba000000, v25
	v_fmac_f32_e32 v50, 0xba000000, v25
	v_mul_f32_e32 v6, v48, v48
	v_pk_add_f32 v[60:61], v[64:65], v[62:63]
	v_fmac_f32_e32 v51, 0xba000000, v25
	v_pk_fma_f32 v[62:63], v[48:49], v[48:49], v[6:7] op_sel_hi:[1,1,0]
	v_mul_f32_e32 v6, v50, v50
	v_pk_add_f32 v[60:61], v[60:61], v[60:61] op_sel_hi:[0,1]
	v_pk_fma_f32 v[64:65], v[50:51], v[50:51], v[6:7] op_sel_hi:[1,1,0]
	v_fmac_f32_e32 v53, 0xba000000, v25
	v_fmac_f32_e32 v55, 0xba000000, v25
	v_fmac_f32_e32 v57, 0xba000000, v25
	v_fmac_f32_e32 v7, 0xba000000, v25
	v_mul_f32_e32 v62, v7, v7
	v_mul_f32_e32 v64, v57, v57
	v_mul_f32_e32 v60, v55, v55
	v_mul_f32_e32 v58, v53, v53
	v_pk_add_f32 v[62:63], v[62:63], v[64:65]
	v_pk_add_f32 v[58:59], v[60:61], v[58:59]
	v_fmac_f32_e32 v66, 0xba000000, v25
	v_pk_add_f32 v[58:59], v[62:63], v[58:59]
	v_fmac_f32_e32 v67, 0xba000000, v25
	v_fmac_f32_e32 v5, 0xba000000, v25
	v_pk_add_f32 v[60:61], v[58:59], v[58:59] op_sel_hi:[0,1]
	v_fmac_f32_e32 v4, 0xba000000, v25
	v_mov_b32_e32 v58, v5
	v_mov_b32_e32 v59, v67
	v_mov_b32_e32 v5, v66
	v_pk_mul_f32 v[62:63], v[58:59], v[58:59]
	v_pk_mul_f32 v[64:65], v[4:5], v[4:5]
	v_fmac_f32_e32 v0, 0xba000000, v25
	v_pk_mov_b32 v[66:67], v[64:65], v[62:63] op_sel:[1,0]
	v_mov_b32_e32 v65, v63
	v_fmac_f32_e32 v1, 0xba000000, v25
	v_fmac_f32_e32 v2, 0xba000000, v25
	v_mul_f32_e32 v6, v0, v0
	v_pk_add_f32 v[62:63], v[66:67], v[64:65]
	v_fmac_f32_e32 v3, 0xba000000, v25
	v_pk_fma_f32 v[64:65], v[0:1], v[0:1], v[6:7] op_sel_hi:[1,1,0]
	v_mul_f32_e32 v6, v2, v2
	v_pk_add_f32 v[62:63], v[62:63], v[62:63] op_sel_hi:[0,1]
	v_pk_fma_f32 v[66:67], v[2:3], v[2:3], v[6:7] op_sel_hi:[1,1,0]
	v_fmac_f32_e32 v27, 0xba000000, v25
	v_fmac_f32_e32 v29, 0xba000000, v25
	v_fmac_f32_e32 v31, 0xba000000, v25
	v_fmac_f32_e32 v30, 0xba000000, v25
	v_mul_f32_e32 v64, v30, v30
	v_mul_f32_e32 v66, v31, v31
	v_mul_f32_e32 v62, v29, v29
	v_mul_f32_e32 v60, v27, v27
	v_pk_add_f32 v[64:65], v[64:65], v[66:67]
	v_pk_add_f32 v[60:61], v[62:63], v[60:61]
	v_mov_b32_e32 v56, v7
	v_pk_add_f32 v[60:61], v[64:65], v[60:61]
	s_nop 0
	v_add_f32_e32 v6, v60, v61
	v_mbcnt_lo_u32_b32 v60, -1, 0
	v_mbcnt_hi_u32_b32 v60, -1, v60
	v_ashrrev_i32_e32 v61, 31, v60
	v_lshl_add_u64 v[60:61], v[60:61], 4, s[12:13]
	global_load_dwordx4 v[60:63], v[60:61], off
	v_mbcnt_lo_u32_b32 v64, -1, 0
	v_mbcnt_hi_u32_b32 v64, -1, v64
	s_waitcnt lgkmcnt(0)
; #define GAS __attribute__((address_space(1)))
; #define FLANE lane_id()
; __device__ __forceinline__ void p6_router(Frame& F) {
;     ...
;                 const float rstd = 1.f / sqrtf(wave_sum(s2) * (1.f / D) + LN_EPS);
;                 float am = 0.f;
; #pragma unroll
;                 for (int j = 0; j < 8; ++j) { const f32x4 g = *((const GAS f32x4*)F.ln1_g + FLANE + 64 * j), b = *((const GAS f32x4*)F.ln1_b + FLANE + 64 * j);
;                     v[j] = v[j] * rstd * g + b; am = fmaxf(am, fmaxf(fmaxf(fabsf(v[j][0]), fabsf(v[j][1])), fmaxf(fabsf(v[j][2]), fabsf(v[j][3])))); }
	s_nop 1
	v_add_f32_dpp v6, v6, v6 quad_perm:[1,0,3,2] row_mask:0xf bank_mask:0xf
	v_ashrrev_i32_e32 v65, 31, v64
	v_lshl_add_u64 v[64:65], v[64:65], 4, s[14:15]
	global_load_dwordx4 v[64:67], v[64:65], off
	s_waitcnt lgkmcnt(0)
	s_nop 1
	v_add_f32_dpp v6, v6, v6 quad_perm:[2,3,0,1] row_mask:0xf bank_mask:0xf
	s_waitcnt lgkmcnt(0)
	s_nop 1
	v_add_f32_dpp v6, v6, v6 row_half_mirror row_mask:0xf bank_mask:0xf
	s_waitcnt lgkmcnt(0)
	s_nop 1
	v_add_f32_dpp v6, v6, v6 row_mirror row_mask:0xf bank_mask:0xf
	s_waitcnt lgkmcnt(0)
	v_mov_b32_e32 v24, v6
	s_nop 1
	v_permlane16_swap_b32_e32 v6, v24
	v_add_f32_e32 v6, v6, v24
	s_waitcnt lgkmcnt(0)
	v_mov_b32_e32 v24, v6
	s_nop 1
	v_permlane32_swap_b32_e32 v6, v24
	v_add_f32_e32 v6, v6, v24
	v_fmamk_f32 v6, v6, 0x3a000000, v166
	v_cmp_gt_f32_e32 vcc, s22, v6
	v_mul_f32_e32 v24, 0x4f800000, v6
	s_nop 0
	v_cndmask_b32_e32 v6, v6, v24, vcc
	v_sqrt_f32_e32 v24, v6
	s_nop 0
	v_add_u32_e32 v26, -1, v24
	v_fma_f32 v28, -v26, v24, v6
	v_cmp_ge_f32_e64 s[4:5], 0, v28
	v_add_u32_e32 v28, 1, v24
	s_nop 0
	v_cndmask_b32_e64 v26, v24, v26, s[4:5]
	v_fma_f32 v24, -v28, v24, v6
	v_cmp_lt_f32_e64 s[4:5], 0, v24
	s_nop 1
	v_cndmask_b32_e64 v24, v26, v28, s[4:5]
	v_mul_f32_e32 v26, 0x37800000, v24
	v_cndmask_b32_e32 v24, v24, v26, vcc
	v_cmp_class_f32_e32 vcc, v6, v167
	s_nop 1
	v_cndmask_b32_e32 v6, v24, v6, vcc
	v_div_scale_f32 v24, s[4:5], v6, v6, 1.0
	v_rcp_f32_e32 v26, v24
	s_add_i32 s4, s42, s77
	s_ashr_i32 s5, s4, 31
	v_fma_f32 v28, -v24, v26, 1.0
	v_fmac_f32_e32 v26, v28, v26
	v_div_scale_f32 v28, vcc, 1.0, v6, 1.0
	v_mul_f32_e32 v32, v28, v26
	v_fma_f32 v52, -v24, v32, v28
	v_fmac_f32_e32 v32, v52, v26
	v_fma_f32 v24, -v24, v32, v28
	v_div_fmas_f32 v24, v24, v26, v32
	v_div_fixup_f32 v24, v24, v6, 1.0
	v_pk_mul_f32 v[68:69], v[36:37], v[24:25] op_sel_hi:[1,0]
	v_pk_mul_f32 v[36:37], v[38:39], v[24:25] op_sel_hi:[1,0]
	v_mov_b32_e32 v52, v55
	v_pk_mul_f32 v[52:53], v[52:53], v[24:25] op_sel_hi:[1,0]
	v_pk_mul_f32 v[4:5], v[4:5], v[24:25] op_sel_hi:[1,0]
	v_pk_mul_f32 v[2:3], v[2:3], v[24:25] op_sel_hi:[1,0]
	v_pk_mul_f32 v[0:1], v[0:1], v[24:25] op_sel_hi:[1,0]
	s_waitcnt vmcnt(0)
	v_pk_fma_f32 v[38:39], v[60:61], v[68:69], v[64:65]
	v_mbcnt_lo_u32_b32 v60, -1, 0
	v_mbcnt_hi_u32_b32 v60, -1, v60
	v_pk_fma_f32 v[36:37], v[62:63], v[36:37], v[66:67]
	v_ashrrev_i32_e32 v61, 31, v60
	v_lshl_add_u64 v[60:61], v[60:61], 4, s[12:13]
	global_load_dwordx4 v[60:63], v[60:61], off offset:1024
	v_mbcnt_lo_u32_b32 v64, -1, 0
	v_mbcnt_hi_u32_b32 v64, -1, v64
	v_pk_mul_f32 v[68:69], v[40:41], v[24:25] op_sel_hi:[1,0]
	v_ashrrev_i32_e32 v65, 31, v64
	v_lshl_add_u64 v[64:65], v[64:65], 4, s[14:15]
	global_load_dwordx4 v[64:67], v[64:65], off offset:1024
	v_pk_mul_f32 v[40:41], v[42:43], v[24:25] op_sel_hi:[1,0]
	v_max_f32_e64 v6, |v36|, |v37|
	v_max3_f32 v6, |v38|, |v39|, v6
	v_pk_mul_f32 v[30:31], v[30:31], v[24:25] op_sel_hi:[1,0]
	s_waitcnt vmcnt(0)
	v_pk_fma_f32 v[42:43], v[60:61], v[68:69], v[64:65]
	v_mbcnt_lo_u32_b32 v60, -1, 0
	v_mbcnt_hi_u32_b32 v60, -1, v60
	v_pk_fma_f32 v[40:41], v[62:63], v[40:41], v[66:67]
	v_ashrrev_i32_e32 v61, 31, v60
	v_lshl_add_u64 v[60:61], v[60:61], 4, s[12:13]
	global_load_dwordx4 v[60:63], v[60:61], off offset:2048
	v_mbcnt_lo_u32_b32 v64, -1, 0
	v_mbcnt_hi_u32_b32 v64, -1, v64
	v_pk_mul_f32 v[68:69], v[44:45], v[24:25] op_sel_hi:[1,0]
	v_ashrrev_i32_e32 v65, 31, v64
	v_lshl_add_u64 v[64:65], v[64:65], 4, s[14:15]
	global_load_dwordx4 v[64:67], v[64:65], off offset:2048
	v_pk_mul_f32 v[44:45], v[46:47], v[24:25] op_sel_hi:[1,0]
	v_max_f32_e64 v26, |v40|, |v41|
	v_max3_f32 v26, |v42|, |v43|, v26
	v_max3_f32 v6, v6, 0, v26
	s_waitcnt vmcnt(0)
	v_pk_fma_f32 v[46:47], v[60:61], v[68:69], v[64:65]
	v_mbcnt_lo_u32_b32 v60, -1, 0
	v_mbcnt_hi_u32_b32 v60, -1, v60
	v_pk_fma_f32 v[44:45], v[62:63], v[44:45], v[66:67]
	v_ashrrev_i32_e32 v61, 31, v60
	v_lshl_add_u64 v[60:61], v[60:61], 4, s[12:13]
	global_load_dwordx4 v[60:63], v[60:61], off offset:3072
	v_mbcnt_lo_u32_b32 v64, -1, 0
	v_mbcnt_hi_u32_b32 v64, -1, v64
	v_pk_mul_f32 v[68:69], v[48:49], v[24:25] op_sel_hi:[1,0]
	v_ashrrev_i32_e32 v65, 31, v64
	v_lshl_add_u64 v[64:65], v[64:65], 4, s[14:15]
	global_load_dwordx4 v[64:67], v[64:65], off offset:3072
	v_pk_mul_f32 v[48:49], v[50:51], v[24:25] op_sel_hi:[1,0]
	v_max_f32_e64 v26, |v44|, |v45|
	v_max3_f32 v26, |v46|, |v47|, v26
	s_waitcnt vmcnt(0)
	v_pk_fma_f32 v[50:51], v[60:61], v[68:69], v[64:65]
	v_mbcnt_lo_u32_b32 v60, -1, 0
	v_mbcnt_hi_u32_b32 v60, -1, v60
	v_pk_fma_f32 v[48:49], v[62:63], v[48:49], v[66:67]
	v_ashrrev_i32_e32 v61, 31, v60
	v_lshl_add_u64 v[60:61], v[60:61], 4, s[12:13]
	v_add_co_u32_e32 v60, vcc, s23, v60
	v_max_f32_e64 v28, |v48|, |v49|
	s_nop 0
	v_addc_co_u32_e32 v61, vcc, 0, v61, vcc
	global_load_dwordx4 v[60:63], v[60:61], off
	v_mbcnt_lo_u32_b32 v64, -1, 0
	v_mbcnt_hi_u32_b32 v64, -1, v64
	v_max3_f32 v28, |v50|, |v51|, v28
	v_ashrrev_i32_e32 v65, 31, v64
	v_lshl_add_u64 v[64:65], v[64:65], 4, s[14:15]
	v_add_co_u32_e32 v64, vcc, s23, v64
	v_max3_f32 v26, v6, v26, v28
	s_nop 0
	v_addc_co_u32_e32 v65, vcc, 0, v65, vcc
	global_load_dwordx4 v[64:67], v[64:65], off
	v_pk_mul_f32 v[6:7], v[56:57], v[24:25] op_sel_hi:[1,0]
	s_waitcnt vmcnt(0)
	v_pk_fma_f32 v[52:53], v[62:63], v[52:53], v[66:67]
	v_pk_fma_f32 v[54:55], v[60:61], v[6:7], v[64:65]
	v_max_f32_e64 v6, |v52|, |v53|
	v_max3_f32 v28, |v54|, |v55|, v6
	v_mbcnt_lo_u32_b32 v6, -1, 0
	v_mbcnt_hi_u32_b32 v6, -1, v6
	s_nop 0
	v_ashrrev_i32_e32 v7, 31, v6
	v_lshl_add_u64 v[6:7], v[6:7], 4, s[12:13]
	v_add_co_u32_e32 v6, vcc, s23, v6
	s_nop 1
	v_addc_co_u32_e32 v7, vcc, 0, v7, vcc
	global_load_dwordx4 v[60:63], v[6:7], off offset:1024
	v_mbcnt_lo_u32_b32 v6, -1, 0
	v_mbcnt_hi_u32_b32 v6, -1, v6
	s_nop 0
	v_ashrrev_i32_e32 v7, 31, v6
	v_lshl_add_u64 v[6:7], v[6:7], 4, s[14:15]
	v_add_co_u32_e32 v6, vcc, s23, v6
	s_nop 1
	v_addc_co_u32_e32 v7, vcc, 0, v7, vcc
	global_load_dwordx4 v[64:67], v[6:7], off offset:1024
	v_pk_mul_f32 v[6:7], v[58:59], v[24:25] op_sel_hi:[1,0]
	s_waitcnt vmcnt(0)
; #define GAS __attribute__((address_space(1)))
; #define FLANE lane_id()
; __device__ __forceinline__ void p6_router(Frame& F) {
;     ...
;                 for (int j = 0; j < 8; ++j) { const f32x4 g = *((const GAS f32x4*)F.ln1_g + FLANE + 64 * j), b = *((const GAS f32x4*)F.ln1_b + FLANE + 64 * j);
;                     v[j] = v[j] * rstd * g + b; am = fmaxf(am, fmaxf(fmaxf(fabsf(v[j][0]), fabsf(v[j][1])), fmaxf(fabsf(v[j][2]), fabsf(v[j][3])))); }
; #pragma unroll
;                 for (int o = 1; o < 64; o <<= 1) am = fmaxf(am, __shfl_xor(am, o));
;                 const float sc = am > 0.f ? am * (1.f / 127.f) : 1.f, inv = 1.f / sc;
; #pragma unroll
;                 for (int j = 0; j < 8; ++j) { const int q0 = (int)__builtin_rintf(v[j][0] * inv), q1 = (int)__builtin_rintf(v[j][1] * inv), q2 = (int)__builtin_rintf(v[j][2] * inv), q3 = (int)__builtin_rintf(v[j][3] * inv);
;                     h1q[(size_t)m * (D / 4) + FLANE + 64 * j] = (unsigned)(q0 & 0xff) | ((unsigned)(q1 & 0xff) << 8) | ((unsigned)(q2 & 0xff) << 16) | ((unsigned)(q3 & 0xff) << 24); }
	v_pk_fma_f32 v[58:59], v[60:61], v[4:5], v[64:65]
	v_pk_fma_f32 v[56:57], v[62:63], v[6:7], v[66:67]
	s_nop 0
	v_max_f32_e64 v4, |v56|, |v57|
	v_max3_f32 v4, |v58|, |v59|, v4
	v_max3_f32 v28, v26, v28, v4
	v_mbcnt_lo_u32_b32 v4, -1, 0
	v_mbcnt_hi_u32_b32 v4, -1, v4
	v_mov_b32_e32 v26, v29
	v_ashrrev_i32_e32 v5, 31, v4
	v_lshl_add_u64 v[4:5], v[4:5], 4, s[12:13]
	v_add_co_u32_e32 v4, vcc, s23, v4
	v_pk_mul_f32 v[26:27], v[26:27], v[24:25] op_sel_hi:[1,0]
	s_nop 0
	v_addc_co_u32_e32 v5, vcc, 0, v5, vcc
	global_load_dwordx4 v[4:7], v[4:5], off offset:2048
	v_mbcnt_lo_u32_b32 v60, -1, 0
	v_mbcnt_hi_u32_b32 v60, -1, v60
	s_nop 0
	v_ashrrev_i32_e32 v61, 31, v60
	v_lshl_add_u64 v[60:61], v[60:61], 4, s[14:15]
	v_add_co_u32_e32 v60, vcc, s23, v60
	s_nop 1
	v_addc_co_u32_e32 v61, vcc, 0, v61, vcc
	global_load_dwordx4 v[62:65], v[60:61], off offset:2048
	s_waitcnt vmcnt(0)
	v_pk_fma_f32 v[60:61], v[2:3], v[6:7], v[64:65]
	v_pk_fma_f32 v[62:63], v[0:1], v[4:5], v[62:63]
	v_max_f32_e64 v0, |v60|, |v61|
	v_max3_f32 v32, |v62|, |v63|, v0
	v_mbcnt_lo_u32_b32 v0, -1, 0
	v_mbcnt_hi_u32_b32 v0, -1, v0
	s_nop 0
	v_ashrrev_i32_e32 v1, 31, v0
	v_lshl_add_u64 v[0:1], v[0:1], 4, s[12:13]
	v_add_co_u32_e32 v0, vcc, s23, v0
	s_nop 1
	v_addc_co_u32_e32 v1, vcc, 0, v1, vcc
	global_load_dwordx4 v[0:3], v[0:1], off offset:3072
	v_mbcnt_lo_u32_b32 v4, -1, 0
	v_mbcnt_hi_u32_b32 v4, -1, v4
	s_nop 0
	v_ashrrev_i32_e32 v5, 31, v4
	v_lshl_add_u64 v[4:5], v[4:5], 4, s[14:15]
	v_add_co_u32_e32 v4, vcc, s23, v4
	s_nop 1
	v_addc_co_u32_e32 v5, vcc, 0, v5, vcc
	global_load_dwordx4 v[4:7], v[4:5], off offset:3072
	s_waitcnt vmcnt(0)
	v_pk_fma_f32 v[2:3], v[26:27], v[2:3], v[6:7]
	v_pk_fma_f32 v[4:5], v[30:31], v[0:1], v[4:5]
	v_max_f32_e64 v0, |v2|, |v3|
	v_max3_f32 v0, |v4|, |v5|, v0
	v_max3_f32 v0, v28, v32, v0
	s_waitcnt lgkmcnt(0)
	s_nop 1
	v_max_f32_dpp v0, v0, v0 quad_perm:[1,0,3,2] row_mask:0xf bank_mask:0xf
	s_waitcnt lgkmcnt(0)
	s_nop 1
	v_max_f32_dpp v0, v0, v0 quad_perm:[2,3,0,1] row_mask:0xf bank_mask:0xf
	s_waitcnt lgkmcnt(0)
	s_nop 1
	v_max_f32_dpp v0, v0, v0 row_half_mirror row_mask:0xf bank_mask:0xf
	s_waitcnt lgkmcnt(0)
	s_nop 1
	v_max_f32_dpp v0, v0, v0 row_mirror row_mask:0xf bank_mask:0xf
	s_waitcnt lgkmcnt(0)
	v_mov_b32_e32 v1, v0
	s_nop 1
	v_permlane16_swap_b32_e32 v0, v1
	v_max_f32_e32 v0, v0, v1
	s_waitcnt lgkmcnt(0)
	v_mov_b32_e32 v1, v0
	s_nop 1
	v_permlane32_swap_b32_e32 v0, v1
	v_max_f32_e32 v0, v0, v1
	v_cmp_lt_f32_e32 vcc, 0, v0
	v_mul_f32_e32 v0, 0x3c010204, v0
	s_nop 0
	v_cndmask_b32_e32 v0, 1.0, v0, vcc
	v_div_scale_f32 v1, s[6:7], v0, v0, 1.0
	v_rcp_f32_e32 v6, v1
	s_lshl_b64 s[6:7], s[4:5], 11
	s_add_u32 s6, s3, s6
	s_addc_u32 s7, s24, s7
	v_fma_f32 v7, -v1, v6, 1.0
	v_fmac_f32_e32 v6, v7, v6
	v_div_scale_f32 v7, vcc, 1.0, v0, 1.0
	v_mul_f32_e32 v26, v7, v6
	v_fma_f32 v27, -v1, v26, v7
	v_fmac_f32_e32 v26, v27, v6
	v_fma_f32 v1, -v1, v26, v7
	v_div_fmas_f32 v1, v1, v6, v26
	v_div_fixup_f32 v1, v1, v0, 1.0
	v_mul_f32_e32 v7, v39, v1
	v_mul_f32_e32 v6, v38, v1
	v_rndne_f32_e32 v7, v7
	v_mul_f32_e32 v26, v36, v1
	v_mul_f32_e32 v27, v37, v1
	v_rndne_f32_e32 v6, v6
	v_cvt_i32_f32_e32 v7, v7
	v_rndne_f32_e32 v26, v26
	v_rndne_f32_e32 v27, v27
	v_cvt_i32_f32_e32 v6, v6
	v_cvt_i32_f32_sdwa v26, v26 dst_sel:WORD_1 dst_unused:UNUSED_PAD src0_sel:DWORD
	v_cvt_i32_f32_e32 v27, v27
	v_lshlrev_b32_e32 v7, 8, v7
	v_and_b32_e32 v7, 0xff00, v7
	v_and_b32_e32 v26, 0xff0000, v26
	v_perm_b32 v6, v27, v6, s1
	v_or3_b32 v26, v6, v7, v26
	v_mbcnt_lo_u32_b32 v6, -1, 0
	v_mbcnt_hi_u32_b32 v6, -1, v6
	v_mul_f32_e32 v27, v41, v1
	v_ashrrev_i32_e32 v7, 31, v6
	v_lshl_add_u64 v[6:7], v[6:7], 2, s[6:7]
	global_store_dword v[6:7], v26, off
	v_mul_f32_e32 v7, v43, v1
	v_mul_f32_e32 v6, v42, v1
	v_rndne_f32_e32 v7, v7
	v_mul_f32_e32 v26, v40, v1
	v_rndne_f32_e32 v6, v6
	v_cvt_i32_f32_e32 v7, v7
	v_rndne_f32_e32 v26, v26
	v_rndne_f32_e32 v27, v27
	v_cvt_i32_f32_e32 v6, v6
	v_cvt_i32_f32_sdwa v26, v26 dst_sel:WORD_1 dst_unused:UNUSED_PAD src0_sel:DWORD
	v_cvt_i32_f32_e32 v27, v27
	v_lshlrev_b32_e32 v7, 8, v7
	v_and_b32_e32 v7, 0xff00, v7
	v_and_b32_e32 v26, 0xff0000, v26
	v_perm_b32 v6, v27, v6, s1
	v_or3_b32 v26, v6, v7, v26
	v_mbcnt_lo_u32_b32 v6, -1, 0
	v_mbcnt_hi_u32_b32 v6, -1, v6
	v_mul_f32_e32 v27, v45, v1
	v_ashrrev_i32_e32 v7, 31, v6
	v_lshl_add_u64 v[6:7], v[6:7], 2, s[6:7]
	global_store_dword v[6:7], v26, off offset:256
	v_mul_f32_e32 v7, v47, v1
	v_mul_f32_e32 v6, v46, v1
	v_rndne_f32_e32 v7, v7
	v_mul_f32_e32 v26, v44, v1
	v_rndne_f32_e32 v6, v6
	v_cvt_i32_f32_e32 v7, v7
	v_rndne_f32_e32 v26, v26
	v_rndne_f32_e32 v27, v27
	v_cvt_i32_f32_e32 v6, v6
	v_cvt_i32_f32_sdwa v26, v26 dst_sel:WORD_1 dst_unused:UNUSED_PAD src0_sel:DWORD
	v_cvt_i32_f32_e32 v27, v27
	v_lshlrev_b32_e32 v7, 8, v7
	v_and_b32_e32 v7, 0xff00, v7
	v_and_b32_e32 v26, 0xff0000, v26
	v_perm_b32 v6, v27, v6, s1
	v_or3_b32 v26, v6, v7, v26
	v_mbcnt_lo_u32_b32 v6, -1, 0
	v_mbcnt_hi_u32_b32 v6, -1, v6
	v_mul_f32_e32 v27, v49, v1
	v_ashrrev_i32_e32 v7, 31, v6
	v_lshl_add_u64 v[6:7], v[6:7], 2, s[6:7]
	global_store_dword v[6:7], v26, off offset:512
	v_mul_f32_e32 v7, v51, v1
	v_mul_f32_e32 v6, v50, v1
	v_rndne_f32_e32 v7, v7
	v_mul_f32_e32 v26, v48, v1
	v_rndne_f32_e32 v6, v6
	v_cvt_i32_f32_e32 v7, v7
	v_rndne_f32_e32 v26, v26
	v_rndne_f32_e32 v27, v27
	v_cvt_i32_f32_e32 v6, v6
	v_cvt_i32_f32_sdwa v26, v26 dst_sel:WORD_1 dst_unused:UNUSED_PAD src0_sel:DWORD
	v_cvt_i32_f32_e32 v27, v27
	v_lshlrev_b32_e32 v7, 8, v7
	v_and_b32_e32 v7, 0xff00, v7
	v_and_b32_e32 v26, 0xff0000, v26
	v_perm_b32 v6, v27, v6, s1
	v_or3_b32 v26, v6, v7, v26
	v_mbcnt_lo_u32_b32 v6, -1, 0
	v_mbcnt_hi_u32_b32 v6, -1, v6
; #define FLANE lane_id()
; __device__ __forceinline__ void p6_router(Frame& F) {
;     ...
;                 for (int j = 0; j < 8; ++j) { const v2u w = raw[rr][j]; v[j] = (f32x4){bf_lo(w.x), bf_hi(w.x), bf_lo(w.y), bf_hi(w.y)}; s += (v[j][0] + v[j][1]) + (v[j][2] + v[j][3]); }
;                 const float mean = wave_sum(s) * (1.f / D); float s2 = 0.f;
;     ...
;                 for (int j = 0; j < 8; ++j) { const int q0 = (int)__builtin_rintf(v[j][0] * inv), q1 = (int)__builtin_rintf(v[j][1] * inv), q2 = (int)__builtin_rintf(v[j][2] * inv), q3 = (int)__builtin_rintf(v[j][3] * inv);
;                     h1q[(size_t)m * (D / 4) + FLANE + 64 * j] = (unsigned)(q0 & 0xff) | ((unsigned)(q1 & 0xff) << 8) | ((unsigned)(q2 & 0xff) << 16) | ((unsigned)(q3 & 0xff) << 24); }
;                 if (FLANE == 0) { st1[2 * m] = mean; st1[2 * m + 1] = rstd; stl[2 * row] = mean; stl[2 * row + 1] = rstd; sxg[m] = sc; sxl[row] = sc; }
	v_mul_f32_e32 v27, v53, v1
	v_ashrrev_i32_e32 v7, 31, v6
	v_lshl_add_u64 v[6:7], v[6:7], 2, s[6:7]
	global_store_dword v[6:7], v26, off offset:768
	v_mul_f32_e32 v7, v55, v1
	v_mul_f32_e32 v6, v54, v1
	v_rndne_f32_e32 v7, v7
	v_mul_f32_e32 v26, v52, v1
	v_rndne_f32_e32 v6, v6
	v_cvt_i32_f32_e32 v7, v7
	v_rndne_f32_e32 v26, v26
	v_rndne_f32_e32 v27, v27
	v_cvt_i32_f32_e32 v6, v6
	v_cvt_i32_f32_sdwa v26, v26 dst_sel:WORD_1 dst_unused:UNUSED_PAD src0_sel:DWORD
	v_cvt_i32_f32_e32 v27, v27
	v_lshlrev_b32_e32 v7, 8, v7
	v_and_b32_e32 v7, 0xff00, v7
	v_and_b32_e32 v26, 0xff0000, v26
	v_perm_b32 v6, v27, v6, s1
	v_or3_b32 v26, v6, v7, v26
	v_mbcnt_lo_u32_b32 v6, -1, 0
	v_mbcnt_hi_u32_b32 v6, -1, v6
	v_mul_f32_e32 v27, v57, v1
	v_ashrrev_i32_e32 v7, 31, v6
	v_lshl_add_u64 v[6:7], v[6:7], 2, s[6:7]
	global_store_dword v[6:7], v26, off offset:1024
	v_mul_f32_e32 v7, v59, v1
	v_mul_f32_e32 v6, v58, v1
	v_rndne_f32_e32 v7, v7
	v_mul_f32_e32 v26, v56, v1
	v_rndne_f32_e32 v6, v6
	v_cvt_i32_f32_e32 v7, v7
	v_rndne_f32_e32 v26, v26
	v_rndne_f32_e32 v27, v27
	v_cvt_i32_f32_e32 v6, v6
	v_cvt_i32_f32_sdwa v26, v26 dst_sel:WORD_1 dst_unused:UNUSED_PAD src0_sel:DWORD
	v_cvt_i32_f32_e32 v27, v27
	v_lshlrev_b32_e32 v7, 8, v7
	v_and_b32_e32 v7, 0xff00, v7
	v_and_b32_e32 v26, 0xff0000, v26
	v_perm_b32 v6, v27, v6, s1
	v_or3_b32 v26, v6, v7, v26
	v_mbcnt_lo_u32_b32 v6, -1, 0
	v_mbcnt_hi_u32_b32 v6, -1, v6
	v_mul_f32_e32 v27, v61, v1
	v_ashrrev_i32_e32 v7, 31, v6
	v_lshl_add_u64 v[6:7], v[6:7], 2, s[6:7]
	global_store_dword v[6:7], v26, off offset:1280
	v_mul_f32_e32 v7, v63, v1
	v_mul_f32_e32 v6, v62, v1
	v_rndne_f32_e32 v7, v7
	v_mul_f32_e32 v26, v60, v1
	v_rndne_f32_e32 v6, v6
	v_cvt_i32_f32_e32 v7, v7
	v_rndne_f32_e32 v26, v26
	v_rndne_f32_e32 v27, v27
	v_mul_f32_e32 v5, v5, v1
	v_cvt_i32_f32_e32 v6, v6
	v_cvt_i32_f32_sdwa v26, v26 dst_sel:WORD_1 dst_unused:UNUSED_PAD src0_sel:DWORD
	v_cvt_i32_f32_e32 v27, v27
	v_mul_f32_e32 v4, v4, v1
	v_rndne_f32_e32 v5, v5
	v_mul_f32_e32 v2, v2, v1
	v_mul_f32_e32 v1, v3, v1
	v_rndne_f32_e32 v4, v4
	v_cvt_i32_f32_e32 v5, v5
	v_rndne_f32_e32 v2, v2
	v_rndne_f32_e32 v1, v1
	v_cvt_i32_f32_e32 v4, v4
	v_cvt_i32_f32_sdwa v2, v2 dst_sel:WORD_1 dst_unused:UNUSED_PAD src0_sel:DWORD
	v_cvt_i32_f32_e32 v1, v1
	v_lshlrev_b32_e32 v7, 8, v7
	v_and_b32_e32 v7, 0xff00, v7
	v_and_b32_e32 v26, 0xff0000, v26
	v_perm_b32 v6, v27, v6, s1
	v_or3_b32 v26, v6, v7, v26
	v_mbcnt_lo_u32_b32 v6, -1, 0
	v_mbcnt_hi_u32_b32 v6, -1, v6
	v_lshlrev_b32_e32 v3, 8, v5
	v_ashrrev_i32_e32 v7, 31, v6
	v_lshl_add_u64 v[6:7], v[6:7], 2, s[6:7]
	v_and_b32_e32 v3, 0xff00, v3
	v_and_b32_e32 v2, 0xff0000, v2
	v_perm_b32 v1, v1, v4, s1
	global_store_dword v[6:7], v26, off offset:1536
	v_or3_b32 v1, v1, v3, v2
	v_mbcnt_lo_u32_b32 v2, -1, 0
	v_mbcnt_hi_u32_b32 v2, -1, v2
	s_nop 0
	v_ashrrev_i32_e32 v3, 31, v2
	v_lshl_add_u64 v[2:3], v[2:3], 2, s[6:7]
	global_store_dword v[2:3], v1, off offset:1792
	v_mbcnt_lo_u32_b32 v1, -1, 0
	v_mbcnt_hi_u32_b32 v1, -1, v1
	s_nop 0
	v_cmp_eq_u32_e32 vcc, 0, v1
	s_and_saveexec_b64 s[6:7], vcc
	s_cbranch_execz .LBB0_1495
	s_lshl_b32 s8, s4, 1
	s_ashr_i32 s9, s8, 31
	s_lshl_b64 s[8:9], s[8:9], 2
	s_add_u32 s8, s27, s8
	s_addc_u32 s9, s64, s9
	v_readlane_b32 s0, v255, 47
	s_lshl_b64 s[4:5], s[4:5], 2
	v_mul_f32_e32 v2, 0x3a000000, v25
	v_mov_b32_e32 v3, v24
	v_mov_b32_e32 v1, s0
	s_add_u32 s4, s25, s4
	v_readlane_b32 s0, v255, 36
	ds_write_b64 v1, v[2:3]
	s_addc_u32 s5, s26, s5
	v_mov_b32_e32 v1, s0
	global_store_dwordx2 v33, v[2:3], s[8:9]
	global_store_dword v33, v0, s[4:5]
	ds_write_b32 v1, v0
.LBB0_1495:
	s_or_b64 exec, exec, s[6:7]
	v_lshlrev_b32_e32 v27, 16, v22
	v_lshlrev_b32_e32 v26, 16, v20
	v_and_b32_e32 v43, 0xffff0000, v22
	v_and_b32_e32 v42, 0xffff0000, v20
	v_lshlrev_b32_e32 v45, 16, v23
	v_lshlrev_b32_e32 v44, 16, v21
	v_and_b32_e32 v47, 0xffff0000, v23
	v_and_b32_e32 v46, 0xffff0000, v21
	v_pk_add_f32 v[0:1], v[26:27], v[42:43]
	v_pk_add_f32 v[2:3], v[44:45], v[46:47]
	v_lshlrev_b32_e32 v25, 16, v19
	v_pk_add_f32 v[0:1], v[0:1], v[2:3]
	v_lshlrev_b32_e32 v24, 16, v18
	v_add_f32_e32 v0, 0, v0
	v_and_b32_e32 v49, 0xffff0000, v19
	v_and_b32_e32 v48, 0xffff0000, v18
	v_add_f32_e32 v6, v0, v1
	v_pk_add_f32 v[0:1], v[24:25], v[48:49]
	v_lshlrev_b32_e32 v28, 16, v16
	v_and_b32_e32 v29, 0xffff0000, v16
	v_lshlrev_b32_e32 v30, 16, v17
	v_and_b32_e32 v31, 0xffff0000, v17
	v_and_b32_e32 v41, 0xffff0000, v14
	v_pk_add_f32 v[0:1], v[0:1], v[0:1] op_sel:[0,1] op_sel_hi:[1,0]
	v_add_f32_e32 v38, v28, v29
	v_add_f32_e32 v36, v30, v31
	v_lshlrev_b32_e32 v7, 16, v14
	v_lshlrev_b32_e32 v39, 16, v15
	v_and_b32_e32 v37, 0xffff0000, v15
	v_mov_b32_e32 v1, v41
	v_pk_add_f32 v[0:1], v[6:7], v[0:1]
	v_pk_add_f32 v[2:3], v[38:39], v[36:37]
	v_lshlrev_b32_e32 v5, 16, v13
	v_lshlrev_b32_e32 v4, 16, v12
	v_and_b32_e32 v51, 0xffff0000, v13
	v_and_b32_e32 v50, 0xffff0000, v12
	v_pk_add_f32 v[16:17], v[0:1], v[2:3]
	v_pk_add_f32 v[18:19], v[4:5], v[50:51]
	v_lshlrev_b32_e32 v0, 16, v10
	v_and_b32_e32 v1, 0xffff0000, v10
	v_lshlrev_b32_e32 v2, 16, v11
	v_and_b32_e32 v3, 0xffff0000, v11
	v_lshlrev_b32_e32 v14, 16, v8
	v_and_b32_e32 v15, 0xffff0000, v8
	v_lshlrev_b32_e32 v13, 16, v9
	v_and_b32_e32 v11, 0xffff0000, v9
	v_pk_add_f32 v[8:9], v[16:17], v[16:17] op_sel:[0,1] op_sel_hi:[1,0]
	v_pk_add_f32 v[16:17], v[18:19], v[18:19] op_sel:[0,1] op_sel_hi:[1,0]
	v_add_f32_e32 v12, v0, v1
	v_add_f32_e32 v10, v2, v3
	v_mov_b32_e32 v9, v14
	v_mov_b32_e32 v17, v15
	v_pk_add_f32 v[8:9], v[8:9], v[16:17]
	v_pk_add_f32 v[16:17], v[12:13], v[10:11]
	s_nop 0
	v_pk_add_f32 v[8:9], v[8:9], v[16:17]
	s_nop 0
	v_add_f32_e32 v6, v8, v9
	s_waitcnt lgkmcnt(0)
; __device__ __forceinline__ void p6_router(Frame& F) {
;     ...
;                 const float mean = wave_sum(s) * (1.f / D); float s2 = 0.f;
; #pragma unroll
;                 for (int j = 0; j < 8; ++j) { v[j] = v[j] - mean; s2 += (v[j][0] * v[j][0] + v[j][1] * v[j][1]) + (v[j][2] * v[j][2] + v[j][3] * v[j][3]); }
;                 const float rstd = 1.f / sqrtf(wave_sum(s2) * (1.f / D) + LN_EPS);
	s_nop 1
	v_add_f32_dpp v6, v6, v6 quad_perm:[1,0,3,2] row_mask:0xf bank_mask:0xf
	s_waitcnt lgkmcnt(0)
	s_nop 1
	v_add_f32_dpp v6, v6, v6 quad_perm:[2,3,0,1] row_mask:0xf bank_mask:0xf
	s_waitcnt lgkmcnt(0)
	s_nop 1
	v_add_f32_dpp v6, v6, v6 row_half_mirror row_mask:0xf bank_mask:0xf
	s_waitcnt lgkmcnt(0)
	s_nop 1
	v_add_f32_dpp v6, v6, v6 row_mirror row_mask:0xf bank_mask:0xf
	s_waitcnt lgkmcnt(0)
	v_mov_b32_e32 v8, v6
	s_nop 1
	v_permlane16_swap_b32_e32 v6, v8
	v_add_f32_e32 v6, v6, v8
	s_waitcnt lgkmcnt(0)
	v_mov_b32_e32 v8, v6
	s_nop 1
	v_permlane32_swap_b32_e32 v6, v8
	v_add_f32_e32 v9, v6, v8
	v_fmac_f32_e32 v46, 0xba000000, v9
	v_fmac_f32_e32 v42, 0xba000000, v9
	v_fmac_f32_e32 v47, 0xba000000, v9
	v_fmac_f32_e32 v43, 0xba000000, v9
	v_fmac_f32_e32 v44, 0xba000000, v9
	v_fmac_f32_e32 v26, 0xba000000, v9
	v_fmac_f32_e32 v45, 0xba000000, v9
	v_fmac_f32_e32 v27, 0xba000000, v9
	v_mov_b32_e32 v21, v43
	v_mov_b32_e32 v17, v42
	v_pk_mul_f32 v[18:19], v[42:43], v[42:43]
	v_pk_mul_f32 v[42:43], v[46:47], v[46:47]
	v_mov_b32_e32 v20, v27
	v_mov_b32_e32 v16, v26
	v_pk_fma_f32 v[26:27], v[26:27], v[26:27], v[18:19]
	v_pk_fma_f32 v[42:43], v[44:45], v[44:45], v[42:43]
	v_fmac_f32_e32 v48, 0xba000000, v9
	v_pk_add_f32 v[26:27], v[26:27], v[42:43]
	v_fmac_f32_e32 v49, 0xba000000, v9
	v_fmac_f32_e32 v25, 0xba000000, v9
	v_pk_add_f32 v[42:43], v[26:27], v[26:27] op_sel_hi:[0,1]
	v_fmac_f32_e32 v24, 0xba000000, v9
	v_mov_b32_e32 v26, v25
	v_mov_b32_e32 v27, v49
	v_mov_b32_e32 v25, v48
	v_mov_b32_e32 v22, v45
	v_mov_b32_e32 v23, v47
	v_mov_b32_e32 v18, v44
	v_mov_b32_e32 v19, v46
	v_pk_mul_f32 v[44:45], v[26:27], v[26:27]
	v_pk_mul_f32 v[46:47], v[24:25], v[24:25]
	v_fmac_f32_e32 v28, 0xba000000, v9
	v_pk_mov_b32 v[48:49], v[46:47], v[44:45] op_sel:[1,0]
	v_mov_b32_e32 v47, v45
	v_fmac_f32_e32 v29, 0xba000000, v9
	v_fmac_f32_e32 v30, 0xba000000, v9
	v_mul_f32_e32 v6, v28, v28
	v_pk_add_f32 v[44:45], v[48:49], v[46:47]
	v_fmac_f32_e32 v31, 0xba000000, v9
	v_pk_fma_f32 v[46:47], v[28:29], v[28:29], v[6:7] op_sel_hi:[1,1,0]
	v_mul_f32_e32 v6, v30, v30
	v_pk_add_f32 v[44:45], v[44:45], v[44:45] op_sel_hi:[0,1]
	v_pk_fma_f32 v[48:49], v[30:31], v[30:31], v[6:7] op_sel_hi:[1,1,0]
	v_fmac_f32_e32 v37, 0xba000000, v9
	v_fmac_f32_e32 v39, 0xba000000, v9
	v_fmac_f32_e32 v41, 0xba000000, v9
	v_fmac_f32_e32 v7, 0xba000000, v9
	v_mul_f32_e32 v46, v7, v7
	v_mul_f32_e32 v48, v41, v41
	v_mul_f32_e32 v44, v39, v39
	v_mul_f32_e32 v42, v37, v37
	v_pk_add_f32 v[46:47], v[46:47], v[48:49]
	v_pk_add_f32 v[42:43], v[44:45], v[42:43]
	v_fmac_f32_e32 v50, 0xba000000, v9
	v_pk_add_f32 v[42:43], v[46:47], v[42:43]
	v_fmac_f32_e32 v51, 0xba000000, v9
	v_fmac_f32_e32 v5, 0xba000000, v9
	v_pk_add_f32 v[44:45], v[42:43], v[42:43] op_sel_hi:[0,1]
	v_fmac_f32_e32 v4, 0xba000000, v9
	v_mov_b32_e32 v42, v5
	v_mov_b32_e32 v43, v51
	v_mov_b32_e32 v5, v50
	v_pk_mul_f32 v[46:47], v[42:43], v[42:43]
	v_pk_mul_f32 v[48:49], v[4:5], v[4:5]
	v_fmac_f32_e32 v0, 0xba000000, v9
	v_pk_mov_b32 v[50:51], v[48:49], v[46:47] op_sel:[1,0]
	v_mov_b32_e32 v49, v47
	v_fmac_f32_e32 v1, 0xba000000, v9
	v_fmac_f32_e32 v2, 0xba000000, v9
	v_mul_f32_e32 v6, v0, v0
	v_pk_add_f32 v[46:47], v[50:51], v[48:49]
	v_fmac_f32_e32 v3, 0xba000000, v9
	v_pk_fma_f32 v[48:49], v[0:1], v[0:1], v[6:7] op_sel_hi:[1,1,0]
	v_mul_f32_e32 v6, v2, v2
	v_pk_add_f32 v[46:47], v[46:47], v[46:47] op_sel_hi:[0,1]
	v_pk_fma_f32 v[50:51], v[2:3], v[2:3], v[6:7] op_sel_hi:[1,1,0]
	v_fmac_f32_e32 v11, 0xba000000, v9
	v_fmac_f32_e32 v13, 0xba000000, v9
	v_fmac_f32_e32 v15, 0xba000000, v9
	v_fmac_f32_e32 v14, 0xba000000, v9
	v_mul_f32_e32 v48, v14, v14
	v_mul_f32_e32 v50, v15, v15
	v_mul_f32_e32 v46, v13, v13
	v_mul_f32_e32 v44, v11, v11
	v_pk_add_f32 v[48:49], v[48:49], v[50:51]
	v_pk_add_f32 v[44:45], v[46:47], v[44:45]
	v_mov_b32_e32 v40, v7
	v_pk_add_f32 v[44:45], v[48:49], v[44:45]
	s_nop 0
	v_add_f32_e32 v6, v44, v45
	v_mbcnt_lo_u32_b32 v44, -1, 0
	v_mbcnt_hi_u32_b32 v44, -1, v44
	v_ashrrev_i32_e32 v45, 31, v44
	v_lshl_add_u64 v[44:45], v[44:45], 4, s[12:13]
	global_load_dwordx4 v[44:47], v[44:45], off
	v_mbcnt_lo_u32_b32 v48, -1, 0
	v_mbcnt_hi_u32_b32 v48, -1, v48
	s_waitcnt lgkmcnt(0)
	s_nop 1
	v_add_f32_dpp v6, v6, v6 quad_perm:[1,0,3,2] row_mask:0xf bank_mask:0xf
	v_ashrrev_i32_e32 v49, 31, v48
	v_lshl_add_u64 v[48:49], v[48:49], 4, s[14:15]
	global_load_dwordx4 v[48:51], v[48:49], off
	s_waitcnt lgkmcnt(0)
	s_nop 1
	v_add_f32_dpp v6, v6, v6 quad_perm:[2,3,0,1] row_mask:0xf bank_mask:0xf
	s_waitcnt lgkmcnt(0)
	s_nop 1
	v_add_f32_dpp v6, v6, v6 row_half_mirror row_mask:0xf bank_mask:0xf
	s_waitcnt lgkmcnt(0)
	s_nop 1
	v_add_f32_dpp v6, v6, v6 row_mirror row_mask:0xf bank_mask:0xf
	s_waitcnt lgkmcnt(0)
	v_mov_b32_e32 v8, v6
	s_nop 1
	v_permlane16_swap_b32_e32 v6, v8
	v_add_f32_e32 v6, v6, v8
	s_waitcnt lgkmcnt(0)
	v_mov_b32_e32 v8, v6
	s_nop 1
	v_permlane32_swap_b32_e32 v6, v8
	v_add_f32_e32 v6, v6, v8
	v_fmamk_f32 v6, v6, 0x3a000000, v166
	v_cmp_gt_f32_e32 vcc, s22, v6
	v_mul_f32_e32 v8, 0x4f800000, v6
	s_nop 0
	v_cndmask_b32_e32 v6, v6, v8, vcc
	v_sqrt_f32_e32 v8, v6
	s_nop 0
	v_add_u32_e32 v10, -1, v8
	v_fma_f32 v12, -v10, v8, v6
	v_cmp_ge_f32_e64 s[4:5], 0, v12
	v_add_u32_e32 v12, 1, v8
	s_nop 0
	v_cndmask_b32_e64 v10, v8, v10, s[4:5]
	v_fma_f32 v8, -v12, v8, v6
	v_cmp_lt_f32_e64 s[4:5], 0, v8
	s_nop 1
	v_cndmask_b32_e64 v8, v10, v12, s[4:5]
	v_mul_f32_e32 v10, 0x37800000, v8
	v_cndmask_b32_e32 v8, v8, v10, vcc
	v_cmp_class_f32_e32 vcc, v6, v167
	s_nop 1
	v_cndmask_b32_e32 v6, v8, v6, vcc
	v_div_scale_f32 v8, s[4:5], v6, v6, 1.0
	v_rcp_f32_e32 v10, v8
	s_add_i32 s4, s42, s79
	s_ashr_i32 s5, s4, 31
	v_fma_f32 v12, -v8, v10, 1.0
	v_fmac_f32_e32 v10, v12, v10
	v_div_scale_f32 v12, vcc, 1.0, v6, 1.0
	v_mul_f32_e32 v32, v12, v10
	v_fma_f32 v36, -v8, v32, v12
	v_fmac_f32_e32 v32, v36, v10
	v_fma_f32 v8, -v8, v32, v12
	v_div_fmas_f32 v8, v8, v10, v32
	v_div_fixup_f32 v8, v8, v6, 1.0
	v_pk_mul_f32 v[52:53], v[16:17], v[8:9] op_sel_hi:[1,0]
	v_pk_mul_f32 v[16:17], v[18:19], v[8:9] op_sel_hi:[1,0]
	v_mov_b32_e32 v36, v39
	v_pk_mul_f32 v[36:37], v[36:37], v[8:9] op_sel_hi:[1,0]
	v_pk_mul_f32 v[4:5], v[4:5], v[8:9] op_sel_hi:[1,0]
	v_pk_mul_f32 v[2:3], v[2:3], v[8:9] op_sel_hi:[1,0]
	v_pk_mul_f32 v[0:1], v[0:1], v[8:9] op_sel_hi:[1,0]
	s_waitcnt vmcnt(0)
; #define GAS __attribute__((address_space(1)))
; #define FLANE lane_id()
; __device__ __forceinline__ void p6_router(Frame& F) {
;     ...
;                 for (int j = 0; j < 8; ++j) { const f32x4 g = *((const GAS f32x4*)F.ln1_g + FLANE + 64 * j), b = *((const GAS f32x4*)F.ln1_b + FLANE + 64 * j);
;                     v[j] = v[j] * rstd * g + b; am = fmaxf(am, fmaxf(fmaxf(fabsf(v[j][0]), fabsf(v[j][1])), fmaxf(fabsf(v[j][2]), fabsf(v[j][3])))); }
; #pragma unroll
;                 for (int o = 1; o < 64; o <<= 1) am = fmaxf(am, __shfl_xor(am, o));
	v_pk_fma_f32 v[18:19], v[44:45], v[52:53], v[48:49]
	v_mbcnt_lo_u32_b32 v44, -1, 0
	v_mbcnt_hi_u32_b32 v44, -1, v44
	v_pk_fma_f32 v[16:17], v[46:47], v[16:17], v[50:51]
	v_ashrrev_i32_e32 v45, 31, v44
	v_lshl_add_u64 v[44:45], v[44:45], 4, s[12:13]
	global_load_dwordx4 v[44:47], v[44:45], off offset:1024
	v_mbcnt_lo_u32_b32 v48, -1, 0
	v_mbcnt_hi_u32_b32 v48, -1, v48
	v_pk_mul_f32 v[52:53], v[20:21], v[8:9] op_sel_hi:[1,0]
	v_ashrrev_i32_e32 v49, 31, v48
	v_lshl_add_u64 v[48:49], v[48:49], 4, s[14:15]
	global_load_dwordx4 v[48:51], v[48:49], off offset:1024
	v_pk_mul_f32 v[20:21], v[22:23], v[8:9] op_sel_hi:[1,0]
	v_max_f32_e64 v6, |v16|, |v17|
	v_max3_f32 v6, |v18|, |v19|, v6
	v_pk_mul_f32 v[14:15], v[14:15], v[8:9] op_sel_hi:[1,0]
	s_waitcnt vmcnt(0)
	v_pk_fma_f32 v[22:23], v[44:45], v[52:53], v[48:49]
	v_mbcnt_lo_u32_b32 v44, -1, 0
	v_mbcnt_hi_u32_b32 v44, -1, v44
	v_pk_fma_f32 v[20:21], v[46:47], v[20:21], v[50:51]
	v_ashrrev_i32_e32 v45, 31, v44
	v_lshl_add_u64 v[44:45], v[44:45], 4, s[12:13]
	global_load_dwordx4 v[44:47], v[44:45], off offset:2048
	v_mbcnt_lo_u32_b32 v48, -1, 0
	v_mbcnt_hi_u32_b32 v48, -1, v48
	v_pk_mul_f32 v[52:53], v[24:25], v[8:9] op_sel_hi:[1,0]
	v_ashrrev_i32_e32 v49, 31, v48
	v_lshl_add_u64 v[48:49], v[48:49], 4, s[14:15]
	global_load_dwordx4 v[48:51], v[48:49], off offset:2048
	v_pk_mul_f32 v[24:25], v[26:27], v[8:9] op_sel_hi:[1,0]
	v_max_f32_e64 v10, |v20|, |v21|
	v_max3_f32 v10, |v22|, |v23|, v10
	v_max3_f32 v6, v6, 0, v10
	s_waitcnt vmcnt(0)
	v_pk_fma_f32 v[26:27], v[44:45], v[52:53], v[48:49]
	v_mbcnt_lo_u32_b32 v44, -1, 0
	v_mbcnt_hi_u32_b32 v44, -1, v44
	v_pk_fma_f32 v[24:25], v[46:47], v[24:25], v[50:51]
	v_ashrrev_i32_e32 v45, 31, v44
	v_lshl_add_u64 v[44:45], v[44:45], 4, s[12:13]
	global_load_dwordx4 v[44:47], v[44:45], off offset:3072
	v_mbcnt_lo_u32_b32 v48, -1, 0
	v_mbcnt_hi_u32_b32 v48, -1, v48
	v_pk_mul_f32 v[52:53], v[28:29], v[8:9] op_sel_hi:[1,0]
	v_ashrrev_i32_e32 v49, 31, v48
	v_lshl_add_u64 v[48:49], v[48:49], 4, s[14:15]
	global_load_dwordx4 v[48:51], v[48:49], off offset:3072
	v_pk_mul_f32 v[28:29], v[30:31], v[8:9] op_sel_hi:[1,0]
	v_max_f32_e64 v10, |v24|, |v25|
	v_max3_f32 v10, |v26|, |v27|, v10
	s_waitcnt vmcnt(0)
	v_pk_fma_f32 v[30:31], v[44:45], v[52:53], v[48:49]
	v_mbcnt_lo_u32_b32 v44, -1, 0
	v_mbcnt_hi_u32_b32 v44, -1, v44
	v_pk_fma_f32 v[28:29], v[46:47], v[28:29], v[50:51]
	v_ashrrev_i32_e32 v45, 31, v44
	v_lshl_add_u64 v[44:45], v[44:45], 4, s[12:13]
	v_add_co_u32_e32 v44, vcc, s23, v44
	v_max_f32_e64 v12, |v28|, |v29|
	s_nop 0
	v_addc_co_u32_e32 v45, vcc, 0, v45, vcc
	global_load_dwordx4 v[44:47], v[44:45], off
	v_mbcnt_lo_u32_b32 v48, -1, 0
	v_mbcnt_hi_u32_b32 v48, -1, v48
	v_max3_f32 v12, |v30|, |v31|, v12
	v_ashrrev_i32_e32 v49, 31, v48
	v_lshl_add_u64 v[48:49], v[48:49], 4, s[14:15]
	v_add_co_u32_e32 v48, vcc, s23, v48
	v_max3_f32 v10, v6, v10, v12
	s_nop 0
	v_addc_co_u32_e32 v49, vcc, 0, v49, vcc
	global_load_dwordx4 v[48:51], v[48:49], off
	v_pk_mul_f32 v[6:7], v[40:41], v[8:9] op_sel_hi:[1,0]
	s_waitcnt vmcnt(0)
	v_pk_fma_f32 v[36:37], v[46:47], v[36:37], v[50:51]
	v_pk_fma_f32 v[38:39], v[44:45], v[6:7], v[48:49]
	v_max_f32_e64 v6, |v36|, |v37|
	v_max3_f32 v12, |v38|, |v39|, v6
	v_mbcnt_lo_u32_b32 v6, -1, 0
	v_mbcnt_hi_u32_b32 v6, -1, v6
	s_nop 0
	v_ashrrev_i32_e32 v7, 31, v6
	v_lshl_add_u64 v[6:7], v[6:7], 4, s[12:13]
	v_add_co_u32_e32 v6, vcc, s23, v6
	s_nop 1
	v_addc_co_u32_e32 v7, vcc, 0, v7, vcc
	global_load_dwordx4 v[44:47], v[6:7], off offset:1024
	v_mbcnt_lo_u32_b32 v6, -1, 0
	v_mbcnt_hi_u32_b32 v6, -1, v6
	s_nop 0
	v_ashrrev_i32_e32 v7, 31, v6
	v_lshl_add_u64 v[6:7], v[6:7], 4, s[14:15]
	v_add_co_u32_e32 v6, vcc, s23, v6
	s_nop 1
	v_addc_co_u32_e32 v7, vcc, 0, v7, vcc
	global_load_dwordx4 v[48:51], v[6:7], off offset:1024
	v_pk_mul_f32 v[6:7], v[42:43], v[8:9] op_sel_hi:[1,0]
	s_waitcnt vmcnt(0)
	v_pk_fma_f32 v[42:43], v[44:45], v[4:5], v[48:49]
	v_pk_fma_f32 v[40:41], v[46:47], v[6:7], v[50:51]
	s_nop 0
	v_max_f32_e64 v4, |v40|, |v41|
	v_max3_f32 v4, |v42|, |v43|, v4
	v_max3_f32 v12, v10, v12, v4
	v_mbcnt_lo_u32_b32 v4, -1, 0
	v_mbcnt_hi_u32_b32 v4, -1, v4
	v_mov_b32_e32 v10, v13
	v_ashrrev_i32_e32 v5, 31, v4
	v_lshl_add_u64 v[4:5], v[4:5], 4, s[12:13]
	v_add_co_u32_e32 v4, vcc, s23, v4
	v_pk_mul_f32 v[10:11], v[10:11], v[8:9] op_sel_hi:[1,0]
	s_nop 0
	v_addc_co_u32_e32 v5, vcc, 0, v5, vcc
	global_load_dwordx4 v[4:7], v[4:5], off offset:2048
	v_mbcnt_lo_u32_b32 v44, -1, 0
	v_mbcnt_hi_u32_b32 v44, -1, v44
	s_nop 0
	v_ashrrev_i32_e32 v45, 31, v44
	v_lshl_add_u64 v[44:45], v[44:45], 4, s[14:15]
	v_add_co_u32_e32 v44, vcc, s23, v44
	s_nop 1
	v_addc_co_u32_e32 v45, vcc, 0, v45, vcc
	global_load_dwordx4 v[46:49], v[44:45], off offset:2048
	s_waitcnt vmcnt(0)
	v_pk_fma_f32 v[44:45], v[2:3], v[6:7], v[48:49]
	v_pk_fma_f32 v[46:47], v[0:1], v[4:5], v[46:47]
	v_max_f32_e64 v0, |v44|, |v45|
	v_max3_f32 v32, |v46|, |v47|, v0
	v_mbcnt_lo_u32_b32 v0, -1, 0
	v_mbcnt_hi_u32_b32 v0, -1, v0
	s_nop 0
	v_ashrrev_i32_e32 v1, 31, v0
	v_lshl_add_u64 v[0:1], v[0:1], 4, s[12:13]
	v_add_co_u32_e32 v0, vcc, s23, v0
	s_nop 1
	v_addc_co_u32_e32 v1, vcc, 0, v1, vcc
	global_load_dwordx4 v[0:3], v[0:1], off offset:3072
	v_mbcnt_lo_u32_b32 v4, -1, 0
	v_mbcnt_hi_u32_b32 v4, -1, v4
	s_nop 0
	v_ashrrev_i32_e32 v5, 31, v4
	v_lshl_add_u64 v[4:5], v[4:5], 4, s[14:15]
	v_add_co_u32_e32 v4, vcc, s23, v4
	s_nop 1
	v_addc_co_u32_e32 v5, vcc, 0, v5, vcc
	global_load_dwordx4 v[4:7], v[4:5], off offset:3072
	s_waitcnt vmcnt(0)
	v_pk_fma_f32 v[2:3], v[10:11], v[2:3], v[6:7]
	v_pk_fma_f32 v[4:5], v[14:15], v[0:1], v[4:5]
	v_max_f32_e64 v0, |v2|, |v3|
	v_max3_f32 v0, |v4|, |v5|, v0
	v_max3_f32 v0, v12, v32, v0
	s_waitcnt lgkmcnt(0)
; #define FLANE lane_id()
; __device__ __forceinline__ void p6_router(Frame& F) {
;     ...
;                 for (int o = 1; o < 64; o <<= 1) am = fmaxf(am, __shfl_xor(am, o));
;                 const float sc = am > 0.f ? am * (1.f / 127.f) : 1.f, inv = 1.f / sc;
; #pragma unroll
;                 for (int j = 0; j < 8; ++j) { const int q0 = (int)__builtin_rintf(v[j][0] * inv), q1 = (int)__builtin_rintf(v[j][1] * inv), q2 = (int)__builtin_rintf(v[j][2] * inv), q3 = (int)__builtin_rintf(v[j][3] * inv);
;                     h1q[(size_t)m * (D / 4) + FLANE + 64 * j] = (unsigned)(q0 & 0xff) | ((unsigned)(q1 & 0xff) << 8) | ((unsigned)(q2 & 0xff) << 16) | ((unsigned)(q3 & 0xff) << 24); }
	s_nop 1
	v_max_f32_dpp v0, v0, v0 quad_perm:[1,0,3,2] row_mask:0xf bank_mask:0xf
	s_waitcnt lgkmcnt(0)
	s_nop 1
	v_max_f32_dpp v0, v0, v0 quad_perm:[2,3,0,1] row_mask:0xf bank_mask:0xf
	s_waitcnt lgkmcnt(0)
	s_nop 1
	v_max_f32_dpp v0, v0, v0 row_half_mirror row_mask:0xf bank_mask:0xf
	s_waitcnt lgkmcnt(0)
	s_nop 1
	v_max_f32_dpp v0, v0, v0 row_mirror row_mask:0xf bank_mask:0xf
	s_waitcnt lgkmcnt(0)
	v_mov_b32_e32 v1, v0
	s_nop 1
	v_permlane16_swap_b32_e32 v0, v1
	v_max_f32_e32 v0, v0, v1
	s_waitcnt lgkmcnt(0)
	v_mov_b32_e32 v1, v0
	s_nop 1
	v_permlane32_swap_b32_e32 v0, v1
	v_max_f32_e32 v0, v0, v1
	v_cmp_lt_f32_e32 vcc, 0, v0
	v_mul_f32_e32 v0, 0x3c010204, v0
	s_nop 0
	v_cndmask_b32_e32 v0, 1.0, v0, vcc
	v_div_scale_f32 v1, s[6:7], v0, v0, 1.0
	v_rcp_f32_e32 v6, v1
	s_lshl_b64 s[6:7], s[4:5], 11
	s_add_u32 s6, s3, s6
	s_addc_u32 s7, s24, s7
	v_fma_f32 v7, -v1, v6, 1.0
	v_fmac_f32_e32 v6, v7, v6
	v_div_scale_f32 v7, vcc, 1.0, v0, 1.0
	v_mul_f32_e32 v10, v7, v6
	v_fma_f32 v11, -v1, v10, v7
	v_fmac_f32_e32 v10, v11, v6
	v_fma_f32 v1, -v1, v10, v7
	v_div_fmas_f32 v1, v1, v6, v10
	v_div_fixup_f32 v1, v1, v0, 1.0
	v_mul_f32_e32 v7, v19, v1
	v_mul_f32_e32 v6, v18, v1
	v_rndne_f32_e32 v7, v7
	v_mul_f32_e32 v10, v16, v1
	v_mul_f32_e32 v11, v17, v1
	v_rndne_f32_e32 v6, v6
	v_cvt_i32_f32_e32 v7, v7
	v_rndne_f32_e32 v10, v10
	v_rndne_f32_e32 v11, v11
	v_cvt_i32_f32_e32 v6, v6
	v_cvt_i32_f32_sdwa v10, v10 dst_sel:WORD_1 dst_unused:UNUSED_PAD src0_sel:DWORD
	v_cvt_i32_f32_e32 v11, v11
	v_lshlrev_b32_e32 v7, 8, v7
	v_and_b32_e32 v7, 0xff00, v7
	v_and_b32_e32 v10, 0xff0000, v10
	v_perm_b32 v6, v11, v6, s1
	v_or3_b32 v10, v6, v7, v10
	v_mbcnt_lo_u32_b32 v6, -1, 0
	v_mbcnt_hi_u32_b32 v6, -1, v6
	v_mul_f32_e32 v11, v21, v1
	v_ashrrev_i32_e32 v7, 31, v6
	v_lshl_add_u64 v[6:7], v[6:7], 2, s[6:7]
	global_store_dword v[6:7], v10, off
	v_mul_f32_e32 v7, v23, v1
	v_mul_f32_e32 v6, v22, v1
	v_rndne_f32_e32 v7, v7
	v_mul_f32_e32 v10, v20, v1
	v_rndne_f32_e32 v6, v6
	v_cvt_i32_f32_e32 v7, v7
	v_rndne_f32_e32 v10, v10
	v_rndne_f32_e32 v11, v11
	v_cvt_i32_f32_e32 v6, v6
	v_cvt_i32_f32_sdwa v10, v10 dst_sel:WORD_1 dst_unused:UNUSED_PAD src0_sel:DWORD
	v_cvt_i32_f32_e32 v11, v11
	v_lshlrev_b32_e32 v7, 8, v7
	v_and_b32_e32 v7, 0xff00, v7
	v_and_b32_e32 v10, 0xff0000, v10
	v_perm_b32 v6, v11, v6, s1
	v_or3_b32 v10, v6, v7, v10
	v_mbcnt_lo_u32_b32 v6, -1, 0
	v_mbcnt_hi_u32_b32 v6, -1, v6
	v_mul_f32_e32 v11, v25, v1
	v_ashrrev_i32_e32 v7, 31, v6
	v_lshl_add_u64 v[6:7], v[6:7], 2, s[6:7]
	global_store_dword v[6:7], v10, off offset:256
	v_mul_f32_e32 v7, v27, v1
	v_mul_f32_e32 v6, v26, v1
	v_rndne_f32_e32 v7, v7
	v_mul_f32_e32 v10, v24, v1
	v_rndne_f32_e32 v6, v6
	v_cvt_i32_f32_e32 v7, v7
	v_rndne_f32_e32 v10, v10
	v_rndne_f32_e32 v11, v11
	v_cvt_i32_f32_e32 v6, v6
	v_cvt_i32_f32_sdwa v10, v10 dst_sel:WORD_1 dst_unused:UNUSED_PAD src0_sel:DWORD
	v_cvt_i32_f32_e32 v11, v11
	v_lshlrev_b32_e32 v7, 8, v7
	v_and_b32_e32 v7, 0xff00, v7
	v_and_b32_e32 v10, 0xff0000, v10
	v_perm_b32 v6, v11, v6, s1
	v_or3_b32 v10, v6, v7, v10
	v_mbcnt_lo_u32_b32 v6, -1, 0
	v_mbcnt_hi_u32_b32 v6, -1, v6
	v_mul_f32_e32 v11, v29, v1
	v_ashrrev_i32_e32 v7, 31, v6
	v_lshl_add_u64 v[6:7], v[6:7], 2, s[6:7]
	global_store_dword v[6:7], v10, off offset:512
	v_mul_f32_e32 v7, v31, v1
	v_mul_f32_e32 v6, v30, v1
	v_rndne_f32_e32 v7, v7
	v_mul_f32_e32 v10, v28, v1
	v_rndne_f32_e32 v6, v6
	v_cvt_i32_f32_e32 v7, v7
	v_rndne_f32_e32 v10, v10
	v_rndne_f32_e32 v11, v11
	v_cvt_i32_f32_e32 v6, v6
	v_cvt_i32_f32_sdwa v10, v10 dst_sel:WORD_1 dst_unused:UNUSED_PAD src0_sel:DWORD
	v_cvt_i32_f32_e32 v11, v11
	v_lshlrev_b32_e32 v7, 8, v7
	v_and_b32_e32 v7, 0xff00, v7
	v_and_b32_e32 v10, 0xff0000, v10
	v_perm_b32 v6, v11, v6, s1
	v_or3_b32 v10, v6, v7, v10
	v_mbcnt_lo_u32_b32 v6, -1, 0
	v_mbcnt_hi_u32_b32 v6, -1, v6
	v_mul_f32_e32 v11, v37, v1
	v_ashrrev_i32_e32 v7, 31, v6
	v_lshl_add_u64 v[6:7], v[6:7], 2, s[6:7]
	global_store_dword v[6:7], v10, off offset:768
	v_mul_f32_e32 v7, v39, v1
	v_mul_f32_e32 v6, v38, v1
	v_rndne_f32_e32 v7, v7
	v_mul_f32_e32 v10, v36, v1
	v_rndne_f32_e32 v6, v6
	v_cvt_i32_f32_e32 v7, v7
	v_rndne_f32_e32 v10, v10
	v_rndne_f32_e32 v11, v11
	v_cvt_i32_f32_e32 v6, v6
	v_cvt_i32_f32_sdwa v10, v10 dst_sel:WORD_1 dst_unused:UNUSED_PAD src0_sel:DWORD
	v_cvt_i32_f32_e32 v11, v11
	v_lshlrev_b32_e32 v7, 8, v7
	v_and_b32_e32 v7, 0xff00, v7
	v_and_b32_e32 v10, 0xff0000, v10
	v_perm_b32 v6, v11, v6, s1
	v_or3_b32 v10, v6, v7, v10
	v_mbcnt_lo_u32_b32 v6, -1, 0
	v_mbcnt_hi_u32_b32 v6, -1, v6
	v_mul_f32_e32 v11, v41, v1
	v_ashrrev_i32_e32 v7, 31, v6
	v_lshl_add_u64 v[6:7], v[6:7], 2, s[6:7]
	global_store_dword v[6:7], v10, off offset:1024
	v_mul_f32_e32 v7, v43, v1
	v_mul_f32_e32 v6, v42, v1
	v_rndne_f32_e32 v7, v7
	v_mul_f32_e32 v10, v40, v1
	v_rndne_f32_e32 v6, v6
	v_cvt_i32_f32_e32 v7, v7
	v_rndne_f32_e32 v10, v10
	v_rndne_f32_e32 v11, v11
	v_cvt_i32_f32_e32 v6, v6
	v_cvt_i32_f32_sdwa v10, v10 dst_sel:WORD_1 dst_unused:UNUSED_PAD src0_sel:DWORD
	v_cvt_i32_f32_e32 v11, v11
	v_lshlrev_b32_e32 v7, 8, v7
	v_and_b32_e32 v7, 0xff00, v7
	v_and_b32_e32 v10, 0xff0000, v10
	v_perm_b32 v6, v11, v6, s1
	v_or3_b32 v10, v6, v7, v10
	v_mbcnt_lo_u32_b32 v6, -1, 0
	v_mbcnt_hi_u32_b32 v6, -1, v6
	v_mul_f32_e32 v11, v45, v1
	v_ashrrev_i32_e32 v7, 31, v6
	v_lshl_add_u64 v[6:7], v[6:7], 2, s[6:7]
	global_store_dword v[6:7], v10, off offset:1280
	v_mul_f32_e32 v7, v47, v1
	v_mul_f32_e32 v6, v46, v1
	v_rndne_f32_e32 v7, v7
	v_mul_f32_e32 v10, v44, v1
	v_rndne_f32_e32 v6, v6
	v_cvt_i32_f32_e32 v7, v7
	v_rndne_f32_e32 v10, v10
	v_rndne_f32_e32 v11, v11
	v_mul_f32_e32 v5, v5, v1
	v_cvt_i32_f32_e32 v6, v6
	v_cvt_i32_f32_sdwa v10, v10 dst_sel:WORD_1 dst_unused:UNUSED_PAD src0_sel:DWORD
	v_cvt_i32_f32_e32 v11, v11
	v_mul_f32_e32 v4, v4, v1
	v_rndne_f32_e32 v5, v5
	v_mul_f32_e32 v2, v2, v1
	v_mul_f32_e32 v1, v3, v1
	v_rndne_f32_e32 v4, v4
	v_cvt_i32_f32_e32 v5, v5
	v_rndne_f32_e32 v2, v2
	v_rndne_f32_e32 v1, v1
	v_cvt_i32_f32_e32 v4, v4
	v_cvt_i32_f32_sdwa v2, v2 dst_sel:WORD_1 dst_unused:UNUSED_PAD src0_sel:DWORD
	v_cvt_i32_f32_e32 v1, v1
	v_lshlrev_b32_e32 v7, 8, v7
	v_and_b32_e32 v7, 0xff00, v7
	v_and_b32_e32 v10, 0xff0000, v10
	v_perm_b32 v6, v11, v6, s1
	v_or3_b32 v10, v6, v7, v10
	v_mbcnt_lo_u32_b32 v6, -1, 0
	v_mbcnt_hi_u32_b32 v6, -1, v6
	v_lshlrev_b32_e32 v3, 8, v5
	v_ashrrev_i32_e32 v7, 31, v6
	v_lshl_add_u64 v[6:7], v[6:7], 2, s[6:7]
	v_and_b32_e32 v3, 0xff00, v3
	v_and_b32_e32 v2, 0xff0000, v2
	v_perm_b32 v1, v1, v4, s1
	global_store_dword v[6:7], v10, off offset:1536
	v_or3_b32 v1, v1, v3, v2
	v_mbcnt_lo_u32_b32 v2, -1, 0
	v_mbcnt_hi_u32_b32 v2, -1, v2
	s_nop 0
	v_ashrrev_i32_e32 v3, 31, v2
	v_lshl_add_u64 v[2:3], v[2:3], 2, s[6:7]
	global_store_dword v[2:3], v1, off offset:1792
	v_mbcnt_lo_u32_b32 v1, -1, 0
	v_mbcnt_hi_u32_b32 v1, -1, v1
	s_nop 0
	v_cmp_eq_u32_e32 vcc, 0, v1
	s_and_saveexec_b64 s[6:7], vcc
	s_cbranch_execz .LBB0_1497
; #define FLANE lane_id()
; __device__ __forceinline__ void p6_router(Frame& F) {
;     ...
;                 if (FLANE == 0) { st1[2 * m] = mean; st1[2 * m + 1] = rstd; stl[2 * row] = mean; stl[2 * row + 1] = rstd; sxg[m] = sc; sxl[row] = sc; }
	s_lshl_b32 s8, s4, 1
	s_ashr_i32 s9, s8, 31
	s_lshl_b64 s[8:9], s[8:9], 2
	s_add_u32 s8, s27, s8
	s_addc_u32 s9, s64, s9
	v_readlane_b32 s0, v255, 49
	s_lshl_b64 s[4:5], s[4:5], 2
	v_mul_f32_e32 v2, 0x3a000000, v9
	v_mov_b32_e32 v3, v8
	v_mov_b32_e32 v1, s0
	s_add_u32 s4, s25, s4
	v_readlane_b32 s0, v255, 38
	ds_write_b64 v1, v[2:3]
	s_addc_u32 s5, s26, s5
	v_mov_b32_e32 v1, s0
	global_store_dwordx2 v33, v[2:3], s[8:9]
	global_store_dword v33, v0, s[4:5]
	ds_write_b32 v1, v0

; #define GAS __attribute__((address_space(1)))
; __device__ __forceinline__ void p9_combine(Frame& F, const LAS int* tstart) {
;     ...
;         const float mean1 = st1[2 * m], rstd1 = st1[2 * m + 1];
;         size_t ro[4]; float gk[4];
; #pragma unroll
;         for (int k = 0; k < 4; ++k) { const int e = topi[4 * m + k]; ro[k] = ((size_t)tstart[e] * 256 + posb[4 * m + k]) * D; gk[k] = gate[4 * m + k]; }
;         f32x4 v[8]; float s = 0.f;
; #pragma unroll
;         for (int j = 0; j < 8; ++j) { const int col = 4 * lane + 256 * j;
;             const v2u zw = *(const GAS v2u*)(z1 + (size_t)m * D + col); const f32x4 zv = (f32x4){bf_lo(zw.x), bf_hi(zw.x), bf_lo(zw.y), bf_hi(zw.y)}, g = *(const GAS f32x4*)(F.ln1_g + col), b = *(const GAS f32x4*)(F.ln1_b + col);
;             f32x4 a = ((zv - mean1) * rstd1 * g + b) * ALPHA;
.LBB0_1798:
	s_ashr_i32 s7, s6, 31
	s_lshl_b64 s[0:1], s[6:7], 2
	s_add_u32 s0, s18, s0
	s_addc_u32 s1, s19, s1
	s_ashr_i32 s9, s8, 31
	global_load_dwordx2 v[118:119], v[116:117], off
	global_load_dwordx2 v[120:121], v[116:117], off offset:512
	global_load_dwordx4 v[0:3], v[74:75], off
	global_load_dwordx4 v[4:7], v[74:75], off offset:1024
	global_load_dwordx4 v[12:15], v[76:77], off
	global_load_dwordx4 v[8:11], v[76:77], off offset:1024
	global_load_dwordx2 v[122:123], v[116:117], off offset:1024
	global_load_dwordx2 v[124:125], v[116:117], off offset:1536
	global_load_dwordx4 v[16:19], v[74:75], off offset:2048
	global_load_dwordx4 v[20:23], v[74:75], off offset:3072
	global_load_dwordx4 v[28:31], v[76:77], off offset:2048
	global_load_dwordx4 v[24:27], v[76:77], off offset:3072
	global_load_dwordx4 v[32:35], v[78:79], off
	global_load_dwordx4 v[40:43], v[80:81], off
	global_load_dwordx2 v[126:127], v[116:117], off offset:2048
	global_load_dwordx2 v[128:129], v[116:117], off offset:2560
	global_load_dwordx4 v[48:51], v[82:83], off
	global_load_dwordx4 v[52:55], v[84:85], off
	global_load_dwordx4 v[56:59], v[86:87], off
	global_load_dwordx4 v[60:63], v[88:89], off
	global_load_dwordx2 v[130:131], v[116:117], off offset:3072
	global_load_dwordx2 v[132:133], v[116:117], off offset:3584
	global_load_dwordx4 v[64:67], v[90:91], off
	global_load_dwordx4 v[68:71], v[92:93], off
	global_load_dwordx4 v[36:39], v[94:95], off
	global_load_dwordx4 v[44:47], v[96:97], off
	global_load_dwordx2 v[152:153], v140, s[0:1]
	s_lshl_b64 s[0:1], s[8:9], 2
	s_add_u32 s26, s20, s0
	s_addc_u32 s27, s21, s1
	global_load_dwordx4 v[144:147], v140, s[26:27]
	s_add_u32 s26, s24, s0
	s_addc_u32 s27, s25, s1
	s_add_u32 s0, s22, s0
	s_addc_u32 s1, s23, s1
	global_load_dword v154, v140, s[26:27]
	global_load_dword v143, v140, s[0:1]
	s_add_i32 s26, s8, 1
	s_ashr_i32 s27, s26, 31
	s_lshl_b64 s[0:1], s[26:27], 2
	s_add_u32 s26, s24, s0
	s_addc_u32 s27, s25, s1
	global_load_dwordx3 v[148:150], v140, s[26:27]
	s_add_u32 s0, s22, s0
	s_addc_u32 s1, s23, s1
	global_load_dword v151, v140, s[0:1]
	s_add_i32 s26, s8, 2
	s_ashr_i32 s27, s26, 31
	s_lshl_b64 s[0:1], s[26:27], 2
	s_add_u32 s0, s22, s0
	s_addc_u32 s1, s23, s1
	global_load_dwordx2 v[156:157], v140, s[0:1]
	s_add_i32 s2, s2, s16
	s_add_i32 s6, s6, s13
	s_add_i32 s8, s8, s14
	v_lshl_add_u64 v[116:117], v[116:117], 0, s[10:11]
	s_cmpk_lt_i32 s2, 0x4000
	s_waitcnt vmcnt(31)
	v_lshlrev_b32_e32 v160, 16, v120
	v_and_b32_e32 v161, 0xffff0000, v120
	v_lshlrev_b32_e32 v162, 16, v121
	v_and_b32_e32 v163, 0xffff0000, v121
	s_waitcnt vmcnt(26)
	v_lshlrev_b32_e32 v164, 16, v122
	v_and_b32_e32 v165, 0xffff0000, v122
	v_lshlrev_b32_e32 v166, 16, v123
	v_and_b32_e32 v167, 0xffff0000, v123
	s_waitcnt vmcnt(25)
	v_lshlrev_b32_e32 v168, 16, v124
	v_and_b32_e32 v169, 0xffff0000, v124
	v_lshlrev_b32_e32 v170, 16, v125
	v_and_b32_e32 v171, 0xffff0000, v125
	s_waitcnt vmcnt(18)
	v_lshlrev_b32_e32 v172, 16, v126
	v_and_b32_e32 v173, 0xffff0000, v126
	v_lshlrev_b32_e32 v174, 16, v127
	v_and_b32_e32 v175, 0xffff0000, v127
	s_waitcnt vmcnt(17)
	v_lshlrev_b32_e32 v176, 16, v128
	v_and_b32_e32 v177, 0xffff0000, v128
	v_lshlrev_b32_e32 v178, 16, v129
	v_and_b32_e32 v179, 0xffff0000, v129
	s_waitcnt vmcnt(12)
	v_lshlrev_b32_e32 v180, 16, v130
	v_and_b32_e32 v181, 0xffff0000, v130
	v_lshlrev_b32_e32 v158, 16, v119
	v_and_b32_e32 v159, 0xffff0000, v119
	s_waitcnt vmcnt(6)
	v_sub_f32_e32 v121, v159, v152
	v_sub_f32_e32 v120, v158, v152
	v_sub_f32_e32 v123, v161, v152
	v_sub_f32_e32 v122, v160, v152
	v_sub_f32_e32 v125, v163, v152
	v_sub_f32_e32 v124, v162, v152
	v_sub_f32_e32 v127, v165, v152
	v_sub_f32_e32 v126, v164, v152
	v_sub_f32_e32 v129, v167, v152
	v_sub_f32_e32 v128, v166, v152
	v_sub_f32_e32 v159, v173, v152
	v_sub_f32_e32 v158, v172, v152
	v_sub_f32_e32 v161, v175, v152
	v_sub_f32_e32 v160, v174, v152
	v_pk_mul_f32 v[124:125], v[152:153], v[124:125] op_sel:[1,0]
	v_pk_mul_f32 v[122:123], v[152:153], v[122:123] op_sel:[1,0]
	v_pk_mul_f32 v[128:129], v[152:153], v[128:129] op_sel:[1,0]
	v_pk_mul_f32 v[126:127], v[152:153], v[126:127] op_sel:[1,0]
	v_pk_mul_f32 v[160:161], v[152:153], v[160:161] op_sel:[1,0]
	v_pk_mul_f32 v[158:159], v[152:153], v[158:159] op_sel:[1,0]
	v_pk_fma_f32 v[4:5], v[4:5], v[122:123], v[8:9]
	v_pk_fma_f32 v[6:7], v[6:7], v[124:125], v[10:11]
	v_pk_fma_f32 v[8:9], v[16:17], v[126:127], v[28:29]
	v_pk_fma_f32 v[10:11], v[18:19], v[128:129], v[30:31]
	v_pk_fma_f32 v[16:17], v[32:33], v[158:159], v[40:41]
	v_pk_fma_f32 v[18:19], v[34:35], v[160:161], v[42:43]
	s_waitcnt vmcnt(5)
	v_lshlrev_b32_e32 v32, 2, v144
	v_lshlrev_b32_e32 v34, 2, v146
	v_lshlrev_b32_e32 v33, 2, v145
	v_lshlrev_b32_e32 v35, 2, v147
	v_add_u32_e32 v32, s3, v32
	v_add_u32_e32 v40, s3, v34
	v_lshlrev_b32_e32 v155, 16, v118
	v_and_b32_e32 v118, 0xffff0000, v118
	v_add_u32_e32 v33, s3, v33
	v_add_u32_e32 v35, s3, v35
	ds_read_b32 v32, v32
	ds_read_b32 v34, v33
	ds_read_b32 v40, v40
	ds_read_b32 v42, v35
	v_lshlrev_b32_e32 v182, 16, v131
	v_and_b32_e32 v183, 0xffff0000, v131
	v_sub_f32_e32 v119, v118, v152
	v_sub_f32_e32 v118, v155, v152
	v_sub_f32_e32 v131, v169, v152
	v_sub_f32_e32 v130, v168, v152
	v_sub_f32_e32 v163, v177, v152
	v_sub_f32_e32 v162, v176, v152
	v_pk_mul_f32 v[118:119], v[152:153], v[118:119] op_sel:[1,0]
	v_pk_mul_f32 v[130:131], v[152:153], v[130:131] op_sel:[1,0]
	v_pk_mul_f32 v[162:163], v[152:153], v[162:163] op_sel:[1,0]
	s_waitcnt vmcnt(4)
	v_ashrrev_i32_e32 v155, 31, v154
	s_waitcnt lgkmcnt(3)
; #define GAS __attribute__((address_space(1)))
; __device__ __forceinline__ void p9_combine(Frame& F, const LAS int* tstart) {
;     ...
;         size_t ro[4]; float gk[4];
; #pragma unroll
;         for (int k = 0; k < 4; ++k) { const int e = topi[4 * m + k]; ro[k] = ((size_t)tstart[e] * 256 + posb[4 * m + k]) * D; gk[k] = gate[4 * m + k]; }
;         f32x4 v[8]; float s = 0.f;
; #pragma unroll
;         for (int j = 0; j < 8; ++j) { const int col = 4 * lane + 256 * j;
;             const v2u zw = *(const GAS v2u*)(z1 + (size_t)m * D + col); const f32x4 zv = (f32x4){bf_lo(zw.x), bf_hi(zw.x), bf_lo(zw.y), bf_hi(zw.y)}, g = *(const GAS f32x4*)(F.ln1_g + col), b = *(const GAS f32x4*)(F.ln1_b + col);
;             f32x4 a = ((zv - mean1) * rstd1 * g + b) * ALPHA;
; #pragma unroll
;             for (int k = 0; k < 4; ++k) { const int w = *(const GAS int*)(yr + ro[k] + col); const f32x2 lo = __builtin_amdgcn_cvt_pk_f32_fp8(w, false), hi = __builtin_amdgcn_cvt_pk_f32_fp8(w, true); const float g = gk[k] * (1.f / 32.f);
;                 a[0] += g * lo.x; a[1] += g * lo.y; a[2] += g * hi.x; a[3] += g * hi.y; }
	v_ashrrev_i32_e32 v33, 31, v32
	v_lshlrev_b32_e32 v186, 16, v133
	v_and_b32_e32 v187, 0xffff0000, v133
	v_pk_fma_f32 v[0:1], v[0:1], v[118:119], v[12:13]
	v_pk_fma_f32 v[12:13], v[20:21], v[130:131], v[24:25]
	v_pk_fma_f32 v[20:21], v[48:49], v[162:163], v[52:53]
	v_lshlrev_b64 v[48:49], 11, v[154:155]
	v_lshlrev_b64 v[32:33], 19, v[32:33]
	v_lshlrev_b32_e32 v184, 16, v132
	v_and_b32_e32 v185, 0xffff0000, v132
	v_sub_f32_e32 v133, v171, v152
	v_sub_f32_e32 v132, v170, v152
	v_sub_f32_e32 v165, v179, v152
	v_sub_f32_e32 v164, v178, v152
	v_sub_f32_e32 v169, v183, v152
	v_sub_f32_e32 v168, v182, v152
	v_sub_f32_e32 v173, v187, v152
	v_sub_f32_e32 v172, v186, v152
	s_waitcnt lgkmcnt(2)
	v_ashrrev_i32_e32 v35, 31, v34
	s_waitcnt vmcnt(2)
	v_ashrrev_i32_e32 v53, 31, v148
	v_mov_b32_e32 v52, v148
	v_lshl_add_u64 v[32:33], v[48:49], 0, v[32:33]
	v_sub_f32_e32 v167, v181, v152
	v_sub_f32_e32 v166, v180, v152
	v_pk_mul_f32 v[120:121], v[152:153], v[120:121] op_sel:[1,0]
	v_pk_mul_f32 v[132:133], v[152:153], v[132:133] op_sel:[1,0]
	v_pk_mul_f32 v[164:165], v[152:153], v[164:165] op_sel:[1,0]
	v_pk_mul_f32 v[168:169], v[152:153], v[168:169] op_sel:[1,0]
	v_pk_mul_f32 v[172:173], v[152:153], v[172:173] op_sel:[1,0]
	v_lshlrev_b64 v[34:35], 19, v[34:35]
	v_lshlrev_b64 v[48:49], 11, v[52:53]
	v_lshl_add_u64 v[32:33], v[72:73], 0, v[32:33]
	v_pk_mul_f32 v[166:167], v[152:153], v[166:167] op_sel:[1,0]
	v_pk_fma_f32 v[2:3], v[2:3], v[120:121], v[14:15]
	v_pk_fma_f32 v[14:15], v[22:23], v[132:133], v[26:27]
	v_pk_fma_f32 v[22:23], v[50:51], v[164:165], v[54:55]
	v_pk_fma_f32 v[26:27], v[58:59], v[168:169], v[62:63]
	v_pk_fma_f32 v[30:31], v[66:67], v[172:173], v[70:71]
	v_lshl_add_u64 v[34:35], v[48:49], 0, v[34:35]
	global_load_dword v49, v[32:33], off
	global_load_dword v51, v[32:33], off offset:256
	global_load_dword v58, v[32:33], off offset:512
	global_load_dword v62, v[32:33], off offset:768
	global_load_dword v66, v[32:33], off offset:1024
	global_load_dword v70, v[32:33], off offset:1280
	global_load_dword v120, v[32:33], off offset:1536
	v_pk_fma_f32 v[24:25], v[56:57], v[166:167], v[60:61]
	s_waitcnt lgkmcnt(1)
	v_ashrrev_i32_e32 v41, 31, v40
	s_waitcnt lgkmcnt(0)
	v_ashrrev_i32_e32 v43, 31, v42
	v_ashrrev_i32_e32 v55, 31, v149
	v_mov_b32_e32 v54, v149
	v_ashrrev_i32_e32 v57, 31, v150
	v_mov_b32_e32 v56, v150
	v_lshlrev_b64 v[40:41], 19, v[40:41]
	v_lshlrev_b64 v[42:43], 19, v[42:43]
	v_lshlrev_b64 v[52:53], 11, v[54:55]
	v_lshlrev_b64 v[54:55], 11, v[56:57]
	v_sub_f32_e32 v171, v185, v152
	v_sub_f32_e32 v170, v184, v152
	v_lshl_add_u64 v[40:41], v[52:53], 0, v[40:41]
	v_lshl_add_u64 v[42:43], v[54:55], 0, v[42:43]
	v_lshl_add_u64 v[34:35], v[72:73], 0, v[34:35]
	v_pk_mul_f32 v[152:153], v[152:153], v[170:171] op_sel:[1,0]
	v_mul_f32_e32 v50, 0x3d000000, v143
	v_lshl_add_u64 v[40:41], v[72:73], 0, v[40:41]
	v_lshl_add_u64 v[42:43], v[72:73], 0, v[42:43]
	global_load_dword v124, v[34:35], off
	global_load_dword v128, v[40:41], off
	global_load_dword v132, v[42:43], off
	global_load_dword v143, v[34:35], off offset:256
	global_load_dword v150, v[40:41], off offset:256
	global_load_dword v154, v[42:43], off offset:256
	global_load_dword v158, v[34:35], off offset:512
	global_load_dword v162, v[40:41], off offset:512
	global_load_dword v166, v[42:43], off offset:512
	global_load_dword v170, v[34:35], off offset:768
	global_load_dword v174, v[40:41], off offset:768
	global_load_dword v178, v[42:43], off offset:768
	global_load_dword v182, v[34:35], off offset:1024
	global_load_dword v186, v[40:41], off offset:1024
	global_load_dword v190, v[42:43], off offset:1024
	global_load_dword v194, v[34:35], off offset:1280
	global_load_dword v198, v[40:41], off offset:1280
	global_load_dword v202, v[42:43], off offset:1280
	global_load_dword v206, v[34:35], off offset:1536
	global_load_dword v210, v[40:41], off offset:1536
	global_load_dword v214, v[42:43], off offset:1536
	s_nop 0
	global_load_dword v33, v[32:33], off offset:1792
	s_nop 0
	global_load_dword v35, v[34:35], off offset:1792
	s_nop 0
	global_load_dword v226, v[40:41], off offset:1792
	global_load_dword v230, v[42:43], off offset:1792
	v_pk_fma_f32 v[28:29], v[64:65], v[152:153], v[68:69]
	s_waitcnt vmcnt(33)
	v_mul_f32_e32 v48, 0x3d000000, v151
	s_waitcnt vmcnt(32)
	v_mul_f32_e32 v32, 0x3d000000, v156
	v_mul_f32_e32 v34, 0x3d000000, v157
	v_pk_mul_f32 v[2:3], v[2:3], s[12:13] op_sel_hi:[1,0]
	v_pk_mul_f32 v[0:1], v[0:1], s[12:13] op_sel_hi:[1,0]
	v_pk_mul_f32 v[6:7], v[6:7], s[12:13] op_sel_hi:[1,0]
	v_pk_mul_f32 v[4:5], v[4:5], s[12:13] op_sel_hi:[1,0]
	v_pk_mul_f32 v[10:11], v[10:11], s[12:13] op_sel_hi:[1,0]
	v_pk_mul_f32 v[8:9], v[8:9], s[12:13] op_sel_hi:[1,0]
	v_pk_mul_f32 v[14:15], v[14:15], s[12:13] op_sel_hi:[1,0]
	v_pk_mul_f32 v[12:13], v[12:13], s[12:13] op_sel_hi:[1,0]
	v_pk_mul_f32 v[18:19], v[18:19], s[12:13] op_sel_hi:[1,0]
	v_pk_mul_f32 v[16:17], v[16:17], s[12:13] op_sel_hi:[1,0]
	v_pk_mul_f32 v[20:21], v[20:21], s[12:13] op_sel_hi:[1,0]
	v_pk_mul_f32 v[22:23], v[22:23], s[12:13] op_sel_hi:[1,0]
	v_pk_mul_f32 v[26:27], v[26:27], s[12:13] op_sel_hi:[1,0]
	v_pk_mul_f32 v[24:25], v[24:25], s[12:13] op_sel_hi:[1,0]
	v_pk_mul_f32 v[30:31], v[30:31], s[12:13] op_sel_hi:[1,0]
	v_pk_mul_f32 v[28:29], v[28:29], s[12:13] op_sel_hi:[1,0]
	s_waitcnt vmcnt(31)
	v_cvt_pk_f32_fp8_e32 v[40:41], v49
	v_cvt_pk_f32_fp8_sdwa v[42:43], v49 src0_sel:WORD_1
	s_waitcnt vmcnt(30)
	v_cvt_pk_f32_fp8_e32 v[52:53], v51
	v_cvt_pk_f32_fp8_sdwa v[54:55], v51 src0_sel:WORD_1
	s_waitcnt vmcnt(29)
	v_cvt_pk_f32_fp8_e32 v[56:57], v58
	v_cvt_pk_f32_fp8_sdwa v[58:59], v58 src0_sel:WORD_1
	s_waitcnt vmcnt(28)
; #define GAS __attribute__((address_space(1)))
; __device__ __forceinline__ void p9_combine(Frame& F, const LAS int* tstart) {
;     ...
; #pragma unroll
;             for (int k = 0; k < 4; ++k) { const int w = *(const GAS int*)(yr + ro[k] + col); const f32x2 lo = __builtin_amdgcn_cvt_pk_f32_fp8(w, false), hi = __builtin_amdgcn_cvt_pk_f32_fp8(w, true); const float g = gk[k] * (1.f / 32.f);
;                 a[0] += g * lo.x; a[1] += g * lo.y; a[2] += g * hi.x; a[3] += g * hi.y; }
;             v[j] = a; s += (a[0] + a[1]) + (a[2] + a[3]); }
	v_cvt_pk_f32_fp8_e32 v[60:61], v62
	v_cvt_pk_f32_fp8_sdwa v[62:63], v62 src0_sel:WORD_1
	s_waitcnt vmcnt(27)
	v_cvt_pk_f32_fp8_e32 v[64:65], v66
	v_cvt_pk_f32_fp8_sdwa v[66:67], v66 src0_sel:WORD_1
	s_waitcnt vmcnt(26)
	v_cvt_pk_f32_fp8_e32 v[68:69], v70
	s_waitcnt vmcnt(24)
	v_cvt_pk_f32_fp8_e32 v[122:123], v124
	v_cvt_pk_f32_fp8_sdwa v[124:125], v124 src0_sel:WORD_1
	s_waitcnt vmcnt(21)
	v_cvt_pk_f32_fp8_e32 v[144:145], v143
	v_cvt_pk_f32_fp8_sdwa v[146:147], v143 src0_sel:WORD_1
	v_cvt_pk_f32_fp8_sdwa v[70:71], v70 src0_sel:WORD_1
	v_cvt_pk_f32_fp8_e32 v[118:119], v120
	v_cvt_pk_f32_fp8_sdwa v[120:121], v120 src0_sel:WORD_1
	v_cvt_pk_f32_fp8_e32 v[126:127], v128
	v_cvt_pk_f32_fp8_sdwa v[128:129], v128 src0_sel:WORD_1
	s_waitcnt vmcnt(20)
	v_cvt_pk_f32_fp8_e32 v[148:149], v150
	v_cvt_pk_f32_fp8_sdwa v[150:151], v150 src0_sel:WORD_1
	s_waitcnt vmcnt(18)
	v_cvt_pk_f32_fp8_e32 v[156:157], v158
	v_cvt_pk_f32_fp8_sdwa v[158:159], v158 src0_sel:WORD_1
	s_waitcnt vmcnt(15)
	v_cvt_pk_f32_fp8_e32 v[168:169], v170
	v_cvt_pk_f32_fp8_sdwa v[170:171], v170 src0_sel:WORD_1
	s_waitcnt vmcnt(12)
	v_cvt_pk_f32_fp8_e32 v[180:181], v182
	v_cvt_pk_f32_fp8_sdwa v[182:183], v182 src0_sel:WORD_1
	s_waitcnt vmcnt(9)
	v_cvt_pk_f32_fp8_e32 v[192:193], v194
	s_waitcnt vmcnt(3)
	v_cvt_pk_f32_fp8_e32 v[216:217], v33
	v_cvt_pk_f32_fp8_sdwa v[218:219], v33 src0_sel:WORD_1
	v_cvt_pk_f32_fp8_e32 v[130:131], v132
	v_cvt_pk_f32_fp8_sdwa v[132:133], v132 src0_sel:WORD_1
	v_cvt_pk_f32_fp8_e32 v[152:153], v154
	v_cvt_pk_f32_fp8_sdwa v[154:155], v154 src0_sel:WORD_1
	v_cvt_pk_f32_fp8_e32 v[160:161], v162
	v_cvt_pk_f32_fp8_sdwa v[162:163], v162 src0_sel:WORD_1
	v_cvt_pk_f32_fp8_e32 v[172:173], v174
	v_cvt_pk_f32_fp8_sdwa v[174:175], v174 src0_sel:WORD_1
	v_cvt_pk_f32_fp8_e32 v[184:185], v186
	v_cvt_pk_f32_fp8_sdwa v[186:187], v186 src0_sel:WORD_1
	v_cvt_pk_f32_fp8_sdwa v[194:195], v194 src0_sel:WORD_1
	v_cvt_pk_f32_fp8_e32 v[196:197], v198
	v_cvt_pk_f32_fp8_e32 v[204:205], v206
	v_cvt_pk_f32_fp8_sdwa v[206:207], v206 src0_sel:WORD_1
	s_waitcnt vmcnt(2)
	v_cvt_pk_f32_fp8_e32 v[220:221], v35
	v_cvt_pk_f32_fp8_sdwa v[222:223], v35 src0_sel:WORD_1
	v_cvt_pk_f32_fp8_e32 v[164:165], v166
	v_cvt_pk_f32_fp8_sdwa v[166:167], v166 src0_sel:WORD_1
	v_cvt_pk_f32_fp8_e32 v[176:177], v178
	v_cvt_pk_f32_fp8_sdwa v[178:179], v178 src0_sel:WORD_1
	v_cvt_pk_f32_fp8_e32 v[188:189], v190
	v_cvt_pk_f32_fp8_sdwa v[190:191], v190 src0_sel:WORD_1
	v_cvt_pk_f32_fp8_sdwa v[198:199], v198 src0_sel:WORD_1
	v_cvt_pk_f32_fp8_e32 v[200:201], v202
	v_cvt_pk_f32_fp8_e32 v[208:209], v210
	v_pk_fma_f32 v[0:1], v[50:51], v[40:41], v[0:1] op_sel_hi:[0,1,1]
	v_pk_fma_f32 v[2:3], v[50:51], v[42:43], v[2:3] op_sel_hi:[0,1,1]
	v_pk_fma_f32 v[4:5], v[50:51], v[52:53], v[4:5] op_sel_hi:[0,1,1]
	v_pk_fma_f32 v[6:7], v[50:51], v[54:55], v[6:7] op_sel_hi:[0,1,1]
	v_cvt_pk_f32_fp8_sdwa v[202:203], v202 src0_sel:WORD_1
	v_cvt_pk_f32_fp8_e32 v[212:213], v214
	v_pk_fma_f32 v[8:9], v[50:51], v[56:57], v[8:9] op_sel_hi:[0,1,1]
	v_pk_fma_f32 v[10:11], v[50:51], v[58:59], v[10:11] op_sel_hi:[0,1,1]
	v_pk_fma_f32 v[12:13], v[50:51], v[60:61], v[12:13] op_sel_hi:[0,1,1]
	v_pk_fma_f32 v[14:15], v[50:51], v[62:63], v[14:15] op_sel_hi:[0,1,1]
	v_pk_fma_f32 v[16:17], v[50:51], v[64:65], v[16:17] op_sel_hi:[0,1,1]
	v_pk_fma_f32 v[18:19], v[50:51], v[66:67], v[18:19] op_sel_hi:[0,1,1]
	v_pk_fma_f32 v[20:21], v[50:51], v[68:69], v[20:21] op_sel_hi:[0,1,1]
	v_pk_fma_f32 v[0:1], v[48:49], v[122:123], v[0:1] op_sel_hi:[0,1,1]
	v_pk_fma_f32 v[2:3], v[48:49], v[124:125], v[2:3] op_sel_hi:[0,1,1]
	v_pk_fma_f32 v[4:5], v[48:49], v[144:145], v[4:5] op_sel_hi:[0,1,1]
	v_pk_fma_f32 v[6:7], v[48:49], v[146:147], v[6:7] op_sel_hi:[0,1,1]
	v_cvt_pk_f32_fp8_sdwa v[210:211], v210 src0_sel:WORD_1
	v_pk_fma_f32 v[22:23], v[50:51], v[70:71], v[22:23] op_sel_hi:[0,1,1]
	v_pk_fma_f32 v[24:25], v[50:51], v[118:119], v[24:25] op_sel_hi:[0,1,1]
	v_pk_fma_f32 v[26:27], v[50:51], v[120:121], v[26:27] op_sel_hi:[0,1,1]
	v_pk_fma_f32 v[8:9], v[48:49], v[156:157], v[8:9] op_sel_hi:[0,1,1]
	v_pk_fma_f32 v[10:11], v[48:49], v[158:159], v[10:11] op_sel_hi:[0,1,1]
	v_pk_fma_f32 v[12:13], v[48:49], v[168:169], v[12:13] op_sel_hi:[0,1,1]
	v_pk_fma_f32 v[14:15], v[48:49], v[170:171], v[14:15] op_sel_hi:[0,1,1]
	v_pk_fma_f32 v[16:17], v[48:49], v[180:181], v[16:17] op_sel_hi:[0,1,1]
	v_pk_fma_f32 v[18:19], v[48:49], v[182:183], v[18:19] op_sel_hi:[0,1,1]
	v_pk_fma_f32 v[20:21], v[48:49], v[192:193], v[20:21] op_sel_hi:[0,1,1]
	v_pk_fma_f32 v[28:29], v[50:51], v[216:217], v[28:29] op_sel_hi:[0,1,1]
	v_pk_fma_f32 v[30:31], v[50:51], v[218:219], v[30:31] op_sel_hi:[0,1,1]
	v_pk_fma_f32 v[0:1], v[32:33], v[126:127], v[0:1] op_sel_hi:[0,1,1]
	v_pk_fma_f32 v[2:3], v[32:33], v[128:129], v[2:3] op_sel_hi:[0,1,1]
	v_pk_fma_f32 v[4:5], v[32:33], v[148:149], v[4:5] op_sel_hi:[0,1,1]
	v_pk_fma_f32 v[6:7], v[32:33], v[150:151], v[6:7] op_sel_hi:[0,1,1]
	v_cvt_pk_f32_fp8_sdwa v[214:215], v214 src0_sel:WORD_1
	s_waitcnt vmcnt(1)
; #define GAS __attribute__((address_space(1)))
; __device__ __forceinline__ float wave_sum(float v) {
; #pragma unroll
;     for (int o = 1; o < 64; o <<= 1) v += __shfl_xor(v, o);
;     return v;
; __device__ __forceinline__ void p9_combine(Frame& F, const LAS int* tstart) {
;     ...
;         for (int j = 0; j < 8; ++j) { const int col = 4 * lane + 256 * j;
;             const v2u zw = *(const GAS v2u*)(z1 + (size_t)m * D + col); const f32x4 zv = (f32x4){bf_lo(zw.x), bf_hi(zw.x), bf_lo(zw.y), bf_hi(zw.y)}, g = *(const GAS f32x4*)(F.ln1_g + col), b = *(const GAS f32x4*)(F.ln1_b + col);
;             f32x4 a = ((zv - mean1) * rstd1 * g + b) * ALPHA;
; #pragma unroll
;             for (int k = 0; k < 4; ++k) { const int w = *(const GAS int*)(yr + ro[k] + col); const f32x2 lo = __builtin_amdgcn_cvt_pk_f32_fp8(w, false), hi = __builtin_amdgcn_cvt_pk_f32_fp8(w, true); const float g = gk[k] * (1.f / 32.f);
;                 a[0] += g * lo.x; a[1] += g * lo.y; a[2] += g * hi.x; a[3] += g * hi.y; }
;             v[j] = a; s += (a[0] + a[1]) + (a[2] + a[3]); }
;         const float mean = wave_sum(s) * (1.f / D); float s2 = 0.f;
	v_cvt_pk_f32_fp8_e32 v[224:225], v226
	v_pk_fma_f32 v[22:23], v[48:49], v[194:195], v[22:23] op_sel_hi:[0,1,1]
	v_pk_fma_f32 v[24:25], v[48:49], v[204:205], v[24:25] op_sel_hi:[0,1,1]
	v_pk_fma_f32 v[26:27], v[48:49], v[206:207], v[26:27] op_sel_hi:[0,1,1]
	v_pk_fma_f32 v[8:9], v[32:33], v[160:161], v[8:9] op_sel_hi:[0,1,1]
	v_pk_fma_f32 v[10:11], v[32:33], v[162:163], v[10:11] op_sel_hi:[0,1,1]
	v_pk_fma_f32 v[12:13], v[32:33], v[172:173], v[12:13] op_sel_hi:[0,1,1]
	v_pk_fma_f32 v[14:15], v[32:33], v[174:175], v[14:15] op_sel_hi:[0,1,1]
	v_pk_fma_f32 v[16:17], v[32:33], v[184:185], v[16:17] op_sel_hi:[0,1,1]
	v_pk_fma_f32 v[18:19], v[32:33], v[186:187], v[18:19] op_sel_hi:[0,1,1]
	v_pk_fma_f32 v[20:21], v[32:33], v[196:197], v[20:21] op_sel_hi:[0,1,1]
	v_pk_fma_f32 v[28:29], v[48:49], v[220:221], v[28:29] op_sel_hi:[0,1,1]
	v_pk_fma_f32 v[30:31], v[48:49], v[222:223], v[30:31] op_sel_hi:[0,1,1]
	v_pk_fma_f32 v[40:41], v[34:35], v[130:131], v[0:1] op_sel_hi:[0,1,1]
	v_pk_fma_f32 v[42:43], v[34:35], v[132:133], v[2:3] op_sel_hi:[0,1,1]
	v_pk_fma_f32 v[48:49], v[34:35], v[152:153], v[4:5] op_sel_hi:[0,1,1]
	v_pk_fma_f32 v[50:51], v[34:35], v[154:155], v[6:7] op_sel_hi:[0,1,1]
	v_cvt_pk_f32_fp8_sdwa v[226:227], v226 src0_sel:WORD_1
	v_pk_fma_f32 v[22:23], v[32:33], v[198:199], v[22:23] op_sel_hi:[0,1,1]
	v_pk_fma_f32 v[24:25], v[32:33], v[208:209], v[24:25] op_sel_hi:[0,1,1]
	v_pk_fma_f32 v[52:53], v[34:35], v[164:165], v[8:9] op_sel_hi:[0,1,1]
	v_pk_fma_f32 v[54:55], v[34:35], v[166:167], v[10:11] op_sel_hi:[0,1,1]
	v_pk_fma_f32 v[56:57], v[34:35], v[176:177], v[12:13] op_sel_hi:[0,1,1]
	v_pk_fma_f32 v[58:59], v[34:35], v[178:179], v[14:15] op_sel_hi:[0,1,1]
	v_pk_fma_f32 v[12:13], v[34:35], v[188:189], v[16:17] op_sel_hi:[0,1,1]
	v_pk_fma_f32 v[60:61], v[34:35], v[190:191], v[18:19] op_sel_hi:[0,1,1]
	v_pk_fma_f32 v[8:9], v[34:35], v[200:201], v[20:21] op_sel_hi:[0,1,1]
	v_mov_b32_e32 v14, v40
	v_mov_b32_e32 v15, v48
	v_mov_b32_e32 v16, v41
	v_mov_b32_e32 v17, v49
	v_mov_b32_e32 v18, v42
	v_mov_b32_e32 v19, v50
	v_mov_b32_e32 v20, v43
	v_mov_b32_e32 v21, v51
	v_pk_fma_f32 v[10:11], v[34:35], v[202:203], v[22:23] op_sel_hi:[0,1,1]
	v_pk_fma_f32 v[4:5], v[34:35], v[212:213], v[24:25] op_sel_hi:[0,1,1]
	v_mov_b32_e32 v22, v52
	v_mov_b32_e32 v23, v54
	v_mov_b32_e32 v24, v53
	v_mov_b32_e32 v25, v55
	v_pk_add_f32 v[14:15], v[14:15], v[16:17]
	v_pk_add_f32 v[16:17], v[18:19], v[20:21]
	v_pk_fma_f32 v[26:27], v[32:33], v[210:211], v[26:27] op_sel_hi:[0,1,1]
	v_pk_add_f32 v[18:19], v[22:23], v[24:25]
	v_pk_add_f32 v[14:15], v[14:15], v[16:17]
	s_waitcnt vmcnt(0)
	v_cvt_pk_f32_fp8_e32 v[228:229], v230
	v_cvt_pk_f32_fp8_sdwa v[230:231], v230 src0_sel:WORD_1
	v_pk_fma_f32 v[6:7], v[34:35], v[214:215], v[26:27] op_sel_hi:[0,1,1]
	v_pk_fma_f32 v[0:1], v[32:33], v[224:225], v[28:29] op_sel_hi:[0,1,1]
	v_pk_add_f32 v[26:27], v[56:57], v[56:57] op_sel:[0,1] op_sel_hi:[1,0]
	v_pk_add_f32 v[28:29], v[58:59], v[58:59] op_sel:[0,1] op_sel_hi:[1,0]
	v_pk_add_f32 v[16:17], v[18:19], v[18:19] op_sel:[0,1] op_sel_hi:[1,0]
	v_add_f32_e32 v14, 0, v14
	v_pk_fma_f32 v[2:3], v[32:33], v[226:227], v[30:31] op_sel_hi:[0,1,1]
	v_mov_b32_e32 v31, v12
	v_mov_b32_e32 v27, v60
	v_mov_b32_e32 v29, v61
	v_mov_b32_e32 v17, v13
	v_add_f32_e32 v30, v14, v15
	v_mov_b32_e32 v32, v8
	v_mov_b32_e32 v33, v10
	v_mov_b32_e32 v62, v9
	v_mov_b32_e32 v63, v11
	v_pk_add_f32 v[18:19], v[26:27], v[28:29]
	v_pk_add_f32 v[14:15], v[30:31], v[16:17]
	v_pk_add_f32 v[20:21], v[32:33], v[62:63]
	v_pk_add_f32 v[14:15], v[14:15], v[18:19]
	v_pk_add_f32 v[64:65], v[4:5], v[4:5] op_sel:[0,1] op_sel_hi:[1,0]
	v_pk_add_f32 v[66:67], v[6:7], v[6:7] op_sel:[0,1] op_sel_hi:[1,0]
	v_pk_fma_f32 v[0:1], v[34:35], v[228:229], v[0:1] op_sel_hi:[0,1,1]
	v_pk_fma_f32 v[2:3], v[34:35], v[230:231], v[2:3] op_sel_hi:[0,1,1]
	v_pk_add_f32 v[20:21], v[20:21], v[20:21] op_sel:[0,1] op_sel_hi:[1,0]
	v_pk_add_f32 v[14:15], v[14:15], v[14:15] op_sel:[0,1] op_sel_hi:[1,0]
	v_mov_b32_e32 v65, v2
	v_mov_b32_e32 v67, v3
	v_mov_b32_e32 v21, v1
	v_mov_b32_e32 v15, v0
	v_pk_add_f32 v[22:23], v[64:65], v[66:67]
	v_pk_add_f32 v[14:15], v[14:15], v[20:21]
	s_nop 0
	v_pk_add_f32 v[14:15], v[14:15], v[22:23]
	s_nop 0
	v_add_f32_e32 v14, v14, v15
	s_waitcnt lgkmcnt(0)
	s_nop 1
	v_add_f32_dpp v14, v14, v14 quad_perm:[1,0,3,2] row_mask:0xf bank_mask:0xf
	s_waitcnt lgkmcnt(0)
	s_nop 1
	v_add_f32_dpp v14, v14, v14 quad_perm:[2,3,0,1] row_mask:0xf bank_mask:0xf
	s_waitcnt lgkmcnt(0)
	s_nop 1
	v_add_f32_dpp v14, v14, v14 row_half_mirror row_mask:0xf bank_mask:0xf
	s_waitcnt lgkmcnt(0)
	s_nop 1
	v_add_f32_dpp v14, v14, v14 row_mirror row_mask:0xf bank_mask:0xf
	s_waitcnt lgkmcnt(0)
	v_mov_b32_e32 v15, v14
	s_nop 1
	v_permlane16_swap_b32_e32 v14, v15
	v_add_f32_e32 v14, v14, v15
	s_waitcnt lgkmcnt(0)
; __device__ __forceinline__ float wave_sum(float v) {
; #pragma unroll
;     for (int o = 1; o < 64; o <<= 1) v += __shfl_xor(v, o);
;     return v;
; __device__ __forceinline__ void p9_combine(Frame& F, const LAS int* tstart) {
;     ...
;         const float mean = wave_sum(s) * (1.f / D); float s2 = 0.f;
; #pragma unroll
;         for (int j = 0; j < 8; ++j) { v[j] = v[j] - mean; s2 += (v[j][0] * v[j][0] + v[j][1] * v[j][1]) + (v[j][2] * v[j][2] + v[j][3] * v[j][3]); }
;         const float rstd = 1.f / sqrtf(wave_sum(s2) * (1.f / D) + LN_EPS);
	v_mov_b32_e32 v15, v14
	s_nop 1
	v_permlane32_swap_b32_e32 v14, v15
	v_add_f32_e32 v14, v14, v15
	v_fmamk_f32 v43, v14, 0xba000000, v43
	v_fmamk_f32 v41, v14, 0xba000000, v41
	v_fmamk_f32 v51, v14, 0xba000000, v51
	v_fmamk_f32 v49, v14, 0xba000000, v49
	v_fmac_f32_e32 v42, 0xba000000, v14
	v_fmac_f32_e32 v40, 0xba000000, v14
	v_fmac_f32_e32 v50, 0xba000000, v14
	v_fmac_f32_e32 v48, 0xba000000, v14
	v_fmamk_f32 v53, v14, 0xba000000, v53
	v_fmac_f32_e32 v52, 0xba000000, v14
	v_fmamk_f32 v55, v14, 0xba000000, v55
	v_fmac_f32_e32 v54, 0xba000000, v14
	v_mov_b32_e32 v16, v41
	v_mov_b32_e32 v17, v49
	v_mov_b32_e32 v20, v43
	v_mov_b32_e32 v21, v51
	v_fmamk_f32 v57, v14, 0xba000000, v57
	v_fmac_f32_e32 v56, 0xba000000, v14
	v_fmamk_f32 v59, v14, 0xba000000, v59
	v_fmac_f32_e32 v58, 0xba000000, v14
	v_fmamk_f32 v61, v14, 0xba000000, v61
	v_fmac_f32_e32 v60, 0xba000000, v14
	v_fmamk_f32 v13, v14, 0xba000000, v13
	v_fmac_f32_e32 v12, 0xba000000, v14
	v_fmamk_f32 v9, v14, 0xba000000, v9
	v_fmac_f32_e32 v8, 0xba000000, v14
	v_fmamk_f32 v11, v14, 0xba000000, v11
	v_fmac_f32_e32 v10, 0xba000000, v14
	v_fmamk_f32 v5, v14, 0xba000000, v5
	v_fmac_f32_e32 v4, 0xba000000, v14
	v_fmamk_f32 v7, v14, 0xba000000, v7
	v_fmac_f32_e32 v6, 0xba000000, v14
	v_fmamk_f32 v3, v14, 0xba000000, v3
	v_fmac_f32_e32 v2, 0xba000000, v14
	v_fmamk_f32 v1, v14, 0xba000000, v1
	v_fmac_f32_e32 v0, 0xba000000, v14
	v_mov_b32_e32 v14, v40
	v_mov_b32_e32 v15, v48
	v_mov_b32_e32 v18, v42
	v_mov_b32_e32 v19, v50
	v_pk_mul_f32 v[22:23], v[54:55], v[54:55]
	v_pk_mul_f32 v[24:25], v[52:53], v[52:53]
	v_pk_mul_f32 v[16:17], v[16:17], v[16:17]
	v_pk_mul_f32 v[20:21], v[20:21], v[20:21]
	v_pk_mov_b32 v[64:65], v[24:25], v[22:23] op_sel:[1,0]
	v_mov_b32_e32 v25, v23
	v_pk_fma_f32 v[14:15], v[14:15], v[14:15], v[16:17]
	v_pk_fma_f32 v[16:17], v[18:19], v[18:19], v[20:21]
	v_mul_f32_e32 v26, v56, v56
	v_mul_f32_e32 v28, v58, v58
	v_pk_add_f32 v[18:19], v[64:65], v[24:25]
	v_pk_add_f32 v[14:15], v[14:15], v[16:17]
	v_pk_fma_f32 v[22:23], v[56:57], v[56:57], v[26:27] op_sel_hi:[1,1,0]
	v_pk_fma_f32 v[26:27], v[58:59], v[58:59], v[28:29] op_sel_hi:[1,1,0]
	v_pk_add_f32 v[16:17], v[18:19], v[18:19] op_sel_hi:[0,1]
	v_pk_add_f32 v[14:15], v[14:15], v[14:15] op_sel_hi:[0,1]
	v_pk_mul_f32 v[30:31], v[10:11], v[10:11]
	v_pk_mul_f32 v[32:33], v[8:9], v[8:9]
	v_mul_f32_e32 v22, v12, v12
	v_mul_f32_e32 v26, v13, v13
	v_mul_f32_e32 v16, v60, v60
	v_mul_f32_e32 v14, v61, v61
	v_pk_mov_b32 v[28:29], v[32:33], v[30:31] op_sel:[1,0]
	v_mov_b32_e32 v33, v31
	v_pk_add_f32 v[18:19], v[22:23], v[26:27]
	v_pk_add_f32 v[14:15], v[16:17], v[14:15]
	v_mul_f32_e32 v34, v4, v4
	v_mul_f32_e32 v62, v6, v6
	v_pk_add_f32 v[20:21], v[28:29], v[32:33]
	v_pk_add_f32 v[14:15], v[18:19], v[14:15]
	v_pk_fma_f32 v[30:31], v[4:5], v[4:5], v[34:35] op_sel_hi:[1,1,0]
	v_pk_fma_f32 v[34:35], v[6:7], v[6:7], v[62:63] op_sel_hi:[1,1,0]
	v_pk_add_f32 v[20:21], v[20:21], v[20:21] op_sel_hi:[0,1]
	v_pk_add_f32 v[14:15], v[14:15], v[14:15] op_sel_hi:[0,1]
	v_mul_f32_e32 v30, v0, v0
	v_mul_f32_e32 v34, v1, v1
	v_mul_f32_e32 v20, v2, v2
	v_mul_f32_e32 v14, v3, v3
	v_pk_add_f32 v[22:23], v[30:31], v[34:35]
	v_pk_add_f32 v[14:15], v[20:21], v[14:15]
	s_nop 0
	v_pk_add_f32 v[14:15], v[22:23], v[14:15]
	s_nop 0
	v_add_f32_e32 v14, v14, v15
	s_waitcnt lgkmcnt(0)
	s_nop 1
	v_add_f32_dpp v14, v14, v14 quad_perm:[1,0,3,2] row_mask:0xf bank_mask:0xf
	s_waitcnt lgkmcnt(0)
	s_nop 1
	v_add_f32_dpp v14, v14, v14 quad_perm:[2,3,0,1] row_mask:0xf bank_mask:0xf
	s_waitcnt lgkmcnt(0)
	s_nop 1
	v_add_f32_dpp v14, v14, v14 row_half_mirror row_mask:0xf bank_mask:0xf
	s_waitcnt lgkmcnt(0)
	s_nop 1
	v_add_f32_dpp v14, v14, v14 row_mirror row_mask:0xf bank_mask:0xf
	s_waitcnt lgkmcnt(0)
	v_mov_b32_e32 v15, v14
	s_nop 1
	v_permlane16_swap_b32_e32 v14, v15
	v_add_f32_e32 v14, v14, v15
	s_waitcnt lgkmcnt(0)
; #define GAS __attribute__((address_space(1)))
; __device__ __forceinline__ void p9_combine(Frame& F, const LAS int* tstart) {
;     ...
;         const float rstd = 1.f / sqrtf(wave_sum(s2) * (1.f / D) + LN_EPS);
; #pragma unroll
;         for (int j = 0; j < 8; ++j) { const int col = 4 * lane + 256 * j; const f32x4 g = *(const GAS f32x4*)(F.ln2_g + col), b = *(const GAS f32x4*)(F.ln2_b + col);
;             *(GAS f32x4*)(F.out + (size_t)m * D + col) = v[j] * rstd * g + b; }
	v_mov_b32_e32 v15, v14
	s_nop 1
	v_permlane32_swap_b32_e32 v14, v15
	v_add_f32_e32 v14, v14, v15
	v_fmamk_f32 v14, v14, 0x3a000000, v141
	v_mul_f32_e32 v15, 0x4f800000, v14
	v_cmp_gt_f32_e32 vcc, s15, v14
	s_nop 1
	v_cndmask_b32_e32 v14, v14, v15, vcc
	v_sqrt_f32_e32 v15, v14
	s_nop 0
	v_add_u32_e32 v16, -1, v15
	v_add_u32_e32 v17, 1, v15
	v_fma_f32 v18, -v16, v15, v14
	v_fma_f32 v19, -v17, v15, v14
	v_cmp_ge_f32_e64 s[0:1], 0, v18
	s_nop 1
	v_cndmask_b32_e64 v15, v15, v16, s[0:1]
	v_cmp_lt_f32_e64 s[0:1], 0, v19
	s_nop 1
	v_cndmask_b32_e64 v15, v15, v17, s[0:1]
	v_mul_f32_e32 v16, 0x37800000, v15
	v_cndmask_b32_e32 v15, v15, v16, vcc
	v_cmp_class_f32_e32 vcc, v14, v142
	s_nop 1
	v_cndmask_b32_e32 v14, v15, v14, vcc
	v_div_scale_f32 v15, s[0:1], v14, v14, 1.0
	v_rcp_f32_e32 v17, v15
	v_div_scale_f32 v16, vcc, 1.0, v14, 1.0
	v_fma_f32 v18, -v15, v17, 1.0
	v_fmac_f32_e32 v17, v18, v17
	v_mul_f32_e32 v18, v16, v17
	v_fma_f32 v19, -v15, v18, v16
	v_fmac_f32_e32 v18, v19, v17
	v_fma_f32 v15, -v15, v18, v16
	v_div_fmas_f32 v15, v15, v17, v18
	v_div_fixup_f32 v22, v15, v14, 1.0
	v_pk_mul_f32 v[14:15], v[40:41], v[22:23] op_sel_hi:[1,0]
	v_pk_mul_f32 v[16:17], v[42:43], v[22:23] op_sel_hi:[1,0]
	v_pk_fma_f32 v[14:15], v[36:37], v[14:15], v[44:45]
	v_pk_fma_f32 v[16:17], v[38:39], v[16:17], v[46:47]
	global_store_dwordx4 v[114:115], v[14:17], off offset:-4096
	global_load_dwordx4 v[14:17], v[94:95], off offset:1024
	s_nop 0
	global_load_dwordx4 v[18:21], v[96:97], off offset:1024
	v_pk_mul_f32 v[24:25], v[50:51], v[22:23] op_sel_hi:[1,0]
	v_pk_mul_f32 v[26:27], v[48:49], v[22:23] op_sel_hi:[1,0]
	v_pk_mul_f32 v[12:13], v[12:13], v[22:23] op_sel_hi:[1,0]
	v_pk_mul_f32 v[10:11], v[10:11], v[22:23] op_sel_hi:[1,0]
	v_pk_mul_f32 v[8:9], v[8:9], v[22:23] op_sel_hi:[1,0]
	v_pk_mul_f32 v[6:7], v[6:7], v[22:23] op_sel_hi:[1,0]
	v_pk_mul_f32 v[4:5], v[4:5], v[22:23] op_sel_hi:[1,0]
	v_pk_mul_f32 v[2:3], v[2:3], v[22:23] op_sel_hi:[1,0]
	v_pk_mul_f32 v[0:1], v[0:1], v[22:23] op_sel_hi:[1,0]
	s_waitcnt vmcnt(0)
	v_pk_fma_f32 v[14:15], v[14:15], v[26:27], v[18:19]
	v_pk_fma_f32 v[16:17], v[16:17], v[24:25], v[20:21]
	global_store_dwordx4 v[114:115], v[14:17], off offset:-3072
	global_load_dwordx4 v[14:17], v[94:95], off offset:2048
	s_nop 0
	global_load_dwordx4 v[18:21], v[96:97], off offset:2048
	v_pk_mul_f32 v[24:25], v[54:55], v[22:23] op_sel_hi:[1,0]
	v_pk_mul_f32 v[26:27], v[52:53], v[22:23] op_sel_hi:[1,0]
	s_waitcnt vmcnt(0)
	v_pk_fma_f32 v[16:17], v[16:17], v[24:25], v[20:21]
	v_pk_fma_f32 v[14:15], v[14:15], v[26:27], v[18:19]
	global_store_dwordx4 v[114:115], v[14:17], off offset:-2048
	global_load_dwordx4 v[14:17], v[94:95], off offset:3072
	s_nop 0
	global_load_dwordx4 v[18:21], v[96:97], off offset:3072
	v_pk_mul_f32 v[24:25], v[58:59], v[22:23] op_sel_hi:[1,0]
	v_pk_mul_f32 v[26:27], v[56:57], v[22:23] op_sel_hi:[1,0]
	s_waitcnt vmcnt(0)
	v_pk_fma_f32 v[16:17], v[16:17], v[24:25], v[20:21]
	v_pk_fma_f32 v[14:15], v[14:15], v[26:27], v[18:19]
	global_store_dwordx4 v[114:115], v[14:17], off offset:-1024
	global_load_dwordx4 v[14:17], v[98:99], off
	s_nop 0
	global_load_dwordx4 v[18:21], v[100:101], off
	v_pk_mul_f32 v[24:25], v[60:61], v[22:23] op_sel_hi:[1,0]
	s_waitcnt vmcnt(0)
	v_pk_fma_f32 v[12:13], v[14:15], v[12:13], v[18:19]
	v_pk_fma_f32 v[14:15], v[16:17], v[24:25], v[20:21]
	global_store_dwordx4 v[114:115], v[12:15], off
	global_load_dwordx4 v[12:15], v[102:103], off
	s_nop 0
	global_load_dwordx4 v[16:19], v[104:105], off
	s_waitcnt vmcnt(0)
	v_pk_fma_f32 v[8:9], v[12:13], v[8:9], v[16:17]
	v_pk_fma_f32 v[10:11], v[14:15], v[10:11], v[18:19]
	global_store_dwordx4 v[114:115], v[8:11], off offset:1024
	global_load_dwordx4 v[8:11], v[106:107], off
	s_nop 0
	global_load_dwordx4 v[12:15], v[108:109], off
	s_waitcnt vmcnt(0)
	v_pk_fma_f32 v[4:5], v[8:9], v[4:5], v[12:13]
	v_pk_fma_f32 v[6:7], v[10:11], v[6:7], v[14:15]
	global_store_dwordx4 v[114:115], v[4:7], off offset:2048
	global_load_dwordx4 v[4:7], v[110:111], off
	s_nop 0
	global_load_dwordx4 v[8:11], v[112:113], off
	s_waitcnt vmcnt(0)
	v_pk_fma_f32 v[0:1], v[4:5], v[0:1], v[8:9]
	v_pk_fma_f32 v[2:3], v[6:7], v[2:3], v[10:11]
	global_store_dwordx4 v[114:115], v[0:3], off offset:3072
	v_lshl_add_u64 v[114:115], v[114:115], 0, s[4:5]
	s_cbranch_scc1 .LBB0_1798
